# static s_setprio 1 for waves 4-7 across each GEMM phase, per-segment flips deleted (on top of v17)
# speedup vs baseline: 1.0189x; 1.0026x over previous
; __device__ __forceinline__ int otid() { int t = threadIdx.x; asm volatile("" : "+v"(t)); return t; }
; #define PG8_STAGE_B(b, h, bp) PG8_STAGE2(PG8_SB(b, h), (bp) + (h) * hstepB, voffB[0], voffB[1])
; #define PG8_STAGE_A(b, h, ap, NX) do { if constexpr (GATHER) { const unsigned _o0 = (NX) ? vn[h][0] : vc[h][0], _o1 = (NX) ? vn[h][1] : vc[h][1]; PG8_STAGE2(PG8_SA(b, h), (ap), _o0, _o1); } \
;         else { PG8_STAGE2(PG8_SA(b, h), (ap) + (h) * hstepA, voffA[0], voffA[1]); } } while (0)
; #define PG8_BAR __builtin_amdgcn_s_barrier()
; template <class Epi, class Sched, bool GATHER, bool LIGHTSKIP = false>
; __device__ __forceinline__ void gemm_phase(LAS unsigned char* lds, LAS unsigned char* xl, const int lda, const int ldb, const int K, const Sched& S, const Epi& E) {
;     const int tid = otid(), wid = __builtin_amdgcn_readfirstlane(tid >> 6), lane = tid & 63, wr = wid >> 2, wc = wid & 3, fr = lane & 15, fq = lane >> 4;
;     const int nt = K / BK;
;     int Rr[2], Cc[2]; unsigned voffA[2], voffB[2];
; #pragma unroll
;     for (int i = 0; i < 2; ++i) { stage_rc(tid * 16 + i * 8192, Rr[i], Cc[i]); const int Rb = Epi::PERM ? ((Rr[i] & ~31) + perm32(Rr[i] & 31)) : Rr[i];
;         voffA[i] = (unsigned)(Rr[i] * lda + Cc[i]) * 2u; voffB[i] = (unsigned)(Rb * ldb + Cc[i]) * 2u; }
;     unsigned vc[2][2], vn[2][2];
;     const size_t kstep = (size_t)(BK * 2);
;     const size_t hstepA = (size_t)HALF * lda * 2, hstepB = (size_t)HALF * ldb * 2;
;     const unsigned ldsw = (unsigned)wid * 1024u;
;     const int aoff = lds_byte(wr * 64 + fr, fq * 8), boff = lds_byte(wc * 32 + fr, fq * 8);
;     ...
;     GUnit cur, nxt; int ui = 0;
;     if (!S.next(0, cur)) return;
;     Acc acc;
; #pragma unroll
;     for (int a = 0; a < 2; ++a)
; #pragma unroll
;         for (int b = 0; b < 2; ++b)
; #pragma unroll
;             for (int m = 0; m < 4; ++m)
; #pragma unroll
;                 for (int n = 0; n < 2; ++n) acc[a][b][m][n] = (f32x4){0.f, 0.f, 0.f, 0.f};
;     bf16x8 At[4][2], B0[2][2], B1[2][2];
;     const char* cA = cur.A; const char* cB = cur.B;
;     if constexpr (GATHER) { S.offsets(cur, lda, vc);
; #pragma unroll
;         for (int h = 0; h < 2; ++h) { vn[h][0] = vc[h][0]; vn[h][1] = vc[h][1]; } }
;     PG8_STAGE_B(0, 0, cB); PG8_STAGE_B(0, 1, cB); PG8_STAGE_A(0, 0, cA, false); PG8_STAGE_A(0, 1, cA, false);
;     if (wr == 1) PG8_BAR;
;     PG8_WAIT_V(2); PG8_BAR;
.LBB0_144:
	s_or_b64 exec, exec, s[8:9]
	v_mov_b32_e32 v10, v0
	s_waitcnt lgkmcnt(0)
	s_barrier
	s_cmpk_gt_i32 s92, 0xbff
	v_readfirstlane_b32 s16, v10
	s_cbranch_scc1 .LBB0_160
	v_lshlrev_b32_e32 v1, 4, v10
	v_add_u32_e32 v2, 0x2000, v1
	v_ashrrev_i32_e32 v3, 31, v2
	v_lshrrev_b32_e32 v3, 22, v3
	v_add_u32_e32 v3, v2, v3
	v_ashrrev_i32_e32 v11, 10, v3
	v_mul_i32_i24_e32 v3, 0x400, v11
	v_sub_u32_e32 v2, v2, v3
	v_lshrrev_b32_e32 v3, 4, v2
	v_bitop3_b32 v2, v3, v2, 32 bitop3:0x6c
	v_ashrrev_i32_e32 v3, 31, v2
	v_lshrrev_b32_e32 v3, 26, v3
	v_add_u32_e32 v3, v2, v3
	v_lshlrev_b32_e32 v4, 3, v11
	v_ashrrev_i32_e32 v12, 6, v3
	v_and_b32_e32 v4, -16, v4
	v_add_u32_e32 v4, v12, v4
	v_and_b32_e32 v5, 3, v12
	s_mov_b32 s5, 0xfffe0
	v_lshrrev_b32_e32 v6, 2, v4
	v_lshlrev_b32_e32 v7, 1, v4
	v_and_b32_e32 v3, 0xc0, v3
	v_and_or_b32 v5, v4, s5, v5
	v_and_b32_e32 v6, 4, v6
	v_and_b32_e32 v7, 24, v7
	v_sub_u32_e32 v2, v2, v3
	v_mov_b32_e32 v3, 1
	v_or3_b32 v5, v5, v6, v7
	v_lshlrev_b32_e32 v6, 5, v11
	v_ashrrev_i16_sdwa v2, v3, sext(v2) dst_sel:DWORD dst_unused:UNUSED_PAD src0_sel:DWORD src1_sel:BYTE_0
	v_and_b32_e32 v6, 32, v6
	v_bfe_i32 v13, v2, 0, 16
	v_add_lshl_u32 v2, v6, v13, 1
	v_lshl_add_u32 v130, v5, 12, v2
	v_lshl_add_u32 v132, v4, 12, v2
	v_bfe_i32 v2, v10, 27, 1
	v_lshrrev_b32_e32 v2, 22, v2
	v_add_u32_e32 v2, v1, v2
	v_and_b32_e32 v2, 0xfffffc00, v2
	v_sub_u32_e32 v1, v1, v2
	v_lshrrev_b32_e32 v2, 4, v1
	v_bitop3_b32 v2, v2, v1, 32 bitop3:0x6c
	v_ashrrev_i32_e32 v1, 31, v1
	v_lshrrev_b32_e32 v1, 26, v1
	s_load_dwordx2 s[8:9], s[70:71], 0xd8
	v_add_u32_e32 v1, v2, v1
	v_ashrrev_i32_e32 v14, 6, v1
	v_ashrrev_i32_e32 v1, 31, v10
	v_lshrrev_b32_e32 v1, 26, v1
	v_add_u32_e32 v1, v10, v1
	v_ashrrev_i32_e32 v15, 6, v1
	s_waitcnt lgkmcnt(0)
	s_add_u32 s0, s8, 0x1c010000
	v_lshlrev_b32_e32 v1, 3, v15
	s_addc_u32 s1, s9, 0
	v_and_b32_e32 v1, -16, v1
	s_add_u32 s2, s8, 0x10000
	v_add_u32_e32 v1, v14, v1
	v_and_b32_e32 v4, 3, v14
	s_addc_u32 s3, s9, 0
	v_and_or_b32 v4, v1, s5, v4
	s_ashr_i32 s5, s92, 31
	s_lshr_b32 s6, s5, 29
	s_add_i32 s6, s92, s6
	s_ashr_i32 s18, s16, 6
	s_ashr_i32 s7, s6, 3
	s_and_b32 s6, s6, -8
	s_ashr_i32 s17, s16, 8
	s_lshl_b32 s4, s18, 10
	s_sub_i32 s10, s92, s6
	s_cmp_lt_i32 s10, 0
	s_movk_i32 s6, 0x181
	s_cselect_b32 s11, s6, 0x180
	s_mul_i32 s10, s10, s11
	s_add_i32 s10, s10, s7
	s_mul_hi_i32 s7, s10, 0x2aaaaaab
	s_lshr_b32 s11, s7, 31
	s_ashr_i32 s7, s7, 4
	s_add_i32 s7, s7, s11
	s_lshl_b32 s11, s7, 2
	s_mulk_i32 s7, 0x60
	s_sub_i32 s7, s10, s7
	s_bfe_i32 s10, s7, 0x80000
	s_bfe_u32 s10, s10, 0x2000d
	s_add_i32 s10, s7, s10
	s_bfe_i32 s12, s10, 0x80000
	s_and_b32 s10, s10, 0xfc
	s_sub_i32 s7, s7, s10
	s_sext_i32_i8 s7, s7
	s_add_i32 s14, s11, s7
	v_lshrrev_b32_e32 v5, 2, v1
	v_lshlrev_b32_e32 v6, 1, v1
	s_sext_i32_i16 s12, s12
	s_ashr_i32 s15, s14, 31
	v_and_b32_e32 v5, 4, v5
	v_and_b32_e32 v6, 24, v6
	s_lshr_b32 s12, s12, 2
	s_lshl_b64 s[10:11], s[14:15], 20
	v_or3_b32 v4, v4, v5, v6
	v_mul_i32_i24_e32 v6, 64, v14
	s_add_u32 s22, s0, s10
	v_sub_u32_e32 v2, v2, v6
	s_addc_u32 s23, s1, s11
	s_bfe_i64 s[10:11], s[12:13], 0x100000
	v_lshlrev_b32_e32 v5, 5, v15
	v_ashrrev_i16_sdwa v2, v3, sext(v2) dst_sel:DWORD dst_unused:UNUSED_PAD src0_sel:DWORD src1_sel:BYTE_0
	s_lshl_b64 s[10:11], s[10:11], 20
	v_and_b32_e32 v5, 32, v5
	v_bfe_i32 v16, v2, 0, 16
	s_add_u32 s28, s2, s10
	v_add_lshl_u32 v2, v5, v16, 1
	s_addc_u32 s29, s3, s11
	s_add_i32 s7, s4, 0
	v_lshl_add_u32 v134, v4, 12, v2
	s_add_i32 m0, s7, 0x10000
	v_lshl_add_u32 v136, v1, 12, v2
	global_load_lds_dwordx4 v134, s[28:29]
	s_add_i32 m0, s7, 0x12000
	s_add_u32 s10, s28, 0x80000
	global_load_lds_dwordx4 v130, s[28:29]
	s_addc_u32 s11, s29, 0
	s_add_i32 m0, s7, 0x14000
	s_add_i32 s26, s7, 0x2000
	global_load_lds_dwordx4 v134, s[10:11]
	s_add_i32 m0, s7, 0x16000
	v_mov_b32_e32 v135, 0
	global_load_lds_dwordx4 v130, s[10:11]
	s_mov_b32 m0, s7
	s_add_u32 s10, s22, 0x80000
	global_load_lds_dwordx4 v136, s[22:23]
	s_mov_b32 m0, s26
	s_addc_u32 s11, s23, 0
	s_add_i32 s27, s7, 0x4000
	global_load_lds_dwordx4 v132, s[22:23]
	s_mov_b32 m0, s27
	s_add_i32 s33, s7, 0x6000
	global_load_lds_dwordx4 v136, s[10:11]
	s_mov_b32 m0, s33
	v_mov_b32_e32 v131, v135
	global_load_lds_dwordx4 v132, s[10:11]
	v_mov_b32_e32 v137, v135
	v_mov_b32_e32 v133, v135
	s_cmp_eq_u32 s17, 1
	s_mov_b32 s34, 0
	v_lshl_add_u64 v[8:9], s[28:29], 0, v[134:135]
	v_lshl_add_u64 v[6:7], s[28:29], 0, v[130:131]
	v_lshl_add_u64 v[2:3], s[22:23], 0, v[136:137]
	s_cselect_b64 s[10:11], -1, 0
	s_cmp_lg_u32 s17, 1
	v_lshl_add_u64 v[4:5], s[22:23], 0, v[132:133]
	s_cbranch_scc1 .LBB0_147
	s_barrier
	s_setprio 1

; #define PG8_STAGE_B(b, h, bp) PG8_STAGE2(PG8_SB(b, h), (bp) + (h) * hstepB, voffB[0], voffB[1])
; #define PG8_STAGE_A(b, h, ap, NX) do { if constexpr (GATHER) { const unsigned _o0 = (NX) ? vn[h][0] : vc[h][0], _o1 = (NX) ? vn[h][1] : vc[h][1]; PG8_STAGE2(PG8_SA(b, h), (ap), _o0, _o1); } \
;         else { PG8_STAGE2(PG8_SA(b, h), (ap) + (h) * hstepA, voffA[0], voffA[1]); } } while (0)
; #define PG8_LDA(dst, b, h) do { _Pragma("unroll") for (int m = 0; m < 4; ++m) _Pragma("unroll") for (int k = 0; k < 2; ++k) dst[m][k] = *(const LAS bf16x8*)(lds + PG8_SA(b, h) + aoff + m * 2048 + k * 1024); } while (0)
; #define PG8_LDB(dst, b, h) do { _Pragma("unroll") for (int n = 0; n < 2; ++n) _Pragma("unroll") for (int k = 0; k < 2; ++k) dst[n][k] = *(const LAS bf16x8*)(lds + PG8_SB(b, h) + boff + n * 2048 + k * 1024); } while (0)
; #define PG8_MMA(ai, bj, At, Bt) do { __builtin_amdgcn_s_setprio(1); _Pragma("unroll") for (int m = 0; m < 4; ++m) _Pragma("unroll") for (int n = 0; n < 2; ++n) _Pragma("unroll") for (int k = 0; k < 2; ++k) \
;         acc[ai][bj][m][n] = __builtin_amdgcn_mfma_f32_16x16x32_bf16(Bt[n][k], At[m][k], acc[ai][bj][m][n], 0, 0, 0); __builtin_amdgcn_s_setprio(0); } while (0)
; #define PG8_WAIT_V(n) asm volatile("s_waitcnt vmcnt(" #n ")" ::: "memory")
; #define PG8_WAIT_L(n) asm volatile("s_waitcnt lgkmcnt(" #n ")" ::: "memory")
; #define PG8_BAR __builtin_amdgcn_s_barrier()
; #define PG8_SCHED __builtin_amdgcn_sched_barrier(0)
; template <class Epi, class Sched, bool GATHER, bool LIGHTSKIP = false>
; __device__ __forceinline__ void gemm_phase(LAS unsigned char* lds, LAS unsigned char* xl, const int lda, const int ldb, const int K, const Sched& S, const Epi& E) {
;     ...
;             PG8_LDB(B0, 0, 0); PG8_LDB(B1, 0, 1); PG8_SCHED; PG8_LDA(At, 0, 0); PG8_STAGE_A(1, 1, a1, false);
;             PG8_WAIT_V(8); PG8_WAIT_L(0); PG8_BAR; PG8_MMA(0, 0, At, B0); PG8_MMA(0, 1, At, B1); PG8_BAR; PG8_SCHED;
;             PG8_LDA(At, 0, 1); PG8_STAGE_B(0, 0, b2); PG8_STAGE_B(0, 1, b2); PG8_STAGE_A(0, 0, a2, last);
.LBB0_153:
	ds_read_b128 v[152:155], v148
	ds_read_b128 v[156:159], v148 offset:1024
	ds_read_b128 v[160:163], v148 offset:2048
	ds_read_b128 v[164:167], v148 offset:3072
	ds_read_b128 v[168:171], v149
	ds_read_b128 v[172:175], v149 offset:1024
	ds_read_b128 v[176:179], v149 offset:2048
	ds_read_b128 v[180:183], v149 offset:3072
	s_add_u32 s28, s22, 0xfff80080
	s_addc_u32 s29, s23, -1
	s_cmp_eq_u32 s47, 28
	s_cselect_b32 s31, s19, s29
	s_cselect_b32 s30, s18, s28
	s_cselect_b32 s29, s21, s46
	s_cselect_b32 s28, s20, s45
	v_lshl_add_u64 v[216:217], s[22:23], 0, v[138:139]
	s_add_i32 m0, s7, 0xc000
	ds_read_b128 v[184:187], v150
	ds_read_b128 v[188:191], v150 offset:1024
	ds_read_b128 v[192:195], v150 offset:2048
	ds_read_b128 v[196:199], v150 offset:3072
	ds_read_b128 v[200:203], v150 offset:4096
	ds_read_b128 v[204:207], v150 offset:5120
	ds_read_b128 v[208:211], v150 offset:6144
	ds_read_b128 v[212:215], v150 offset:7168
	global_load_lds_dwordx4 v[216:217], off
	v_lshl_add_u64 v[216:217], s[22:23], 0, v[140:141]
	s_add_i32 m0, s7, 0xe000
	s_nop 0
	global_load_lds_dwordx4 v[216:217], off
	s_waitcnt vmcnt(8)
	s_waitcnt lgkmcnt(0)
	s_barrier
	s_waitcnt lgkmcnt(0)
	v_mfma_f32_16x16x32_bf16 v[126:129], v[152:155], v[184:187], v[126:129]
	v_mfma_f32_16x16x32_bf16 v[122:125], v[160:163], v[184:187], v[122:125]
	v_mfma_f32_16x16x32_bf16 v[118:121], v[152:155], v[192:195], v[118:121]
	v_mfma_f32_16x16x32_bf16 v[114:117], v[160:163], v[192:195], v[114:117]
	v_mfma_f32_16x16x32_bf16 v[102:105], v[152:155], v[200:203], v[102:105]
	v_mfma_f32_16x16x32_bf16 v[98:101], v[160:163], v[200:203], v[98:101]
	v_mfma_f32_16x16x32_bf16 v[86:89], v[152:155], v[208:211], v[86:89]
	v_mfma_f32_16x16x32_bf16 v[82:85], v[160:163], v[208:211], v[82:85]
	v_mfma_f32_16x16x32_bf16 v[126:129], v[156:159], v[188:191], v[126:129]
	v_mfma_f32_16x16x32_bf16 v[122:125], v[164:167], v[188:191], v[122:125]
	v_mfma_f32_16x16x32_bf16 v[118:121], v[156:159], v[196:199], v[118:121]
	v_mfma_f32_16x16x32_bf16 v[114:117], v[164:167], v[196:199], v[114:117]
	v_mfma_f32_16x16x32_bf16 v[102:105], v[156:159], v[204:207], v[102:105]
	v_mfma_f32_16x16x32_bf16 v[98:101], v[164:167], v[204:207], v[98:101]
	v_mfma_f32_16x16x32_bf16 v[86:89], v[156:159], v[212:215], v[86:89]
	v_mfma_f32_16x16x32_bf16 v[82:85], v[164:167], v[212:215], v[82:85]
	v_mfma_f32_16x16x32_bf16 v[110:113], v[168:171], v[184:187], v[110:113]
	v_mfma_f32_16x16x32_bf16 v[106:109], v[176:179], v[184:187], v[106:109]
	v_mfma_f32_16x16x32_bf16 v[94:97], v[168:171], v[192:195], v[94:97]
	v_mfma_f32_16x16x32_bf16 v[90:93], v[176:179], v[192:195], v[90:93]
	v_mfma_f32_16x16x32_bf16 v[78:81], v[168:171], v[200:203], v[78:81]
	v_mfma_f32_16x16x32_bf16 v[74:77], v[176:179], v[200:203], v[74:77]
	v_mfma_f32_16x16x32_bf16 v[70:73], v[168:171], v[208:211], v[70:73]
	v_mfma_f32_16x16x32_bf16 v[66:69], v[176:179], v[208:211], v[66:69]
	v_mfma_f32_16x16x32_bf16 v[110:113], v[172:175], v[188:191], v[110:113]
	v_mfma_f32_16x16x32_bf16 v[106:109], v[180:183], v[188:191], v[106:109]
	v_mfma_f32_16x16x32_bf16 v[94:97], v[172:175], v[196:199], v[94:97]
	v_mfma_f32_16x16x32_bf16 v[90:93], v[180:183], v[196:199], v[90:93]
	v_mfma_f32_16x16x32_bf16 v[78:81], v[172:175], v[204:207], v[78:81]
	v_mfma_f32_16x16x32_bf16 v[74:77], v[180:183], v[204:207], v[74:77]
	v_mfma_f32_16x16x32_bf16 v[70:73], v[172:175], v[212:215], v[70:73]
	v_mfma_f32_16x16x32_bf16 v[66:69], v[180:183], v[212:215], v[66:69]
	s_barrier
	s_add_i32 s48, s38, s4
	v_lshl_add_u64 v[216:217], s[28:29], 0, v[134:135]
	s_mov_b32 m0, s48
	ds_read_b128 v[184:187], v150 offset:16384
	ds_read_b128 v[188:191], v150 offset:17408
	ds_read_b128 v[192:195], v150 offset:18432
	ds_read_b128 v[196:199], v150 offset:19456
	ds_read_b128 v[200:203], v150 offset:20480
	ds_read_b128 v[204:207], v150 offset:21504
	ds_read_b128 v[208:211], v150 offset:22528
	ds_read_b128 v[212:215], v150 offset:23552
	global_load_lds_dwordx4 v[216:217], off
	s_add_i32 m0, s48, 0x2000
	s_add_u32 s48, s28, 0x80000
	v_lshl_add_u64 v[218:219], s[28:29], 0, v[130:131]
	s_addc_u32 s49, s29, 0
	s_add_i32 s50, s39, s4
	global_load_lds_dwordx4 v[218:219], off
	v_lshl_add_u64 v[220:221], s[48:49], 0, v[134:135]
	s_mov_b32 m0, s50
	v_lshl_add_u64 v[222:223], s[30:31], 0, v[132:133]
	global_load_lds_dwordx4 v[220:221], off
	v_lshl_add_u64 v[220:221], s[48:49], 0, v[130:131]
	s_add_i32 m0, s50, 0x2000
	s_nop 0
	global_load_lds_dwordx4 v[220:221], off
	v_lshl_add_u64 v[220:221], s[30:31], 0, v[136:137]
	s_mov_b32 m0, s7
	s_nop 0
	global_load_lds_dwordx4 v[220:221], off
	s_mov_b32 m0, s26
	s_nop 0
	global_load_lds_dwordx4 v[222:223], off
	s_waitcnt vmcnt(8)
	s_waitcnt lgkmcnt(0)
	s_barrier
; #define PG8_STAGE_A(b, h, ap, NX) do { if constexpr (GATHER) { const unsigned _o0 = (NX) ? vn[h][0] : vc[h][0], _o1 = (NX) ? vn[h][1] : vc[h][1]; PG8_STAGE2(PG8_SA(b, h), (ap), _o0, _o1); } \
;         else { PG8_STAGE2(PG8_SA(b, h), (ap) + (h) * hstepA, voffA[0], voffA[1]); } } while (0)
; #define PG8_LDA(dst, b, h) do { _Pragma("unroll") for (int m = 0; m < 4; ++m) _Pragma("unroll") for (int k = 0; k < 2; ++k) dst[m][k] = *(const LAS bf16x8*)(lds + PG8_SA(b, h) + aoff + m * 2048 + k * 1024); } while (0)
; #define PG8_LDB(dst, b, h) do { _Pragma("unroll") for (int n = 0; n < 2; ++n) _Pragma("unroll") for (int k = 0; k < 2; ++k) dst[n][k] = *(const LAS bf16x8*)(lds + PG8_SB(b, h) + boff + n * 2048 + k * 1024); } while (0)
; #define PG8_MMA(ai, bj, At, Bt) do { __builtin_amdgcn_s_setprio(1); _Pragma("unroll") for (int m = 0; m < 4; ++m) _Pragma("unroll") for (int n = 0; n < 2; ++n) _Pragma("unroll") for (int k = 0; k < 2; ++k) \
;         acc[ai][bj][m][n] = __builtin_amdgcn_mfma_f32_16x16x32_bf16(Bt[n][k], At[m][k], acc[ai][bj][m][n], 0, 0, 0); __builtin_amdgcn_s_setprio(0); } while (0)
; #define PG8_WAIT_V(n) asm volatile("s_waitcnt vmcnt(" #n ")" ::: "memory")
; #define PG8_WAIT_L(n) asm volatile("s_waitcnt lgkmcnt(" #n ")" ::: "memory")
; #define PG8_BAR __builtin_amdgcn_s_barrier()
; #define PG8_SCHED __builtin_amdgcn_sched_barrier(0)
; template <class Epi, class Sched, bool GATHER, bool LIGHTSKIP = false>
; __device__ __forceinline__ void gemm_phase(LAS unsigned char* lds, LAS unsigned char* xl, const int lda, const int ldb, const int K, const Sched& S, const Epi& E) {
;     ...
;             PG8_WAIT_V(8); PG8_WAIT_L(0); PG8_BAR; if (!light) { PG8_MMA(1, 0, At, B0); PG8_MMA(1, 1, At, B1); } PG8_BAR; PG8_SCHED;
;             PG8_LDB(B0, 1, 0); PG8_LDB(B1, 1, 1); PG8_SCHED; PG8_LDA(At, 1, 0); PG8_STAGE_A(0, 1, a2, last);
;             PG8_WAIT_V(8); PG8_WAIT_L(0); PG8_BAR; PG8_MMA(0, 0, At, B0); PG8_MMA(0, 1, At, B1); PG8_BAR; PG8_SCHED;
	s_waitcnt lgkmcnt(0)
	v_mfma_f32_16x16x32_bf16 v[62:65], v[152:155], v[184:187], v[62:65]
	v_mfma_f32_16x16x32_bf16 v[58:61], v[160:163], v[184:187], v[58:61]
	v_mfma_f32_16x16x32_bf16 v[54:57], v[152:155], v[192:195], v[54:57]
	v_mfma_f32_16x16x32_bf16 v[50:53], v[160:163], v[192:195], v[50:53]
	v_mfma_f32_16x16x32_bf16 v[38:41], v[152:155], v[200:203], v[38:41]
	v_mfma_f32_16x16x32_bf16 v[34:37], v[160:163], v[200:203], v[34:37]
	v_mfma_f32_16x16x32_bf16 v[22:25], v[152:155], v[208:211], v[22:25]
	v_mfma_f32_16x16x32_bf16 v[18:21], v[160:163], v[208:211], v[18:21]
	v_mfma_f32_16x16x32_bf16 v[62:65], v[156:159], v[188:191], v[62:65]
	v_mfma_f32_16x16x32_bf16 v[58:61], v[164:167], v[188:191], v[58:61]
	v_mfma_f32_16x16x32_bf16 v[54:57], v[156:159], v[196:199], v[54:57]
	v_mfma_f32_16x16x32_bf16 v[50:53], v[164:167], v[196:199], v[50:53]
	v_mfma_f32_16x16x32_bf16 v[38:41], v[156:159], v[204:207], v[38:41]
	v_mfma_f32_16x16x32_bf16 v[34:37], v[164:167], v[204:207], v[34:37]
	v_mfma_f32_16x16x32_bf16 v[22:25], v[156:159], v[212:215], v[22:25]
	v_mfma_f32_16x16x32_bf16 v[18:21], v[164:167], v[212:215], v[18:21]
	v_mfma_f32_16x16x32_bf16 v[46:49], v[168:171], v[184:187], v[46:49]
	v_mfma_f32_16x16x32_bf16 v[42:45], v[176:179], v[184:187], v[42:45]
	v_mfma_f32_16x16x32_bf16 v[30:33], v[168:171], v[192:195], v[30:33]
	v_mfma_f32_16x16x32_bf16 v[26:29], v[176:179], v[192:195], v[26:29]
	v_mfma_f32_16x16x32_bf16 v[14:17], v[168:171], v[200:203], v[14:17]
	v_mfma_f32_16x16x32_bf16 v[10:13], v[176:179], v[200:203], v[10:13]
	v_mfma_f32_16x16x32_bf16 v[6:9], v[168:171], v[208:211], v[6:9]
	v_mfma_f32_16x16x32_bf16 v[2:5], v[176:179], v[208:211], v[2:5]
	v_mfma_f32_16x16x32_bf16 v[46:49], v[172:175], v[188:191], v[46:49]
	v_mfma_f32_16x16x32_bf16 v[42:45], v[180:183], v[188:191], v[42:45]
	v_mfma_f32_16x16x32_bf16 v[30:33], v[172:175], v[196:199], v[30:33]
	v_mfma_f32_16x16x32_bf16 v[26:29], v[180:183], v[196:199], v[26:29]
	v_mfma_f32_16x16x32_bf16 v[14:17], v[172:175], v[204:207], v[14:17]
	v_mfma_f32_16x16x32_bf16 v[10:13], v[180:183], v[204:207], v[10:13]
	v_mfma_f32_16x16x32_bf16 v[6:9], v[172:175], v[212:215], v[6:9]
	v_mfma_f32_16x16x32_bf16 v[2:5], v[180:183], v[212:215], v[2:5]
	s_barrier
	s_add_i32 s48, 0, 0x18000
	v_add_u32_e32 v151, s48, v146
	s_add_i32 s49, 0, 0x1c000
	ds_read_b128 v[152:155], v151
	ds_read_b128 v[156:159], v151 offset:1024
	ds_read_b128 v[160:163], v151 offset:2048
	ds_read_b128 v[164:167], v151 offset:3072
	v_add_u32_e32 v151, s49, v146
	ds_read_b128 v[168:171], v151
	ds_read_b128 v[172:175], v151 offset:1024
	ds_read_b128 v[176:179], v151 offset:2048
	ds_read_b128 v[180:183], v151 offset:3072
	s_add_u32 s30, s30, 0x80000
	s_addc_u32 s31, s31, 0
	s_mov_b32 m0, s27
	v_lshl_add_u64 v[224:225], s[30:31], 0, v[136:137]
	ds_read_b128 v[184:187], v150 offset:32768
	ds_read_b128 v[188:191], v150 offset:33792
	ds_read_b128 v[192:195], v150 offset:34816
	ds_read_b128 v[196:199], v150 offset:35840
	ds_read_b128 v[200:203], v150 offset:36864
	ds_read_b128 v[204:207], v150 offset:37888
	ds_read_b128 v[208:211], v150 offset:38912
	ds_read_b128 v[212:215], v150 offset:39936
	global_load_lds_dwordx4 v[224:225], off
	v_lshl_add_u64 v[224:225], s[30:31], 0, v[132:133]
	s_mov_b32 m0, s33
	s_nop 0
	global_load_lds_dwordx4 v[224:225], off
	s_waitcnt vmcnt(8)
	s_waitcnt lgkmcnt(0)
	s_barrier
	s_waitcnt lgkmcnt(0)
	v_mfma_f32_16x16x32_bf16 v[126:129], v[152:155], v[184:187], v[126:129]
	v_mfma_f32_16x16x32_bf16 v[122:125], v[160:163], v[184:187], v[122:125]
	v_mfma_f32_16x16x32_bf16 v[118:121], v[152:155], v[192:195], v[118:121]
	v_mfma_f32_16x16x32_bf16 v[114:117], v[160:163], v[192:195], v[114:117]
	v_mfma_f32_16x16x32_bf16 v[102:105], v[152:155], v[200:203], v[102:105]
	v_mfma_f32_16x16x32_bf16 v[98:101], v[160:163], v[200:203], v[98:101]
	v_mfma_f32_16x16x32_bf16 v[86:89], v[152:155], v[208:211], v[86:89]
	v_mfma_f32_16x16x32_bf16 v[82:85], v[160:163], v[208:211], v[82:85]
	v_mfma_f32_16x16x32_bf16 v[126:129], v[156:159], v[188:191], v[126:129]
	v_mfma_f32_16x16x32_bf16 v[122:125], v[164:167], v[188:191], v[122:125]
	v_mfma_f32_16x16x32_bf16 v[118:121], v[156:159], v[196:199], v[118:121]
	v_mfma_f32_16x16x32_bf16 v[114:117], v[164:167], v[196:199], v[114:117]
	v_mfma_f32_16x16x32_bf16 v[102:105], v[156:159], v[204:207], v[102:105]
	v_mfma_f32_16x16x32_bf16 v[98:101], v[164:167], v[204:207], v[98:101]
	v_mfma_f32_16x16x32_bf16 v[86:89], v[156:159], v[212:215], v[86:89]
	v_mfma_f32_16x16x32_bf16 v[82:85], v[164:167], v[212:215], v[82:85]
	v_mfma_f32_16x16x32_bf16 v[110:113], v[168:171], v[184:187], v[110:113]
	v_mfma_f32_16x16x32_bf16 v[106:109], v[176:179], v[184:187], v[106:109]
	v_mfma_f32_16x16x32_bf16 v[94:97], v[168:171], v[192:195], v[94:97]
	v_mfma_f32_16x16x32_bf16 v[90:93], v[176:179], v[192:195], v[90:93]
	v_mfma_f32_16x16x32_bf16 v[78:81], v[168:171], v[200:203], v[78:81]
	v_mfma_f32_16x16x32_bf16 v[74:77], v[176:179], v[200:203], v[74:77]
	v_mfma_f32_16x16x32_bf16 v[70:73], v[168:171], v[208:211], v[70:73]
	v_mfma_f32_16x16x32_bf16 v[66:69], v[176:179], v[208:211], v[66:69]
	v_mfma_f32_16x16x32_bf16 v[110:113], v[172:175], v[188:191], v[110:113]
	v_mfma_f32_16x16x32_bf16 v[106:109], v[180:183], v[188:191], v[106:109]
	v_mfma_f32_16x16x32_bf16 v[94:97], v[172:175], v[196:199], v[94:97]
	v_mfma_f32_16x16x32_bf16 v[90:93], v[180:183], v[196:199], v[90:93]
	v_mfma_f32_16x16x32_bf16 v[78:81], v[172:175], v[204:207], v[78:81]
	v_mfma_f32_16x16x32_bf16 v[74:77], v[180:183], v[204:207], v[74:77]
	v_mfma_f32_16x16x32_bf16 v[70:73], v[172:175], v[212:215], v[70:73]
	v_mfma_f32_16x16x32_bf16 v[66:69], v[180:183], v[212:215], v[66:69]
	s_barrier
; #define PG8_STAGE_B(b, h, bp) PG8_STAGE2(PG8_SB(b, h), (bp) + (h) * hstepB, voffB[0], voffB[1])
; #define PG8_STAGE_A(b, h, ap, NX) do { if constexpr (GATHER) { const unsigned _o0 = (NX) ? vn[h][0] : vc[h][0], _o1 = (NX) ? vn[h][1] : vc[h][1]; PG8_STAGE2(PG8_SA(b, h), (ap), _o0, _o1); } \
;         else { PG8_STAGE2(PG8_SA(b, h), (ap) + (h) * hstepA, voffA[0], voffA[1]); } } while (0)
; #define PG8_LDA(dst, b, h) do { _Pragma("unroll") for (int m = 0; m < 4; ++m) _Pragma("unroll") for (int k = 0; k < 2; ++k) dst[m][k] = *(const LAS bf16x8*)(lds + PG8_SA(b, h) + aoff + m * 2048 + k * 1024); } while (0)
; #define PG8_MMA(ai, bj, At, Bt) do { __builtin_amdgcn_s_setprio(1); _Pragma("unroll") for (int m = 0; m < 4; ++m) _Pragma("unroll") for (int n = 0; n < 2; ++n) _Pragma("unroll") for (int k = 0; k < 2; ++k) \
;         acc[ai][bj][m][n] = __builtin_amdgcn_mfma_f32_16x16x32_bf16(Bt[n][k], At[m][k], acc[ai][bj][m][n], 0, 0, 0); __builtin_amdgcn_s_setprio(0); } while (0)
; #define PG8_WAIT_V(n) asm volatile("s_waitcnt vmcnt(" #n ")" ::: "memory")
; #define PG8_WAIT_L(n) asm volatile("s_waitcnt lgkmcnt(" #n ")" ::: "memory")
; #define PG8_BAR __builtin_amdgcn_s_barrier()
; #define PG8_SCHED __builtin_amdgcn_sched_barrier(0)
; template <class Epi, class Sched, bool GATHER, bool LIGHTSKIP = false>
; __device__ __forceinline__ void gemm_phase(LAS unsigned char* lds, LAS unsigned char* xl, const int lda, const int ldb, const int K, const Sched& S, const Epi& E) {
;     ...
;             PG8_LDA(At, 1, 1); PG8_STAGE_B(1, 0, b3); PG8_STAGE_B(1, 1, b3); PG8_STAGE_A(1, 0, a3, last);
;             PG8_WAIT_V(8); PG8_WAIT_L(0); PG8_BAR; if (!light) { PG8_MMA(1, 0, At, B0); PG8_MMA(1, 1, At, B1); } PG8_BAR; PG8_SCHED;
;         }
;         if (wr == 0) PG8_BAR;
	s_add_i32 s30, s48, s4
	v_lshl_add_u64 v[216:217], v[216:217], 0, s[14:15]
	s_mov_b32 m0, s30
	ds_read_b128 v[184:187], v150 offset:49152
	ds_read_b128 v[188:191], v150 offset:50176
	ds_read_b128 v[192:195], v150 offset:51200
	ds_read_b128 v[196:199], v150 offset:52224
	ds_read_b128 v[200:203], v150 offset:53248
	ds_read_b128 v[204:207], v150 offset:54272
	ds_read_b128 v[208:211], v150 offset:55296
	ds_read_b128 v[212:215], v150 offset:56320
	global_load_lds_dwordx4 v[216:217], off
	s_add_i32 m0, s30, 0x2000
	s_add_u32 s28, s28, 0x80080
	v_lshl_add_u64 v[216:217], v[218:219], 0, s[14:15]
	s_addc_u32 s29, s29, 0
	s_add_i32 s30, s49, s4
	global_load_lds_dwordx4 v[216:217], off
	v_lshl_add_u64 v[216:217], s[28:29], 0, v[134:135]
	s_mov_b32 m0, s30
	s_nop 0
	global_load_lds_dwordx4 v[216:217], off
	v_lshl_add_u64 v[216:217], s[28:29], 0, v[130:131]
	s_add_i32 m0, s30, 0x2000
	s_nop 0
	global_load_lds_dwordx4 v[216:217], off
	v_lshl_add_u64 v[216:217], v[220:221], 0, s[14:15]
	s_mov_b32 m0, s35
	s_nop 0
	global_load_lds_dwordx4 v[216:217], off
	v_lshl_add_u64 v[216:217], v[222:223], 0, s[14:15]
	s_mov_b32 m0, s36
	s_nop 0
	global_load_lds_dwordx4 v[216:217], off
	s_waitcnt vmcnt(8)
	s_waitcnt lgkmcnt(0)
	s_barrier
	s_waitcnt lgkmcnt(0)
	v_mfma_f32_16x16x32_bf16 v[62:65], v[152:155], v[184:187], v[62:65]
	v_mfma_f32_16x16x32_bf16 v[58:61], v[160:163], v[184:187], v[58:61]
	v_mfma_f32_16x16x32_bf16 v[54:57], v[152:155], v[192:195], v[54:57]
	v_mfma_f32_16x16x32_bf16 v[50:53], v[160:163], v[192:195], v[50:53]
	v_mfma_f32_16x16x32_bf16 v[38:41], v[152:155], v[200:203], v[38:41]
	v_mfma_f32_16x16x32_bf16 v[34:37], v[160:163], v[200:203], v[34:37]
	v_mfma_f32_16x16x32_bf16 v[22:25], v[152:155], v[208:211], v[22:25]
	v_mfma_f32_16x16x32_bf16 v[18:21], v[160:163], v[208:211], v[18:21]
	v_mfma_f32_16x16x32_bf16 v[62:65], v[156:159], v[188:191], v[62:65]
	v_mfma_f32_16x16x32_bf16 v[58:61], v[164:167], v[188:191], v[58:61]
	v_mfma_f32_16x16x32_bf16 v[54:57], v[156:159], v[196:199], v[54:57]
	v_mfma_f32_16x16x32_bf16 v[50:53], v[164:167], v[196:199], v[50:53]
	v_mfma_f32_16x16x32_bf16 v[38:41], v[156:159], v[204:207], v[38:41]
	v_mfma_f32_16x16x32_bf16 v[34:37], v[164:167], v[204:207], v[34:37]
	v_mfma_f32_16x16x32_bf16 v[22:25], v[156:159], v[212:215], v[22:25]
	v_mfma_f32_16x16x32_bf16 v[18:21], v[164:167], v[212:215], v[18:21]
	v_mfma_f32_16x16x32_bf16 v[46:49], v[168:171], v[184:187], v[46:49]
	v_mfma_f32_16x16x32_bf16 v[42:45], v[176:179], v[184:187], v[42:45]
	v_mfma_f32_16x16x32_bf16 v[30:33], v[168:171], v[192:195], v[30:33]
	v_mfma_f32_16x16x32_bf16 v[26:29], v[176:179], v[192:195], v[26:29]
	v_mfma_f32_16x16x32_bf16 v[14:17], v[168:171], v[200:203], v[14:17]
	v_mfma_f32_16x16x32_bf16 v[10:13], v[176:179], v[200:203], v[10:13]
	v_mfma_f32_16x16x32_bf16 v[6:9], v[168:171], v[208:211], v[6:9]
	v_mfma_f32_16x16x32_bf16 v[2:5], v[176:179], v[208:211], v[2:5]
	v_mfma_f32_16x16x32_bf16 v[46:49], v[172:175], v[188:191], v[46:49]
	v_mfma_f32_16x16x32_bf16 v[42:45], v[180:183], v[188:191], v[42:45]
	v_mfma_f32_16x16x32_bf16 v[30:33], v[172:175], v[196:199], v[30:33]
	v_mfma_f32_16x16x32_bf16 v[26:29], v[180:183], v[196:199], v[26:29]
	v_mfma_f32_16x16x32_bf16 v[14:17], v[172:175], v[204:207], v[14:17]
	v_mfma_f32_16x16x32_bf16 v[10:13], v[180:183], v[204:207], v[10:13]
	v_mfma_f32_16x16x32_bf16 v[6:9], v[172:175], v[212:215], v[6:9]
	v_mfma_f32_16x16x32_bf16 v[2:5], v[180:183], v[212:215], v[2:5]
	s_barrier
	s_add_i32 s47, s47, 2
	s_add_u32 s22, s22, 0x100
	s_addc_u32 s23, s23, 0
	s_add_u32 s45, s45, 0x100
	s_addc_u32 s46, s46, 0
	s_cmp_gt_u32 s47, 29
	s_cbranch_scc0 .LBB0_153
	s_and_b64 vcc, exec, s[16:17]
	s_cbranch_vccz .LBB0_156
	s_barrier

; #define PG8_WAIT_V(n) asm volatile("s_waitcnt vmcnt(" #n ")" ::: "memory")
; #define PG8_BAR __builtin_amdgcn_s_barrier()
; template <class Epi, class Sched, bool GATHER, bool LIGHTSKIP = false>
; __device__ __forceinline__ void gemm_phase(LAS unsigned char* lds, LAS unsigned char* xl, const int lda, const int ldb, const int K, const Sched& S, const Epi& E) {
;     ...
;     PG8_WAIT_V(0);
;     PG8_BAR;
.LBB0_159:
	s_waitcnt vmcnt(0)
	s_barrier
	s_setprio 0

; #define LAS __attribute__((address_space(3)))
; __device__ __forceinline__ bf16x8 pack8(const f32x4 x, const f32x4 y) { u32x4 w; w.x = cvt_pk_bf16(x[0], x[1]); w.y = cvt_pk_bf16(x[2], x[3]); w.z = cvt_pk_bf16(y[0], y[1]); w.w = cvt_pk_bf16(y[2], y[3]); return __builtin_bit_cast(bf16x8, w); }
; #define GC_DMA(sg, bufi) do { _Pragma("unroll") for (int _k = 0; _k < 4; ++_k) { const int _pc = wid + 8 * _k; \
;         __builtin_amdgcn_global_load_lds((const unsigned*)(pimg0 + (size_t)(sg) * 32768 + _pc * 1024 + lane * 16), (LAS unsigned*)(lds + (bufi) * 32768 + _pc * 1024), 16, 0, 0); } } while (0)
; __device__ __forceinline__ void ph_gdn_combine(const Params& p, LAS unsigned char* lds) {
;     ...
;     for (int sg = 0; sg < 16; ++sg) {
;         const int cur = sg & 1;
;         f32x4 qv[8];
; #pragma unroll
;         for (int a = 0; a < 8; ++a) { sin0[((size_t)sg * 64 + wid * 8 + a) * 64 + lane] = S[a]; qv[a] = qf0[((size_t)sg * 64 + wid * 8 + a) * 64 + lane]; }
;         asm volatile("s_waitcnt vmcnt(0)" ::: "memory"); __builtin_amdgcn_s_barrier();
;         if (sg + 1 < 16) GC_DMA(sg + 1, cur ^ 1);
;         const LAS unsigned char* PI = lds + cur * 32768;
;         bf16x8 SB[4];
; #pragma unroll
;         for (int s = 0; s < 4; ++s) SB[s] = pack8(S[2 * s], S[2 * s + 1]);
; #pragma unroll
;         for (int a = 0; a < 8; ++a) { f32x4 acc = qv[a];
; #pragma unroll
;             for (int s = 0; s < 4; ++s) acc = __builtin_amdgcn_mfma_f32_16x16x32_bf16(frag256(PI, 16 * a + m16, 4 * s + q4), SB[s], acc, 0, 0, 0);
;             S[a] = acc; }
;     }
.LBB0_456:
	v_lshl_add_u64 v[48:49], s[28:29], 0, v[130:131]
	v_add_co_u32_e32 v52, vcc, s1, v48
	v_lshl_add_u64 v[50:51], s[8:9], 0, v[130:131]
	s_nop 0
	v_addc_co_u32_e32 v53, vcc, 0, v49, vcc
	v_add_co_u32_e32 v48, vcc, s3, v48
	v_cvt_pk_bf16_f32 v42, v14, v15
	s_nop 0
	v_addc_co_u32_e32 v49, vcc, 0, v49, vcc
	v_add_co_u32_e32 v54, vcc, s2, v50
	global_store_dwordx4 v[48:49], v[14:17], off offset:-4096
	s_nop 0
	v_addc_co_u32_e32 v55, vcc, 0, v51, vcc
	v_add_co_u32_e32 v74, vcc, s4, v50
	v_cvt_pk_bf16_f32 v43, v16, v17
	s_nop 0
	v_addc_co_u32_e32 v75, vcc, 0, v51, vcc
	global_load_dwordx4 v[14:17], v[74:75], off offset:-4096
	v_cvt_pk_bf16_f32 v44, v22, v23
	global_store_dwordx4 v[52:53], v[22:25], off offset:1024
	v_cvt_pk_bf16_f32 v45, v24, v25
	global_load_dwordx4 v[22:25], v[54:55], off offset:1024
	v_cvt_pk_bf16_f32 v46, v26, v27
	global_store_dwordx4 v[52:53], v[26:29], off offset:2048
	v_cvt_pk_bf16_f32 v47, v28, v29
	global_load_dwordx4 v[26:29], v[54:55], off offset:2048
	s_and_b32 s5, s93, 0x8000
	global_store_dwordx4 v[52:53], v[18:21], off offset:3072
	global_load_dwordx4 v[50:53], v[54:55], off offset:3072
	s_xor_b32 s6, s5, 0x8000
	global_store_dwordx4 v[48:49], v[6:9], off
	global_load_dwordx4 v[54:57], v[74:75], off
	v_add_u32_e32 v76, s5, v1
	global_store_dwordx4 v[48:49], v[10:13], off offset:1024
	global_load_dwordx4 v[58:61], v[74:75], off offset:1024
	s_add_i32 s5, s0, s6
	global_store_dwordx4 v[48:49], v[2:5], off offset:2048
	global_load_dwordx4 v[62:65], v[74:75], off offset:2048
	v_lshl_add_u64 v[66:67], s[14:15], 0, v[130:131]
	global_store_dwordx4 v[48:49], v[30:33], off offset:3072
	global_load_dwordx4 v[30:33], v[74:75], off offset:3072
	s_mov_b32 m0, s5
	v_lshl_add_u64 v[68:69], s[16:17], 0, v[130:131]
	s_waitcnt vmcnt(0)
	s_barrier
	global_load_lds_dwordx4 v[66:67], off
	s_add_i32 m0, s5, 0x2000
	v_lshl_add_u64 v[70:71], s[18:19], 0, v[130:131]
	global_load_lds_dwordx4 v[68:69], off
	s_add_i32 m0, s5, 0x4000
	v_lshl_add_u64 v[72:73], s[22:23], 0, v[130:131]
	global_load_lds_dwordx4 v[70:71], off
	s_add_i32 m0, s5, 0x6000
	v_add_u32_e32 v77, v76, v34
	global_load_lds_dwordx4 v[72:73], off
	ds_read_b128 v[66:69], v77
	ds_read_b128 v[70:73], v77 offset:4096
	v_add_u32_e32 v74, v76, v35
	v_cvt_pk_bf16_f32 v48, v18, v19
	v_cvt_pk_bf16_f32 v49, v20, v21
	v_cvt_pk_bf16_f32 v6, v6, v7
	v_cvt_pk_bf16_f32 v7, v8, v9
	v_cvt_pk_bf16_f32 v8, v10, v11
	v_cvt_pk_bf16_f32 v9, v12, v13
	s_add_i32 s93, s93, 0x8000
	s_add_u32 s14, s14, 0x8000
	s_addc_u32 s15, s15, 0
	s_add_u32 s16, s16, 0x8000
	s_addc_u32 s17, s17, 0
	s_add_u32 s18, s18, 0x8000
	s_addc_u32 s19, s19, 0
	s_add_u32 s22, s22, 0x8000
	s_addc_u32 s23, s23, 0
	s_add_u32 s8, s8, 0x10000
	s_addc_u32 s9, s9, 0
	s_add_u32 s28, s28, 0x10000
	s_addc_u32 s29, s29, 0
	s_cmp_lg_u32 s93, 0x78000
	s_waitcnt vmcnt(0) lgkmcnt(0)
	v_mfma_f32_16x16x32_bf16 v[14:17], v[66:69], v[42:45], v[14:17]
	ds_read_b128 v[66:69], v77 offset:8192
	v_mfma_f32_16x16x32_bf16 v[22:25], v[70:73], v[42:45], v[22:25]
	ds_read_b128 v[70:73], v77 offset:12288
	s_waitcnt lgkmcnt(1)
	v_mfma_f32_16x16x32_bf16 v[26:29], v[66:69], v[42:45], v[26:29]
	s_waitcnt lgkmcnt(0)
	v_mfma_f32_16x16x32_bf16 v[18:21], v[70:73], v[42:45], v[50:53]
	s_nop 2
	ds_read_b128 v[50:53], v74
	ds_read_b128 v[66:69], v74 offset:4096
	s_waitcnt lgkmcnt(1)
	v_mfma_f32_16x16x32_bf16 v[14:17], v[50:53], v[46:49], v[14:17]
	ds_read_b128 v[50:53], v77 offset:16384
	ds_read_b128 v[70:73], v77 offset:20480
	s_waitcnt lgkmcnt(1)
	v_mfma_f32_16x16x32_bf16 v[50:53], v[50:53], v[42:45], v[54:57]
	v_mfma_f32_16x16x32_bf16 v[22:25], v[66:69], v[46:49], v[22:25]
	s_waitcnt lgkmcnt(0)
	v_mfma_f32_16x16x32_bf16 v[54:57], v[70:73], v[42:45], v[58:61]
	s_nop 2
	ds_read_b128 v[58:61], v74 offset:8192
	ds_read_b128 v[66:69], v74 offset:12288
	s_waitcnt lgkmcnt(1)
	v_mfma_f32_16x16x32_bf16 v[26:29], v[58:61], v[46:49], v[26:29]
	ds_read_b128 v[58:61], v77 offset:24576
	ds_read_b128 v[70:73], v77 offset:28672
	s_waitcnt lgkmcnt(2)
	v_mfma_f32_16x16x32_bf16 v[18:21], v[66:69], v[46:49], v[18:21]
	v_add_u32_e32 v66, v76, v36
	v_add_u32_e32 v67, v76, v37
	s_waitcnt lgkmcnt(1)
	v_mfma_f32_16x16x32_bf16 v[58:61], v[58:61], v[42:45], v[62:65]
	s_waitcnt lgkmcnt(0)
	v_mfma_f32_16x16x32_bf16 v[10:13], v[70:73], v[42:45], v[30:33]
	s_nop 2
	ds_read_b128 v[30:33], v66
	ds_read_b128 v[42:45], v66 offset:4096
	s_waitcnt lgkmcnt(1)
	v_mfma_f32_16x16x32_bf16 v[14:17], v[30:33], v[6:9], v[14:17]
	ds_read_b128 v[30:33], v74 offset:16384
	ds_read_b128 v[62:65], v74 offset:20480
	s_waitcnt lgkmcnt(1)
	v_mfma_f32_16x16x32_bf16 v[30:33], v[30:33], v[46:49], v[50:53]
	v_mfma_f32_16x16x32_bf16 v[22:25], v[42:45], v[6:9], v[22:25]
	s_waitcnt lgkmcnt(0)
	v_mfma_f32_16x16x32_bf16 v[42:45], v[62:65], v[46:49], v[54:57]
	ds_read_b128 v[50:53], v66 offset:8192
	s_nop 1
	ds_read_b128 v[54:57], v66 offset:12288
	s_waitcnt lgkmcnt(1)
	v_mfma_f32_16x16x32_bf16 v[26:29], v[50:53], v[6:9], v[26:29]
	ds_read_b128 v[50:53], v74 offset:24576
	ds_read_b128 v[62:65], v74 offset:28672
	s_waitcnt lgkmcnt(1)
	v_mfma_f32_16x16x32_bf16 v[50:53], v[50:53], v[46:49], v[58:61]
	s_nop 2
	v_cvt_pk_bf16_f32 v58, v2, v3
	v_cvt_pk_bf16_f32 v59, v4, v5
	v_mfma_f32_16x16x32_bf16 v[2:5], v[54:57], v[6:9], v[18:21]
	v_cvt_pk_bf16_f32 v60, v38, v39
	v_cvt_pk_bf16_f32 v61, v40, v41
	s_nop 0
	ds_read_b128 v[18:21], v67
	ds_read_b128 v[38:41], v67 offset:4096
	s_waitcnt lgkmcnt(2)
	v_mfma_f32_16x16x32_bf16 v[10:13], v[62:65], v[46:49], v[10:13]
	s_waitcnt lgkmcnt(1)
	v_mfma_f32_16x16x32_bf16 v[14:17], v[18:21], v[58:61], v[14:17]
	ds_read_b128 v[18:21], v66 offset:16384
	ds_read_b128 v[46:49], v66 offset:20480
	s_waitcnt lgkmcnt(1)
	v_mfma_f32_16x16x32_bf16 v[30:33], v[18:21], v[6:9], v[30:33]
	v_mfma_f32_16x16x32_bf16 v[22:25], v[38:41], v[58:61], v[22:25]
	s_waitcnt lgkmcnt(0)
	v_mfma_f32_16x16x32_bf16 v[38:41], v[46:49], v[6:9], v[42:45]
	ds_read_b128 v[18:21], v67 offset:8192
	s_nop 1
	ds_read_b128 v[42:45], v67 offset:12288
	s_waitcnt lgkmcnt(1)
	v_mfma_f32_16x16x32_bf16 v[26:29], v[18:21], v[58:61], v[26:29]
	ds_read_b128 v[18:21], v66 offset:24576
	ds_read_b128 v[46:49], v66 offset:28672
	ds_read_b128 v[54:57], v67 offset:16384
	s_waitcnt lgkmcnt(2)
	v_mfma_f32_16x16x32_bf16 v[50:53], v[18:21], v[6:9], v[50:53]
	v_mfma_f32_16x16x32_bf16 v[18:21], v[42:45], v[58:61], v[2:5]
	s_nop 2
	ds_read_b128 v[2:5], v67 offset:20480
	ds_read_b128 v[42:45], v67 offset:24576
	ds_read_b128 v[62:65], v67 offset:28672
	s_waitcnt lgkmcnt(4)
	v_mfma_f32_16x16x32_bf16 v[46:49], v[46:49], v[6:9], v[10:13]
	s_waitcnt lgkmcnt(3)
	v_mfma_f32_16x16x32_bf16 v[6:9], v[54:57], v[58:61], v[30:33]
	s_waitcnt lgkmcnt(0)
	v_mfma_f32_16x16x32_bf16 v[30:33], v[62:65], v[58:61], v[46:49]
	v_mfma_f32_16x16x32_bf16 v[10:13], v[2:5], v[58:61], v[38:41]
	v_mfma_f32_16x16x32_bf16 v[2:5], v[42:45], v[58:61], v[50:53]
	s_nop 5
	v_mov_b32_e32 v38, v30
	v_mov_b32_e32 v39, v31
	v_mov_b32_e32 v40, v32
	v_mov_b32_e32 v41, v33
	s_cbranch_scc1 .LBB0_456
; template <class Epi, class Sched, bool GATHER, bool LIGHTSKIP = false>
; __device__ __forceinline__ void gemm_phase(LAS unsigned char* lds, LAS unsigned char* xl, const int lda, const int ldb, const int K, const Sched& S, const Epi& E) {
;     const int tid = otid(), wid = __builtin_amdgcn_readfirstlane(tid >> 6), lane = tid & 63, wr = wid >> 2, wc = wid & 3, fr = lane & 15, fq = lane >> 4;
;     const int nt = K / BK;
;     int Rr[2], Cc[2]; unsigned voffA[2], voffB[2];
; #pragma unroll
;     for (int i = 0; i < 2; ++i) { stage_rc(tid * 16 + i * 8192, Rr[i], Cc[i]); const int Rb = Epi::PERM ? ((Rr[i] & ~31) + perm32(Rr[i] & 31)) : Rr[i];
;         voffA[i] = (unsigned)(Rr[i] * lda + Cc[i]) * 2u; voffB[i] = (unsigned)(Rb * ldb + Cc[i]) * 2u; }
;     unsigned vc[2][2], vn[2][2];
;     const size_t kstep = (size_t)(BK * 2);
;     const size_t hstepA = (size_t)HALF * lda * 2, hstepB = (size_t)HALF * ldb * 2;
;     const unsigned ldsw = (unsigned)wid * 1024u;
;     const int aoff = lds_byte(wr * 64 + fr, fq * 8), boff = lds_byte(wc * 32 + fr, fq * 8);
;     ...
;     GUnit cur, nxt; int ui = 0;
;     if (!S.next(0, cur)) return;
;     Acc acc;
; #pragma unroll
;     for (int a = 0; a < 2; ++a)
; #pragma unroll
;         for (int b = 0; b < 2; ++b)
; #pragma unroll
;             for (int m = 0; m < 4; ++m)
; #pragma unroll
;                 for (int n = 0; n < 2; ++n) acc[a][b][m][n] = (f32x4){0.f, 0.f, 0.f, 0.f};
; __device__ __forceinline__ void ph_gdn_combine(const Params& p, LAS unsigned char* lds) {
;     ...
;         f32x4 qv[8];
; #pragma unroll
;         for (int a = 0; a < 8; ++a) { sin0[((size_t)sg * 64 + wid * 8 + a) * 64 + lane] = S[a]; qv[a] = qf0[((size_t)sg * 64 + wid * 8 + a) * 64 + lane]; }
;         asm volatile("s_waitcnt vmcnt(0)" ::: "memory"); __builtin_amdgcn_s_barrier();
;         if (sg + 1 < 16) GC_DMA(sg + 1, cur ^ 1);
;         const LAS unsigned char* PI = lds + cur * 32768;
;         bf16x8 SB[4];
; #pragma unroll
;         for (int s = 0; s < 4; ++s) SB[s] = pack8(S[2 * s], S[2 * s + 1]);
; #pragma unroll
;         for (int a = 0; a < 8; ++a) { f32x4 acc = qv[a];
; #pragma unroll
;             for (int s = 0; s < 4; ++s) acc = __builtin_amdgcn_mfma_f32_16x16x32_bf16(frag256(PI, 16 * a + m16, 4 * s + q4), SB[s], acc, 0, 0, 0);
;             S[a] = acc; }
;     }
;     asm volatile("s_waitcnt vmcnt(0)" ::: "memory"); __syncthreads();
	s_add_u32 s0, s10, s12
	s_addc_u32 s1, s11, s13
	s_add_u32 s0, s0, s20
	s_addc_u32 s1, s1, s21
	v_mov_b32_e32 v131, 0
	v_lshl_add_u64 v[34:35], s[0:1], 0, v[130:131]
	v_add_co_u32_e32 v36, vcc, 0x45c20000, v34
	s_mov_b32 s1, 0xfffe0
	s_nop 0
	v_addc_co_u32_e32 v37, vcc, 0, v35, vcc
	global_store_dwordx4 v[36:37], v[14:17], off
	global_store_dwordx4 v[36:37], v[22:25], off offset:1024
	global_store_dwordx4 v[36:37], v[26:29], off offset:2048
	global_store_dwordx4 v[36:37], v[18:21], off offset:3072
	v_add_co_u32_e32 v14, vcc, 0x45c21000, v34
	v_mov_b32_e32 v137, v131
	s_nop 0
	v_addc_co_u32_e32 v15, vcc, 0, v35, vcc
	global_store_dwordx4 v[14:15], v[6:9], off
	global_store_dwordx4 v[14:15], v[10:13], off offset:1024
	global_store_dwordx4 v[14:15], v[2:5], off offset:2048
	global_store_dwordx4 v[14:15], v[30:33], off offset:3072
	v_mov_b32_e32 v15, v0
	s_waitcnt vmcnt(0)
	s_barrier
	s_waitcnt vmcnt(0)
	s_barrier
	s_load_dwordx2 s[8:9], s[70:71], 0xd8
	v_mov_b32_e32 v133, v131
	v_ashrrev_i32_e32 v2, 31, v15
	v_lshrrev_b32_e32 v2, 26, v2
	v_add_u32_e32 v2, v15, v2
	v_ashrrev_i32_e32 v10, 6, v2
	v_bfe_i32 v2, v15, 27, 1
	v_lshlrev_b32_e32 v1, 4, v15
	v_lshrrev_b32_e32 v2, 22, v2
	v_add_u32_e32 v2, v1, v2
	v_and_b32_e32 v2, 0xfffffc00, v2
	v_sub_u32_e32 v2, v1, v2
	v_lshrrev_b32_e32 v3, 4, v2
	v_bitop3_b32 v3, v3, v2, 32 bitop3:0x6c
	v_ashrrev_i32_e32 v2, 31, v2
	v_lshrrev_b32_e32 v2, 26, v2
	v_add_u32_e32 v2, v3, v2
	v_ashrrev_i32_e32 v11, 6, v2
	v_lshlrev_b32_e32 v4, 3, v10
	v_mul_i32_i24_e32 v5, 64, v11
	v_and_b32_e32 v4, -16, v4
	v_sub_u32_e32 v3, v3, v5
	v_mov_b32_e32 v5, 1
	v_add_u32_e32 v2, v11, v4
	v_lshlrev_b32_e32 v4, 5, v10
	v_ashrrev_i16_sdwa v3, v5, sext(v3) dst_sel:DWORD dst_unused:UNUSED_PAD src0_sel:DWORD src1_sel:BYTE_0
	v_and_b32_e32 v4, 32, v4
	v_bfe_i32 v12, v3, 0, 16
	v_and_b32_e32 v7, 3, v11
	v_add_lshl_u32 v4, v4, v12, 1
	v_add_u32_e32 v1, 0x2000, v1
	v_lshlrev_b32_e32 v3, 1, v2
	v_lshrrev_b32_e32 v6, 2, v2
	v_and_or_b32 v7, v2, s1, v7
	v_lshl_add_u32 v132, v2, 12, v4
	v_ashrrev_i32_e32 v2, 31, v1
	v_lshrrev_b32_e32 v2, 22, v2
	v_add_u32_e32 v2, v1, v2
	v_ashrrev_i32_e32 v13, 10, v2
	v_mul_i32_i24_e32 v2, 0x400, v13
	v_sub_u32_e32 v1, v1, v2
	v_and_b32_e32 v3, 24, v3
	v_and_b32_e32 v6, 4, v6
	v_lshrrev_b32_e32 v2, 4, v1
	v_or3_b32 v3, v7, v6, v3
	v_bitop3_b32 v1, v2, v1, 32 bitop3:0x6c
	v_lshl_add_u32 v130, v3, 12, v4
	v_ashrrev_i32_e32 v3, 31, v1
	v_lshrrev_b32_e32 v3, 26, v3
	v_readfirstlane_b32 s2, v15
	v_add_u32_e32 v3, v1, v3
	v_lshlrev_b32_e32 v2, 3, v13
	v_ashrrev_i32_e32 v14, 6, v3
	v_and_b32_e32 v3, 0xc0, v3
	s_ashr_i32 s5, s2, 6
	s_ashr_i32 s0, s2, 8
	v_and_b32_e32 v2, -16, v2
	v_sub_u32_e32 v1, v1, v3
	s_lshl_b32 s22, s5, 10
	v_add_u32_e32 v2, v14, v2
	v_ashrrev_i16_sdwa v1, v5, sext(v1) dst_sel:DWORD dst_unused:UNUSED_PAD src0_sel:DWORD src1_sel:BYTE_0
	v_and_b32_e32 v5, 3, v14
	s_cmp_gt_u32 s92, 7
	v_and_or_b32 v5, v2, s1, v5
	s_cselect_b64 s[10:11], -1, 0
	s_add_i32 s1, s92, 0x78
	s_cmp_lt_u32 s92, 8
	s_cselect_b32 s1, s92, s1
	s_and_b32 s6, s1, 0x7f
	s_and_b64 s[12:13], s[10:11], exec
	s_cselect_b32 s4, 0x100000, 0
	s_waitcnt lgkmcnt(0)
	s_add_u32 s18, s8, s4
	s_addc_u32 s19, s9, 0
	s_add_u32 s12, s18, 0x44450000
	s_addc_u32 s13, s19, 0
	s_lshl_b32 s1, s6, 20
	s_add_u32 s7, s8, s1
	s_addc_u32 s17, s9, 0
	s_add_u32 s14, s7, 0x2810000
	v_lshlrev_b32_e32 v4, 5, v13
	v_bfe_i32 v16, v1, 0, 16
	v_lshlrev_b32_e32 v1, 1, v2
	v_lshrrev_b32_e32 v3, 2, v2
	s_addc_u32 s15, s17, 0
	s_add_i32 s3, s22, 0
	v_and_b32_e32 v4, 32, v4
	v_and_b32_e32 v1, 24, v1
	v_and_b32_e32 v3, 4, v3
	s_add_i32 m0, s3, 0x10000
	v_or3_b32 v1, v5, v3, v1
	v_add_lshl_u32 v3, v4, v16, 1
	global_load_lds_dwordx4 v130, s[14:15]
	s_add_i32 m0, s3, 0x12000
	v_lshl_add_u32 v136, v1, 12, v3
	s_add_u32 s16, s7, 0x2890000
	global_load_lds_dwordx4 v136, s[14:15]
	s_addc_u32 s17, s17, 0
	s_add_i32 m0, s3, 0x14000
	s_add_i32 s7, s3, 0x2000
	global_load_lds_dwordx4 v130, s[16:17]
	s_add_i32 m0, s3, 0x16000
	v_lshl_add_u32 v134, v2, 12, v3
	global_load_lds_dwordx4 v136, s[16:17]
	s_mov_b32 m0, s3
	s_add_u32 s16, s18, 0x444d0000
	global_load_lds_dwordx4 v132, s[12:13]
	s_mov_b32 m0, s7
	s_addc_u32 s17, s19, 0
	s_add_i32 s26, s3, 0x4000
	global_load_lds_dwordx4 v134, s[12:13]
	s_mov_b32 m0, s26
	s_add_i32 s27, s3, 0x6000
	global_load_lds_dwordx4 v132, s[16:17]
	s_mov_b32 m0, s27
	v_mov_b32_e32 v135, v131
	global_load_lds_dwordx4 v134, s[16:17]
	v_lshl_add_u64 v[8:9], s[14:15], 0, v[130:131]
	v_lshl_add_u64 v[6:7], s[14:15], 0, v[136:137]
	v_lshl_add_u64 v[4:5], s[12:13], 0, v[132:133]
	s_cmp_lg_u32 s0, 1
	v_lshl_add_u64 v[2:3], s[12:13], 0, v[134:135]
	s_cbranch_scc1 .LBB0_459
	s_barrier
	s_setprio 1

; #define PG8_STAGE_B(b, h, bp) PG8_STAGE2(PG8_SB(b, h), (bp) + (h) * hstepB, voffB[0], voffB[1])
; #define PG8_STAGE_A(b, h, ap, NX) do { if constexpr (GATHER) { const unsigned _o0 = (NX) ? vn[h][0] : vc[h][0], _o1 = (NX) ? vn[h][1] : vc[h][1]; PG8_STAGE2(PG8_SA(b, h), (ap), _o0, _o1); } \
;         else { PG8_STAGE2(PG8_SA(b, h), (ap) + (h) * hstepA, voffA[0], voffA[1]); } } while (0)
; #define PG8_LDA(dst, b, h) do { _Pragma("unroll") for (int m = 0; m < 4; ++m) _Pragma("unroll") for (int k = 0; k < 2; ++k) dst[m][k] = *(const LAS bf16x8*)(lds + PG8_SA(b, h) + aoff + m * 2048 + k * 1024); } while (0)
; #define PG8_LDB(dst, b, h) do { _Pragma("unroll") for (int n = 0; n < 2; ++n) _Pragma("unroll") for (int k = 0; k < 2; ++k) dst[n][k] = *(const LAS bf16x8*)(lds + PG8_SB(b, h) + boff + n * 2048 + k * 1024); } while (0)
; #define PG8_MMA(ai, bj, At, Bt) do { __builtin_amdgcn_s_setprio(1); _Pragma("unroll") for (int m = 0; m < 4; ++m) _Pragma("unroll") for (int n = 0; n < 2; ++n) _Pragma("unroll") for (int k = 0; k < 2; ++k) \
;         acc[ai][bj][m][n] = __builtin_amdgcn_mfma_f32_16x16x32_bf16(Bt[n][k], At[m][k], acc[ai][bj][m][n], 0, 0, 0); __builtin_amdgcn_s_setprio(0); } while (0)
; #define PG8_WAIT_V(n) asm volatile("s_waitcnt vmcnt(" #n ")" ::: "memory")
; #define PG8_WAIT_L(n) asm volatile("s_waitcnt lgkmcnt(" #n ")" ::: "memory")
; #define PG8_BAR __builtin_amdgcn_s_barrier()
; #define PG8_SCHED __builtin_amdgcn_sched_barrier(0)
; template <class Epi, class Sched, bool GATHER, bool LIGHTSKIP = false>
; __device__ __forceinline__ void gemm_phase(LAS unsigned char* lds, LAS unsigned char* xl, const int lda, const int ldb, const int K, const Sched& S, const Epi& E) {
;     ...
;             PG8_LDB(B0, 0, 0); PG8_LDB(B1, 0, 1); PG8_SCHED; PG8_LDA(At, 0, 0); PG8_STAGE_A(1, 1, a1, false);
;             PG8_WAIT_V(8); PG8_WAIT_L(0); PG8_BAR; PG8_MMA(0, 0, At, B0); PG8_MMA(0, 1, At, B1); PG8_BAR; PG8_SCHED;
;             PG8_LDA(At, 0, 1); PG8_STAGE_B(0, 0, b2); PG8_STAGE_B(0, 1, b2); PG8_STAGE_A(0, 0, a2, last);
.LBB0_460:
	ds_read_b128 v[148:151], v143
	ds_read_b128 v[152:155], v143 offset:1024
	ds_read_b128 v[156:159], v143 offset:2048
	ds_read_b128 v[160:163], v143 offset:3072
	ds_read_b128 v[164:167], v144
	ds_read_b128 v[168:171], v144 offset:1024
	ds_read_b128 v[172:175], v144 offset:2048
	ds_read_b128 v[176:179], v144 offset:3072
	s_add_u32 s22, s18, s20
	s_addc_u32 s23, s19, s21
	s_add_u32 s22, s22, 0x44450100
	s_addc_u32 s23, s23, 0
	s_add_u32 s47, s34, s20
	s_addc_u32 s48, s35, s21
	s_cmpk_eq_i32 s20, 0xf00
	s_cselect_b32 s29, s13, s23
	s_cselect_b32 s28, s12, s22
	s_cselect_b32 s23, s15, s48
	s_cselect_b32 s22, s14, s47
	s_mov_b32 m0, s37
	v_lshl_add_u64 v[212:213], v[138:139], 0, s[20:21]
	ds_read_b128 v[180:183], v145
	ds_read_b128 v[184:187], v145 offset:1024
	ds_read_b128 v[188:191], v145 offset:2048
	ds_read_b128 v[192:195], v145 offset:3072
	ds_read_b128 v[196:199], v145 offset:4096
	ds_read_b128 v[200:203], v145 offset:5120
	ds_read_b128 v[204:207], v145 offset:6144
	ds_read_b128 v[208:211], v145 offset:7168
	global_load_lds_dwordx4 v[212:213], off
	v_lshl_add_u64 v[212:213], v[140:141], 0, s[20:21]
	s_mov_b32 m0, s38
	s_nop 0
	global_load_lds_dwordx4 v[212:213], off
	s_waitcnt vmcnt(8)
	s_waitcnt lgkmcnt(0)
	s_barrier
	s_waitcnt lgkmcnt(0)
	v_mfma_f32_16x16x32_bf16 v[126:129], v[148:151], v[180:183], v[126:129]
	v_mfma_f32_16x16x32_bf16 v[122:125], v[156:159], v[180:183], v[122:125]
	v_mfma_f32_16x16x32_bf16 v[118:121], v[148:151], v[188:191], v[118:121]
	v_mfma_f32_16x16x32_bf16 v[114:117], v[156:159], v[188:191], v[114:117]
	v_mfma_f32_16x16x32_bf16 v[102:105], v[148:151], v[196:199], v[102:105]
	v_mfma_f32_16x16x32_bf16 v[98:101], v[156:159], v[196:199], v[98:101]
	v_mfma_f32_16x16x32_bf16 v[86:89], v[148:151], v[204:207], v[86:89]
	v_mfma_f32_16x16x32_bf16 v[82:85], v[156:159], v[204:207], v[82:85]
	v_mfma_f32_16x16x32_bf16 v[126:129], v[152:155], v[184:187], v[126:129]
	v_mfma_f32_16x16x32_bf16 v[122:125], v[160:163], v[184:187], v[122:125]
	v_mfma_f32_16x16x32_bf16 v[118:121], v[152:155], v[192:195], v[118:121]
	v_mfma_f32_16x16x32_bf16 v[114:117], v[160:163], v[192:195], v[114:117]
	v_mfma_f32_16x16x32_bf16 v[102:105], v[152:155], v[200:203], v[102:105]
	v_mfma_f32_16x16x32_bf16 v[98:101], v[160:163], v[200:203], v[98:101]
	v_mfma_f32_16x16x32_bf16 v[86:89], v[152:155], v[208:211], v[86:89]
	v_mfma_f32_16x16x32_bf16 v[82:85], v[160:163], v[208:211], v[82:85]
	v_mfma_f32_16x16x32_bf16 v[110:113], v[164:167], v[180:183], v[110:113]
	v_mfma_f32_16x16x32_bf16 v[106:109], v[172:175], v[180:183], v[106:109]
	v_mfma_f32_16x16x32_bf16 v[94:97], v[164:167], v[188:191], v[94:97]
	v_mfma_f32_16x16x32_bf16 v[90:93], v[172:175], v[188:191], v[90:93]
	v_mfma_f32_16x16x32_bf16 v[78:81], v[164:167], v[196:199], v[78:81]
	v_mfma_f32_16x16x32_bf16 v[74:77], v[172:175], v[196:199], v[74:77]
	v_mfma_f32_16x16x32_bf16 v[70:73], v[164:167], v[204:207], v[70:73]
	v_mfma_f32_16x16x32_bf16 v[66:69], v[172:175], v[204:207], v[66:69]
	v_mfma_f32_16x16x32_bf16 v[110:113], v[168:171], v[184:187], v[110:113]
	v_mfma_f32_16x16x32_bf16 v[106:109], v[176:179], v[184:187], v[106:109]
	v_mfma_f32_16x16x32_bf16 v[94:97], v[168:171], v[192:195], v[94:97]
	v_mfma_f32_16x16x32_bf16 v[90:93], v[176:179], v[192:195], v[90:93]
	v_mfma_f32_16x16x32_bf16 v[78:81], v[168:171], v[200:203], v[78:81]
	v_mfma_f32_16x16x32_bf16 v[74:77], v[176:179], v[200:203], v[74:77]
	v_mfma_f32_16x16x32_bf16 v[70:73], v[168:171], v[208:211], v[70:73]
	v_mfma_f32_16x16x32_bf16 v[66:69], v[176:179], v[208:211], v[66:69]
	s_barrier
	s_mov_b32 m0, s39
	v_lshl_add_u64 v[212:213], s[22:23], 0, v[130:131]
	s_add_u32 s48, s22, 0x80000
	ds_read_b128 v[180:183], v145 offset:16384
	ds_read_b128 v[184:187], v145 offset:17408
	ds_read_b128 v[188:191], v145 offset:18432
	ds_read_b128 v[192:195], v145 offset:19456
	ds_read_b128 v[196:199], v145 offset:20480
	ds_read_b128 v[200:203], v145 offset:21504
	ds_read_b128 v[204:207], v145 offset:22528
	ds_read_b128 v[208:211], v145 offset:23552
	global_load_lds_dwordx4 v[212:213], off
	v_lshl_add_u64 v[214:215], s[22:23], 0, v[136:137]
	s_mov_b32 m0, s40
	s_addc_u32 s49, s23, 0
	global_load_lds_dwordx4 v[214:215], off
	v_lshl_add_u64 v[216:217], s[48:49], 0, v[130:131]
	s_mov_b32 m0, s41
	v_lshl_add_u64 v[218:219], s[28:29], 0, v[134:135]
	global_load_lds_dwordx4 v[216:217], off
	v_lshl_add_u64 v[216:217], s[48:49], 0, v[136:137]
	s_mov_b32 m0, s42
	s_nop 0
	global_load_lds_dwordx4 v[216:217], off
	v_lshl_add_u64 v[216:217], s[28:29], 0, v[132:133]
	s_mov_b32 m0, s3
	s_nop 0
	global_load_lds_dwordx4 v[216:217], off
	s_mov_b32 m0, s7
	s_nop 0
	global_load_lds_dwordx4 v[218:219], off
	s_waitcnt vmcnt(8)
	s_waitcnt lgkmcnt(0)
	s_barrier
; #define PG8_STAGE_A(b, h, ap, NX) do { if constexpr (GATHER) { const unsigned _o0 = (NX) ? vn[h][0] : vc[h][0], _o1 = (NX) ? vn[h][1] : vc[h][1]; PG8_STAGE2(PG8_SA(b, h), (ap), _o0, _o1); } \
;         else { PG8_STAGE2(PG8_SA(b, h), (ap) + (h) * hstepA, voffA[0], voffA[1]); } } while (0)
; #define PG8_LDA(dst, b, h) do { _Pragma("unroll") for (int m = 0; m < 4; ++m) _Pragma("unroll") for (int k = 0; k < 2; ++k) dst[m][k] = *(const LAS bf16x8*)(lds + PG8_SA(b, h) + aoff + m * 2048 + k * 1024); } while (0)
; #define PG8_LDB(dst, b, h) do { _Pragma("unroll") for (int n = 0; n < 2; ++n) _Pragma("unroll") for (int k = 0; k < 2; ++k) dst[n][k] = *(const LAS bf16x8*)(lds + PG8_SB(b, h) + boff + n * 2048 + k * 1024); } while (0)
; #define PG8_MMA(ai, bj, At, Bt) do { __builtin_amdgcn_s_setprio(1); _Pragma("unroll") for (int m = 0; m < 4; ++m) _Pragma("unroll") for (int n = 0; n < 2; ++n) _Pragma("unroll") for (int k = 0; k < 2; ++k) \
;         acc[ai][bj][m][n] = __builtin_amdgcn_mfma_f32_16x16x32_bf16(Bt[n][k], At[m][k], acc[ai][bj][m][n], 0, 0, 0); __builtin_amdgcn_s_setprio(0); } while (0)
; #define PG8_WAIT_V(n) asm volatile("s_waitcnt vmcnt(" #n ")" ::: "memory")
; #define PG8_WAIT_L(n) asm volatile("s_waitcnt lgkmcnt(" #n ")" ::: "memory")
; #define PG8_BAR __builtin_amdgcn_s_barrier()
; #define PG8_SCHED __builtin_amdgcn_sched_barrier(0)
; template <class Epi, class Sched, bool GATHER, bool LIGHTSKIP = false>
; __device__ __forceinline__ void gemm_phase(LAS unsigned char* lds, LAS unsigned char* xl, const int lda, const int ldb, const int K, const Sched& S, const Epi& E) {
;     ...
;             PG8_WAIT_V(8); PG8_WAIT_L(0); PG8_BAR; if (!light) { PG8_MMA(1, 0, At, B0); PG8_MMA(1, 1, At, B1); } PG8_BAR; PG8_SCHED;
;             PG8_LDB(B0, 1, 0); PG8_LDB(B1, 1, 1); PG8_SCHED; PG8_LDA(At, 1, 0); PG8_STAGE_A(0, 1, a2, last);
;             PG8_WAIT_V(8); PG8_WAIT_L(0); PG8_BAR; PG8_MMA(0, 0, At, B0); PG8_MMA(0, 1, At, B1); PG8_BAR; PG8_SCHED;
	s_waitcnt lgkmcnt(0)
	v_mfma_f32_16x16x32_bf16 v[62:65], v[148:151], v[180:183], v[62:65]
	v_mfma_f32_16x16x32_bf16 v[58:61], v[156:159], v[180:183], v[58:61]
	v_mfma_f32_16x16x32_bf16 v[54:57], v[148:151], v[188:191], v[54:57]
	v_mfma_f32_16x16x32_bf16 v[50:53], v[156:159], v[188:191], v[50:53]
	v_mfma_f32_16x16x32_bf16 v[38:41], v[148:151], v[196:199], v[38:41]
	v_mfma_f32_16x16x32_bf16 v[34:37], v[156:159], v[196:199], v[34:37]
	v_mfma_f32_16x16x32_bf16 v[22:25], v[148:151], v[204:207], v[22:25]
	v_mfma_f32_16x16x32_bf16 v[18:21], v[156:159], v[204:207], v[18:21]
	v_mfma_f32_16x16x32_bf16 v[62:65], v[152:155], v[184:187], v[62:65]
	v_mfma_f32_16x16x32_bf16 v[58:61], v[160:163], v[184:187], v[58:61]
	v_mfma_f32_16x16x32_bf16 v[54:57], v[152:155], v[192:195], v[54:57]
	v_mfma_f32_16x16x32_bf16 v[50:53], v[160:163], v[192:195], v[50:53]
	v_mfma_f32_16x16x32_bf16 v[38:41], v[152:155], v[200:203], v[38:41]
	v_mfma_f32_16x16x32_bf16 v[34:37], v[160:163], v[200:203], v[34:37]
	v_mfma_f32_16x16x32_bf16 v[22:25], v[152:155], v[208:211], v[22:25]
	v_mfma_f32_16x16x32_bf16 v[18:21], v[160:163], v[208:211], v[18:21]
	v_mfma_f32_16x16x32_bf16 v[46:49], v[164:167], v[180:183], v[46:49]
	v_mfma_f32_16x16x32_bf16 v[42:45], v[172:175], v[180:183], v[42:45]
	v_mfma_f32_16x16x32_bf16 v[30:33], v[164:167], v[188:191], v[30:33]
	v_mfma_f32_16x16x32_bf16 v[26:29], v[172:175], v[188:191], v[26:29]
	v_mfma_f32_16x16x32_bf16 v[14:17], v[164:167], v[196:199], v[14:17]
	v_mfma_f32_16x16x32_bf16 v[10:13], v[172:175], v[196:199], v[10:13]
	v_mfma_f32_16x16x32_bf16 v[6:9], v[164:167], v[204:207], v[6:9]
	v_mfma_f32_16x16x32_bf16 v[2:5], v[172:175], v[204:207], v[2:5]
	v_mfma_f32_16x16x32_bf16 v[46:49], v[168:171], v[184:187], v[46:49]
	v_mfma_f32_16x16x32_bf16 v[42:45], v[176:179], v[184:187], v[42:45]
	v_mfma_f32_16x16x32_bf16 v[30:33], v[168:171], v[192:195], v[30:33]
	v_mfma_f32_16x16x32_bf16 v[26:29], v[176:179], v[192:195], v[26:29]
	v_mfma_f32_16x16x32_bf16 v[14:17], v[168:171], v[200:203], v[14:17]
	v_mfma_f32_16x16x32_bf16 v[10:13], v[176:179], v[200:203], v[10:13]
	v_mfma_f32_16x16x32_bf16 v[6:9], v[168:171], v[208:211], v[6:9]
	v_mfma_f32_16x16x32_bf16 v[2:5], v[176:179], v[208:211], v[2:5]
	s_barrier
	ds_read_b128 v[148:151], v146
	ds_read_b128 v[152:155], v146 offset:1024
	ds_read_b128 v[156:159], v146 offset:2048
	ds_read_b128 v[160:163], v146 offset:3072
	ds_read_b128 v[164:167], v147
	ds_read_b128 v[168:171], v147 offset:1024
	ds_read_b128 v[172:175], v147 offset:2048
	ds_read_b128 v[176:179], v147 offset:3072
	s_add_u32 s28, s28, 0x80000
	s_addc_u32 s29, s29, 0
	s_mov_b32 m0, s26
	v_lshl_add_u64 v[220:221], s[28:29], 0, v[132:133]
	ds_read_b128 v[180:183], v145 offset:32768
	ds_read_b128 v[184:187], v145 offset:33792
	ds_read_b128 v[188:191], v145 offset:34816
	ds_read_b128 v[192:195], v145 offset:35840
	ds_read_b128 v[196:199], v145 offset:36864
	ds_read_b128 v[200:203], v145 offset:37888
	ds_read_b128 v[204:207], v145 offset:38912
	ds_read_b128 v[208:211], v145 offset:39936
	global_load_lds_dwordx4 v[220:221], off
	v_lshl_add_u64 v[220:221], s[28:29], 0, v[134:135]
	s_mov_b32 m0, s27
	s_nop 0
	global_load_lds_dwordx4 v[220:221], off
	s_waitcnt vmcnt(8)
	s_waitcnt lgkmcnt(0)
	s_barrier
	s_waitcnt lgkmcnt(0)
	v_mfma_f32_16x16x32_bf16 v[126:129], v[148:151], v[180:183], v[126:129]
	v_mfma_f32_16x16x32_bf16 v[122:125], v[156:159], v[180:183], v[122:125]
	v_mfma_f32_16x16x32_bf16 v[118:121], v[148:151], v[188:191], v[118:121]
	v_mfma_f32_16x16x32_bf16 v[114:117], v[156:159], v[188:191], v[114:117]
	v_mfma_f32_16x16x32_bf16 v[102:105], v[148:151], v[196:199], v[102:105]
	v_mfma_f32_16x16x32_bf16 v[98:101], v[156:159], v[196:199], v[98:101]
	v_mfma_f32_16x16x32_bf16 v[86:89], v[148:151], v[204:207], v[86:89]
	v_mfma_f32_16x16x32_bf16 v[82:85], v[156:159], v[204:207], v[82:85]
	v_mfma_f32_16x16x32_bf16 v[126:129], v[152:155], v[184:187], v[126:129]
	v_mfma_f32_16x16x32_bf16 v[122:125], v[160:163], v[184:187], v[122:125]
	v_mfma_f32_16x16x32_bf16 v[118:121], v[152:155], v[192:195], v[118:121]
	v_mfma_f32_16x16x32_bf16 v[114:117], v[160:163], v[192:195], v[114:117]
	v_mfma_f32_16x16x32_bf16 v[102:105], v[152:155], v[200:203], v[102:105]
	v_mfma_f32_16x16x32_bf16 v[98:101], v[160:163], v[200:203], v[98:101]
	v_mfma_f32_16x16x32_bf16 v[86:89], v[152:155], v[208:211], v[86:89]
	v_mfma_f32_16x16x32_bf16 v[82:85], v[160:163], v[208:211], v[82:85]
	v_mfma_f32_16x16x32_bf16 v[110:113], v[164:167], v[180:183], v[110:113]
	v_mfma_f32_16x16x32_bf16 v[106:109], v[172:175], v[180:183], v[106:109]
	v_mfma_f32_16x16x32_bf16 v[94:97], v[164:167], v[188:191], v[94:97]
	v_mfma_f32_16x16x32_bf16 v[90:93], v[172:175], v[188:191], v[90:93]
	v_mfma_f32_16x16x32_bf16 v[78:81], v[164:167], v[196:199], v[78:81]
	v_mfma_f32_16x16x32_bf16 v[74:77], v[172:175], v[196:199], v[74:77]
	v_mfma_f32_16x16x32_bf16 v[70:73], v[164:167], v[204:207], v[70:73]
	v_mfma_f32_16x16x32_bf16 v[66:69], v[172:175], v[204:207], v[66:69]
	v_mfma_f32_16x16x32_bf16 v[110:113], v[168:171], v[184:187], v[110:113]
	v_mfma_f32_16x16x32_bf16 v[106:109], v[176:179], v[184:187], v[106:109]
	v_mfma_f32_16x16x32_bf16 v[94:97], v[168:171], v[192:195], v[94:97]
	v_mfma_f32_16x16x32_bf16 v[90:93], v[176:179], v[192:195], v[90:93]
	v_mfma_f32_16x16x32_bf16 v[78:81], v[168:171], v[200:203], v[78:81]
	v_mfma_f32_16x16x32_bf16 v[74:77], v[176:179], v[200:203], v[74:77]
	v_mfma_f32_16x16x32_bf16 v[70:73], v[168:171], v[208:211], v[70:73]
	v_mfma_f32_16x16x32_bf16 v[66:69], v[176:179], v[208:211], v[66:69]
	s_barrier
; __device__ __forceinline__ unsigned cvt_pk_bf16(float lo, float hi) { const f32x2 v = {lo, hi}; return __builtin_bit_cast(unsigned, __builtin_convertvector(v, bf16x2_t)); }
; #define PG8_STAGE_B(b, h, bp) PG8_STAGE2(PG8_SB(b, h), (bp) + (h) * hstepB, voffB[0], voffB[1])
; #define PG8_STAGE_A(b, h, ap, NX) do { if constexpr (GATHER) { const unsigned _o0 = (NX) ? vn[h][0] : vc[h][0], _o1 = (NX) ? vn[h][1] : vc[h][1]; PG8_STAGE2(PG8_SA(b, h), (ap), _o0, _o1); } \
;         else { PG8_STAGE2(PG8_SA(b, h), (ap) + (h) * hstepA, voffA[0], voffA[1]); } } while (0)
; #define PG8_LDA(dst, b, h) do { _Pragma("unroll") for (int m = 0; m < 4; ++m) _Pragma("unroll") for (int k = 0; k < 2; ++k) dst[m][k] = *(const LAS bf16x8*)(lds + PG8_SA(b, h) + aoff + m * 2048 + k * 1024); } while (0)
; #define PG8_WAIT_V(n) asm volatile("s_waitcnt vmcnt(" #n ")" ::: "memory")
; #define PG8_WAIT_L(n) asm volatile("s_waitcnt lgkmcnt(" #n ")" ::: "memory")
; template <class Epi, class Sched, bool GATHER, bool LIGHTSKIP = false>
; __device__ __forceinline__ void gemm_phase(LAS unsigned char* lds, LAS unsigned char* xl, const int lda, const int ldb, const int K, const Sched& S, const Epi& E) {
;     ...
;             PG8_LDA(At, 1, 1); PG8_STAGE_B(1, 0, b3); PG8_STAGE_B(1, 1, b3); PG8_STAGE_A(1, 0, a3, last);
;             PG8_WAIT_V(8); PG8_WAIT_L(0); PG8_BAR; if (!light) { PG8_MMA(1, 0, At, B0); PG8_MMA(1, 1, At, B1); } PG8_BAR; PG8_SCHED;
;         }
;         if (wr == 0) PG8_BAR;
;         E(acc, cur, wr, wc, fr, fq, xl, wid, lane);
;     __device__ __forceinline__ void operator()(Acc& acc, const GUnit& u, int wr, int wc, int fr, int fq, LAS unsigned char*, int, int) const {
;         const int row0 = u.x0 + wr * 64 + fr, col0 = u.x1 + wc * 32 + 8 * fq;
; #pragma unroll
;         for (int ai = 0; ai < 2; ++ai)
; #pragma unroll
;             for (int m = 0; m < 4; ++m) { bf16_t* rowp = O + (size_t)(row0 + ai * HALF + m * 16) * ldc + col0;
; #pragma unroll
;                 for (int bj = 0; bj < 2; ++bj) { const f32x4 v0 = acc[ai][bj][m][0], v1 = acc[ai][bj][m][1];
;                     u32x4 w; w.x = cvt_pk_bf16(v0[0], v0[1]); w.y = cvt_pk_bf16(v0[2], v0[3]); w.z = cvt_pk_bf16(v1[0], v1[1]); w.w = cvt_pk_bf16(v1[2], v1[3]);
;                     if constexpr (NT) __builtin_nontemporal_store(w, (u32x4*)(rowp + bj * HALF)); else *(u32x4*)(rowp + bj * HALF) = w; } }
	s_mov_b32 m0, s43
	v_lshl_add_u64 v[212:213], v[212:213], 0, s[16:17]
	s_add_u32 s22, s22, 0x80080
	ds_read_b128 v[180:183], v145 offset:49152
	ds_read_b128 v[184:187], v145 offset:50176
	ds_read_b128 v[188:191], v145 offset:51200
	ds_read_b128 v[192:195], v145 offset:52224
	ds_read_b128 v[196:199], v145 offset:53248
	ds_read_b128 v[200:203], v145 offset:54272
	ds_read_b128 v[204:207], v145 offset:55296
	ds_read_b128 v[208:211], v145 offset:56320
	global_load_lds_dwordx4 v[212:213], off
	v_lshl_add_u64 v[212:213], v[214:215], 0, s[16:17]
	s_mov_b32 m0, s44
	s_addc_u32 s23, s23, 0
	global_load_lds_dwordx4 v[212:213], off
	v_lshl_add_u64 v[212:213], s[22:23], 0, v[130:131]
	s_mov_b32 m0, s45
	s_nop 0
	global_load_lds_dwordx4 v[212:213], off
	v_lshl_add_u64 v[212:213], s[22:23], 0, v[136:137]
	s_mov_b32 m0, s46
	s_nop 0
	global_load_lds_dwordx4 v[212:213], off
	v_lshl_add_u64 v[212:213], v[216:217], 0, s[16:17]
	s_mov_b32 m0, s31
	s_nop 0
	global_load_lds_dwordx4 v[212:213], off
	v_lshl_add_u64 v[212:213], v[218:219], 0, s[16:17]
	s_mov_b32 m0, s33
	s_nop 0
	global_load_lds_dwordx4 v[212:213], off
	s_waitcnt vmcnt(8)
	s_waitcnt lgkmcnt(0)
	s_barrier
	s_waitcnt lgkmcnt(0)
	v_mfma_f32_16x16x32_bf16 v[62:65], v[148:151], v[180:183], v[62:65]
	v_mfma_f32_16x16x32_bf16 v[58:61], v[156:159], v[180:183], v[58:61]
	v_mfma_f32_16x16x32_bf16 v[54:57], v[148:151], v[188:191], v[54:57]
	v_mfma_f32_16x16x32_bf16 v[50:53], v[156:159], v[188:191], v[50:53]
	v_mfma_f32_16x16x32_bf16 v[38:41], v[148:151], v[196:199], v[38:41]
	v_mfma_f32_16x16x32_bf16 v[34:37], v[156:159], v[196:199], v[34:37]
	v_mfma_f32_16x16x32_bf16 v[22:25], v[148:151], v[204:207], v[22:25]
	v_mfma_f32_16x16x32_bf16 v[18:21], v[156:159], v[204:207], v[18:21]
	v_mfma_f32_16x16x32_bf16 v[62:65], v[152:155], v[184:187], v[62:65]
	v_mfma_f32_16x16x32_bf16 v[58:61], v[160:163], v[184:187], v[58:61]
	v_mfma_f32_16x16x32_bf16 v[54:57], v[152:155], v[192:195], v[54:57]
	v_mfma_f32_16x16x32_bf16 v[50:53], v[160:163], v[192:195], v[50:53]
	v_mfma_f32_16x16x32_bf16 v[38:41], v[152:155], v[200:203], v[38:41]
	v_mfma_f32_16x16x32_bf16 v[34:37], v[160:163], v[200:203], v[34:37]
	v_mfma_f32_16x16x32_bf16 v[22:25], v[152:155], v[208:211], v[22:25]
	v_mfma_f32_16x16x32_bf16 v[18:21], v[160:163], v[208:211], v[18:21]
	v_mfma_f32_16x16x32_bf16 v[46:49], v[164:167], v[180:183], v[46:49]
	v_mfma_f32_16x16x32_bf16 v[42:45], v[172:175], v[180:183], v[42:45]
	v_mfma_f32_16x16x32_bf16 v[30:33], v[164:167], v[188:191], v[30:33]
	v_mfma_f32_16x16x32_bf16 v[26:29], v[172:175], v[188:191], v[26:29]
	v_mfma_f32_16x16x32_bf16 v[14:17], v[164:167], v[196:199], v[14:17]
	v_mfma_f32_16x16x32_bf16 v[10:13], v[172:175], v[196:199], v[10:13]
	v_mfma_f32_16x16x32_bf16 v[6:9], v[164:167], v[204:207], v[6:9]
	v_mfma_f32_16x16x32_bf16 v[2:5], v[172:175], v[204:207], v[2:5]
	v_mfma_f32_16x16x32_bf16 v[46:49], v[168:171], v[184:187], v[46:49]
	v_mfma_f32_16x16x32_bf16 v[42:45], v[176:179], v[184:187], v[42:45]
	v_mfma_f32_16x16x32_bf16 v[30:33], v[168:171], v[192:195], v[30:33]
	v_mfma_f32_16x16x32_bf16 v[26:29], v[176:179], v[192:195], v[26:29]
	v_mfma_f32_16x16x32_bf16 v[14:17], v[168:171], v[200:203], v[14:17]
	v_mfma_f32_16x16x32_bf16 v[10:13], v[176:179], v[200:203], v[10:13]
	v_mfma_f32_16x16x32_bf16 v[6:9], v[168:171], v[208:211], v[6:9]
	v_mfma_f32_16x16x32_bf16 v[2:5], v[176:179], v[208:211], v[2:5]
	s_barrier
	s_add_i32 s36, s36, 2
	s_add_u32 s20, s20, 0x100
	s_addc_u32 s21, s21, 0
	s_cmp_gt_u32 s36, 29
	s_cbranch_scc0 .LBB0_460
	s_cmpk_lt_u32 s2, 0x100
	s_cbranch_scc0 .LBB0_463
	s_barrier
.LBB0_463:
	s_lshr_b32 s2, s92, 3
	s_and_b32 s3, s92, 7
	s_add_u32 s8, s8, 0x44650000
	s_addc_u32 s9, s9, 0
	s_and_b64 s[10:11], s[10:11], exec
	s_cselect_b32 s7, 0x100, 0
	v_add_u32_e32 v132, s7, v1
	v_lshl_or_b32 v1, s6, 8, v142
	v_ashrrev_i32_e32 v133, 31, v132
	v_or_b32_e32 v1, s30, v1
	v_lshlrev_b64 v[130:131], 12, v[132:133]
	v_lshl_add_u64 v[134:135], s[8:9], 0, v[130:131]
	v_lshlrev_b32_e32 v130, 1, v1
	v_mov_b32_e32 v131, 0
	v_lshl_add_u64 v[134:135], v[134:135], 0, v[130:131]
	s_mov_b64 s[6:7], 0x80000
	v_cvt_pk_bf16_f32 v70, v70, v71
	v_cvt_pk_bf16_f32 v71, v72, v73
	v_cvt_pk_bf16_f32 v72, v66, v67
	v_lshl_add_u64 v[66:67], v[134:135], 0, s[6:7]
	s_mov_b32 s6, 0x80000
	v_cvt_pk_bf16_f32 v62, v62, v63
	v_cvt_pk_bf16_f32 v63, v64, v65
	v_cvt_pk_bf16_f32 v64, v58, v59
	v_add_co_u32_e32 v58, vcc, s6, v134
	v_cvt_pk_bf16_f32 v46, v46, v47
	v_cvt_pk_bf16_f32 v47, v48, v49
	v_cvt_pk_bf16_f32 v48, v42, v43
	v_cvt_pk_bf16_f32 v49, v44, v45
	s_mov_b64 s[6:7], 0x90000
	v_cvt_pk_bf16_f32 v110, v110, v111
	v_cvt_pk_bf16_f32 v111, v112, v113
	v_cvt_pk_bf16_f32 v112, v106, v107
	v_or_b32_e32 v106, 16, v132
	v_addc_co_u32_e32 v59, vcc, 0, v135, vcc
	global_store_dwordx4 v[66:67], v[46:49], off offset:256
	v_ashrrev_i32_e32 v107, 31, v106
	v_cvt_pk_bf16_f32 v94, v94, v95
	v_lshl_add_u64 v[46:47], v[134:135], 0, s[6:7]
	s_mov_b32 s6, 0x90000
	v_cvt_pk_bf16_f32 v95, v96, v97
	v_cvt_pk_bf16_f32 v96, v90, v91
	v_or_b32_e32 v90, 32, v132
	v_add_co_u32_e32 v48, vcc, s6, v134
	v_cvt_pk_bf16_f32 v30, v30, v31
	v_cvt_pk_bf16_f32 v31, v32, v33
	v_cvt_pk_bf16_f32 v32, v26, v27
	v_cvt_pk_bf16_f32 v33, v28, v29
	s_mov_b64 s[6:7], 0xa0000
	v_lshlrev_b64 v[106:107], 12, v[106:107]
	v_ashrrev_i32_e32 v91, 31, v90
	v_cvt_pk_bf16_f32 v78, v78, v79
	v_cvt_pk_bf16_f32 v79, v80, v81
	v_cvt_pk_bf16_f32 v80, v74, v75
	v_or_b32_e32 v74, 48, v132
	v_addc_co_u32_e32 v49, vcc, 0, v135, vcc
	global_store_dwordx4 v[46:47], v[30:33], off offset:256
	v_cvt_pk_bf16_f32 v113, v108, v109
	v_lshl_add_u64 v[106:107], s[8:9], 0, v[106:107]
	v_lshl_add_u64 v[30:31], v[134:135], 0, s[6:7]
; template <class Epi, class Sched, bool GATHER, bool LIGHTSKIP = false>
; __device__ __forceinline__ void gemm_phase(LAS unsigned char* lds, LAS unsigned char* xl, const int lda, const int ldb, const int K, const Sched& S, const Epi& E) {
;     const int tid = otid(), wid = __builtin_amdgcn_readfirstlane(tid >> 6), lane = tid & 63, wr = wid >> 2, wc = wid & 3, fr = lane & 15, fq = lane >> 4;
;     const int nt = K / BK;
;     int Rr[2], Cc[2]; unsigned voffA[2], voffB[2];
; #pragma unroll
;     for (int i = 0; i < 2; ++i) { stage_rc(tid * 16 + i * 8192, Rr[i], Cc[i]); const int Rb = Epi::PERM ? ((Rr[i] & ~31) + perm32(Rr[i] & 31)) : Rr[i];
;         voffA[i] = (unsigned)(Rr[i] * lda + Cc[i]) * 2u; voffB[i] = (unsigned)(Rb * ldb + Cc[i]) * 2u; }
;     unsigned vc[2][2], vn[2][2];
;     const size_t kstep = (size_t)(BK * 2);
;     const size_t hstepA = (size_t)HALF * lda * 2, hstepB = (size_t)HALF * ldb * 2;
;     const unsigned ldsw = (unsigned)wid * 1024u;
;     const int aoff = lds_byte(wr * 64 + fr, fq * 8), boff = lds_byte(wc * 32 + fr, fq * 8);
;     ...
;     GUnit cur, nxt; int ui = 0;
;     if (!S.next(0, cur)) return;
;     Acc acc;
; #pragma unroll
;     for (int a = 0; a < 2; ++a)
; #pragma unroll
;         for (int b = 0; b < 2; ++b)
; #pragma unroll
;             for (int m = 0; m < 4; ++m)
; #pragma unroll
;                 for (int n = 0; n < 2; ++n) acc[a][b][m][n] = (f32x4){0.f, 0.f, 0.f, 0.f};
;     bf16x8 At[4][2], B0[2][2], B1[2][2];
;     const char* cA = cur.A; const char* cB = cur.B;
;     __device__ __forceinline__ void operator()(Acc& acc, const GUnit& u, int wr, int wc, int fr, int fq, LAS unsigned char*, int, int) const {
;         const int row0 = u.x0 + wr * 64 + fr, col0 = u.x1 + wc * 32 + 8 * fq;
; #pragma unroll
;         for (int ai = 0; ai < 2; ++ai)
; #pragma unroll
;             for (int m = 0; m < 4; ++m) { bf16_t* rowp = O + (size_t)(row0 + ai * HALF + m * 16) * ldc + col0;
; #pragma unroll
;                 for (int bj = 0; bj < 2; ++bj) { const f32x4 v0 = acc[ai][bj][m][0], v1 = acc[ai][bj][m][1];
;                     u32x4 w; w.x = cvt_pk_bf16(v0[0], v0[1]); w.y = cvt_pk_bf16(v0[2], v0[3]); w.z = cvt_pk_bf16(v1[0], v1[1]); w.w = cvt_pk_bf16(v1[2], v1[3]);
;                     if constexpr (NT) __builtin_nontemporal_store(w, (u32x4*)(rowp + bj * HALF)); else *(u32x4*)(rowp + bj * HALF) = w; } }
	s_mov_b32 s6, 0xa0000
	v_lshlrev_b64 v[90:91], 12, v[90:91]
	v_ashrrev_i32_e32 v75, 31, v74
	v_add_co_u32_e32 v32, vcc, s6, v134
	v_cvt_pk_bf16_f32 v14, v14, v15
	v_cvt_pk_bf16_f32 v15, v16, v17
	v_cvt_pk_bf16_f32 v16, v10, v11
	v_cvt_pk_bf16_f32 v17, v12, v13
	s_mov_b64 s[6:7], 0xb0000
	global_store_dwordx4 v[134:135], v[110:113], off offset:256
	v_cvt_pk_bf16_f32 v97, v92, v93
	v_lshl_add_u64 v[90:91], s[8:9], 0, v[90:91]
	v_lshl_add_u64 v[110:111], v[106:107], 0, v[130:131]
	v_lshlrev_b64 v[74:75], 12, v[74:75]
	v_addc_co_u32_e32 v33, vcc, 0, v135, vcc
	global_store_dwordx4 v[30:31], v[14:17], off offset:256
	global_store_dwordx4 v[110:111], v[94:97], off offset:256
	v_cvt_pk_bf16_f32 v81, v76, v77
	v_lshl_add_u64 v[14:15], v[134:135], 0, s[6:7]
	s_mov_b32 s6, 0xb0000
	v_lshl_add_u64 v[94:95], v[90:91], 0, v[130:131]
	v_lshl_add_u64 v[74:75], s[8:9], 0, v[74:75]
	v_add_co_u32_e32 v16, vcc, s6, v134
	v_cvt_pk_bf16_f32 v126, v126, v127
	v_cvt_pk_bf16_f32 v127, v128, v129
	v_cvt_pk_bf16_f32 v128, v122, v123
	v_cvt_pk_bf16_f32 v129, v124, v125
	v_cvt_pk_bf16_f32 v106, v118, v119
	v_cvt_pk_bf16_f32 v107, v120, v121
	v_cvt_pk_bf16_f32 v108, v114, v115
	v_cvt_pk_bf16_f32 v109, v116, v117
	v_cvt_pk_bf16_f32 v90, v102, v103
	v_cvt_pk_bf16_f32 v91, v104, v105
	v_cvt_pk_bf16_f32 v92, v98, v99
	v_cvt_pk_bf16_f32 v93, v100, v101
	global_store_dwordx4 v[94:95], v[78:81], off offset:256
	v_cvt_pk_bf16_f32 v76, v82, v83
	v_cvt_pk_bf16_f32 v77, v84, v85
	v_lshl_add_u64 v[78:79], v[74:75], 0, v[130:131]
	v_cvt_pk_bf16_f32 v74, v86, v87
	v_cvt_pk_bf16_f32 v75, v88, v89
	v_cvt_pk_bf16_f32 v73, v68, v69
	v_cvt_pk_bf16_f32 v65, v60, v61
	v_cvt_pk_bf16_f32 v42, v54, v55
	v_cvt_pk_bf16_f32 v43, v56, v57
	v_cvt_pk_bf16_f32 v44, v50, v51
	v_cvt_pk_bf16_f32 v45, v52, v53
	v_cvt_pk_bf16_f32 v26, v38, v39
	v_cvt_pk_bf16_f32 v27, v40, v41
	v_cvt_pk_bf16_f32 v28, v34, v35
	v_cvt_pk_bf16_f32 v29, v36, v37
	v_cvt_pk_bf16_f32 v10, v22, v23
	v_cvt_pk_bf16_f32 v11, v24, v25
	v_cvt_pk_bf16_f32 v12, v18, v19
	v_cvt_pk_bf16_f32 v13, v20, v21
	v_addc_co_u32_e32 v17, vcc, 0, v135, vcc
	v_cvt_pk_bf16_f32 v6, v6, v7
	v_cvt_pk_bf16_f32 v7, v8, v9
	v_cvt_pk_bf16_f32 v8, v2, v3
	v_cvt_pk_bf16_f32 v9, v4, v5
	global_store_dwordx4 v[134:135], v[126:129], off
	global_store_dwordx4 v[110:111], v[106:109], off
	global_store_dwordx4 v[94:95], v[90:93], off
	global_store_dwordx4 v[78:79], v[74:77], off
	global_store_dwordx4 v[78:79], v[70:73], off offset:256
	global_store_dwordx4 v[58:59], v[62:65], off
	global_store_dwordx4 v[48:49], v[42:45], off
	global_store_dwordx4 v[32:33], v[26:29], off
	global_store_dwordx4 v[16:17], v[10:13], off
	global_store_dwordx4 v[14:15], v[6:9], off offset:256
	v_mov_b32_e32 v15, v0
	s_waitcnt vmcnt(0)
	s_barrier
	s_setprio 0
	s_load_dwordx2 s[8:9], s[70:71], 0xd8
	s_mov_b32 s7, 0xfffe0
	v_ashrrev_i32_e32 v2, 31, v15
	v_lshrrev_b32_e32 v2, 26, v2
	v_add_u32_e32 v2, v15, v2
	v_ashrrev_i32_e32 v10, 6, v2
	v_bfe_i32 v2, v15, 27, 1
	v_lshlrev_b32_e32 v1, 4, v15
	v_lshrrev_b32_e32 v2, 22, v2
	v_add_u32_e32 v2, v1, v2
	v_and_b32_e32 v2, 0xfffffc00, v2
	v_sub_u32_e32 v2, v1, v2
	v_lshrrev_b32_e32 v3, 4, v2
	v_bitop3_b32 v3, v3, v2, 32 bitop3:0x6c
	v_ashrrev_i32_e32 v2, 31, v2
	v_lshrrev_b32_e32 v2, 26, v2
	v_add_u32_e32 v2, v3, v2
	v_ashrrev_i32_e32 v11, 6, v2
	v_lshlrev_b32_e32 v4, 3, v10
	v_mul_i32_i24_e32 v5, 64, v11
	v_and_b32_e32 v4, -16, v4
	v_sub_u32_e32 v3, v3, v5
	v_mov_b32_e32 v5, 1
	v_add_u32_e32 v2, v11, v4
	v_lshlrev_b32_e32 v4, 5, v10
	v_ashrrev_i16_sdwa v3, v5, sext(v3) dst_sel:DWORD dst_unused:UNUSED_PAD src0_sel:DWORD src1_sel:BYTE_0
	v_and_b32_e32 v4, 32, v4
	v_bfe_i32 v12, v3, 0, 16
	v_and_b32_e32 v7, 3, v11
	v_add_lshl_u32 v4, v4, v12, 1
	v_add_u32_e32 v1, 0x2000, v1
	v_lshlrev_b32_e32 v3, 1, v2
	v_lshrrev_b32_e32 v6, 2, v2
	v_and_or_b32 v7, v2, s7, v7
	v_lshl_add_u32 v132, v2, 12, v4
	v_ashrrev_i32_e32 v2, 31, v1
	v_lshrrev_b32_e32 v2, 22, v2
	v_add_u32_e32 v2, v1, v2
	v_ashrrev_i32_e32 v13, 10, v2
	v_readfirstlane_b32 s6, v15
	v_mul_i32_i24_e32 v2, 0x400, v13
	v_sub_u32_e32 v1, v1, v2
	s_ashr_i32 s15, s6, 6
	s_ashr_i32 s14, s6, 8
	v_and_b32_e32 v3, 24, v3
	v_and_b32_e32 v6, 4, v6
	v_lshrrev_b32_e32 v2, 4, v1
	s_lshl_b32 s20, s15, 10
	s_lshl_b32 s16, s2, 20
	v_or3_b32 v3, v7, v6, v3
	v_bitop3_b32 v1, v2, v1, 32 bitop3:0x6c
	s_waitcnt lgkmcnt(0)
	s_add_u32 s17, s8, s16
	v_lshl_add_u32 v130, v3, 12, v4
	v_ashrrev_i32_e32 v3, 31, v1
	s_addc_u32 s19, s9, 0
	v_lshrrev_b32_e32 v3, 26, v3
	s_add_u32 s10, s17, 0x44450000
	v_add_u32_e32 v3, v1, v3
	s_addc_u32 s11, s19, 0
	s_lshl_b32 s18, s3, 20
	v_lshlrev_b32_e32 v2, 3, v13
	v_ashrrev_i32_e32 v14, 6, v3
	v_and_b32_e32 v3, 0xc0, v3
	s_add_u32 s21, s8, s18
	v_and_b32_e32 v2, -16, v2
	v_sub_u32_e32 v1, v1, v3
	s_addc_u32 s23, s9, 0
	v_add_u32_e32 v2, v14, v2
	v_ashrrev_i16_sdwa v1, v5, sext(v1) dst_sel:DWORD dst_unused:UNUSED_PAD src0_sel:DWORD src1_sel:BYTE_0
	v_and_b32_e32 v5, 3, v14
	s_add_u32 s12, s21, 0x3010000
	v_lshlrev_b32_e32 v4, 5, v13
	v_bfe_i32 v16, v1, 0, 16
	v_lshlrev_b32_e32 v1, 1, v2
	v_lshrrev_b32_e32 v3, 2, v2
	v_and_or_b32 v5, v2, s7, v5
	s_addc_u32 s13, s23, 0
	s_add_i32 s7, s20, 0
	v_and_b32_e32 v4, 32, v4
	v_and_b32_e32 v1, 24, v1
	v_and_b32_e32 v3, 4, v3
	s_add_i32 m0, s7, 0x10000
	v_or3_b32 v1, v5, v3, v1
	v_add_lshl_u32 v3, v4, v16, 1
	global_load_lds_dwordx4 v130, s[12:13]
	s_add_i32 m0, s7, 0x12000
	v_lshl_add_u32 v136, v1, 12, v3
	s_add_u32 s22, s21, 0x3090000
	global_load_lds_dwordx4 v136, s[12:13]
	s_addc_u32 s23, s23, 0
	s_add_i32 m0, s7, 0x14000
	s_add_i32 s26, s7, 0x2000
	global_load_lds_dwordx4 v130, s[22:23]
	s_add_i32 m0, s7, 0x16000
	v_lshl_add_u32 v134, v2, 12, v3
	global_load_lds_dwordx4 v136, s[22:23]
	s_mov_b32 m0, s7
	s_add_u32 s22, s17, 0x444d0000
	global_load_lds_dwordx4 v132, s[10:11]
	s_mov_b32 m0, s26
	s_addc_u32 s23, s19, 0
	s_add_i32 s27, s7, 0x4000
	global_load_lds_dwordx4 v134, s[10:11]
	s_mov_b32 m0, s27
	s_add_i32 s28, s7, 0x6000
	global_load_lds_dwordx4 v132, s[22:23]
	s_mov_b32 m0, s28
	v_mov_b32_e32 v137, v131
	global_load_lds_dwordx4 v134, s[22:23]
	v_mov_b32_e32 v133, v131
	v_mov_b32_e32 v135, v131
	v_lshl_add_u64 v[8:9], s[12:13], 0, v[130:131]
	v_lshl_add_u64 v[6:7], s[12:13], 0, v[136:137]
	v_lshl_add_u64 v[4:5], s[10:11], 0, v[132:133]
	s_cmp_lg_u32 s14, 1
	v_lshl_add_u64 v[2:3], s[10:11], 0, v[134:135]
	s_cbranch_scc1 .LBB0_465
	s_barrier
	s_setprio 1

; #define PG8_STAGE_B(b, h, bp) PG8_STAGE2(PG8_SB(b, h), (bp) + (h) * hstepB, voffB[0], voffB[1])
; #define PG8_STAGE_A(b, h, ap, NX) do { if constexpr (GATHER) { const unsigned _o0 = (NX) ? vn[h][0] : vc[h][0], _o1 = (NX) ? vn[h][1] : vc[h][1]; PG8_STAGE2(PG8_SA(b, h), (ap), _o0, _o1); } \
;         else { PG8_STAGE2(PG8_SA(b, h), (ap) + (h) * hstepA, voffA[0], voffA[1]); } } while (0)
; #define PG8_LDA(dst, b, h) do { _Pragma("unroll") for (int m = 0; m < 4; ++m) _Pragma("unroll") for (int k = 0; k < 2; ++k) dst[m][k] = *(const LAS bf16x8*)(lds + PG8_SA(b, h) + aoff + m * 2048 + k * 1024); } while (0)
; #define PG8_LDB(dst, b, h) do { _Pragma("unroll") for (int n = 0; n < 2; ++n) _Pragma("unroll") for (int k = 0; k < 2; ++k) dst[n][k] = *(const LAS bf16x8*)(lds + PG8_SB(b, h) + boff + n * 2048 + k * 1024); } while (0)
; #define PG8_MMA(ai, bj, At, Bt) do { __builtin_amdgcn_s_setprio(1); _Pragma("unroll") for (int m = 0; m < 4; ++m) _Pragma("unroll") for (int n = 0; n < 2; ++n) _Pragma("unroll") for (int k = 0; k < 2; ++k) \
;         acc[ai][bj][m][n] = __builtin_amdgcn_mfma_f32_16x16x32_bf16(Bt[n][k], At[m][k], acc[ai][bj][m][n], 0, 0, 0); __builtin_amdgcn_s_setprio(0); } while (0)
; #define PG8_WAIT_V(n) asm volatile("s_waitcnt vmcnt(" #n ")" ::: "memory")
; #define PG8_WAIT_L(n) asm volatile("s_waitcnt lgkmcnt(" #n ")" ::: "memory")
; #define PG8_BAR __builtin_amdgcn_s_barrier()
; #define PG8_SCHED __builtin_amdgcn_sched_barrier(0)
; template <class Epi, class Sched, bool GATHER, bool LIGHTSKIP = false>
; __device__ __forceinline__ void gemm_phase(LAS unsigned char* lds, LAS unsigned char* xl, const int lda, const int ldb, const int K, const Sched& S, const Epi& E) {
;     ...
;             PG8_LDB(B0, 0, 0); PG8_LDB(B1, 0, 1); PG8_SCHED; PG8_LDA(At, 0, 0); PG8_STAGE_A(1, 1, a1, false);
;             PG8_WAIT_V(8); PG8_WAIT_L(0); PG8_BAR; PG8_MMA(0, 0, At, B0); PG8_MMA(0, 1, At, B1); PG8_BAR; PG8_SCHED;
;             PG8_LDA(At, 0, 1); PG8_STAGE_B(0, 0, b2); PG8_STAGE_B(0, 1, b2); PG8_STAGE_A(0, 0, a2, last);
.LBB0_466:
	ds_read_b128 v[148:151], v143
	ds_read_b128 v[152:155], v143 offset:1024
	ds_read_b128 v[156:159], v143 offset:2048
	ds_read_b128 v[160:163], v143 offset:3072
	ds_read_b128 v[164:167], v144
	ds_read_b128 v[168:171], v144 offset:1024
	ds_read_b128 v[172:175], v144 offset:2048
	ds_read_b128 v[176:179], v144 offset:3072
	s_add_u32 s20, s16, s18
	s_addc_u32 s21, s17, s19
	s_add_u32 s20, s20, 0x44450100
	s_addc_u32 s21, s21, 0
	s_add_u32 s42, s33, s18
	s_addc_u32 s43, s34, s19
	s_cmpk_eq_i32 s18, 0xf00
	s_cselect_b32 s23, s11, s21
	s_cselect_b32 s22, s10, s20
	s_cselect_b32 s21, s13, s43
	s_cselect_b32 s20, s12, s42
	s_mov_b32 m0, s36
	v_lshl_add_u64 v[212:213], v[138:139], 0, s[18:19]
	ds_read_b128 v[180:183], v145
	ds_read_b128 v[184:187], v145 offset:1024
	ds_read_b128 v[188:191], v145 offset:2048
	ds_read_b128 v[192:195], v145 offset:3072
	ds_read_b128 v[196:199], v145 offset:4096
	ds_read_b128 v[200:203], v145 offset:5120
	ds_read_b128 v[204:207], v145 offset:6144
	ds_read_b128 v[208:211], v145 offset:7168
	global_load_lds_dwordx4 v[212:213], off
	v_lshl_add_u64 v[212:213], v[140:141], 0, s[18:19]
	s_mov_b32 m0, s37
	s_nop 0
	global_load_lds_dwordx4 v[212:213], off
	s_waitcnt vmcnt(8)
	s_waitcnt lgkmcnt(0)
	s_barrier
	s_waitcnt lgkmcnt(0)
	v_mfma_f32_16x16x32_bf16 v[126:129], v[148:151], v[180:183], v[126:129]
	v_mfma_f32_16x16x32_bf16 v[122:125], v[156:159], v[180:183], v[122:125]
	v_mfma_f32_16x16x32_bf16 v[118:121], v[148:151], v[188:191], v[118:121]
	v_mfma_f32_16x16x32_bf16 v[114:117], v[156:159], v[188:191], v[114:117]
	v_mfma_f32_16x16x32_bf16 v[102:105], v[148:151], v[196:199], v[102:105]
	v_mfma_f32_16x16x32_bf16 v[98:101], v[156:159], v[196:199], v[98:101]
	v_mfma_f32_16x16x32_bf16 v[86:89], v[148:151], v[204:207], v[86:89]
	v_mfma_f32_16x16x32_bf16 v[82:85], v[156:159], v[204:207], v[82:85]
	v_mfma_f32_16x16x32_bf16 v[126:129], v[152:155], v[184:187], v[126:129]
	v_mfma_f32_16x16x32_bf16 v[122:125], v[160:163], v[184:187], v[122:125]
	v_mfma_f32_16x16x32_bf16 v[118:121], v[152:155], v[192:195], v[118:121]
	v_mfma_f32_16x16x32_bf16 v[114:117], v[160:163], v[192:195], v[114:117]
	v_mfma_f32_16x16x32_bf16 v[102:105], v[152:155], v[200:203], v[102:105]
	v_mfma_f32_16x16x32_bf16 v[98:101], v[160:163], v[200:203], v[98:101]
	v_mfma_f32_16x16x32_bf16 v[86:89], v[152:155], v[208:211], v[86:89]
	v_mfma_f32_16x16x32_bf16 v[82:85], v[160:163], v[208:211], v[82:85]
	v_mfma_f32_16x16x32_bf16 v[110:113], v[164:167], v[180:183], v[110:113]
	v_mfma_f32_16x16x32_bf16 v[106:109], v[172:175], v[180:183], v[106:109]
	v_mfma_f32_16x16x32_bf16 v[94:97], v[164:167], v[188:191], v[94:97]
	v_mfma_f32_16x16x32_bf16 v[90:93], v[172:175], v[188:191], v[90:93]
	v_mfma_f32_16x16x32_bf16 v[78:81], v[164:167], v[196:199], v[78:81]
	v_mfma_f32_16x16x32_bf16 v[74:77], v[172:175], v[196:199], v[74:77]
	v_mfma_f32_16x16x32_bf16 v[70:73], v[164:167], v[204:207], v[70:73]
	v_mfma_f32_16x16x32_bf16 v[66:69], v[172:175], v[204:207], v[66:69]
	v_mfma_f32_16x16x32_bf16 v[110:113], v[168:171], v[184:187], v[110:113]
	v_mfma_f32_16x16x32_bf16 v[106:109], v[176:179], v[184:187], v[106:109]
	v_mfma_f32_16x16x32_bf16 v[94:97], v[168:171], v[192:195], v[94:97]
	v_mfma_f32_16x16x32_bf16 v[90:93], v[176:179], v[192:195], v[90:93]
	v_mfma_f32_16x16x32_bf16 v[78:81], v[168:171], v[200:203], v[78:81]
	v_mfma_f32_16x16x32_bf16 v[74:77], v[176:179], v[200:203], v[74:77]
	v_mfma_f32_16x16x32_bf16 v[70:73], v[168:171], v[208:211], v[70:73]
	v_mfma_f32_16x16x32_bf16 v[66:69], v[176:179], v[208:211], v[66:69]
	s_barrier
	s_mov_b32 m0, s0
	v_lshl_add_u64 v[212:213], s[20:21], 0, v[130:131]
	s_add_u32 s42, s20, 0x80000
	ds_read_b128 v[180:183], v145 offset:16384
	ds_read_b128 v[184:187], v145 offset:17408
	ds_read_b128 v[188:191], v145 offset:18432
	ds_read_b128 v[192:195], v145 offset:19456
	ds_read_b128 v[196:199], v145 offset:20480
	ds_read_b128 v[200:203], v145 offset:21504
	ds_read_b128 v[204:207], v145 offset:22528
	ds_read_b128 v[208:211], v145 offset:23552
	global_load_lds_dwordx4 v[212:213], off
	v_lshl_add_u64 v[214:215], s[20:21], 0, v[136:137]
	s_mov_b32 m0, s38
	s_addc_u32 s43, s21, 0
	global_load_lds_dwordx4 v[214:215], off
	v_lshl_add_u64 v[216:217], s[42:43], 0, v[130:131]
	s_mov_b32 m0, s1
	v_lshl_add_u64 v[218:219], s[22:23], 0, v[134:135]
	global_load_lds_dwordx4 v[216:217], off
	v_lshl_add_u64 v[216:217], s[42:43], 0, v[136:137]
	s_mov_b32 m0, s39
	s_nop 0
	global_load_lds_dwordx4 v[216:217], off
	v_lshl_add_u64 v[216:217], s[22:23], 0, v[132:133]
	s_mov_b32 m0, s7
	s_nop 0
	global_load_lds_dwordx4 v[216:217], off
	s_mov_b32 m0, s26
	s_nop 0
	global_load_lds_dwordx4 v[218:219], off
	s_waitcnt vmcnt(8)
	s_waitcnt lgkmcnt(0)
	s_barrier
; #define PG8_STAGE_A(b, h, ap, NX) do { if constexpr (GATHER) { const unsigned _o0 = (NX) ? vn[h][0] : vc[h][0], _o1 = (NX) ? vn[h][1] : vc[h][1]; PG8_STAGE2(PG8_SA(b, h), (ap), _o0, _o1); } \
;         else { PG8_STAGE2(PG8_SA(b, h), (ap) + (h) * hstepA, voffA[0], voffA[1]); } } while (0)
; #define PG8_LDA(dst, b, h) do { _Pragma("unroll") for (int m = 0; m < 4; ++m) _Pragma("unroll") for (int k = 0; k < 2; ++k) dst[m][k] = *(const LAS bf16x8*)(lds + PG8_SA(b, h) + aoff + m * 2048 + k * 1024); } while (0)
; #define PG8_LDB(dst, b, h) do { _Pragma("unroll") for (int n = 0; n < 2; ++n) _Pragma("unroll") for (int k = 0; k < 2; ++k) dst[n][k] = *(const LAS bf16x8*)(lds + PG8_SB(b, h) + boff + n * 2048 + k * 1024); } while (0)
; #define PG8_MMA(ai, bj, At, Bt) do { __builtin_amdgcn_s_setprio(1); _Pragma("unroll") for (int m = 0; m < 4; ++m) _Pragma("unroll") for (int n = 0; n < 2; ++n) _Pragma("unroll") for (int k = 0; k < 2; ++k) \
;         acc[ai][bj][m][n] = __builtin_amdgcn_mfma_f32_16x16x32_bf16(Bt[n][k], At[m][k], acc[ai][bj][m][n], 0, 0, 0); __builtin_amdgcn_s_setprio(0); } while (0)
; #define PG8_WAIT_V(n) asm volatile("s_waitcnt vmcnt(" #n ")" ::: "memory")
; #define PG8_WAIT_L(n) asm volatile("s_waitcnt lgkmcnt(" #n ")" ::: "memory")
; #define PG8_BAR __builtin_amdgcn_s_barrier()
; #define PG8_SCHED __builtin_amdgcn_sched_barrier(0)
; template <class Epi, class Sched, bool GATHER, bool LIGHTSKIP = false>
; __device__ __forceinline__ void gemm_phase(LAS unsigned char* lds, LAS unsigned char* xl, const int lda, const int ldb, const int K, const Sched& S, const Epi& E) {
;     ...
;             PG8_WAIT_V(8); PG8_WAIT_L(0); PG8_BAR; if (!light) { PG8_MMA(1, 0, At, B0); PG8_MMA(1, 1, At, B1); } PG8_BAR; PG8_SCHED;
;             PG8_LDB(B0, 1, 0); PG8_LDB(B1, 1, 1); PG8_SCHED; PG8_LDA(At, 1, 0); PG8_STAGE_A(0, 1, a2, last);
;             PG8_WAIT_V(8); PG8_WAIT_L(0); PG8_BAR; PG8_MMA(0, 0, At, B0); PG8_MMA(0, 1, At, B1); PG8_BAR; PG8_SCHED;
	s_waitcnt lgkmcnt(0)
	v_mfma_f32_16x16x32_bf16 v[62:65], v[148:151], v[180:183], v[62:65]
	v_mfma_f32_16x16x32_bf16 v[58:61], v[156:159], v[180:183], v[58:61]
	v_mfma_f32_16x16x32_bf16 v[54:57], v[148:151], v[188:191], v[54:57]
	v_mfma_f32_16x16x32_bf16 v[50:53], v[156:159], v[188:191], v[50:53]
	v_mfma_f32_16x16x32_bf16 v[38:41], v[148:151], v[196:199], v[38:41]
	v_mfma_f32_16x16x32_bf16 v[34:37], v[156:159], v[196:199], v[34:37]
	v_mfma_f32_16x16x32_bf16 v[22:25], v[148:151], v[204:207], v[22:25]
	v_mfma_f32_16x16x32_bf16 v[18:21], v[156:159], v[204:207], v[18:21]
	v_mfma_f32_16x16x32_bf16 v[62:65], v[152:155], v[184:187], v[62:65]
	v_mfma_f32_16x16x32_bf16 v[58:61], v[160:163], v[184:187], v[58:61]
	v_mfma_f32_16x16x32_bf16 v[54:57], v[152:155], v[192:195], v[54:57]
	v_mfma_f32_16x16x32_bf16 v[50:53], v[160:163], v[192:195], v[50:53]
	v_mfma_f32_16x16x32_bf16 v[38:41], v[152:155], v[200:203], v[38:41]
	v_mfma_f32_16x16x32_bf16 v[34:37], v[160:163], v[200:203], v[34:37]
	v_mfma_f32_16x16x32_bf16 v[22:25], v[152:155], v[208:211], v[22:25]
	v_mfma_f32_16x16x32_bf16 v[18:21], v[160:163], v[208:211], v[18:21]
	v_mfma_f32_16x16x32_bf16 v[46:49], v[164:167], v[180:183], v[46:49]
	v_mfma_f32_16x16x32_bf16 v[42:45], v[172:175], v[180:183], v[42:45]
	v_mfma_f32_16x16x32_bf16 v[30:33], v[164:167], v[188:191], v[30:33]
	v_mfma_f32_16x16x32_bf16 v[26:29], v[172:175], v[188:191], v[26:29]
	v_mfma_f32_16x16x32_bf16 v[14:17], v[164:167], v[196:199], v[14:17]
	v_mfma_f32_16x16x32_bf16 v[10:13], v[172:175], v[196:199], v[10:13]
	v_mfma_f32_16x16x32_bf16 v[6:9], v[164:167], v[204:207], v[6:9]
	v_mfma_f32_16x16x32_bf16 v[2:5], v[172:175], v[204:207], v[2:5]
	v_mfma_f32_16x16x32_bf16 v[46:49], v[168:171], v[184:187], v[46:49]
	v_mfma_f32_16x16x32_bf16 v[42:45], v[176:179], v[184:187], v[42:45]
	v_mfma_f32_16x16x32_bf16 v[30:33], v[168:171], v[192:195], v[30:33]
	v_mfma_f32_16x16x32_bf16 v[26:29], v[176:179], v[192:195], v[26:29]
	v_mfma_f32_16x16x32_bf16 v[14:17], v[168:171], v[200:203], v[14:17]
	v_mfma_f32_16x16x32_bf16 v[10:13], v[176:179], v[200:203], v[10:13]
	v_mfma_f32_16x16x32_bf16 v[6:9], v[168:171], v[208:211], v[6:9]
	v_mfma_f32_16x16x32_bf16 v[2:5], v[176:179], v[208:211], v[2:5]
	s_barrier
	ds_read_b128 v[148:151], v146
	ds_read_b128 v[152:155], v146 offset:1024
	ds_read_b128 v[156:159], v146 offset:2048
	ds_read_b128 v[160:163], v146 offset:3072
	ds_read_b128 v[164:167], v147
	ds_read_b128 v[168:171], v147 offset:1024
	ds_read_b128 v[172:175], v147 offset:2048
	ds_read_b128 v[176:179], v147 offset:3072
	s_add_u32 s22, s22, 0x80000
	s_addc_u32 s23, s23, 0
	s_mov_b32 m0, s27
	v_lshl_add_u64 v[220:221], s[22:23], 0, v[132:133]
	ds_read_b128 v[180:183], v145 offset:32768
	ds_read_b128 v[184:187], v145 offset:33792
	ds_read_b128 v[188:191], v145 offset:34816
	ds_read_b128 v[192:195], v145 offset:35840
	ds_read_b128 v[196:199], v145 offset:36864
	ds_read_b128 v[200:203], v145 offset:37888
	ds_read_b128 v[204:207], v145 offset:38912
	ds_read_b128 v[208:211], v145 offset:39936
	global_load_lds_dwordx4 v[220:221], off
	v_lshl_add_u64 v[220:221], s[22:23], 0, v[134:135]
	s_mov_b32 m0, s28
	s_nop 0
	global_load_lds_dwordx4 v[220:221], off
	s_waitcnt vmcnt(8)
	s_waitcnt lgkmcnt(0)
	s_barrier
	s_waitcnt lgkmcnt(0)
	v_mfma_f32_16x16x32_bf16 v[126:129], v[148:151], v[180:183], v[126:129]
	v_mfma_f32_16x16x32_bf16 v[122:125], v[156:159], v[180:183], v[122:125]
	v_mfma_f32_16x16x32_bf16 v[118:121], v[148:151], v[188:191], v[118:121]
	v_mfma_f32_16x16x32_bf16 v[114:117], v[156:159], v[188:191], v[114:117]
	v_mfma_f32_16x16x32_bf16 v[102:105], v[148:151], v[196:199], v[102:105]
	v_mfma_f32_16x16x32_bf16 v[98:101], v[156:159], v[196:199], v[98:101]
	v_mfma_f32_16x16x32_bf16 v[86:89], v[148:151], v[204:207], v[86:89]
	v_mfma_f32_16x16x32_bf16 v[82:85], v[156:159], v[204:207], v[82:85]
	v_mfma_f32_16x16x32_bf16 v[126:129], v[152:155], v[184:187], v[126:129]
	v_mfma_f32_16x16x32_bf16 v[122:125], v[160:163], v[184:187], v[122:125]
	v_mfma_f32_16x16x32_bf16 v[118:121], v[152:155], v[192:195], v[118:121]
	v_mfma_f32_16x16x32_bf16 v[114:117], v[160:163], v[192:195], v[114:117]
	v_mfma_f32_16x16x32_bf16 v[102:105], v[152:155], v[200:203], v[102:105]
	v_mfma_f32_16x16x32_bf16 v[98:101], v[160:163], v[200:203], v[98:101]
	v_mfma_f32_16x16x32_bf16 v[86:89], v[152:155], v[208:211], v[86:89]
	v_mfma_f32_16x16x32_bf16 v[82:85], v[160:163], v[208:211], v[82:85]
	v_mfma_f32_16x16x32_bf16 v[110:113], v[164:167], v[180:183], v[110:113]
	v_mfma_f32_16x16x32_bf16 v[106:109], v[172:175], v[180:183], v[106:109]
	v_mfma_f32_16x16x32_bf16 v[94:97], v[164:167], v[188:191], v[94:97]
	v_mfma_f32_16x16x32_bf16 v[90:93], v[172:175], v[188:191], v[90:93]
	v_mfma_f32_16x16x32_bf16 v[78:81], v[164:167], v[196:199], v[78:81]
	v_mfma_f32_16x16x32_bf16 v[74:77], v[172:175], v[196:199], v[74:77]
	v_mfma_f32_16x16x32_bf16 v[70:73], v[164:167], v[204:207], v[70:73]
	v_mfma_f32_16x16x32_bf16 v[66:69], v[172:175], v[204:207], v[66:69]
	v_mfma_f32_16x16x32_bf16 v[110:113], v[168:171], v[184:187], v[110:113]
	v_mfma_f32_16x16x32_bf16 v[106:109], v[176:179], v[184:187], v[106:109]
	v_mfma_f32_16x16x32_bf16 v[94:97], v[168:171], v[192:195], v[94:97]
	v_mfma_f32_16x16x32_bf16 v[90:93], v[176:179], v[192:195], v[90:93]
	v_mfma_f32_16x16x32_bf16 v[78:81], v[168:171], v[200:203], v[78:81]
	v_mfma_f32_16x16x32_bf16 v[74:77], v[176:179], v[200:203], v[74:77]
	v_mfma_f32_16x16x32_bf16 v[70:73], v[168:171], v[208:211], v[70:73]
	v_mfma_f32_16x16x32_bf16 v[66:69], v[176:179], v[208:211], v[66:69]
	s_barrier
; #define PG8_STAGE_B(b, h, bp) PG8_STAGE2(PG8_SB(b, h), (bp) + (h) * hstepB, voffB[0], voffB[1])
; #define PG8_STAGE_A(b, h, ap, NX) do { if constexpr (GATHER) { const unsigned _o0 = (NX) ? vn[h][0] : vc[h][0], _o1 = (NX) ? vn[h][1] : vc[h][1]; PG8_STAGE2(PG8_SA(b, h), (ap), _o0, _o1); } \
;         else { PG8_STAGE2(PG8_SA(b, h), (ap) + (h) * hstepA, voffA[0], voffA[1]); } } while (0)
; #define PG8_LDA(dst, b, h) do { _Pragma("unroll") for (int m = 0; m < 4; ++m) _Pragma("unroll") for (int k = 0; k < 2; ++k) dst[m][k] = *(const LAS bf16x8*)(lds + PG8_SA(b, h) + aoff + m * 2048 + k * 1024); } while (0)
; #define PG8_MMA(ai, bj, At, Bt) do { __builtin_amdgcn_s_setprio(1); _Pragma("unroll") for (int m = 0; m < 4; ++m) _Pragma("unroll") for (int n = 0; n < 2; ++n) _Pragma("unroll") for (int k = 0; k < 2; ++k) \
;         acc[ai][bj][m][n] = __builtin_amdgcn_mfma_f32_16x16x32_bf16(Bt[n][k], At[m][k], acc[ai][bj][m][n], 0, 0, 0); __builtin_amdgcn_s_setprio(0); } while (0)
; #define PG8_WAIT_V(n) asm volatile("s_waitcnt vmcnt(" #n ")" ::: "memory")
; #define PG8_WAIT_L(n) asm volatile("s_waitcnt lgkmcnt(" #n ")" ::: "memory")
; #define PG8_BAR __builtin_amdgcn_s_barrier()
; #define PG8_SCHED __builtin_amdgcn_sched_barrier(0)
; template <class Epi, class Sched, bool GATHER, bool LIGHTSKIP = false>
; __device__ __forceinline__ void gemm_phase(LAS unsigned char* lds, LAS unsigned char* xl, const int lda, const int ldb, const int K, const Sched& S, const Epi& E) {
;     ...
;             PG8_LDA(At, 1, 1); PG8_STAGE_B(1, 0, b3); PG8_STAGE_B(1, 1, b3); PG8_STAGE_A(1, 0, a3, last);
;             PG8_WAIT_V(8); PG8_WAIT_L(0); PG8_BAR; if (!light) { PG8_MMA(1, 0, At, B0); PG8_MMA(1, 1, At, B1); } PG8_BAR; PG8_SCHED;
;         }
;         if (wr == 0) PG8_BAR;
	s_mov_b32 m0, s4
	v_lshl_add_u64 v[212:213], v[212:213], 0, s[14:15]
	s_add_u32 s20, s20, 0x80080
	ds_read_b128 v[180:183], v145 offset:49152
	ds_read_b128 v[184:187], v145 offset:50176
	ds_read_b128 v[188:191], v145 offset:51200
	ds_read_b128 v[192:195], v145 offset:52224
	ds_read_b128 v[196:199], v145 offset:53248
	ds_read_b128 v[200:203], v145 offset:54272
	ds_read_b128 v[204:207], v145 offset:55296
	ds_read_b128 v[208:211], v145 offset:56320
	global_load_lds_dwordx4 v[212:213], off
	v_lshl_add_u64 v[212:213], v[214:215], 0, s[14:15]
	s_mov_b32 m0, s40
	s_addc_u32 s21, s21, 0
	global_load_lds_dwordx4 v[212:213], off
	v_lshl_add_u64 v[212:213], s[20:21], 0, v[130:131]
	s_mov_b32 m0, s5
	s_nop 0
	global_load_lds_dwordx4 v[212:213], off
	v_lshl_add_u64 v[212:213], s[20:21], 0, v[136:137]
	s_mov_b32 m0, s41
	s_nop 0
	global_load_lds_dwordx4 v[212:213], off
	v_lshl_add_u64 v[212:213], v[216:217], 0, s[14:15]
	s_mov_b32 m0, s30
	s_nop 0
	global_load_lds_dwordx4 v[212:213], off
	v_lshl_add_u64 v[212:213], v[218:219], 0, s[14:15]
	s_mov_b32 m0, s31
	s_nop 0
	global_load_lds_dwordx4 v[212:213], off
	s_waitcnt vmcnt(8)
	s_waitcnt lgkmcnt(0)
	s_barrier
	s_waitcnt lgkmcnt(0)
	v_mfma_f32_16x16x32_bf16 v[62:65], v[148:151], v[180:183], v[62:65]
	v_mfma_f32_16x16x32_bf16 v[58:61], v[156:159], v[180:183], v[58:61]
	v_mfma_f32_16x16x32_bf16 v[54:57], v[148:151], v[188:191], v[54:57]
	v_mfma_f32_16x16x32_bf16 v[50:53], v[156:159], v[188:191], v[50:53]
	v_mfma_f32_16x16x32_bf16 v[38:41], v[148:151], v[196:199], v[38:41]
	v_mfma_f32_16x16x32_bf16 v[34:37], v[156:159], v[196:199], v[34:37]
	v_mfma_f32_16x16x32_bf16 v[22:25], v[148:151], v[204:207], v[22:25]
	v_mfma_f32_16x16x32_bf16 v[18:21], v[156:159], v[204:207], v[18:21]
	v_mfma_f32_16x16x32_bf16 v[62:65], v[152:155], v[184:187], v[62:65]
	v_mfma_f32_16x16x32_bf16 v[58:61], v[160:163], v[184:187], v[58:61]
	v_mfma_f32_16x16x32_bf16 v[54:57], v[152:155], v[192:195], v[54:57]
	v_mfma_f32_16x16x32_bf16 v[50:53], v[160:163], v[192:195], v[50:53]
	v_mfma_f32_16x16x32_bf16 v[38:41], v[152:155], v[200:203], v[38:41]
	v_mfma_f32_16x16x32_bf16 v[34:37], v[160:163], v[200:203], v[34:37]
	v_mfma_f32_16x16x32_bf16 v[22:25], v[152:155], v[208:211], v[22:25]
	v_mfma_f32_16x16x32_bf16 v[18:21], v[160:163], v[208:211], v[18:21]
	v_mfma_f32_16x16x32_bf16 v[46:49], v[164:167], v[180:183], v[46:49]
	v_mfma_f32_16x16x32_bf16 v[42:45], v[172:175], v[180:183], v[42:45]
	v_mfma_f32_16x16x32_bf16 v[30:33], v[164:167], v[188:191], v[30:33]
	v_mfma_f32_16x16x32_bf16 v[26:29], v[172:175], v[188:191], v[26:29]
	v_mfma_f32_16x16x32_bf16 v[14:17], v[164:167], v[196:199], v[14:17]
	v_mfma_f32_16x16x32_bf16 v[10:13], v[172:175], v[196:199], v[10:13]
	v_mfma_f32_16x16x32_bf16 v[6:9], v[164:167], v[204:207], v[6:9]
	v_mfma_f32_16x16x32_bf16 v[2:5], v[172:175], v[204:207], v[2:5]
	v_mfma_f32_16x16x32_bf16 v[46:49], v[168:171], v[184:187], v[46:49]
	v_mfma_f32_16x16x32_bf16 v[42:45], v[176:179], v[184:187], v[42:45]
	v_mfma_f32_16x16x32_bf16 v[30:33], v[168:171], v[192:195], v[30:33]
	v_mfma_f32_16x16x32_bf16 v[26:29], v[176:179], v[192:195], v[26:29]
	v_mfma_f32_16x16x32_bf16 v[14:17], v[168:171], v[200:203], v[14:17]
	v_mfma_f32_16x16x32_bf16 v[10:13], v[176:179], v[200:203], v[10:13]
	v_mfma_f32_16x16x32_bf16 v[6:9], v[168:171], v[208:211], v[6:9]
	v_mfma_f32_16x16x32_bf16 v[2:5], v[176:179], v[208:211], v[2:5]
	s_barrier
	s_add_i32 s35, s35, 2
	s_add_u32 s18, s18, 0x100
	s_addc_u32 s19, s19, 0
	s_cmp_gt_u32 s35, 29
	s_cbranch_scc0 .LBB0_466
	s_cmpk_lt_u32 s6, 0x100
	s_cbranch_scc0 .LBB0_469
	s_barrier
; __device__ __forceinline__ unsigned cvt_pk_bf16(float lo, float hi) { const f32x2 v = {lo, hi}; return __builtin_bit_cast(unsigned, __builtin_convertvector(v, bf16x2_t)); }
;     __device__ __forceinline__ void operator()(Acc& acc, const GUnit& u, int wr, int wc, int fr, int fq, LAS unsigned char*, int, int) const {
;         const int row0 = u.x0 + wr * 64 + fr, col0 = u.x1 + wc * 32 + 8 * fq;
; #pragma unroll
;         for (int ai = 0; ai < 2; ++ai)
; #pragma unroll
;             for (int m = 0; m < 4; ++m) { bf16_t* rowp = O + (size_t)(row0 + ai * HALF + m * 16) * ldc + col0;
; #pragma unroll
;                 for (int bj = 0; bj < 2; ++bj) { const f32x4 v0 = acc[ai][bj][m][0], v1 = acc[ai][bj][m][1];
;                     u32x4 w; w.x = cvt_pk_bf16(v0[0], v0[1]); w.y = cvt_pk_bf16(v0[2], v0[3]); w.z = cvt_pk_bf16(v1[0], v1[1]); w.w = cvt_pk_bf16(v1[2], v1[3]);
;                     if constexpr (NT) __builtin_nontemporal_store(w, (u32x4*)(rowp + bj * HALF)); else *(u32x4*)(rowp + bj * HALF) = w; } }
.LBB0_469:
	v_lshl_add_u32 v130, s2, 8, v1
	s_add_u32 s0, s8, 0x44850000
	v_lshl_or_b32 v1, s3, 8, v142
	v_ashrrev_i32_e32 v131, 31, v130
	v_cvt_pk_bf16_f32 v110, v110, v111
	v_cvt_pk_bf16_f32 v111, v112, v113
	v_cvt_pk_bf16_f32 v112, v106, v107
	v_or_b32_e32 v106, 16, v130
	v_cvt_pk_bf16_f32 v94, v94, v95
	v_cvt_pk_bf16_f32 v95, v96, v97
	v_cvt_pk_bf16_f32 v96, v90, v91
	v_or_b32_e32 v90, 32, v130
	v_cvt_pk_bf16_f32 v78, v78, v79
	v_cvt_pk_bf16_f32 v79, v80, v81
	v_cvt_pk_bf16_f32 v80, v74, v75
	v_or_b32_e32 v74, 48, v130
	s_addc_u32 s1, s9, 0
	v_or_b32_e32 v1, s29, v1
	v_lshlrev_b64 v[132:133], 12, v[130:131]
	v_ashrrev_i32_e32 v107, 31, v106
	v_ashrrev_i32_e32 v91, 31, v90
	v_ashrrev_i32_e32 v75, 31, v74
	v_lshl_add_u64 v[132:133], s[0:1], 0, v[132:133]
	v_lshlrev_b32_e32 v134, 1, v1
	v_mov_b32_e32 v135, 0
	v_lshlrev_b64 v[106:107], 12, v[106:107]
	v_lshlrev_b64 v[90:91], 12, v[90:91]
	v_lshlrev_b64 v[74:75], 12, v[74:75]
	v_lshl_add_u64 v[132:133], v[132:133], 0, v[134:135]
	v_lshl_add_u64 v[106:107], s[0:1], 0, v[106:107]
	v_lshl_add_u64 v[90:91], s[0:1], 0, v[90:91]
	v_lshl_add_u64 v[74:75], s[0:1], 0, v[74:75]
	s_mov_b64 s[0:1], 0x80000
	v_cvt_pk_bf16_f32 v70, v70, v71
	v_cvt_pk_bf16_f32 v71, v72, v73
	v_cvt_pk_bf16_f32 v72, v66, v67
	v_lshl_add_u64 v[66:67], v[132:133], 0, s[0:1]
	s_mov_b32 s0, 0x80000
	v_cvt_pk_bf16_f32 v62, v62, v63
	v_cvt_pk_bf16_f32 v63, v64, v65
	v_cvt_pk_bf16_f32 v64, v58, v59
	v_add_co_u32_e32 v58, vcc, s0, v132
	v_cvt_pk_bf16_f32 v46, v46, v47
	v_cvt_pk_bf16_f32 v47, v48, v49
	v_cvt_pk_bf16_f32 v48, v42, v43
	v_cvt_pk_bf16_f32 v49, v44, v45
	s_mov_b64 s[0:1], 0x90000
	v_addc_co_u32_e32 v59, vcc, 0, v133, vcc
	global_store_dwordx4 v[66:67], v[46:49], off offset:256
	v_cvt_pk_bf16_f32 v30, v30, v31
	v_cvt_pk_bf16_f32 v31, v32, v33
	v_lshl_add_u64 v[46:47], v[132:133], 0, s[0:1]
	s_mov_b32 s0, 0x90000
	v_add_co_u32_e32 v48, vcc, s0, v132
	v_cvt_pk_bf16_f32 v32, v26, v27
	v_cvt_pk_bf16_f32 v33, v28, v29
	s_mov_b64 s[0:1], 0xa0000
	v_addc_co_u32_e32 v49, vcc, 0, v133, vcc
	global_store_dwordx4 v[46:47], v[30:33], off offset:256
	v_cvt_pk_bf16_f32 v113, v108, v109
	v_cvt_pk_bf16_f32 v14, v14, v15
	v_lshl_add_u64 v[30:31], v[132:133], 0, s[0:1]
	s_mov_b32 s0, 0xa0000
	v_add_co_u32_e32 v32, vcc, s0, v132
	v_cvt_pk_bf16_f32 v15, v16, v17
	v_cvt_pk_bf16_f32 v16, v10, v11
	v_cvt_pk_bf16_f32 v17, v12, v13
	s_mov_b64 s[0:1], 0xb0000
	global_store_dwordx4 v[132:133], v[110:113], off offset:256
	v_cvt_pk_bf16_f32 v97, v92, v93
	v_addc_co_u32_e32 v33, vcc, 0, v133, vcc
	v_lshl_add_u64 v[110:111], v[106:107], 0, v[134:135]
	global_store_dwordx4 v[30:31], v[14:17], off offset:256
	global_store_dwordx4 v[110:111], v[94:97], off offset:256
	v_cvt_pk_bf16_f32 v81, v76, v77
	v_lshl_add_u64 v[14:15], v[132:133], 0, s[0:1]
	s_mov_b32 s0, 0xb0000
	v_lshl_add_u64 v[94:95], v[90:91], 0, v[134:135]
	v_add_co_u32_e32 v16, vcc, s0, v132
	v_cvt_pk_bf16_f32 v126, v126, v127
	v_cvt_pk_bf16_f32 v127, v128, v129
	v_cvt_pk_bf16_f32 v128, v122, v123
	v_cvt_pk_bf16_f32 v129, v124, v125
	v_cvt_pk_bf16_f32 v106, v118, v119
	v_cvt_pk_bf16_f32 v107, v120, v121
	v_cvt_pk_bf16_f32 v108, v114, v115
	v_cvt_pk_bf16_f32 v109, v116, v117
	v_cvt_pk_bf16_f32 v90, v102, v103
	v_cvt_pk_bf16_f32 v91, v104, v105
	v_cvt_pk_bf16_f32 v92, v98, v99
	v_cvt_pk_bf16_f32 v93, v100, v101
	global_store_dwordx4 v[94:95], v[78:81], off offset:256
	v_cvt_pk_bf16_f32 v76, v82, v83
	v_cvt_pk_bf16_f32 v77, v84, v85
	v_lshl_add_u64 v[78:79], v[74:75], 0, v[134:135]
	v_cvt_pk_bf16_f32 v74, v86, v87
	v_cvt_pk_bf16_f32 v75, v88, v89
	v_cvt_pk_bf16_f32 v73, v68, v69
	v_cvt_pk_bf16_f32 v65, v60, v61
	v_cvt_pk_bf16_f32 v42, v54, v55
	v_cvt_pk_bf16_f32 v43, v56, v57
	v_cvt_pk_bf16_f32 v44, v50, v51
	v_cvt_pk_bf16_f32 v45, v52, v53
	v_cvt_pk_bf16_f32 v26, v38, v39
	v_cvt_pk_bf16_f32 v27, v40, v41
	v_cvt_pk_bf16_f32 v28, v34, v35
	v_cvt_pk_bf16_f32 v29, v36, v37
	v_cvt_pk_bf16_f32 v10, v22, v23
	v_cvt_pk_bf16_f32 v11, v24, v25
	v_cvt_pk_bf16_f32 v12, v18, v19
	v_cvt_pk_bf16_f32 v13, v20, v21
	v_addc_co_u32_e32 v17, vcc, 0, v133, vcc
	v_cvt_pk_bf16_f32 v6, v6, v7
	v_cvt_pk_bf16_f32 v7, v8, v9
	v_cvt_pk_bf16_f32 v8, v2, v3
	v_cvt_pk_bf16_f32 v9, v4, v5
	global_store_dwordx4 v[132:133], v[126:129], off
	global_store_dwordx4 v[110:111], v[106:109], off
	global_store_dwordx4 v[94:95], v[90:93], off
	global_store_dwordx4 v[78:79], v[74:77], off
	global_store_dwordx4 v[78:79], v[70:73], off offset:256
	global_store_dwordx4 v[58:59], v[62:65], off
	global_store_dwordx4 v[48:49], v[42:45], off
	global_store_dwordx4 v[32:33], v[26:29], off
	global_store_dwordx4 v[16:17], v[10:13], off
	global_store_dwordx4 v[14:15], v[6:9], off offset:256
	s_waitcnt vmcnt(0)
	s_barrier
	s_setprio 0

; __device__ __forceinline__ int otid() { int t = threadIdx.x; asm volatile("" : "+v"(t)); return t; }
; #define PG8_STAGE_B(b, h, bp) PG8_STAGE2(PG8_SB(b, h), (bp) + (h) * hstepB, voffB[0], voffB[1])
; #define PG8_STAGE_A(b, h, ap, NX) do { if constexpr (GATHER) { const unsigned _o0 = (NX) ? vn[h][0] : vc[h][0], _o1 = (NX) ? vn[h][1] : vc[h][1]; PG8_STAGE2(PG8_SA(b, h), (ap), _o0, _o1); } \
;         else { PG8_STAGE2(PG8_SA(b, h), (ap) + (h) * hstepA, voffA[0], voffA[1]); } } while (0)
; #define PG8_BAR __builtin_amdgcn_s_barrier()
; template <class Epi, class Sched, bool GATHER, bool LIGHTSKIP = false>
; __device__ __forceinline__ void gemm_phase(LAS unsigned char* lds, LAS unsigned char* xl, const int lda, const int ldb, const int K, const Sched& S, const Epi& E) {
;     const int tid = otid(), wid = __builtin_amdgcn_readfirstlane(tid >> 6), lane = tid & 63, wr = wid >> 2, wc = wid & 3, fr = lane & 15, fq = lane >> 4;
;     const int nt = K / BK;
;     int Rr[2], Cc[2]; unsigned voffA[2], voffB[2];
; #pragma unroll
;     for (int i = 0; i < 2; ++i) { stage_rc(tid * 16 + i * 8192, Rr[i], Cc[i]); const int Rb = Epi::PERM ? ((Rr[i] & ~31) + perm32(Rr[i] & 31)) : Rr[i];
;         voffA[i] = (unsigned)(Rr[i] * lda + Cc[i]) * 2u; voffB[i] = (unsigned)(Rb * ldb + Cc[i]) * 2u; }
;     unsigned vc[2][2], vn[2][2];
;     const size_t kstep = (size_t)(BK * 2);
;     const size_t hstepA = (size_t)HALF * lda * 2, hstepB = (size_t)HALF * ldb * 2;
;     const unsigned ldsw = (unsigned)wid * 1024u;
;     const int aoff = lds_byte(wr * 64 + fr, fq * 8), boff = lds_byte(wc * 32 + fr, fq * 8);
;     ...
;     GUnit cur, nxt; int ui = 0;
;     if (!S.next(0, cur)) return;
;     Acc acc;
; #pragma unroll
;     for (int a = 0; a < 2; ++a)
; #pragma unroll
;         for (int b = 0; b < 2; ++b)
; #pragma unroll
;             for (int m = 0; m < 4; ++m)
; #pragma unroll
;                 for (int n = 0; n < 2; ++n) acc[a][b][m][n] = (f32x4){0.f, 0.f, 0.f, 0.f};
;     bf16x8 At[4][2], B0[2][2], B1[2][2];
;     const char* cA = cur.A; const char* cB = cur.B;
;     if constexpr (GATHER) { S.offsets(cur, lda, vc);
; #pragma unroll
;         for (int h = 0; h < 2; ++h) { vn[h][0] = vc[h][0]; vn[h][1] = vc[h][1]; } }
;     PG8_STAGE_B(0, 0, cB); PG8_STAGE_B(0, 1, cB); PG8_STAGE_A(0, 0, cA, false); PG8_STAGE_A(0, 1, cA, false);
;     if (wr == 1) PG8_BAR;
;     PG8_WAIT_V(2); PG8_BAR;
.LBB0_818:
	v_ashrrev_i32_e32 v2, 31, v10
	v_lshrrev_b32_e32 v2, 26, v2
	v_add_u32_e32 v2, v10, v2
	v_ashrrev_i32_e32 v11, 6, v2
	v_bfe_i32 v2, v10, 27, 1
	v_lshlrev_b32_e32 v1, 4, v10
	v_lshrrev_b32_e32 v2, 22, v2
	v_add_u32_e32 v2, v1, v2
	v_and_b32_e32 v2, 0xfffffc00, v2
	v_sub_u32_e32 v2, v1, v2
	v_lshrrev_b32_e32 v3, 4, v2
	v_bitop3_b32 v3, v3, v2, 32 bitop3:0x6c
	v_ashrrev_i32_e32 v2, 31, v2
	v_lshrrev_b32_e32 v2, 26, v2
	v_add_u32_e32 v2, v3, v2
	v_ashrrev_i32_e32 v12, 6, v2
	v_lshlrev_b32_e32 v4, 3, v11
	v_mul_i32_i24_e32 v5, 64, v12
	v_and_b32_e32 v4, -16, v4
	v_sub_u32_e32 v3, v3, v5
	v_mov_b32_e32 v5, 1
	v_add_u32_e32 v2, v12, v4
	v_lshlrev_b32_e32 v4, 5, v11
	v_ashrrev_i16_sdwa v3, v5, sext(v3) dst_sel:DWORD dst_unused:UNUSED_PAD src0_sel:DWORD src1_sel:BYTE_0
	v_and_b32_e32 v4, 32, v4
	v_bfe_i32 v13, v3, 0, 16
	v_and_b32_e32 v7, 3, v12
	s_mov_b32 s5, 0xfffe0
	v_add_lshl_u32 v4, v4, v13, 1
	v_add_u32_e32 v1, 0x2000, v1
	v_lshlrev_b32_e32 v3, 1, v2
	v_lshrrev_b32_e32 v6, 2, v2
	v_and_or_b32 v7, v2, s5, v7
	v_lshl_add_u32 v130, v2, 12, v4
	v_ashrrev_i32_e32 v2, 31, v1
	v_lshrrev_b32_e32 v2, 22, v2
	v_add_u32_e32 v2, v1, v2
	v_ashrrev_i32_e32 v14, 10, v2
	v_mul_i32_i24_e32 v2, 0x400, v14
	v_sub_u32_e32 v1, v1, v2
	v_and_b32_e32 v3, 24, v3
	v_and_b32_e32 v6, 4, v6
	v_lshrrev_b32_e32 v2, 4, v1
	v_or3_b32 v3, v7, v6, v3
	v_bitop3_b32 v1, v2, v1, 32 bitop3:0x6c
	v_lshl_add_u32 v132, v3, 12, v4
	v_ashrrev_i32_e32 v3, 31, v1
	v_lshrrev_b32_e32 v3, 26, v3
	v_add_u32_e32 v3, v1, v3
	v_lshlrev_b32_e32 v2, 3, v14
	v_ashrrev_i32_e32 v15, 6, v3
	v_and_b32_e32 v3, 0xc0, v3
	v_and_b32_e32 v2, -16, v2
	v_sub_u32_e32 v1, v1, v3
	s_ashr_i32 s12, s28, 6
	v_add_u32_e32 v2, v15, v2
	v_ashrrev_i16_sdwa v1, v5, sext(v1) dst_sel:DWORD dst_unused:UNUSED_PAD src0_sel:DWORD src1_sel:BYTE_0
	v_and_b32_e32 v5, 3, v15
	v_and_or_b32 v5, v2, s5, v5
	s_lshl_b32 s5, s12, 10
	v_lshlrev_b32_e32 v4, 5, v14
	v_bfe_i32 v16, v1, 0, 16
	v_lshlrev_b32_e32 v1, 1, v2
	v_lshrrev_b32_e32 v3, 2, v2
	s_add_i32 s6, s5, 0
	v_and_b32_e32 v4, 32, v4
	v_and_b32_e32 v1, 24, v1
	v_and_b32_e32 v3, 4, v3
	s_add_i32 m0, s6, 0x10000
	v_or3_b32 v1, v5, v3, v1
	v_add_lshl_u32 v3, v4, v16, 1
	s_ashr_i32 s13, s28, 8
	global_load_lds_dwordx4 v132, s[42:43]
	s_add_i32 m0, s6, 0x12000
	v_lshl_add_u32 v136, v1, 12, v3
	s_add_u32 s14, s42, 0x80000
	global_load_lds_dwordx4 v136, s[42:43]
	s_addc_u32 s15, s43, 0
	s_add_i32 m0, s6, 0x14000
	s_add_i32 s7, s6, 0x2000
	global_load_lds_dwordx4 v132, s[14:15]
	s_add_i32 m0, s6, 0x16000
	v_lshl_add_u32 v134, v2, 12, v3
	global_load_lds_dwordx4 v136, s[14:15]
	s_mov_b32 m0, s6
	s_add_u32 s14, s40, 0x80000
	global_load_lds_dwordx4 v130, s[40:41]
	s_mov_b32 m0, s7
	s_addc_u32 s15, s41, 0
	s_add_i32 s26, s6, 0x4000
	global_load_lds_dwordx4 v134, s[40:41]
	s_mov_b32 m0, s26
	s_add_i32 s27, s6, 0x6000
	global_load_lds_dwordx4 v130, s[14:15]
	s_mov_b32 m0, s27
	v_mov_b32_e32 v133, 0
	global_load_lds_dwordx4 v134, s[14:15]
	v_mov_b32_e32 v137, v133
	v_mov_b32_e32 v131, v133
	v_mov_b32_e32 v135, v133
	s_cmp_eq_u32 s13, 1
	v_lshl_add_u64 v[8:9], s[42:43], 0, v[132:133]
	s_mov_b32 s31, 0
	v_lshl_add_u64 v[6:7], s[42:43], 0, v[136:137]
	v_lshl_add_u64 v[2:3], s[40:41], 0, v[130:131]
	s_cselect_b64 s[14:15], -1, 0
	s_cmp_lg_u32 s13, 1
	v_lshl_add_u64 v[4:5], s[40:41], 0, v[134:135]
	s_cbranch_scc1 .LBB0_820
	s_barrier
	s_setprio 1

; #define PG8_STAGE_B(b, h, bp) PG8_STAGE2(PG8_SB(b, h), (bp) + (h) * hstepB, voffB[0], voffB[1])
; #define PG8_STAGE_A(b, h, ap, NX) do { if constexpr (GATHER) { const unsigned _o0 = (NX) ? vn[h][0] : vc[h][0], _o1 = (NX) ? vn[h][1] : vc[h][1]; PG8_STAGE2(PG8_SA(b, h), (ap), _o0, _o1); } \
;         else { PG8_STAGE2(PG8_SA(b, h), (ap) + (h) * hstepA, voffA[0], voffA[1]); } } while (0)
; #define PG8_LDA(dst, b, h) do { _Pragma("unroll") for (int m = 0; m < 4; ++m) _Pragma("unroll") for (int k = 0; k < 2; ++k) dst[m][k] = *(const LAS bf16x8*)(lds + PG8_SA(b, h) + aoff + m * 2048 + k * 1024); } while (0)
; #define PG8_LDB(dst, b, h) do { _Pragma("unroll") for (int n = 0; n < 2; ++n) _Pragma("unroll") for (int k = 0; k < 2; ++k) dst[n][k] = *(const LAS bf16x8*)(lds + PG8_SB(b, h) + boff + n * 2048 + k * 1024); } while (0)
; #define PG8_MMA(ai, bj, At, Bt) do { __builtin_amdgcn_s_setprio(1); _Pragma("unroll") for (int m = 0; m < 4; ++m) _Pragma("unroll") for (int n = 0; n < 2; ++n) _Pragma("unroll") for (int k = 0; k < 2; ++k) \
;         acc[ai][bj][m][n] = __builtin_amdgcn_mfma_f32_16x16x32_bf16(Bt[n][k], At[m][k], acc[ai][bj][m][n], 0, 0, 0); __builtin_amdgcn_s_setprio(0); } while (0)
; #define PG8_WAIT_V(n) asm volatile("s_waitcnt vmcnt(" #n ")" ::: "memory")
; #define PG8_WAIT_L(n) asm volatile("s_waitcnt lgkmcnt(" #n ")" ::: "memory")
; #define PG8_BAR __builtin_amdgcn_s_barrier()
; #define PG8_SCHED __builtin_amdgcn_sched_barrier(0)
; template <class Epi, class Sched, bool GATHER, bool LIGHTSKIP = false>
; __device__ __forceinline__ void gemm_phase(LAS unsigned char* lds, LAS unsigned char* xl, const int lda, const int ldb, const int K, const Sched& S, const Epi& E) {
;     ...
;             PG8_LDB(B0, 0, 0); PG8_LDB(B1, 0, 1); PG8_SCHED; PG8_LDA(At, 0, 0); PG8_STAGE_A(1, 1, a1, false);
;             PG8_WAIT_V(8); PG8_WAIT_L(0); PG8_BAR; PG8_MMA(0, 0, At, B0); PG8_MMA(0, 1, At, B1); PG8_BAR; PG8_SCHED;
;             PG8_LDA(At, 0, 1); PG8_STAGE_B(0, 0, b2); PG8_STAGE_B(0, 1, b2); PG8_STAGE_A(0, 0, a2, last);
.LBB0_830:
	ds_read_b128 v[146:149], v152
	ds_read_b128 v[156:159], v152 offset:1024
	ds_read_b128 v[160:163], v152 offset:2048
	ds_read_b128 v[164:167], v152 offset:3072
	ds_read_b128 v[168:171], v153
	ds_read_b128 v[172:175], v153 offset:1024
	ds_read_b128 v[176:179], v153 offset:2048
	ds_read_b128 v[180:183], v153 offset:3072
	s_add_u32 s42, s40, 0xfff80080
	s_addc_u32 s43, s41, -1
	s_cmp_eq_u32 s57, 28
	s_cselect_b32 s45, s37, s43
	s_cselect_b32 s44, s36, s42
	s_cselect_b32 s43, s39, s56
	s_cselect_b32 s42, s38, s55
	v_lshl_add_u64 v[216:217], s[40:41], 0, v[138:139]
	s_add_i32 m0, s6, 0xc000
	ds_read_b128 v[184:187], v154
	ds_read_b128 v[188:191], v154 offset:1024
	ds_read_b128 v[192:195], v154 offset:2048
	ds_read_b128 v[196:199], v154 offset:3072
	ds_read_b128 v[200:203], v154 offset:4096
	ds_read_b128 v[204:207], v154 offset:5120
	ds_read_b128 v[208:211], v154 offset:6144
	ds_read_b128 v[212:215], v154 offset:7168
	global_load_lds_dwordx4 v[216:217], off
	v_lshl_add_u64 v[216:217], s[40:41], 0, v[140:141]
	s_add_i32 m0, s6, 0xe000
	s_nop 0
	global_load_lds_dwordx4 v[216:217], off
	s_waitcnt vmcnt(8)
	s_waitcnt lgkmcnt(0)
	s_barrier
	s_waitcnt lgkmcnt(0)
	v_mfma_f32_16x16x32_bf16 v[126:129], v[146:149], v[184:187], v[126:129]
	v_mfma_f32_16x16x32_bf16 v[122:125], v[160:163], v[184:187], v[122:125]
	v_mfma_f32_16x16x32_bf16 v[110:113], v[146:149], v[192:195], v[110:113]
	v_mfma_f32_16x16x32_bf16 v[106:109], v[160:163], v[192:195], v[106:109]
	v_mfma_f32_16x16x32_bf16 v[94:97], v[146:149], v[200:203], v[94:97]
	v_mfma_f32_16x16x32_bf16 v[90:93], v[160:163], v[200:203], v[90:93]
	v_mfma_f32_16x16x32_bf16 v[78:81], v[146:149], v[208:211], v[78:81]
	v_mfma_f32_16x16x32_bf16 v[74:77], v[160:163], v[208:211], v[74:77]
	v_mfma_f32_16x16x32_bf16 v[126:129], v[156:159], v[188:191], v[126:129]
	v_mfma_f32_16x16x32_bf16 v[122:125], v[164:167], v[188:191], v[122:125]
	v_mfma_f32_16x16x32_bf16 v[110:113], v[156:159], v[196:199], v[110:113]
	v_mfma_f32_16x16x32_bf16 v[106:109], v[164:167], v[196:199], v[106:109]
	v_mfma_f32_16x16x32_bf16 v[94:97], v[156:159], v[204:207], v[94:97]
	v_mfma_f32_16x16x32_bf16 v[90:93], v[164:167], v[204:207], v[90:93]
	v_mfma_f32_16x16x32_bf16 v[78:81], v[156:159], v[212:215], v[78:81]
	v_mfma_f32_16x16x32_bf16 v[74:77], v[164:167], v[212:215], v[74:77]
	v_mfma_f32_16x16x32_bf16 v[118:121], v[168:171], v[184:187], v[118:121]
	v_mfma_f32_16x16x32_bf16 v[114:117], v[176:179], v[184:187], v[114:117]
	v_mfma_f32_16x16x32_bf16 v[102:105], v[168:171], v[192:195], v[102:105]
	v_mfma_f32_16x16x32_bf16 v[98:101], v[176:179], v[192:195], v[98:101]
	v_mfma_f32_16x16x32_bf16 v[86:89], v[168:171], v[200:203], v[86:89]
	v_mfma_f32_16x16x32_bf16 v[82:85], v[176:179], v[200:203], v[82:85]
	v_mfma_f32_16x16x32_bf16 v[70:73], v[168:171], v[208:211], v[70:73]
	v_mfma_f32_16x16x32_bf16 v[66:69], v[176:179], v[208:211], v[66:69]
	v_mfma_f32_16x16x32_bf16 v[118:121], v[172:175], v[188:191], v[118:121]
	v_mfma_f32_16x16x32_bf16 v[114:117], v[180:183], v[188:191], v[114:117]
	v_mfma_f32_16x16x32_bf16 v[102:105], v[172:175], v[196:199], v[102:105]
	v_mfma_f32_16x16x32_bf16 v[98:101], v[180:183], v[196:199], v[98:101]
	v_mfma_f32_16x16x32_bf16 v[86:89], v[172:175], v[204:207], v[86:89]
	v_mfma_f32_16x16x32_bf16 v[82:85], v[180:183], v[204:207], v[82:85]
	v_mfma_f32_16x16x32_bf16 v[70:73], v[172:175], v[212:215], v[70:73]
	v_mfma_f32_16x16x32_bf16 v[66:69], v[180:183], v[212:215], v[66:69]
	s_barrier
	s_add_i32 s58, s50, s5
	v_lshl_add_u64 v[216:217], s[42:43], 0, v[132:133]
	s_mov_b32 m0, s58
	ds_read_b128 v[184:187], v154 offset:16384
	ds_read_b128 v[188:191], v154 offset:17408
	ds_read_b128 v[192:195], v154 offset:18432
	ds_read_b128 v[196:199], v154 offset:19456
	ds_read_b128 v[200:203], v154 offset:20480
	ds_read_b128 v[204:207], v154 offset:21504
	ds_read_b128 v[208:211], v154 offset:22528
	ds_read_b128 v[212:215], v154 offset:23552
	global_load_lds_dwordx4 v[216:217], off
	s_add_i32 m0, s58, 0x2000
	s_add_u32 s58, s42, 0x80000
	v_lshl_add_u64 v[218:219], s[42:43], 0, v[136:137]
	s_addc_u32 s59, s43, 0
	s_add_i32 s60, s51, s5
	global_load_lds_dwordx4 v[218:219], off
	v_lshl_add_u64 v[220:221], s[58:59], 0, v[132:133]
	s_mov_b32 m0, s60
	v_lshl_add_u64 v[222:223], s[44:45], 0, v[134:135]
	global_load_lds_dwordx4 v[220:221], off
	v_lshl_add_u64 v[220:221], s[58:59], 0, v[136:137]
	s_add_i32 m0, s60, 0x2000
	s_nop 0
	global_load_lds_dwordx4 v[220:221], off
	v_lshl_add_u64 v[220:221], s[44:45], 0, v[130:131]
	s_mov_b32 m0, s6
	s_nop 0
	global_load_lds_dwordx4 v[220:221], off
	s_mov_b32 m0, s7
	s_nop 0
	global_load_lds_dwordx4 v[222:223], off
	s_waitcnt vmcnt(8)
	s_waitcnt lgkmcnt(0)
	s_barrier
; #define PG8_STAGE_A(b, h, ap, NX) do { if constexpr (GATHER) { const unsigned _o0 = (NX) ? vn[h][0] : vc[h][0], _o1 = (NX) ? vn[h][1] : vc[h][1]; PG8_STAGE2(PG8_SA(b, h), (ap), _o0, _o1); } \
;         else { PG8_STAGE2(PG8_SA(b, h), (ap) + (h) * hstepA, voffA[0], voffA[1]); } } while (0)
; #define PG8_LDA(dst, b, h) do { _Pragma("unroll") for (int m = 0; m < 4; ++m) _Pragma("unroll") for (int k = 0; k < 2; ++k) dst[m][k] = *(const LAS bf16x8*)(lds + PG8_SA(b, h) + aoff + m * 2048 + k * 1024); } while (0)
; #define PG8_LDB(dst, b, h) do { _Pragma("unroll") for (int n = 0; n < 2; ++n) _Pragma("unroll") for (int k = 0; k < 2; ++k) dst[n][k] = *(const LAS bf16x8*)(lds + PG8_SB(b, h) + boff + n * 2048 + k * 1024); } while (0)
; #define PG8_MMA(ai, bj, At, Bt) do { __builtin_amdgcn_s_setprio(1); _Pragma("unroll") for (int m = 0; m < 4; ++m) _Pragma("unroll") for (int n = 0; n < 2; ++n) _Pragma("unroll") for (int k = 0; k < 2; ++k) \
;         acc[ai][bj][m][n] = __builtin_amdgcn_mfma_f32_16x16x32_bf16(Bt[n][k], At[m][k], acc[ai][bj][m][n], 0, 0, 0); __builtin_amdgcn_s_setprio(0); } while (0)
; #define PG8_WAIT_V(n) asm volatile("s_waitcnt vmcnt(" #n ")" ::: "memory")
; #define PG8_WAIT_L(n) asm volatile("s_waitcnt lgkmcnt(" #n ")" ::: "memory")
; #define PG8_BAR __builtin_amdgcn_s_barrier()
; #define PG8_SCHED __builtin_amdgcn_sched_barrier(0)
; template <class Epi, class Sched, bool GATHER, bool LIGHTSKIP = false>
; __device__ __forceinline__ void gemm_phase(LAS unsigned char* lds, LAS unsigned char* xl, const int lda, const int ldb, const int K, const Sched& S, const Epi& E) {
;     ...
;             PG8_WAIT_V(8); PG8_WAIT_L(0); PG8_BAR; if (!light) { PG8_MMA(1, 0, At, B0); PG8_MMA(1, 1, At, B1); } PG8_BAR; PG8_SCHED;
;             PG8_LDB(B0, 1, 0); PG8_LDB(B1, 1, 1); PG8_SCHED; PG8_LDA(At, 1, 0); PG8_STAGE_A(0, 1, a2, last);
;             PG8_WAIT_V(8); PG8_WAIT_L(0); PG8_BAR; PG8_MMA(0, 0, At, B0); PG8_MMA(0, 1, At, B1); PG8_BAR; PG8_SCHED;
	s_waitcnt lgkmcnt(0)
	v_mfma_f32_16x16x32_bf16 v[62:65], v[146:149], v[184:187], v[62:65]
	v_mfma_f32_16x16x32_bf16 v[58:61], v[160:163], v[184:187], v[58:61]
	v_mfma_f32_16x16x32_bf16 v[46:49], v[146:149], v[192:195], v[46:49]
	v_mfma_f32_16x16x32_bf16 v[42:45], v[160:163], v[192:195], v[42:45]
	v_mfma_f32_16x16x32_bf16 v[30:33], v[146:149], v[200:203], v[30:33]
	v_mfma_f32_16x16x32_bf16 v[26:29], v[160:163], v[200:203], v[26:29]
	v_mfma_f32_16x16x32_bf16 v[14:17], v[146:149], v[208:211], v[14:17]
	v_mfma_f32_16x16x32_bf16 v[10:13], v[160:163], v[208:211], v[10:13]
	v_mfma_f32_16x16x32_bf16 v[62:65], v[156:159], v[188:191], v[62:65]
	v_mfma_f32_16x16x32_bf16 v[58:61], v[164:167], v[188:191], v[58:61]
	v_mfma_f32_16x16x32_bf16 v[46:49], v[156:159], v[196:199], v[46:49]
	v_mfma_f32_16x16x32_bf16 v[42:45], v[164:167], v[196:199], v[42:45]
	v_mfma_f32_16x16x32_bf16 v[30:33], v[156:159], v[204:207], v[30:33]
	v_mfma_f32_16x16x32_bf16 v[26:29], v[164:167], v[204:207], v[26:29]
	v_mfma_f32_16x16x32_bf16 v[14:17], v[156:159], v[212:215], v[14:17]
	v_mfma_f32_16x16x32_bf16 v[10:13], v[164:167], v[212:215], v[10:13]
	v_mfma_f32_16x16x32_bf16 v[54:57], v[168:171], v[184:187], v[54:57]
	v_mfma_f32_16x16x32_bf16 v[50:53], v[176:179], v[184:187], v[50:53]
	v_mfma_f32_16x16x32_bf16 v[38:41], v[168:171], v[192:195], v[38:41]
	v_mfma_f32_16x16x32_bf16 v[34:37], v[176:179], v[192:195], v[34:37]
	v_mfma_f32_16x16x32_bf16 v[22:25], v[168:171], v[200:203], v[22:25]
	v_mfma_f32_16x16x32_bf16 v[18:21], v[176:179], v[200:203], v[18:21]
	v_mfma_f32_16x16x32_bf16 v[6:9], v[168:171], v[208:211], v[6:9]
	v_mfma_f32_16x16x32_bf16 v[2:5], v[176:179], v[208:211], v[2:5]
	v_mfma_f32_16x16x32_bf16 v[54:57], v[172:175], v[188:191], v[54:57]
	v_mfma_f32_16x16x32_bf16 v[50:53], v[180:183], v[188:191], v[50:53]
	v_mfma_f32_16x16x32_bf16 v[38:41], v[172:175], v[196:199], v[38:41]
	v_mfma_f32_16x16x32_bf16 v[34:37], v[180:183], v[196:199], v[34:37]
	v_mfma_f32_16x16x32_bf16 v[22:25], v[172:175], v[204:207], v[22:25]
	v_mfma_f32_16x16x32_bf16 v[18:21], v[180:183], v[204:207], v[18:21]
	v_mfma_f32_16x16x32_bf16 v[6:9], v[172:175], v[212:215], v[6:9]
	v_mfma_f32_16x16x32_bf16 v[2:5], v[180:183], v[212:215], v[2:5]
	s_barrier
	s_add_i32 s58, 0, 0x18000
	v_add_u32_e32 v155, s58, v150
	s_add_i32 s59, 0, 0x1c000
	ds_read_b128 v[146:149], v155
	ds_read_b128 v[156:159], v155 offset:1024
	ds_read_b128 v[160:163], v155 offset:2048
	ds_read_b128 v[164:167], v155 offset:3072
	v_add_u32_e32 v155, s59, v150
	ds_read_b128 v[168:171], v155
	ds_read_b128 v[172:175], v155 offset:1024
	ds_read_b128 v[176:179], v155 offset:2048
	ds_read_b128 v[180:183], v155 offset:3072
	s_add_u32 s44, s44, 0x80000
	s_addc_u32 s45, s45, 0
	s_mov_b32 m0, s26
	v_lshl_add_u64 v[224:225], s[44:45], 0, v[130:131]
	ds_read_b128 v[184:187], v154 offset:32768
	ds_read_b128 v[188:191], v154 offset:33792
	ds_read_b128 v[192:195], v154 offset:34816
	ds_read_b128 v[196:199], v154 offset:35840
	ds_read_b128 v[200:203], v154 offset:36864
	ds_read_b128 v[204:207], v154 offset:37888
	ds_read_b128 v[208:211], v154 offset:38912
	ds_read_b128 v[212:215], v154 offset:39936
	global_load_lds_dwordx4 v[224:225], off
	v_lshl_add_u64 v[224:225], s[44:45], 0, v[134:135]
	s_mov_b32 m0, s27
	s_nop 0
	global_load_lds_dwordx4 v[224:225], off
	s_waitcnt vmcnt(8)
	s_waitcnt lgkmcnt(0)
	s_barrier
	s_waitcnt lgkmcnt(0)
	v_mfma_f32_16x16x32_bf16 v[126:129], v[146:149], v[184:187], v[126:129]
	v_mfma_f32_16x16x32_bf16 v[122:125], v[160:163], v[184:187], v[122:125]
	v_mfma_f32_16x16x32_bf16 v[110:113], v[146:149], v[192:195], v[110:113]
	v_mfma_f32_16x16x32_bf16 v[106:109], v[160:163], v[192:195], v[106:109]
	v_mfma_f32_16x16x32_bf16 v[94:97], v[146:149], v[200:203], v[94:97]
	v_mfma_f32_16x16x32_bf16 v[90:93], v[160:163], v[200:203], v[90:93]
	v_mfma_f32_16x16x32_bf16 v[78:81], v[146:149], v[208:211], v[78:81]
	v_mfma_f32_16x16x32_bf16 v[74:77], v[160:163], v[208:211], v[74:77]
	v_mfma_f32_16x16x32_bf16 v[126:129], v[156:159], v[188:191], v[126:129]
	v_mfma_f32_16x16x32_bf16 v[122:125], v[164:167], v[188:191], v[122:125]
	v_mfma_f32_16x16x32_bf16 v[110:113], v[156:159], v[196:199], v[110:113]
	v_mfma_f32_16x16x32_bf16 v[106:109], v[164:167], v[196:199], v[106:109]
	v_mfma_f32_16x16x32_bf16 v[94:97], v[156:159], v[204:207], v[94:97]
	v_mfma_f32_16x16x32_bf16 v[90:93], v[164:167], v[204:207], v[90:93]
	v_mfma_f32_16x16x32_bf16 v[78:81], v[156:159], v[212:215], v[78:81]
	v_mfma_f32_16x16x32_bf16 v[74:77], v[164:167], v[212:215], v[74:77]
	v_mfma_f32_16x16x32_bf16 v[118:121], v[168:171], v[184:187], v[118:121]
	v_mfma_f32_16x16x32_bf16 v[114:117], v[176:179], v[184:187], v[114:117]
	v_mfma_f32_16x16x32_bf16 v[102:105], v[168:171], v[192:195], v[102:105]
	v_mfma_f32_16x16x32_bf16 v[98:101], v[176:179], v[192:195], v[98:101]
	v_mfma_f32_16x16x32_bf16 v[86:89], v[168:171], v[200:203], v[86:89]
	v_mfma_f32_16x16x32_bf16 v[82:85], v[176:179], v[200:203], v[82:85]
	v_mfma_f32_16x16x32_bf16 v[70:73], v[168:171], v[208:211], v[70:73]
	v_mfma_f32_16x16x32_bf16 v[66:69], v[176:179], v[208:211], v[66:69]
	v_mfma_f32_16x16x32_bf16 v[118:121], v[172:175], v[188:191], v[118:121]
	v_mfma_f32_16x16x32_bf16 v[114:117], v[180:183], v[188:191], v[114:117]
	v_mfma_f32_16x16x32_bf16 v[102:105], v[172:175], v[196:199], v[102:105]
	v_mfma_f32_16x16x32_bf16 v[98:101], v[180:183], v[196:199], v[98:101]
	v_mfma_f32_16x16x32_bf16 v[86:89], v[172:175], v[204:207], v[86:89]
	v_mfma_f32_16x16x32_bf16 v[82:85], v[180:183], v[204:207], v[82:85]
	v_mfma_f32_16x16x32_bf16 v[70:73], v[172:175], v[212:215], v[70:73]
	v_mfma_f32_16x16x32_bf16 v[66:69], v[180:183], v[212:215], v[66:69]
	s_barrier
; #define PG8_STAGE_B(b, h, bp) PG8_STAGE2(PG8_SB(b, h), (bp) + (h) * hstepB, voffB[0], voffB[1])
; #define PG8_STAGE_A(b, h, ap, NX) do { if constexpr (GATHER) { const unsigned _o0 = (NX) ? vn[h][0] : vc[h][0], _o1 = (NX) ? vn[h][1] : vc[h][1]; PG8_STAGE2(PG8_SA(b, h), (ap), _o0, _o1); } \
;         else { PG8_STAGE2(PG8_SA(b, h), (ap) + (h) * hstepA, voffA[0], voffA[1]); } } while (0)
; #define PG8_LDA(dst, b, h) do { _Pragma("unroll") for (int m = 0; m < 4; ++m) _Pragma("unroll") for (int k = 0; k < 2; ++k) dst[m][k] = *(const LAS bf16x8*)(lds + PG8_SA(b, h) + aoff + m * 2048 + k * 1024); } while (0)
; #define PG8_MMA(ai, bj, At, Bt) do { __builtin_amdgcn_s_setprio(1); _Pragma("unroll") for (int m = 0; m < 4; ++m) _Pragma("unroll") for (int n = 0; n < 2; ++n) _Pragma("unroll") for (int k = 0; k < 2; ++k) \
;         acc[ai][bj][m][n] = __builtin_amdgcn_mfma_f32_16x16x32_bf16(Bt[n][k], At[m][k], acc[ai][bj][m][n], 0, 0, 0); __builtin_amdgcn_s_setprio(0); } while (0)
; #define PG8_WAIT_V(n) asm volatile("s_waitcnt vmcnt(" #n ")" ::: "memory")
; #define PG8_WAIT_L(n) asm volatile("s_waitcnt lgkmcnt(" #n ")" ::: "memory")
; #define PG8_BAR __builtin_amdgcn_s_barrier()
; #define PG8_SCHED __builtin_amdgcn_sched_barrier(0)
; template <class Epi, class Sched, bool GATHER, bool LIGHTSKIP = false>
; __device__ __forceinline__ void gemm_phase(LAS unsigned char* lds, LAS unsigned char* xl, const int lda, const int ldb, const int K, const Sched& S, const Epi& E) {
;     ...
;             PG8_LDA(At, 1, 1); PG8_STAGE_B(1, 0, b3); PG8_STAGE_B(1, 1, b3); PG8_STAGE_A(1, 0, a3, last);
;             PG8_WAIT_V(8); PG8_WAIT_L(0); PG8_BAR; if (!light) { PG8_MMA(1, 0, At, B0); PG8_MMA(1, 1, At, B1); } PG8_BAR; PG8_SCHED;
;         }
;         if (wr == 0) PG8_BAR;
	s_add_i32 s44, s58, s5
	v_lshl_add_u64 v[216:217], v[216:217], 0, s[22:23]
	s_mov_b32 m0, s44
	ds_read_b128 v[184:187], v154 offset:49152
	ds_read_b128 v[188:191], v154 offset:50176
	ds_read_b128 v[192:195], v154 offset:51200
	ds_read_b128 v[196:199], v154 offset:52224
	ds_read_b128 v[200:203], v154 offset:53248
	ds_read_b128 v[204:207], v154 offset:54272
	ds_read_b128 v[208:211], v154 offset:55296
	ds_read_b128 v[212:215], v154 offset:56320
	global_load_lds_dwordx4 v[216:217], off
	s_add_i32 m0, s44, 0x2000
	s_add_u32 s42, s42, 0x80080
	v_lshl_add_u64 v[216:217], v[218:219], 0, s[22:23]
	s_addc_u32 s43, s43, 0
	s_add_i32 s44, s59, s5
	global_load_lds_dwordx4 v[216:217], off
	v_lshl_add_u64 v[216:217], s[42:43], 0, v[132:133]
	s_mov_b32 m0, s44
	s_nop 0
	global_load_lds_dwordx4 v[216:217], off
	v_lshl_add_u64 v[216:217], s[42:43], 0, v[136:137]
	s_add_i32 m0, s44, 0x2000
	s_nop 0
	global_load_lds_dwordx4 v[216:217], off
	v_lshl_add_u64 v[216:217], v[220:221], 0, s[22:23]
	s_mov_b32 m0, s46
	s_nop 0
	global_load_lds_dwordx4 v[216:217], off
	v_lshl_add_u64 v[216:217], v[222:223], 0, s[22:23]
	s_mov_b32 m0, s47
	s_nop 0
	global_load_lds_dwordx4 v[216:217], off
	s_waitcnt vmcnt(8)
	s_waitcnt lgkmcnt(0)
	s_barrier
	s_waitcnt lgkmcnt(0)
	v_mfma_f32_16x16x32_bf16 v[62:65], v[146:149], v[184:187], v[62:65]
	v_mfma_f32_16x16x32_bf16 v[58:61], v[160:163], v[184:187], v[58:61]
	v_mfma_f32_16x16x32_bf16 v[46:49], v[146:149], v[192:195], v[46:49]
	v_mfma_f32_16x16x32_bf16 v[42:45], v[160:163], v[192:195], v[42:45]
	v_mfma_f32_16x16x32_bf16 v[30:33], v[146:149], v[200:203], v[30:33]
	v_mfma_f32_16x16x32_bf16 v[26:29], v[160:163], v[200:203], v[26:29]
	v_mfma_f32_16x16x32_bf16 v[14:17], v[146:149], v[208:211], v[14:17]
	v_mfma_f32_16x16x32_bf16 v[10:13], v[160:163], v[208:211], v[10:13]
	v_mfma_f32_16x16x32_bf16 v[62:65], v[156:159], v[188:191], v[62:65]
	v_mfma_f32_16x16x32_bf16 v[58:61], v[164:167], v[188:191], v[58:61]
	v_mfma_f32_16x16x32_bf16 v[46:49], v[156:159], v[196:199], v[46:49]
	v_mfma_f32_16x16x32_bf16 v[42:45], v[164:167], v[196:199], v[42:45]
	v_mfma_f32_16x16x32_bf16 v[30:33], v[156:159], v[204:207], v[30:33]
	v_mfma_f32_16x16x32_bf16 v[26:29], v[164:167], v[204:207], v[26:29]
	v_mfma_f32_16x16x32_bf16 v[14:17], v[156:159], v[212:215], v[14:17]
	v_mfma_f32_16x16x32_bf16 v[10:13], v[164:167], v[212:215], v[10:13]
	v_mfma_f32_16x16x32_bf16 v[54:57], v[168:171], v[184:187], v[54:57]
	v_mfma_f32_16x16x32_bf16 v[50:53], v[176:179], v[184:187], v[50:53]
	v_mfma_f32_16x16x32_bf16 v[38:41], v[168:171], v[192:195], v[38:41]
	v_mfma_f32_16x16x32_bf16 v[34:37], v[176:179], v[192:195], v[34:37]
	v_mfma_f32_16x16x32_bf16 v[22:25], v[168:171], v[200:203], v[22:25]
	v_mfma_f32_16x16x32_bf16 v[18:21], v[176:179], v[200:203], v[18:21]
	v_mfma_f32_16x16x32_bf16 v[6:9], v[168:171], v[208:211], v[6:9]
	v_mfma_f32_16x16x32_bf16 v[2:5], v[176:179], v[208:211], v[2:5]
	v_mfma_f32_16x16x32_bf16 v[54:57], v[172:175], v[188:191], v[54:57]
	v_mfma_f32_16x16x32_bf16 v[50:53], v[180:183], v[188:191], v[50:53]
	v_mfma_f32_16x16x32_bf16 v[38:41], v[172:175], v[196:199], v[38:41]
	v_mfma_f32_16x16x32_bf16 v[34:37], v[180:183], v[196:199], v[34:37]
	v_mfma_f32_16x16x32_bf16 v[22:25], v[172:175], v[204:207], v[22:25]
	v_mfma_f32_16x16x32_bf16 v[18:21], v[180:183], v[204:207], v[18:21]
	v_mfma_f32_16x16x32_bf16 v[6:9], v[172:175], v[212:215], v[6:9]
	v_mfma_f32_16x16x32_bf16 v[2:5], v[180:183], v[212:215], v[2:5]
	s_barrier
	s_add_i32 s57, s57, 2
	s_add_u32 s40, s40, 0x100
	s_addc_u32 s41, s41, 0
	s_add_u32 s55, s55, 0x100
	s_addc_u32 s56, s56, 0
	s_cmp_gt_u32 s57, 29
	s_cbranch_scc0 .LBB0_830
	s_and_b64 vcc, exec, s[28:29]
	s_cbranch_vccz .LBB0_833
	s_barrier

; __device__ __forceinline__ int otid() { int t = threadIdx.x; asm volatile("" : "+v"(t)); return t; }
; template <class Epi, class Sched, bool GATHER, bool LIGHTSKIP = false>
; __device__ __forceinline__ void gemm_phase(LAS unsigned char* lds, LAS unsigned char* xl, const int lda, const int ldb, const int K, const Sched& S, const Epi& E) {
;     const int tid = otid(), wid = __builtin_amdgcn_readfirstlane(tid >> 6), lane = tid & 63, wr = wid >> 2, wc = wid & 3, fr = lane & 15, fq = lane >> 4;
;     const int nt = K / BK;
;     int Rr[2], Cc[2]; unsigned voffA[2], voffB[2];
; #pragma unroll
;     for (int i = 0; i < 2; ++i) { stage_rc(tid * 16 + i * 8192, Rr[i], Cc[i]); const int Rb = Epi::PERM ? ((Rr[i] & ~31) + perm32(Rr[i] & 31)) : Rr[i];
;         voffA[i] = (unsigned)(Rr[i] * lda + Cc[i]) * 2u; voffB[i] = (unsigned)(Rb * ldb + Cc[i]) * 2u; }
;     unsigned vc[2][2], vn[2][2];
;     const size_t kstep = (size_t)(BK * 2);
;     const size_t hstepA = (size_t)HALF * lda * 2, hstepB = (size_t)HALF * ldb * 2;
;     const unsigned ldsw = (unsigned)wid * 1024u;
;     const int aoff = lds_byte(wr * 64 + fr, fq * 8), boff = lds_byte(wc * 32 + fr, fq * 8);
;     ...
;     GUnit cur, nxt; int ui = 0;
;     if (!S.next(0, cur)) return;
;     Acc acc;
; #pragma unroll
;     for (int a = 0; a < 2; ++a)
; #pragma unroll
;         for (int b = 0; b < 2; ++b)
; #pragma unroll
;             for (int m = 0; m < 4; ++m)
; #pragma unroll
;                 for (int n = 0; n < 2; ++n) acc[a][b][m][n] = (f32x4){0.f, 0.f, 0.f, 0.f};
;     bf16x8 At[4][2], B0[2][2], B1[2][2];
;     const char* cA = cur.A; const char* cB = cur.B;
;     if constexpr (GATHER) { S.offsets(cur, lda, vc);
; #pragma unroll
;         for (int h = 0; h < 2; ++h) { vn[h][0] = vc[h][0]; vn[h][1] = vc[h][1]; } }
;     PG8_STAGE_B(0, 0, cB); PG8_STAGE_B(0, 1, cB); PG8_STAGE_A(0, 0, cA, false); PG8_STAGE_A(0, 1, cA, false);
;     if (wr == 1) PG8_BAR;
;     PG8_WAIT_V(2); PG8_BAR;
;     __device__ __forceinline__ bool next(int i, GUnit& u) const {
;         if (i > 0 || c >= 128 || (c >= 64) != (which != 0)) return false;
;         const int L = c & 63, b = L >> 5, h = (L >> 3) & 3, t8 = L & 7;
;         if (c < 64) { u.A = kx + ((size_t)(b * 256) * 2048 + h * 512) * 2; u.B = wq2 + ((size_t)(t8 * 256) * 2048 + h * 512) * 2; u.x0 = b * 1024 + h * 256; u.x1 = t8 * 256; u.pm = 0; u.pn = 0; }
.LBB0_852:
	s_waitcnt vmcnt(0)
	s_barrier
	s_setprio 0
	s_load_dwordx2 s[10:11], s[70:71], 0xd8
.LBB0_853:
	v_mov_b32_e32 v13, v0
	s_cmp_gt_i32 s92, 63
	v_readfirstlane_b32 s0, v13
	s_cbranch_scc1 .LBB0_861
	v_lshlrev_b32_e32 v1, 4, v13
	v_add_u32_e32 v2, 0x2000, v1
	v_ashrrev_i32_e32 v3, 31, v2
	v_lshrrev_b32_e32 v3, 22, v3
	v_add_u32_e32 v3, v2, v3
	v_ashrrev_i32_e32 v10, 10, v3
	v_mul_i32_i24_e32 v3, 0x400, v10
	v_sub_u32_e32 v2, v2, v3
	v_lshrrev_b32_e32 v3, 4, v2
	v_bitop3_b32 v2, v3, v2, 32 bitop3:0x6c
	v_ashrrev_i32_e32 v3, 31, v2
	v_lshrrev_b32_e32 v3, 26, v3
	v_add_u32_e32 v3, v2, v3
	v_lshlrev_b32_e32 v4, 3, v10
	v_ashrrev_i32_e32 v11, 6, v3
	v_and_b32_e32 v4, -16, v4
	v_add_u32_e32 v4, v11, v4
	v_and_b32_e32 v5, 3, v11
	s_mov_b32 s1, 0xfffe0
	v_lshrrev_b32_e32 v6, 2, v4
	v_lshlrev_b32_e32 v7, 1, v4
	v_and_b32_e32 v3, 0xc0, v3
	v_and_or_b32 v5, v4, s1, v5
	v_and_b32_e32 v6, 4, v6
	v_and_b32_e32 v7, 24, v7
	v_sub_u32_e32 v2, v2, v3
	v_mov_b32_e32 v3, 1
	v_or3_b32 v5, v5, v6, v7
	v_lshlrev_b32_e32 v6, 5, v10
	v_ashrrev_i16_sdwa v2, v3, sext(v2) dst_sel:DWORD dst_unused:UNUSED_PAD src0_sel:DWORD src1_sel:BYTE_0
	v_and_b32_e32 v6, 32, v6
	v_bfe_i32 v12, v2, 0, 16
	v_add_lshl_u32 v2, v6, v12, 1
	v_lshl_add_u32 v130, v5, 12, v2
	v_lshl_add_u32 v132, v4, 12, v2
	v_bfe_i32 v2, v13, 27, 1
	v_lshrrev_b32_e32 v2, 22, v2
	v_add_u32_e32 v2, v1, v2
	v_and_b32_e32 v2, 0xfffffc00, v2
	v_sub_u32_e32 v1, v1, v2
	v_lshrrev_b32_e32 v2, 4, v1
	v_bitop3_b32 v2, v2, v1, 32 bitop3:0x6c
	v_ashrrev_i32_e32 v1, 31, v1
	v_lshrrev_b32_e32 v1, 26, v1
	v_add_u32_e32 v1, v2, v1
	v_ashrrev_i32_e32 v14, 6, v1
	v_ashrrev_i32_e32 v1, 31, v13
	v_lshrrev_b32_e32 v1, 26, v1
	v_add_u32_e32 v1, v13, v1
	v_ashrrev_i32_e32 v15, 6, v1
	v_lshlrev_b32_e32 v1, 3, v15
	v_and_b32_e32 v1, -16, v1
	s_bfe_u32 s2, s92, 0x10005
	s_bfe_u32 s3, s92, 0x20003
	s_ashr_i32 s16, s0, 6
	v_add_u32_e32 v1, v14, v1
	v_and_b32_e32 v4, 3, v14
	s_lshl_b32 s20, s3, 10
	s_lshl_b32 s18, s2, 20
	s_ashr_i32 s17, s0, 8
	s_lshl_b32 s22, s16, 10
	v_and_or_b32 v4, v1, s1, v4
	s_and_b32 s1, s92, 7
	s_or_b32 s4, s18, s20
	s_waitcnt lgkmcnt(0)
	s_add_u32 s19, s10, s4
	s_addc_u32 s23, s11, 0
	v_lshrrev_b32_e32 v5, 2, v1
	v_lshlrev_b32_e32 v6, 1, v1
	s_add_u32 s12, s19, 0x44650000
	v_and_b32_e32 v5, 4, v5
	v_and_b32_e32 v6, 24, v6
	s_addc_u32 s13, s23, 0
	s_lshl_b32 s21, s1, 20
	v_or3_b32 v4, v4, v5, v6
	v_mul_i32_i24_e32 v6, 64, v14
	s_or_b32 s4, s20, s21
	v_sub_u32_e32 v2, v2, v6
	s_add_u32 s5, s10, s4
	v_lshlrev_b32_e32 v5, 5, v15
	v_ashrrev_i16_sdwa v2, v3, sext(v2) dst_sel:DWORD dst_unused:UNUSED_PAD src0_sel:DWORD src1_sel:BYTE_0
	s_addc_u32 s7, s11, 0
	v_and_b32_e32 v5, 32, v5
	v_bfe_i32 v16, v2, 0, 16
	s_add_u32 s14, s5, 0x46b30000
	v_add_lshl_u32 v2, v5, v16, 1
	s_addc_u32 s15, s7, 0
	s_add_i32 s4, s22, 0
	v_lshl_add_u32 v134, v4, 12, v2
	s_add_i32 m0, s4, 0x10000
	v_lshl_add_u32 v136, v1, 12, v2
	global_load_lds_dwordx4 v134, s[14:15]
	s_add_i32 m0, s4, 0x12000
	s_add_u32 s6, s5, 0x46bb0000
	global_load_lds_dwordx4 v130, s[14:15]
	s_addc_u32 s7, s7, 0
	s_add_i32 m0, s4, 0x14000
	s_add_i32 s5, s4, 0x2000
	global_load_lds_dwordx4 v134, s[6:7]
	s_add_i32 m0, s4, 0x16000
	s_add_u32 s26, s19, 0x446d0000
	global_load_lds_dwordx4 v130, s[6:7]
	s_mov_b32 m0, s4
	s_addc_u32 s27, s23, 0
	global_load_lds_dwordx4 v136, s[12:13]
	s_mov_b32 m0, s5
	s_add_i32 s6, s4, 0x4000
	global_load_lds_dwordx4 v132, s[12:13]
	s_mov_b32 m0, s6
	s_add_i32 s7, s4, 0x6000
	global_load_lds_dwordx4 v136, s[26:27]
	s_mov_b32 m0, s7
	v_mov_b32_e32 v135, 0
	global_load_lds_dwordx4 v132, s[26:27]
	v_mov_b32_e32 v131, v135
	v_mov_b32_e32 v137, v135
	v_mov_b32_e32 v133, v135
	v_lshl_add_u64 v[8:9], s[14:15], 0, v[134:135]
	v_lshl_add_u64 v[6:7], s[14:15], 0, v[130:131]
	v_lshl_add_u64 v[4:5], s[12:13], 0, v[136:137]
	s_cmp_lg_u32 s17, 1
	v_lshl_add_u64 v[2:3], s[12:13], 0, v[132:133]
	s_cbranch_scc1 .LBB0_856
	s_barrier
	s_setprio 1

; #define PG8_STAGE_B(b, h, bp) PG8_STAGE2(PG8_SB(b, h), (bp) + (h) * hstepB, voffB[0], voffB[1])
; #define PG8_STAGE_A(b, h, ap, NX) do { if constexpr (GATHER) { const unsigned _o0 = (NX) ? vn[h][0] : vc[h][0], _o1 = (NX) ? vn[h][1] : vc[h][1]; PG8_STAGE2(PG8_SA(b, h), (ap), _o0, _o1); } \
;         else { PG8_STAGE2(PG8_SA(b, h), (ap) + (h) * hstepA, voffA[0], voffA[1]); } } while (0)
; #define PG8_LDA(dst, b, h) do { _Pragma("unroll") for (int m = 0; m < 4; ++m) _Pragma("unroll") for (int k = 0; k < 2; ++k) dst[m][k] = *(const LAS bf16x8*)(lds + PG8_SA(b, h) + aoff + m * 2048 + k * 1024); } while (0)
; #define PG8_LDB(dst, b, h) do { _Pragma("unroll") for (int n = 0; n < 2; ++n) _Pragma("unroll") for (int k = 0; k < 2; ++k) dst[n][k] = *(const LAS bf16x8*)(lds + PG8_SB(b, h) + boff + n * 2048 + k * 1024); } while (0)
; #define PG8_MMA(ai, bj, At, Bt) do { __builtin_amdgcn_s_setprio(1); _Pragma("unroll") for (int m = 0; m < 4; ++m) _Pragma("unroll") for (int n = 0; n < 2; ++n) _Pragma("unroll") for (int k = 0; k < 2; ++k) \
;         acc[ai][bj][m][n] = __builtin_amdgcn_mfma_f32_16x16x32_bf16(Bt[n][k], At[m][k], acc[ai][bj][m][n], 0, 0, 0); __builtin_amdgcn_s_setprio(0); } while (0)
; #define PG8_WAIT_V(n) asm volatile("s_waitcnt vmcnt(" #n ")" ::: "memory")
; #define PG8_WAIT_L(n) asm volatile("s_waitcnt lgkmcnt(" #n ")" ::: "memory")
; #define PG8_BAR __builtin_amdgcn_s_barrier()
; #define PG8_SCHED __builtin_amdgcn_sched_barrier(0)
; template <class Epi, class Sched, bool GATHER, bool LIGHTSKIP = false>
; __device__ __forceinline__ void gemm_phase(LAS unsigned char* lds, LAS unsigned char* xl, const int lda, const int ldb, const int K, const Sched& S, const Epi& E) {
;     ...
;             PG8_LDB(B0, 0, 0); PG8_LDB(B1, 0, 1); PG8_SCHED; PG8_LDA(At, 0, 0); PG8_STAGE_A(1, 1, a1, false);
;             PG8_WAIT_V(8); PG8_WAIT_L(0); PG8_BAR; PG8_MMA(0, 0, At, B0); PG8_MMA(0, 1, At, B1); PG8_BAR; PG8_SCHED;
;             PG8_LDA(At, 0, 1); PG8_STAGE_B(0, 0, b2); PG8_STAGE_B(0, 1, b2); PG8_STAGE_A(0, 0, a2, last);
.LBB0_857:
	ds_read_b128 v[148:151], v143
	ds_read_b128 v[152:155], v143 offset:1024
	ds_read_b128 v[156:159], v143 offset:2048
	ds_read_b128 v[160:163], v143 offset:3072
	ds_read_b128 v[164:167], v144
	ds_read_b128 v[168:171], v144 offset:1024
	ds_read_b128 v[172:175], v144 offset:2048
	ds_read_b128 v[176:179], v144 offset:3072
	s_add_u32 s22, s18, s20
	s_addc_u32 s23, s19, s21
	s_add_u32 s22, s22, 0x44650100
	s_addc_u32 s23, s23, 0
	s_add_u32 s45, s31, s20
	s_addc_u32 s46, s33, s21
	s_cmpk_eq_i32 s20, 0x300
	s_cselect_b32 s29, s13, s23
	s_cselect_b32 s28, s12, s22
	s_cselect_b32 s23, s15, s46
	s_cselect_b32 s22, s14, s45
	s_mov_b32 m0, s35
	v_lshl_add_u64 v[212:213], v[138:139], 0, s[20:21]
	ds_read_b128 v[180:183], v145
	ds_read_b128 v[184:187], v145 offset:1024
	ds_read_b128 v[188:191], v145 offset:2048
	ds_read_b128 v[192:195], v145 offset:3072
	ds_read_b128 v[196:199], v145 offset:4096
	ds_read_b128 v[200:203], v145 offset:5120
	ds_read_b128 v[204:207], v145 offset:6144
	ds_read_b128 v[208:211], v145 offset:7168
	global_load_lds_dwordx4 v[212:213], off
	v_lshl_add_u64 v[212:213], v[140:141], 0, s[20:21]
	s_mov_b32 m0, s36
	s_nop 0
	global_load_lds_dwordx4 v[212:213], off
	s_waitcnt vmcnt(8)
	s_waitcnt lgkmcnt(0)
	s_barrier
	s_waitcnt lgkmcnt(0)
	v_mfma_f32_16x16x32_bf16 v[126:129], v[148:151], v[180:183], v[126:129]
	v_mfma_f32_16x16x32_bf16 v[122:125], v[156:159], v[180:183], v[122:125]
	v_mfma_f32_16x16x32_bf16 v[118:121], v[148:151], v[188:191], v[118:121]
	v_mfma_f32_16x16x32_bf16 v[114:117], v[156:159], v[188:191], v[114:117]
	v_mfma_f32_16x16x32_bf16 v[102:105], v[148:151], v[196:199], v[102:105]
	v_mfma_f32_16x16x32_bf16 v[98:101], v[156:159], v[196:199], v[98:101]
	v_mfma_f32_16x16x32_bf16 v[86:89], v[148:151], v[204:207], v[86:89]
	v_mfma_f32_16x16x32_bf16 v[82:85], v[156:159], v[204:207], v[82:85]
	v_mfma_f32_16x16x32_bf16 v[126:129], v[152:155], v[184:187], v[126:129]
	v_mfma_f32_16x16x32_bf16 v[122:125], v[160:163], v[184:187], v[122:125]
	v_mfma_f32_16x16x32_bf16 v[118:121], v[152:155], v[192:195], v[118:121]
	v_mfma_f32_16x16x32_bf16 v[114:117], v[160:163], v[192:195], v[114:117]
	v_mfma_f32_16x16x32_bf16 v[102:105], v[152:155], v[200:203], v[102:105]
	v_mfma_f32_16x16x32_bf16 v[98:101], v[160:163], v[200:203], v[98:101]
	v_mfma_f32_16x16x32_bf16 v[86:89], v[152:155], v[208:211], v[86:89]
	v_mfma_f32_16x16x32_bf16 v[82:85], v[160:163], v[208:211], v[82:85]
	v_mfma_f32_16x16x32_bf16 v[110:113], v[164:167], v[180:183], v[110:113]
	v_mfma_f32_16x16x32_bf16 v[106:109], v[172:175], v[180:183], v[106:109]
	v_mfma_f32_16x16x32_bf16 v[94:97], v[164:167], v[188:191], v[94:97]
	v_mfma_f32_16x16x32_bf16 v[90:93], v[172:175], v[188:191], v[90:93]
	v_mfma_f32_16x16x32_bf16 v[78:81], v[164:167], v[196:199], v[78:81]
	v_mfma_f32_16x16x32_bf16 v[74:77], v[172:175], v[196:199], v[74:77]
	v_mfma_f32_16x16x32_bf16 v[70:73], v[164:167], v[204:207], v[70:73]
	v_mfma_f32_16x16x32_bf16 v[66:69], v[172:175], v[204:207], v[66:69]
	v_mfma_f32_16x16x32_bf16 v[110:113], v[168:171], v[184:187], v[110:113]
	v_mfma_f32_16x16x32_bf16 v[106:109], v[176:179], v[184:187], v[106:109]
	v_mfma_f32_16x16x32_bf16 v[94:97], v[168:171], v[192:195], v[94:97]
	v_mfma_f32_16x16x32_bf16 v[90:93], v[176:179], v[192:195], v[90:93]
	v_mfma_f32_16x16x32_bf16 v[78:81], v[168:171], v[200:203], v[78:81]
	v_mfma_f32_16x16x32_bf16 v[74:77], v[176:179], v[200:203], v[74:77]
	v_mfma_f32_16x16x32_bf16 v[70:73], v[168:171], v[208:211], v[70:73]
	v_mfma_f32_16x16x32_bf16 v[66:69], v[176:179], v[208:211], v[66:69]
	s_barrier
	s_mov_b32 m0, s37
	v_lshl_add_u64 v[212:213], s[22:23], 0, v[134:135]
	s_add_u32 s46, s22, 0x80000
	ds_read_b128 v[180:183], v145 offset:16384
	ds_read_b128 v[184:187], v145 offset:17408
	ds_read_b128 v[188:191], v145 offset:18432
	ds_read_b128 v[192:195], v145 offset:19456
	ds_read_b128 v[196:199], v145 offset:20480
	ds_read_b128 v[200:203], v145 offset:21504
	ds_read_b128 v[204:207], v145 offset:22528
	ds_read_b128 v[208:211], v145 offset:23552
	global_load_lds_dwordx4 v[212:213], off
	v_lshl_add_u64 v[214:215], s[22:23], 0, v[130:131]
	s_mov_b32 m0, s38
	s_addc_u32 s47, s23, 0
	global_load_lds_dwordx4 v[214:215], off
	v_lshl_add_u64 v[216:217], s[46:47], 0, v[134:135]
	s_mov_b32 m0, s39
	v_lshl_add_u64 v[218:219], s[28:29], 0, v[132:133]
	global_load_lds_dwordx4 v[216:217], off
	v_lshl_add_u64 v[216:217], s[46:47], 0, v[130:131]
	s_mov_b32 m0, s40
	s_nop 0
	global_load_lds_dwordx4 v[216:217], off
	v_lshl_add_u64 v[216:217], s[28:29], 0, v[136:137]
	s_mov_b32 m0, s4
	s_nop 0
	global_load_lds_dwordx4 v[216:217], off
	s_mov_b32 m0, s5
	s_nop 0
	global_load_lds_dwordx4 v[218:219], off
	s_waitcnt vmcnt(8)
	s_waitcnt lgkmcnt(0)
	s_barrier
; #define PG8_STAGE_A(b, h, ap, NX) do { if constexpr (GATHER) { const unsigned _o0 = (NX) ? vn[h][0] : vc[h][0], _o1 = (NX) ? vn[h][1] : vc[h][1]; PG8_STAGE2(PG8_SA(b, h), (ap), _o0, _o1); } \
;         else { PG8_STAGE2(PG8_SA(b, h), (ap) + (h) * hstepA, voffA[0], voffA[1]); } } while (0)
; #define PG8_LDA(dst, b, h) do { _Pragma("unroll") for (int m = 0; m < 4; ++m) _Pragma("unroll") for (int k = 0; k < 2; ++k) dst[m][k] = *(const LAS bf16x8*)(lds + PG8_SA(b, h) + aoff + m * 2048 + k * 1024); } while (0)
; #define PG8_LDB(dst, b, h) do { _Pragma("unroll") for (int n = 0; n < 2; ++n) _Pragma("unroll") for (int k = 0; k < 2; ++k) dst[n][k] = *(const LAS bf16x8*)(lds + PG8_SB(b, h) + boff + n * 2048 + k * 1024); } while (0)
; #define PG8_MMA(ai, bj, At, Bt) do { __builtin_amdgcn_s_setprio(1); _Pragma("unroll") for (int m = 0; m < 4; ++m) _Pragma("unroll") for (int n = 0; n < 2; ++n) _Pragma("unroll") for (int k = 0; k < 2; ++k) \
;         acc[ai][bj][m][n] = __builtin_amdgcn_mfma_f32_16x16x32_bf16(Bt[n][k], At[m][k], acc[ai][bj][m][n], 0, 0, 0); __builtin_amdgcn_s_setprio(0); } while (0)
; #define PG8_WAIT_V(n) asm volatile("s_waitcnt vmcnt(" #n ")" ::: "memory")
; #define PG8_WAIT_L(n) asm volatile("s_waitcnt lgkmcnt(" #n ")" ::: "memory")
; #define PG8_BAR __builtin_amdgcn_s_barrier()
; #define PG8_SCHED __builtin_amdgcn_sched_barrier(0)
; template <class Epi, class Sched, bool GATHER, bool LIGHTSKIP = false>
; __device__ __forceinline__ void gemm_phase(LAS unsigned char* lds, LAS unsigned char* xl, const int lda, const int ldb, const int K, const Sched& S, const Epi& E) {
;     ...
;             PG8_WAIT_V(8); PG8_WAIT_L(0); PG8_BAR; if (!light) { PG8_MMA(1, 0, At, B0); PG8_MMA(1, 1, At, B1); } PG8_BAR; PG8_SCHED;
;             PG8_LDB(B0, 1, 0); PG8_LDB(B1, 1, 1); PG8_SCHED; PG8_LDA(At, 1, 0); PG8_STAGE_A(0, 1, a2, last);
;             PG8_WAIT_V(8); PG8_WAIT_L(0); PG8_BAR; PG8_MMA(0, 0, At, B0); PG8_MMA(0, 1, At, B1); PG8_BAR; PG8_SCHED;
	s_waitcnt lgkmcnt(0)
	v_mfma_f32_16x16x32_bf16 v[62:65], v[148:151], v[180:183], v[62:65]
	v_mfma_f32_16x16x32_bf16 v[58:61], v[156:159], v[180:183], v[58:61]
	v_mfma_f32_16x16x32_bf16 v[54:57], v[148:151], v[188:191], v[54:57]
	v_mfma_f32_16x16x32_bf16 v[50:53], v[156:159], v[188:191], v[50:53]
	v_mfma_f32_16x16x32_bf16 v[38:41], v[148:151], v[196:199], v[38:41]
	v_mfma_f32_16x16x32_bf16 v[34:37], v[156:159], v[196:199], v[34:37]
	v_mfma_f32_16x16x32_bf16 v[22:25], v[148:151], v[204:207], v[22:25]
	v_mfma_f32_16x16x32_bf16 v[18:21], v[156:159], v[204:207], v[18:21]
	v_mfma_f32_16x16x32_bf16 v[62:65], v[152:155], v[184:187], v[62:65]
	v_mfma_f32_16x16x32_bf16 v[58:61], v[160:163], v[184:187], v[58:61]
	v_mfma_f32_16x16x32_bf16 v[54:57], v[152:155], v[192:195], v[54:57]
	v_mfma_f32_16x16x32_bf16 v[50:53], v[160:163], v[192:195], v[50:53]
	v_mfma_f32_16x16x32_bf16 v[38:41], v[152:155], v[200:203], v[38:41]
	v_mfma_f32_16x16x32_bf16 v[34:37], v[160:163], v[200:203], v[34:37]
	v_mfma_f32_16x16x32_bf16 v[22:25], v[152:155], v[208:211], v[22:25]
	v_mfma_f32_16x16x32_bf16 v[18:21], v[160:163], v[208:211], v[18:21]
	v_mfma_f32_16x16x32_bf16 v[46:49], v[164:167], v[180:183], v[46:49]
	v_mfma_f32_16x16x32_bf16 v[42:45], v[172:175], v[180:183], v[42:45]
	v_mfma_f32_16x16x32_bf16 v[30:33], v[164:167], v[188:191], v[30:33]
	v_mfma_f32_16x16x32_bf16 v[26:29], v[172:175], v[188:191], v[26:29]
	v_mfma_f32_16x16x32_bf16 v[14:17], v[164:167], v[196:199], v[14:17]
	v_mfma_f32_16x16x32_bf16 v[10:13], v[172:175], v[196:199], v[10:13]
	v_mfma_f32_16x16x32_bf16 v[6:9], v[164:167], v[204:207], v[6:9]
	v_mfma_f32_16x16x32_bf16 v[2:5], v[172:175], v[204:207], v[2:5]
	v_mfma_f32_16x16x32_bf16 v[46:49], v[168:171], v[184:187], v[46:49]
	v_mfma_f32_16x16x32_bf16 v[42:45], v[176:179], v[184:187], v[42:45]
	v_mfma_f32_16x16x32_bf16 v[30:33], v[168:171], v[192:195], v[30:33]
	v_mfma_f32_16x16x32_bf16 v[26:29], v[176:179], v[192:195], v[26:29]
	v_mfma_f32_16x16x32_bf16 v[14:17], v[168:171], v[200:203], v[14:17]
	v_mfma_f32_16x16x32_bf16 v[10:13], v[176:179], v[200:203], v[10:13]
	v_mfma_f32_16x16x32_bf16 v[6:9], v[168:171], v[208:211], v[6:9]
	v_mfma_f32_16x16x32_bf16 v[2:5], v[176:179], v[208:211], v[2:5]
	s_barrier
	ds_read_b128 v[148:151], v146
	ds_read_b128 v[152:155], v146 offset:1024
	ds_read_b128 v[156:159], v146 offset:2048
	ds_read_b128 v[160:163], v146 offset:3072
	ds_read_b128 v[164:167], v147
	ds_read_b128 v[168:171], v147 offset:1024
	ds_read_b128 v[172:175], v147 offset:2048
	ds_read_b128 v[176:179], v147 offset:3072
	s_add_u32 s28, s28, 0x80000
	s_addc_u32 s29, s29, 0
	s_mov_b32 m0, s6
	v_lshl_add_u64 v[220:221], s[28:29], 0, v[136:137]
	ds_read_b128 v[180:183], v145 offset:32768
	ds_read_b128 v[184:187], v145 offset:33792
	ds_read_b128 v[188:191], v145 offset:34816
	ds_read_b128 v[192:195], v145 offset:35840
	ds_read_b128 v[196:199], v145 offset:36864
	ds_read_b128 v[200:203], v145 offset:37888
	ds_read_b128 v[204:207], v145 offset:38912
	ds_read_b128 v[208:211], v145 offset:39936
	global_load_lds_dwordx4 v[220:221], off
	v_lshl_add_u64 v[220:221], s[28:29], 0, v[132:133]
	s_mov_b32 m0, s7
	s_nop 0
	global_load_lds_dwordx4 v[220:221], off
	s_waitcnt vmcnt(8)
	s_waitcnt lgkmcnt(0)
	s_barrier
	s_waitcnt lgkmcnt(0)
	v_mfma_f32_16x16x32_bf16 v[126:129], v[148:151], v[180:183], v[126:129]
	v_mfma_f32_16x16x32_bf16 v[122:125], v[156:159], v[180:183], v[122:125]
	v_mfma_f32_16x16x32_bf16 v[118:121], v[148:151], v[188:191], v[118:121]
	v_mfma_f32_16x16x32_bf16 v[114:117], v[156:159], v[188:191], v[114:117]
	v_mfma_f32_16x16x32_bf16 v[102:105], v[148:151], v[196:199], v[102:105]
	v_mfma_f32_16x16x32_bf16 v[98:101], v[156:159], v[196:199], v[98:101]
	v_mfma_f32_16x16x32_bf16 v[86:89], v[148:151], v[204:207], v[86:89]
	v_mfma_f32_16x16x32_bf16 v[82:85], v[156:159], v[204:207], v[82:85]
	v_mfma_f32_16x16x32_bf16 v[126:129], v[152:155], v[184:187], v[126:129]
	v_mfma_f32_16x16x32_bf16 v[122:125], v[160:163], v[184:187], v[122:125]
	v_mfma_f32_16x16x32_bf16 v[118:121], v[152:155], v[192:195], v[118:121]
	v_mfma_f32_16x16x32_bf16 v[114:117], v[160:163], v[192:195], v[114:117]
	v_mfma_f32_16x16x32_bf16 v[102:105], v[152:155], v[200:203], v[102:105]
	v_mfma_f32_16x16x32_bf16 v[98:101], v[160:163], v[200:203], v[98:101]
	v_mfma_f32_16x16x32_bf16 v[86:89], v[152:155], v[208:211], v[86:89]
	v_mfma_f32_16x16x32_bf16 v[82:85], v[160:163], v[208:211], v[82:85]
	v_mfma_f32_16x16x32_bf16 v[110:113], v[164:167], v[180:183], v[110:113]
	v_mfma_f32_16x16x32_bf16 v[106:109], v[172:175], v[180:183], v[106:109]
	v_mfma_f32_16x16x32_bf16 v[94:97], v[164:167], v[188:191], v[94:97]
	v_mfma_f32_16x16x32_bf16 v[90:93], v[172:175], v[188:191], v[90:93]
	v_mfma_f32_16x16x32_bf16 v[78:81], v[164:167], v[196:199], v[78:81]
	v_mfma_f32_16x16x32_bf16 v[74:77], v[172:175], v[196:199], v[74:77]
	v_mfma_f32_16x16x32_bf16 v[70:73], v[164:167], v[204:207], v[70:73]
	v_mfma_f32_16x16x32_bf16 v[66:69], v[172:175], v[204:207], v[66:69]
	v_mfma_f32_16x16x32_bf16 v[110:113], v[168:171], v[184:187], v[110:113]
	v_mfma_f32_16x16x32_bf16 v[106:109], v[176:179], v[184:187], v[106:109]
	v_mfma_f32_16x16x32_bf16 v[94:97], v[168:171], v[192:195], v[94:97]
	v_mfma_f32_16x16x32_bf16 v[90:93], v[176:179], v[192:195], v[90:93]
	v_mfma_f32_16x16x32_bf16 v[78:81], v[168:171], v[200:203], v[78:81]
	v_mfma_f32_16x16x32_bf16 v[74:77], v[176:179], v[200:203], v[74:77]
	v_mfma_f32_16x16x32_bf16 v[70:73], v[168:171], v[208:211], v[70:73]
	v_mfma_f32_16x16x32_bf16 v[66:69], v[176:179], v[208:211], v[66:69]
	s_barrier
; __device__ __forceinline__ unsigned cvt_pk_bf16(float lo, float hi) { const f32x2 v = {lo, hi}; return __builtin_bit_cast(unsigned, __builtin_convertvector(v, bf16x2_t)); }
; #define PG8_STAGE_B(b, h, bp) PG8_STAGE2(PG8_SB(b, h), (bp) + (h) * hstepB, voffB[0], voffB[1])
; #define PG8_STAGE_A(b, h, ap, NX) do { if constexpr (GATHER) { const unsigned _o0 = (NX) ? vn[h][0] : vc[h][0], _o1 = (NX) ? vn[h][1] : vc[h][1]; PG8_STAGE2(PG8_SA(b, h), (ap), _o0, _o1); } \
;         else { PG8_STAGE2(PG8_SA(b, h), (ap) + (h) * hstepA, voffA[0], voffA[1]); } } while (0)
; #define PG8_LDA(dst, b, h) do { _Pragma("unroll") for (int m = 0; m < 4; ++m) _Pragma("unroll") for (int k = 0; k < 2; ++k) dst[m][k] = *(const LAS bf16x8*)(lds + PG8_SA(b, h) + aoff + m * 2048 + k * 1024); } while (0)
; #define PG8_WAIT_V(n) asm volatile("s_waitcnt vmcnt(" #n ")" ::: "memory")
; #define PG8_WAIT_L(n) asm volatile("s_waitcnt lgkmcnt(" #n ")" ::: "memory")
; template <class Epi, class Sched, bool GATHER, bool LIGHTSKIP = false>
; __device__ __forceinline__ void gemm_phase(LAS unsigned char* lds, LAS unsigned char* xl, const int lda, const int ldb, const int K, const Sched& S, const Epi& E) {
;     ...
;             PG8_LDA(At, 1, 1); PG8_STAGE_B(1, 0, b3); PG8_STAGE_B(1, 1, b3); PG8_STAGE_A(1, 0, a3, last);
;             PG8_WAIT_V(8); PG8_WAIT_L(0); PG8_BAR; if (!light) { PG8_MMA(1, 0, At, B0); PG8_MMA(1, 1, At, B1); } PG8_BAR; PG8_SCHED;
;         }
;         if (wr == 0) PG8_BAR;
;         E(acc, cur, wr, wc, fr, fq, xl, wid, lane);
;     __device__ __forceinline__ void operator()(Acc& acc, const GUnit& u, int wr, int wc, int fr, int fq, LAS unsigned char*, int, int) const {
;         const int row0 = u.x0 + wr * 64 + fr, col0 = u.x1 + wc * 32 + 8 * fq;
; #pragma unroll
;         for (int ai = 0; ai < 2; ++ai)
; #pragma unroll
;             for (int m = 0; m < 4; ++m) { bf16_t* rowp = O + (size_t)(row0 + ai * HALF + m * 16) * ldc + col0;
; #pragma unroll
;                 for (int bj = 0; bj < 2; ++bj) { const f32x4 v0 = acc[ai][bj][m][0], v1 = acc[ai][bj][m][1];
;                     u32x4 w; w.x = cvt_pk_bf16(v0[0], v0[1]); w.y = cvt_pk_bf16(v0[2], v0[3]); w.z = cvt_pk_bf16(v1[0], v1[1]); w.w = cvt_pk_bf16(v1[2], v1[3]);
;                     if constexpr (NT) __builtin_nontemporal_store(w, (u32x4*)(rowp + bj * HALF)); else *(u32x4*)(rowp + bj * HALF) = w; } }
	s_mov_b32 m0, s41
	v_lshl_add_u64 v[212:213], v[212:213], 0, s[16:17]
	s_add_u32 s22, s22, 0x80080
	ds_read_b128 v[180:183], v145 offset:49152
	ds_read_b128 v[184:187], v145 offset:50176
	ds_read_b128 v[188:191], v145 offset:51200
	ds_read_b128 v[192:195], v145 offset:52224
	ds_read_b128 v[196:199], v145 offset:53248
	ds_read_b128 v[200:203], v145 offset:54272
	ds_read_b128 v[204:207], v145 offset:55296
	ds_read_b128 v[208:211], v145 offset:56320
	global_load_lds_dwordx4 v[212:213], off
	v_lshl_add_u64 v[212:213], v[214:215], 0, s[16:17]
	s_mov_b32 m0, s42
	s_addc_u32 s23, s23, 0
	global_load_lds_dwordx4 v[212:213], off
	v_lshl_add_u64 v[212:213], s[22:23], 0, v[134:135]
	s_mov_b32 m0, s43
	s_nop 0
	global_load_lds_dwordx4 v[212:213], off
	v_lshl_add_u64 v[212:213], s[22:23], 0, v[130:131]
	s_mov_b32 m0, s44
	s_nop 0
	global_load_lds_dwordx4 v[212:213], off
	v_lshl_add_u64 v[212:213], v[216:217], 0, s[16:17]
	s_mov_b32 m0, s27
	s_nop 0
	global_load_lds_dwordx4 v[212:213], off
	v_lshl_add_u64 v[212:213], v[218:219], 0, s[16:17]
	s_mov_b32 m0, s30
	s_nop 0
	global_load_lds_dwordx4 v[212:213], off
	s_waitcnt vmcnt(8)
	s_waitcnt lgkmcnt(0)
	s_barrier
	s_waitcnt lgkmcnt(0)
	v_mfma_f32_16x16x32_bf16 v[62:65], v[148:151], v[180:183], v[62:65]
	v_mfma_f32_16x16x32_bf16 v[58:61], v[156:159], v[180:183], v[58:61]
	v_mfma_f32_16x16x32_bf16 v[54:57], v[148:151], v[188:191], v[54:57]
	v_mfma_f32_16x16x32_bf16 v[50:53], v[156:159], v[188:191], v[50:53]
	v_mfma_f32_16x16x32_bf16 v[38:41], v[148:151], v[196:199], v[38:41]
	v_mfma_f32_16x16x32_bf16 v[34:37], v[156:159], v[196:199], v[34:37]
	v_mfma_f32_16x16x32_bf16 v[22:25], v[148:151], v[204:207], v[22:25]
	v_mfma_f32_16x16x32_bf16 v[18:21], v[156:159], v[204:207], v[18:21]
	v_mfma_f32_16x16x32_bf16 v[62:65], v[152:155], v[184:187], v[62:65]
	v_mfma_f32_16x16x32_bf16 v[58:61], v[160:163], v[184:187], v[58:61]
	v_mfma_f32_16x16x32_bf16 v[54:57], v[152:155], v[192:195], v[54:57]
	v_mfma_f32_16x16x32_bf16 v[50:53], v[160:163], v[192:195], v[50:53]
	v_mfma_f32_16x16x32_bf16 v[38:41], v[152:155], v[200:203], v[38:41]
	v_mfma_f32_16x16x32_bf16 v[34:37], v[160:163], v[200:203], v[34:37]
	v_mfma_f32_16x16x32_bf16 v[22:25], v[152:155], v[208:211], v[22:25]
	v_mfma_f32_16x16x32_bf16 v[18:21], v[160:163], v[208:211], v[18:21]
	v_mfma_f32_16x16x32_bf16 v[46:49], v[164:167], v[180:183], v[46:49]
	v_mfma_f32_16x16x32_bf16 v[42:45], v[172:175], v[180:183], v[42:45]
	v_mfma_f32_16x16x32_bf16 v[30:33], v[164:167], v[188:191], v[30:33]
	v_mfma_f32_16x16x32_bf16 v[26:29], v[172:175], v[188:191], v[26:29]
	v_mfma_f32_16x16x32_bf16 v[14:17], v[164:167], v[196:199], v[14:17]
	v_mfma_f32_16x16x32_bf16 v[10:13], v[172:175], v[196:199], v[10:13]
	v_mfma_f32_16x16x32_bf16 v[6:9], v[164:167], v[204:207], v[6:9]
	v_mfma_f32_16x16x32_bf16 v[2:5], v[172:175], v[204:207], v[2:5]
	v_mfma_f32_16x16x32_bf16 v[46:49], v[168:171], v[184:187], v[46:49]
	v_mfma_f32_16x16x32_bf16 v[42:45], v[176:179], v[184:187], v[42:45]
	v_mfma_f32_16x16x32_bf16 v[30:33], v[168:171], v[192:195], v[30:33]
	v_mfma_f32_16x16x32_bf16 v[26:29], v[176:179], v[192:195], v[26:29]
	v_mfma_f32_16x16x32_bf16 v[14:17], v[168:171], v[200:203], v[14:17]
	v_mfma_f32_16x16x32_bf16 v[10:13], v[176:179], v[200:203], v[10:13]
	v_mfma_f32_16x16x32_bf16 v[6:9], v[168:171], v[208:211], v[6:9]
	v_mfma_f32_16x16x32_bf16 v[2:5], v[176:179], v[208:211], v[2:5]
	s_barrier
	s_add_i32 s34, s34, 2
	s_add_u32 s20, s20, 0x100
	s_addc_u32 s21, s21, 0
	s_cmp_gt_u32 s34, 5
	s_cbranch_scc0 .LBB0_857
	s_cmpk_lt_u32 s0, 0x100
	s_cbranch_scc0 .LBB0_860
	s_barrier
.LBB0_860:
	s_lshl_b32 s0, s2, 10
	s_lshl_b32 s2, s3, 8
	s_or_b32 s0, s0, s2
	v_add_u32_e32 v130, s0, v1
	s_add_u32 s2, s10, 0x2c010000
	v_lshl_or_b32 v1, s1, 8, v142
	v_ashrrev_i32_e32 v131, 31, v130
	s_addc_u32 s3, s11, 0
	v_or_b32_e32 v1, s26, v1
	v_lshlrev_b64 v[132:133], 12, v[130:131]
	v_lshl_add_u64 v[132:133], s[2:3], 0, v[132:133]
	v_lshlrev_b32_e32 v134, 1, v1
	v_mov_b32_e32 v135, 0
	v_lshl_add_u64 v[132:133], v[132:133], 0, v[134:135]
	s_mov_b64 s[0:1], 0x80000
	v_cvt_pk_bf16_f32 v70, v70, v71
	v_cvt_pk_bf16_f32 v71, v72, v73
	v_cvt_pk_bf16_f32 v72, v66, v67
	v_lshl_add_u64 v[66:67], v[132:133], 0, s[0:1]
	s_mov_b32 s0, 0x80000
	v_cvt_pk_bf16_f32 v62, v62, v63
	v_cvt_pk_bf16_f32 v63, v64, v65
	v_cvt_pk_bf16_f32 v64, v58, v59
	v_add_co_u32_e32 v58, vcc, s0, v132
	v_cvt_pk_bf16_f32 v46, v46, v47
	v_cvt_pk_bf16_f32 v47, v48, v49
	v_cvt_pk_bf16_f32 v48, v42, v43
	v_cvt_pk_bf16_f32 v49, v44, v45
	s_mov_b64 s[0:1], 0x90000
	v_cvt_pk_bf16_f32 v110, v110, v111
	v_cvt_pk_bf16_f32 v111, v112, v113
	v_cvt_pk_bf16_f32 v112, v106, v107
	v_or_b32_e32 v106, 16, v130
	v_addc_co_u32_e32 v59, vcc, 0, v133, vcc
	global_store_dwordx4 v[66:67], v[46:49], off offset:256
	v_ashrrev_i32_e32 v107, 31, v106
	v_cvt_pk_bf16_f32 v94, v94, v95
	v_lshl_add_u64 v[46:47], v[132:133], 0, s[0:1]
	s_mov_b32 s0, 0x90000
	v_cvt_pk_bf16_f32 v95, v96, v97
	v_cvt_pk_bf16_f32 v96, v90, v91
	v_or_b32_e32 v90, 32, v130
	v_add_co_u32_e32 v48, vcc, s0, v132
	v_cvt_pk_bf16_f32 v30, v30, v31
	v_cvt_pk_bf16_f32 v31, v32, v33
	v_cvt_pk_bf16_f32 v32, v26, v27
	v_cvt_pk_bf16_f32 v33, v28, v29
	s_mov_b64 s[0:1], 0xa0000
	v_lshlrev_b64 v[106:107], 12, v[106:107]
	v_ashrrev_i32_e32 v91, 31, v90
	v_cvt_pk_bf16_f32 v78, v78, v79
	v_cvt_pk_bf16_f32 v79, v80, v81
	v_cvt_pk_bf16_f32 v80, v74, v75
	v_or_b32_e32 v74, 48, v130
	v_addc_co_u32_e32 v49, vcc, 0, v133, vcc
	global_store_dwordx4 v[46:47], v[30:33], off offset:256
	v_cvt_pk_bf16_f32 v113, v108, v109
	v_lshl_add_u64 v[106:107], s[2:3], 0, v[106:107]
	v_lshl_add_u64 v[30:31], v[132:133], 0, s[0:1]
	s_mov_b32 s0, 0xa0000
; template <class Epi, class Sched, bool GATHER, bool LIGHTSKIP = false>
; __device__ __forceinline__ void gemm_phase(LAS unsigned char* lds, LAS unsigned char* xl, const int lda, const int ldb, const int K, const Sched& S, const Epi& E) {
;     const int tid = otid(), wid = __builtin_amdgcn_readfirstlane(tid >> 6), lane = tid & 63, wr = wid >> 2, wc = wid & 3, fr = lane & 15, fq = lane >> 4;
;     const int nt = K / BK;
;     int Rr[2], Cc[2]; unsigned voffA[2], voffB[2];
; #pragma unroll
;     for (int i = 0; i < 2; ++i) { stage_rc(tid * 16 + i * 8192, Rr[i], Cc[i]); const int Rb = Epi::PERM ? ((Rr[i] & ~31) + perm32(Rr[i] & 31)) : Rr[i];
;         voffA[i] = (unsigned)(Rr[i] * lda + Cc[i]) * 2u; voffB[i] = (unsigned)(Rb * ldb + Cc[i]) * 2u; }
;     unsigned vc[2][2], vn[2][2];
;     const size_t kstep = (size_t)(BK * 2);
;     const size_t hstepA = (size_t)HALF * lda * 2, hstepB = (size_t)HALF * ldb * 2;
;     const unsigned ldsw = (unsigned)wid * 1024u;
;     const int aoff = lds_byte(wr * 64 + fr, fq * 8), boff = lds_byte(wc * 32 + fr, fq * 8);
;     ...
;     GUnit cur, nxt; int ui = 0;
;     if (!S.next(0, cur)) return;
;     Acc acc;
; #pragma unroll
;     for (int a = 0; a < 2; ++a)
; #pragma unroll
;         for (int b = 0; b < 2; ++b)
; #pragma unroll
;             for (int m = 0; m < 4; ++m)
; #pragma unroll
;                 for (int n = 0; n < 2; ++n) acc[a][b][m][n] = (f32x4){0.f, 0.f, 0.f, 0.f};
;     bf16x8 At[4][2], B0[2][2], B1[2][2];
;     const char* cA = cur.A; const char* cB = cur.B;
;     __device__ __forceinline__ void operator()(Acc& acc, const GUnit& u, int wr, int wc, int fr, int fq, LAS unsigned char*, int, int) const {
;         const int row0 = u.x0 + wr * 64 + fr, col0 = u.x1 + wc * 32 + 8 * fq;
; #pragma unroll
;         for (int ai = 0; ai < 2; ++ai)
; #pragma unroll
;             for (int m = 0; m < 4; ++m) { bf16_t* rowp = O + (size_t)(row0 + ai * HALF + m * 16) * ldc + col0;
; #pragma unroll
;                 for (int bj = 0; bj < 2; ++bj) { const f32x4 v0 = acc[ai][bj][m][0], v1 = acc[ai][bj][m][1];
;                     u32x4 w; w.x = cvt_pk_bf16(v0[0], v0[1]); w.y = cvt_pk_bf16(v0[2], v0[3]); w.z = cvt_pk_bf16(v1[0], v1[1]); w.w = cvt_pk_bf16(v1[2], v1[3]);
;                     if constexpr (NT) __builtin_nontemporal_store(w, (u32x4*)(rowp + bj * HALF)); else *(u32x4*)(rowp + bj * HALF) = w; } }
	v_lshlrev_b64 v[90:91], 12, v[90:91]
	v_ashrrev_i32_e32 v75, 31, v74
	v_add_co_u32_e32 v32, vcc, s0, v132
	v_cvt_pk_bf16_f32 v14, v14, v15
	v_cvt_pk_bf16_f32 v15, v16, v17
	v_cvt_pk_bf16_f32 v16, v10, v11
	v_cvt_pk_bf16_f32 v17, v12, v13
	s_mov_b64 s[0:1], 0xb0000
	global_store_dwordx4 v[132:133], v[110:113], off offset:256
	v_cvt_pk_bf16_f32 v97, v92, v93
	v_lshl_add_u64 v[90:91], s[2:3], 0, v[90:91]
	v_lshl_add_u64 v[110:111], v[106:107], 0, v[134:135]
	v_lshlrev_b64 v[74:75], 12, v[74:75]
	v_addc_co_u32_e32 v33, vcc, 0, v133, vcc
	global_store_dwordx4 v[30:31], v[14:17], off offset:256
	global_store_dwordx4 v[110:111], v[94:97], off offset:256
	v_cvt_pk_bf16_f32 v81, v76, v77
	v_lshl_add_u64 v[14:15], v[132:133], 0, s[0:1]
	s_mov_b32 s0, 0xb0000
	v_lshl_add_u64 v[94:95], v[90:91], 0, v[134:135]
	v_lshl_add_u64 v[74:75], s[2:3], 0, v[74:75]
	v_add_co_u32_e32 v16, vcc, s0, v132
	v_cvt_pk_bf16_f32 v126, v126, v127
	v_cvt_pk_bf16_f32 v127, v128, v129
	v_cvt_pk_bf16_f32 v128, v122, v123
	v_cvt_pk_bf16_f32 v129, v124, v125
	v_cvt_pk_bf16_f32 v106, v118, v119
	v_cvt_pk_bf16_f32 v107, v120, v121
	v_cvt_pk_bf16_f32 v108, v114, v115
	v_cvt_pk_bf16_f32 v109, v116, v117
	v_cvt_pk_bf16_f32 v90, v102, v103
	v_cvt_pk_bf16_f32 v91, v104, v105
	v_cvt_pk_bf16_f32 v92, v98, v99
	v_cvt_pk_bf16_f32 v93, v100, v101
	global_store_dwordx4 v[94:95], v[78:81], off offset:256
	v_cvt_pk_bf16_f32 v76, v82, v83
	v_cvt_pk_bf16_f32 v77, v84, v85
	v_lshl_add_u64 v[78:79], v[74:75], 0, v[134:135]
	v_cvt_pk_bf16_f32 v74, v86, v87
	v_cvt_pk_bf16_f32 v75, v88, v89
	v_cvt_pk_bf16_f32 v73, v68, v69
	v_cvt_pk_bf16_f32 v65, v60, v61
	v_cvt_pk_bf16_f32 v42, v54, v55
	v_cvt_pk_bf16_f32 v43, v56, v57
	v_cvt_pk_bf16_f32 v44, v50, v51
	v_cvt_pk_bf16_f32 v45, v52, v53
	v_cvt_pk_bf16_f32 v26, v38, v39
	v_cvt_pk_bf16_f32 v27, v40, v41
	v_cvt_pk_bf16_f32 v28, v34, v35
	v_cvt_pk_bf16_f32 v29, v36, v37
	v_cvt_pk_bf16_f32 v10, v22, v23
	v_cvt_pk_bf16_f32 v11, v24, v25
	v_cvt_pk_bf16_f32 v12, v18, v19
	v_cvt_pk_bf16_f32 v13, v20, v21
	v_addc_co_u32_e32 v17, vcc, 0, v133, vcc
	v_cvt_pk_bf16_f32 v6, v6, v7
	v_cvt_pk_bf16_f32 v7, v8, v9
	v_cvt_pk_bf16_f32 v8, v2, v3
	v_cvt_pk_bf16_f32 v9, v4, v5
	global_store_dwordx4 v[132:133], v[126:129], off
	global_store_dwordx4 v[110:111], v[106:109], off
	global_store_dwordx4 v[94:95], v[90:93], off
	global_store_dwordx4 v[78:79], v[74:77], off
	global_store_dwordx4 v[78:79], v[70:73], off offset:256
	global_store_dwordx4 v[58:59], v[62:65], off
	global_store_dwordx4 v[48:49], v[42:45], off
	global_store_dwordx4 v[32:33], v[26:29], off
	global_store_dwordx4 v[16:17], v[10:13], off
	global_store_dwordx4 v[14:15], v[6:9], off offset:256
	s_waitcnt vmcnt(0)
	s_barrier
	s_setprio 0
	s_load_dwordx2 s[10:11], s[70:71], 0xd8
.LBB0_861:
	v_mov_b32_e32 v13, v0
	s_and_b32 s0, s92, 0xffffffc0
	s_cmp_lg_u32 s0, 64
	v_readfirstlane_b32 s0, v13
	s_cbranch_scc1 .LBB0_869
	v_lshlrev_b32_e32 v1, 4, v13
	v_add_u32_e32 v2, 0x2000, v1
	v_ashrrev_i32_e32 v3, 31, v2
	v_lshrrev_b32_e32 v3, 22, v3
	v_add_u32_e32 v3, v2, v3
	v_ashrrev_i32_e32 v10, 10, v3
	v_mul_i32_i24_e32 v3, 0x400, v10
	v_sub_u32_e32 v2, v2, v3
	v_lshrrev_b32_e32 v3, 4, v2
	v_bitop3_b32 v2, v3, v2, 32 bitop3:0x6c
	v_ashrrev_i32_e32 v3, 31, v2
	v_lshrrev_b32_e32 v3, 26, v3
	v_add_u32_e32 v3, v2, v3
	v_lshlrev_b32_e32 v4, 3, v10
	v_ashrrev_i32_e32 v11, 6, v3
	v_and_b32_e32 v4, -16, v4
	v_add_u32_e32 v4, v11, v4
	v_and_b32_e32 v5, 3, v11
	s_mov_b32 s1, 0xfffe0
	v_lshrrev_b32_e32 v6, 2, v4
	v_lshlrev_b32_e32 v7, 1, v4
	v_and_b32_e32 v3, 0xc0, v3
	v_and_or_b32 v5, v4, s1, v5
	v_and_b32_e32 v6, 4, v6
	v_and_b32_e32 v7, 24, v7
	v_sub_u32_e32 v2, v2, v3
	v_mov_b32_e32 v3, 1
	v_or3_b32 v5, v5, v6, v7
	v_lshlrev_b32_e32 v6, 5, v10
	v_ashrrev_i16_sdwa v2, v3, sext(v2) dst_sel:DWORD dst_unused:UNUSED_PAD src0_sel:DWORD src1_sel:BYTE_0
	v_and_b32_e32 v6, 32, v6
	v_bfe_i32 v12, v2, 0, 16
	v_add_lshl_u32 v2, v6, v12, 1
	v_lshl_add_u32 v130, v5, 12, v2
	v_lshl_add_u32 v132, v4, 12, v2
	v_bfe_i32 v2, v13, 27, 1
	v_lshrrev_b32_e32 v2, 22, v2
	v_add_u32_e32 v2, v1, v2
	v_and_b32_e32 v2, 0xfffffc00, v2
	v_sub_u32_e32 v1, v1, v2
	v_lshrrev_b32_e32 v2, 4, v1
	v_bitop3_b32 v2, v2, v1, 32 bitop3:0x6c
	v_ashrrev_i32_e32 v1, 31, v1
	v_lshrrev_b32_e32 v1, 26, v1
	v_add_u32_e32 v1, v2, v1
	v_ashrrev_i32_e32 v14, 6, v1
	v_ashrrev_i32_e32 v1, 31, v13
	v_lshrrev_b32_e32 v1, 26, v1
	v_add_u32_e32 v1, v13, v1
	v_ashrrev_i32_e32 v15, 6, v1
	v_lshlrev_b32_e32 v1, 3, v15
	v_and_b32_e32 v1, -16, v1
	v_add_u32_e32 v1, v14, v1
	v_and_b32_e32 v4, 3, v14
	v_and_or_b32 v4, v1, s1, v4
	s_bfe_u32 s1, s92, 0x20003
	s_and_b32 s3, s92, 7
	s_ashr_i32 s16, s0, 6
	s_lshl_b32 s20, s1, 10
	s_lshl_b32 s18, s3, 20
	s_ashr_i32 s17, s0, 8
	s_lshl_b32 s22, s16, 10
	s_bfe_u32 s2, s92, 0x10005
	s_or_b32 s4, s20, s18
	s_waitcnt lgkmcnt(0)
	s_add_u32 s19, s10, s4
	s_addc_u32 s23, s11, 0
	v_lshrrev_b32_e32 v5, 2, v1
	v_lshlrev_b32_e32 v6, 1, v1
	s_add_u32 s12, s19, 0x3810000
	v_and_b32_e32 v5, 4, v5
	v_and_b32_e32 v6, 24, v6
	s_addc_u32 s13, s23, 0
	s_lshl_b32 s21, s2, 20
	v_or3_b32 v4, v4, v5, v6
	v_mul_i32_i24_e32 v6, 64, v14
	s_or_b32 s4, s21, s20
	v_sub_u32_e32 v2, v2, v6
	s_add_u32 s5, s10, s4
	v_lshlrev_b32_e32 v5, 5, v15
	v_ashrrev_i16_sdwa v2, v3, sext(v2) dst_sel:DWORD dst_unused:UNUSED_PAD src0_sel:DWORD src1_sel:BYTE_0
	s_addc_u32 s7, s11, 0
	v_and_b32_e32 v5, 32, v5
	v_bfe_i32 v16, v2, 0, 16
	s_add_u32 s14, s5, 0x44850000
	v_add_lshl_u32 v2, v5, v16, 1
	s_addc_u32 s15, s7, 0
	s_add_i32 s4, s22, 0
	v_lshl_add_u32 v134, v4, 12, v2
	s_add_i32 m0, s4, 0x10000
	v_lshl_add_u32 v136, v1, 12, v2
	global_load_lds_dwordx4 v134, s[14:15]
	s_add_i32 m0, s4, 0x12000
	s_add_u32 s6, s5, 0x448d0000
	global_load_lds_dwordx4 v130, s[14:15]
	s_addc_u32 s7, s7, 0
	s_add_i32 m0, s4, 0x14000
	s_add_i32 s5, s4, 0x2000
	global_load_lds_dwordx4 v134, s[6:7]
	s_add_i32 m0, s4, 0x16000
	s_add_u32 s26, s19, 0x3890000
	global_load_lds_dwordx4 v130, s[6:7]
	s_mov_b32 m0, s4
	s_addc_u32 s27, s23, 0
	global_load_lds_dwordx4 v136, s[12:13]
	s_mov_b32 m0, s5
	s_add_i32 s6, s4, 0x4000
	global_load_lds_dwordx4 v132, s[12:13]
	s_mov_b32 m0, s6
	s_add_i32 s7, s4, 0x6000
	global_load_lds_dwordx4 v136, s[26:27]
	s_mov_b32 m0, s7
	v_mov_b32_e32 v135, 0
	global_load_lds_dwordx4 v132, s[26:27]
	v_mov_b32_e32 v131, v135
	v_mov_b32_e32 v137, v135
	v_mov_b32_e32 v133, v135
	v_lshl_add_u64 v[8:9], s[14:15], 0, v[134:135]
	v_lshl_add_u64 v[6:7], s[14:15], 0, v[130:131]
	v_lshl_add_u64 v[4:5], s[12:13], 0, v[136:137]
	s_cmp_lg_u32 s17, 1
	v_lshl_add_u64 v[2:3], s[12:13], 0, v[132:133]
	s_cbranch_scc1 .LBB0_864
	s_barrier
	s_setprio 1

; #define PG8_STAGE_B(b, h, bp) PG8_STAGE2(PG8_SB(b, h), (bp) + (h) * hstepB, voffB[0], voffB[1])
; #define PG8_STAGE_A(b, h, ap, NX) do { if constexpr (GATHER) { const unsigned _o0 = (NX) ? vn[h][0] : vc[h][0], _o1 = (NX) ? vn[h][1] : vc[h][1]; PG8_STAGE2(PG8_SA(b, h), (ap), _o0, _o1); } \
;         else { PG8_STAGE2(PG8_SA(b, h), (ap) + (h) * hstepA, voffA[0], voffA[1]); } } while (0)
; #define PG8_LDA(dst, b, h) do { _Pragma("unroll") for (int m = 0; m < 4; ++m) _Pragma("unroll") for (int k = 0; k < 2; ++k) dst[m][k] = *(const LAS bf16x8*)(lds + PG8_SA(b, h) + aoff + m * 2048 + k * 1024); } while (0)
; #define PG8_LDB(dst, b, h) do { _Pragma("unroll") for (int n = 0; n < 2; ++n) _Pragma("unroll") for (int k = 0; k < 2; ++k) dst[n][k] = *(const LAS bf16x8*)(lds + PG8_SB(b, h) + boff + n * 2048 + k * 1024); } while (0)
; #define PG8_MMA(ai, bj, At, Bt) do { __builtin_amdgcn_s_setprio(1); _Pragma("unroll") for (int m = 0; m < 4; ++m) _Pragma("unroll") for (int n = 0; n < 2; ++n) _Pragma("unroll") for (int k = 0; k < 2; ++k) \
;         acc[ai][bj][m][n] = __builtin_amdgcn_mfma_f32_16x16x32_bf16(Bt[n][k], At[m][k], acc[ai][bj][m][n], 0, 0, 0); __builtin_amdgcn_s_setprio(0); } while (0)
; #define PG8_WAIT_V(n) asm volatile("s_waitcnt vmcnt(" #n ")" ::: "memory")
; #define PG8_WAIT_L(n) asm volatile("s_waitcnt lgkmcnt(" #n ")" ::: "memory")
; #define PG8_BAR __builtin_amdgcn_s_barrier()
; #define PG8_SCHED __builtin_amdgcn_sched_barrier(0)
; template <class Epi, class Sched, bool GATHER, bool LIGHTSKIP = false>
; __device__ __forceinline__ void gemm_phase(LAS unsigned char* lds, LAS unsigned char* xl, const int lda, const int ldb, const int K, const Sched& S, const Epi& E) {
;     ...
;             PG8_LDB(B0, 0, 0); PG8_LDB(B1, 0, 1); PG8_SCHED; PG8_LDA(At, 0, 0); PG8_STAGE_A(1, 1, a1, false);
;             PG8_WAIT_V(8); PG8_WAIT_L(0); PG8_BAR; PG8_MMA(0, 0, At, B0); PG8_MMA(0, 1, At, B1); PG8_BAR; PG8_SCHED;
;             PG8_LDA(At, 0, 1); PG8_STAGE_B(0, 0, b2); PG8_STAGE_B(0, 1, b2); PG8_STAGE_A(0, 0, a2, last);
;             PG8_WAIT_V(8); PG8_WAIT_L(0); PG8_BAR; if (!light) { PG8_MMA(1, 0, At, B0); PG8_MMA(1, 1, At, B1); } PG8_BAR; PG8_SCHED;
.LBB0_865:
	ds_read_b128 v[148:151], v143
	ds_read_b128 v[152:155], v143 offset:1024
	ds_read_b128 v[156:159], v143 offset:2048
	ds_read_b128 v[160:163], v143 offset:3072
	ds_read_b128 v[164:167], v144
	ds_read_b128 v[168:171], v144 offset:1024
	ds_read_b128 v[172:175], v144 offset:2048
	ds_read_b128 v[176:179], v144 offset:3072
	s_add_u32 s22, s18, s20
	s_addc_u32 s23, s19, s21
	s_add_u32 s22, s22, 0x3810100
	s_addc_u32 s23, s23, 0
	s_add_u32 s45, s31, s20
	s_addc_u32 s46, s33, s21
	s_cmpk_eq_i32 s20, 0x300
	s_cselect_b32 s29, s13, s23
	s_cselect_b32 s28, s12, s22
	s_cselect_b32 s23, s15, s46
	s_cselect_b32 s22, s14, s45
	s_mov_b32 m0, s35
	v_lshl_add_u64 v[212:213], v[138:139], 0, s[20:21]
	ds_read_b128 v[180:183], v145
	ds_read_b128 v[184:187], v145 offset:1024
	ds_read_b128 v[188:191], v145 offset:2048
	ds_read_b128 v[192:195], v145 offset:3072
	ds_read_b128 v[196:199], v145 offset:4096
	ds_read_b128 v[200:203], v145 offset:5120
	ds_read_b128 v[204:207], v145 offset:6144
	ds_read_b128 v[208:211], v145 offset:7168
	global_load_lds_dwordx4 v[212:213], off
	v_lshl_add_u64 v[212:213], v[140:141], 0, s[20:21]
	s_mov_b32 m0, s36
	s_nop 0
	global_load_lds_dwordx4 v[212:213], off
	s_waitcnt vmcnt(8)
	s_waitcnt lgkmcnt(0)
	s_barrier
	s_waitcnt lgkmcnt(0)
	v_mfma_f32_16x16x32_bf16 v[126:129], v[148:151], v[180:183], v[126:129]
	v_mfma_f32_16x16x32_bf16 v[122:125], v[156:159], v[180:183], v[122:125]
	v_mfma_f32_16x16x32_bf16 v[118:121], v[148:151], v[188:191], v[118:121]
	v_mfma_f32_16x16x32_bf16 v[114:117], v[156:159], v[188:191], v[114:117]
	v_mfma_f32_16x16x32_bf16 v[102:105], v[148:151], v[196:199], v[102:105]
	v_mfma_f32_16x16x32_bf16 v[98:101], v[156:159], v[196:199], v[98:101]
	v_mfma_f32_16x16x32_bf16 v[86:89], v[148:151], v[204:207], v[86:89]
	v_mfma_f32_16x16x32_bf16 v[82:85], v[156:159], v[204:207], v[82:85]
	v_mfma_f32_16x16x32_bf16 v[126:129], v[152:155], v[184:187], v[126:129]
	v_mfma_f32_16x16x32_bf16 v[122:125], v[160:163], v[184:187], v[122:125]
	v_mfma_f32_16x16x32_bf16 v[118:121], v[152:155], v[192:195], v[118:121]
	v_mfma_f32_16x16x32_bf16 v[114:117], v[160:163], v[192:195], v[114:117]
	v_mfma_f32_16x16x32_bf16 v[102:105], v[152:155], v[200:203], v[102:105]
	v_mfma_f32_16x16x32_bf16 v[98:101], v[160:163], v[200:203], v[98:101]
	v_mfma_f32_16x16x32_bf16 v[86:89], v[152:155], v[208:211], v[86:89]
	v_mfma_f32_16x16x32_bf16 v[82:85], v[160:163], v[208:211], v[82:85]
	v_mfma_f32_16x16x32_bf16 v[110:113], v[164:167], v[180:183], v[110:113]
	v_mfma_f32_16x16x32_bf16 v[106:109], v[172:175], v[180:183], v[106:109]
	v_mfma_f32_16x16x32_bf16 v[94:97], v[164:167], v[188:191], v[94:97]
	v_mfma_f32_16x16x32_bf16 v[90:93], v[172:175], v[188:191], v[90:93]
	v_mfma_f32_16x16x32_bf16 v[78:81], v[164:167], v[196:199], v[78:81]
	v_mfma_f32_16x16x32_bf16 v[74:77], v[172:175], v[196:199], v[74:77]
	v_mfma_f32_16x16x32_bf16 v[70:73], v[164:167], v[204:207], v[70:73]
	v_mfma_f32_16x16x32_bf16 v[66:69], v[172:175], v[204:207], v[66:69]
	v_mfma_f32_16x16x32_bf16 v[110:113], v[168:171], v[184:187], v[110:113]
	v_mfma_f32_16x16x32_bf16 v[106:109], v[176:179], v[184:187], v[106:109]
	v_mfma_f32_16x16x32_bf16 v[94:97], v[168:171], v[192:195], v[94:97]
	v_mfma_f32_16x16x32_bf16 v[90:93], v[176:179], v[192:195], v[90:93]
	v_mfma_f32_16x16x32_bf16 v[78:81], v[168:171], v[200:203], v[78:81]
	v_mfma_f32_16x16x32_bf16 v[74:77], v[176:179], v[200:203], v[74:77]
	v_mfma_f32_16x16x32_bf16 v[70:73], v[168:171], v[208:211], v[70:73]
	v_mfma_f32_16x16x32_bf16 v[66:69], v[176:179], v[208:211], v[66:69]
	s_barrier
	s_mov_b32 m0, s37
	v_lshl_add_u64 v[212:213], s[22:23], 0, v[134:135]
	s_add_u32 s46, s22, 0x80000
	ds_read_b128 v[180:183], v145 offset:16384
	ds_read_b128 v[184:187], v145 offset:17408
	ds_read_b128 v[188:191], v145 offset:18432
	ds_read_b128 v[192:195], v145 offset:19456
	ds_read_b128 v[196:199], v145 offset:20480
	ds_read_b128 v[200:203], v145 offset:21504
	ds_read_b128 v[204:207], v145 offset:22528
	ds_read_b128 v[208:211], v145 offset:23552
	global_load_lds_dwordx4 v[212:213], off
	v_lshl_add_u64 v[214:215], s[22:23], 0, v[130:131]
	s_mov_b32 m0, s38
	s_addc_u32 s47, s23, 0
	global_load_lds_dwordx4 v[214:215], off
	v_lshl_add_u64 v[216:217], s[46:47], 0, v[134:135]
	s_mov_b32 m0, s39
	v_lshl_add_u64 v[218:219], s[28:29], 0, v[132:133]
	global_load_lds_dwordx4 v[216:217], off
	v_lshl_add_u64 v[216:217], s[46:47], 0, v[130:131]
	s_mov_b32 m0, s40
	s_nop 0
	global_load_lds_dwordx4 v[216:217], off
	v_lshl_add_u64 v[216:217], s[28:29], 0, v[136:137]
	s_mov_b32 m0, s4
	s_nop 0
	global_load_lds_dwordx4 v[216:217], off
	s_mov_b32 m0, s5
	s_nop 0
	global_load_lds_dwordx4 v[218:219], off
	s_waitcnt vmcnt(8)
	s_waitcnt lgkmcnt(0)
	s_barrier
; #define PG8_STAGE_A(b, h, ap, NX) do { if constexpr (GATHER) { const unsigned _o0 = (NX) ? vn[h][0] : vc[h][0], _o1 = (NX) ? vn[h][1] : vc[h][1]; PG8_STAGE2(PG8_SA(b, h), (ap), _o0, _o1); } \
;         else { PG8_STAGE2(PG8_SA(b, h), (ap) + (h) * hstepA, voffA[0], voffA[1]); } } while (0)
; #define PG8_LDA(dst, b, h) do { _Pragma("unroll") for (int m = 0; m < 4; ++m) _Pragma("unroll") for (int k = 0; k < 2; ++k) dst[m][k] = *(const LAS bf16x8*)(lds + PG8_SA(b, h) + aoff + m * 2048 + k * 1024); } while (0)
; #define PG8_LDB(dst, b, h) do { _Pragma("unroll") for (int n = 0; n < 2; ++n) _Pragma("unroll") for (int k = 0; k < 2; ++k) dst[n][k] = *(const LAS bf16x8*)(lds + PG8_SB(b, h) + boff + n * 2048 + k * 1024); } while (0)
; #define PG8_MMA(ai, bj, At, Bt) do { __builtin_amdgcn_s_setprio(1); _Pragma("unroll") for (int m = 0; m < 4; ++m) _Pragma("unroll") for (int n = 0; n < 2; ++n) _Pragma("unroll") for (int k = 0; k < 2; ++k) \
;         acc[ai][bj][m][n] = __builtin_amdgcn_mfma_f32_16x16x32_bf16(Bt[n][k], At[m][k], acc[ai][bj][m][n], 0, 0, 0); __builtin_amdgcn_s_setprio(0); } while (0)
; #define PG8_WAIT_V(n) asm volatile("s_waitcnt vmcnt(" #n ")" ::: "memory")
; #define PG8_WAIT_L(n) asm volatile("s_waitcnt lgkmcnt(" #n ")" ::: "memory")
; #define PG8_BAR __builtin_amdgcn_s_barrier()
; #define PG8_SCHED __builtin_amdgcn_sched_barrier(0)
; template <class Epi, class Sched, bool GATHER, bool LIGHTSKIP = false>
; __device__ __forceinline__ void gemm_phase(LAS unsigned char* lds, LAS unsigned char* xl, const int lda, const int ldb, const int K, const Sched& S, const Epi& E) {
;     ...
;             PG8_WAIT_V(8); PG8_WAIT_L(0); PG8_BAR; if (!light) { PG8_MMA(1, 0, At, B0); PG8_MMA(1, 1, At, B1); } PG8_BAR; PG8_SCHED;
;             PG8_LDB(B0, 1, 0); PG8_LDB(B1, 1, 1); PG8_SCHED; PG8_LDA(At, 1, 0); PG8_STAGE_A(0, 1, a2, last);
;             PG8_WAIT_V(8); PG8_WAIT_L(0); PG8_BAR; PG8_MMA(0, 0, At, B0); PG8_MMA(0, 1, At, B1); PG8_BAR; PG8_SCHED;
	s_waitcnt lgkmcnt(0)
	v_mfma_f32_16x16x32_bf16 v[62:65], v[148:151], v[180:183], v[62:65]
	v_mfma_f32_16x16x32_bf16 v[58:61], v[156:159], v[180:183], v[58:61]
	v_mfma_f32_16x16x32_bf16 v[54:57], v[148:151], v[188:191], v[54:57]
	v_mfma_f32_16x16x32_bf16 v[50:53], v[156:159], v[188:191], v[50:53]
	v_mfma_f32_16x16x32_bf16 v[38:41], v[148:151], v[196:199], v[38:41]
	v_mfma_f32_16x16x32_bf16 v[34:37], v[156:159], v[196:199], v[34:37]
	v_mfma_f32_16x16x32_bf16 v[22:25], v[148:151], v[204:207], v[22:25]
	v_mfma_f32_16x16x32_bf16 v[18:21], v[156:159], v[204:207], v[18:21]
	v_mfma_f32_16x16x32_bf16 v[62:65], v[152:155], v[184:187], v[62:65]
	v_mfma_f32_16x16x32_bf16 v[58:61], v[160:163], v[184:187], v[58:61]
	v_mfma_f32_16x16x32_bf16 v[54:57], v[152:155], v[192:195], v[54:57]
	v_mfma_f32_16x16x32_bf16 v[50:53], v[160:163], v[192:195], v[50:53]
	v_mfma_f32_16x16x32_bf16 v[38:41], v[152:155], v[200:203], v[38:41]
	v_mfma_f32_16x16x32_bf16 v[34:37], v[160:163], v[200:203], v[34:37]
	v_mfma_f32_16x16x32_bf16 v[22:25], v[152:155], v[208:211], v[22:25]
	v_mfma_f32_16x16x32_bf16 v[18:21], v[160:163], v[208:211], v[18:21]
	v_mfma_f32_16x16x32_bf16 v[46:49], v[164:167], v[180:183], v[46:49]
	v_mfma_f32_16x16x32_bf16 v[42:45], v[172:175], v[180:183], v[42:45]
	v_mfma_f32_16x16x32_bf16 v[30:33], v[164:167], v[188:191], v[30:33]
	v_mfma_f32_16x16x32_bf16 v[26:29], v[172:175], v[188:191], v[26:29]
	v_mfma_f32_16x16x32_bf16 v[14:17], v[164:167], v[196:199], v[14:17]
	v_mfma_f32_16x16x32_bf16 v[10:13], v[172:175], v[196:199], v[10:13]
	v_mfma_f32_16x16x32_bf16 v[6:9], v[164:167], v[204:207], v[6:9]
	v_mfma_f32_16x16x32_bf16 v[2:5], v[172:175], v[204:207], v[2:5]
	v_mfma_f32_16x16x32_bf16 v[46:49], v[168:171], v[184:187], v[46:49]
	v_mfma_f32_16x16x32_bf16 v[42:45], v[176:179], v[184:187], v[42:45]
	v_mfma_f32_16x16x32_bf16 v[30:33], v[168:171], v[192:195], v[30:33]
	v_mfma_f32_16x16x32_bf16 v[26:29], v[176:179], v[192:195], v[26:29]
	v_mfma_f32_16x16x32_bf16 v[14:17], v[168:171], v[200:203], v[14:17]
	v_mfma_f32_16x16x32_bf16 v[10:13], v[176:179], v[200:203], v[10:13]
	v_mfma_f32_16x16x32_bf16 v[6:9], v[168:171], v[208:211], v[6:9]
	v_mfma_f32_16x16x32_bf16 v[2:5], v[176:179], v[208:211], v[2:5]
	s_barrier
	ds_read_b128 v[148:151], v146
	ds_read_b128 v[152:155], v146 offset:1024
	ds_read_b128 v[156:159], v146 offset:2048
	ds_read_b128 v[160:163], v146 offset:3072
	ds_read_b128 v[164:167], v147
	ds_read_b128 v[168:171], v147 offset:1024
	ds_read_b128 v[172:175], v147 offset:2048
	ds_read_b128 v[176:179], v147 offset:3072
	s_add_u32 s28, s28, 0x80000
	s_addc_u32 s29, s29, 0
	s_mov_b32 m0, s6
	v_lshl_add_u64 v[220:221], s[28:29], 0, v[136:137]
	ds_read_b128 v[180:183], v145 offset:32768
	ds_read_b128 v[184:187], v145 offset:33792
	ds_read_b128 v[188:191], v145 offset:34816
	ds_read_b128 v[192:195], v145 offset:35840
	ds_read_b128 v[196:199], v145 offset:36864
	ds_read_b128 v[200:203], v145 offset:37888
	ds_read_b128 v[204:207], v145 offset:38912
	ds_read_b128 v[208:211], v145 offset:39936
	global_load_lds_dwordx4 v[220:221], off
	v_lshl_add_u64 v[220:221], s[28:29], 0, v[132:133]
	s_mov_b32 m0, s7
	s_nop 0
	global_load_lds_dwordx4 v[220:221], off
	s_waitcnt vmcnt(8)
	s_waitcnt lgkmcnt(0)
	s_barrier
	s_waitcnt lgkmcnt(0)
	v_mfma_f32_16x16x32_bf16 v[126:129], v[148:151], v[180:183], v[126:129]
	v_mfma_f32_16x16x32_bf16 v[122:125], v[156:159], v[180:183], v[122:125]
	v_mfma_f32_16x16x32_bf16 v[118:121], v[148:151], v[188:191], v[118:121]
	v_mfma_f32_16x16x32_bf16 v[114:117], v[156:159], v[188:191], v[114:117]
	v_mfma_f32_16x16x32_bf16 v[102:105], v[148:151], v[196:199], v[102:105]
	v_mfma_f32_16x16x32_bf16 v[98:101], v[156:159], v[196:199], v[98:101]
	v_mfma_f32_16x16x32_bf16 v[86:89], v[148:151], v[204:207], v[86:89]
	v_mfma_f32_16x16x32_bf16 v[82:85], v[156:159], v[204:207], v[82:85]
	v_mfma_f32_16x16x32_bf16 v[126:129], v[152:155], v[184:187], v[126:129]
	v_mfma_f32_16x16x32_bf16 v[122:125], v[160:163], v[184:187], v[122:125]
	v_mfma_f32_16x16x32_bf16 v[118:121], v[152:155], v[192:195], v[118:121]
	v_mfma_f32_16x16x32_bf16 v[114:117], v[160:163], v[192:195], v[114:117]
	v_mfma_f32_16x16x32_bf16 v[102:105], v[152:155], v[200:203], v[102:105]
	v_mfma_f32_16x16x32_bf16 v[98:101], v[160:163], v[200:203], v[98:101]
	v_mfma_f32_16x16x32_bf16 v[86:89], v[152:155], v[208:211], v[86:89]
	v_mfma_f32_16x16x32_bf16 v[82:85], v[160:163], v[208:211], v[82:85]
	v_mfma_f32_16x16x32_bf16 v[110:113], v[164:167], v[180:183], v[110:113]
	v_mfma_f32_16x16x32_bf16 v[106:109], v[172:175], v[180:183], v[106:109]
	v_mfma_f32_16x16x32_bf16 v[94:97], v[164:167], v[188:191], v[94:97]
	v_mfma_f32_16x16x32_bf16 v[90:93], v[172:175], v[188:191], v[90:93]
	v_mfma_f32_16x16x32_bf16 v[78:81], v[164:167], v[196:199], v[78:81]
	v_mfma_f32_16x16x32_bf16 v[74:77], v[172:175], v[196:199], v[74:77]
	v_mfma_f32_16x16x32_bf16 v[70:73], v[164:167], v[204:207], v[70:73]
	v_mfma_f32_16x16x32_bf16 v[66:69], v[172:175], v[204:207], v[66:69]
	v_mfma_f32_16x16x32_bf16 v[110:113], v[168:171], v[184:187], v[110:113]
	v_mfma_f32_16x16x32_bf16 v[106:109], v[176:179], v[184:187], v[106:109]
	v_mfma_f32_16x16x32_bf16 v[94:97], v[168:171], v[192:195], v[94:97]
	v_mfma_f32_16x16x32_bf16 v[90:93], v[176:179], v[192:195], v[90:93]
	v_mfma_f32_16x16x32_bf16 v[78:81], v[168:171], v[200:203], v[78:81]
	v_mfma_f32_16x16x32_bf16 v[74:77], v[176:179], v[200:203], v[74:77]
	v_mfma_f32_16x16x32_bf16 v[70:73], v[168:171], v[208:211], v[70:73]
	v_mfma_f32_16x16x32_bf16 v[66:69], v[176:179], v[208:211], v[66:69]
	s_barrier
; #define PG8_STAGE_B(b, h, bp) PG8_STAGE2(PG8_SB(b, h), (bp) + (h) * hstepB, voffB[0], voffB[1])
; #define PG8_STAGE_A(b, h, ap, NX) do { if constexpr (GATHER) { const unsigned _o0 = (NX) ? vn[h][0] : vc[h][0], _o1 = (NX) ? vn[h][1] : vc[h][1]; PG8_STAGE2(PG8_SA(b, h), (ap), _o0, _o1); } \
;         else { PG8_STAGE2(PG8_SA(b, h), (ap) + (h) * hstepA, voffA[0], voffA[1]); } } while (0)
; #define PG8_LDA(dst, b, h) do { _Pragma("unroll") for (int m = 0; m < 4; ++m) _Pragma("unroll") for (int k = 0; k < 2; ++k) dst[m][k] = *(const LAS bf16x8*)(lds + PG8_SA(b, h) + aoff + m * 2048 + k * 1024); } while (0)
; #define PG8_MMA(ai, bj, At, Bt) do { __builtin_amdgcn_s_setprio(1); _Pragma("unroll") for (int m = 0; m < 4; ++m) _Pragma("unroll") for (int n = 0; n < 2; ++n) _Pragma("unroll") for (int k = 0; k < 2; ++k) \
;         acc[ai][bj][m][n] = __builtin_amdgcn_mfma_f32_16x16x32_bf16(Bt[n][k], At[m][k], acc[ai][bj][m][n], 0, 0, 0); __builtin_amdgcn_s_setprio(0); } while (0)
; #define PG8_WAIT_V(n) asm volatile("s_waitcnt vmcnt(" #n ")" ::: "memory")
; #define PG8_WAIT_L(n) asm volatile("s_waitcnt lgkmcnt(" #n ")" ::: "memory")
; #define PG8_BAR __builtin_amdgcn_s_barrier()
; #define PG8_SCHED __builtin_amdgcn_sched_barrier(0)
; template <class Epi, class Sched, bool GATHER, bool LIGHTSKIP = false>
; __device__ __forceinline__ void gemm_phase(LAS unsigned char* lds, LAS unsigned char* xl, const int lda, const int ldb, const int K, const Sched& S, const Epi& E) {
;     ...
;             PG8_LDA(At, 1, 1); PG8_STAGE_B(1, 0, b3); PG8_STAGE_B(1, 1, b3); PG8_STAGE_A(1, 0, a3, last);
;             PG8_WAIT_V(8); PG8_WAIT_L(0); PG8_BAR; if (!light) { PG8_MMA(1, 0, At, B0); PG8_MMA(1, 1, At, B1); } PG8_BAR; PG8_SCHED;
;         }
;         if (wr == 0) PG8_BAR;
	s_mov_b32 m0, s41
	v_lshl_add_u64 v[212:213], v[212:213], 0, s[16:17]
	s_add_u32 s22, s22, 0x80080
	ds_read_b128 v[180:183], v145 offset:49152
	ds_read_b128 v[184:187], v145 offset:50176
	ds_read_b128 v[188:191], v145 offset:51200
	ds_read_b128 v[192:195], v145 offset:52224
	ds_read_b128 v[196:199], v145 offset:53248
	ds_read_b128 v[200:203], v145 offset:54272
	ds_read_b128 v[204:207], v145 offset:55296
	ds_read_b128 v[208:211], v145 offset:56320
	global_load_lds_dwordx4 v[212:213], off
	v_lshl_add_u64 v[212:213], v[214:215], 0, s[16:17]
	s_mov_b32 m0, s42
	s_addc_u32 s23, s23, 0
	global_load_lds_dwordx4 v[212:213], off
	v_lshl_add_u64 v[212:213], s[22:23], 0, v[134:135]
	s_mov_b32 m0, s43
	s_nop 0
	global_load_lds_dwordx4 v[212:213], off
	v_lshl_add_u64 v[212:213], s[22:23], 0, v[130:131]
	s_mov_b32 m0, s44
	s_nop 0
	global_load_lds_dwordx4 v[212:213], off
	v_lshl_add_u64 v[212:213], v[216:217], 0, s[16:17]
	s_mov_b32 m0, s27
	s_nop 0
	global_load_lds_dwordx4 v[212:213], off
	v_lshl_add_u64 v[212:213], v[218:219], 0, s[16:17]
	s_mov_b32 m0, s30
	s_nop 0
	global_load_lds_dwordx4 v[212:213], off
	s_waitcnt vmcnt(8)
	s_waitcnt lgkmcnt(0)
	s_barrier
	s_waitcnt lgkmcnt(0)
	v_mfma_f32_16x16x32_bf16 v[62:65], v[148:151], v[180:183], v[62:65]
	v_mfma_f32_16x16x32_bf16 v[58:61], v[156:159], v[180:183], v[58:61]
	v_mfma_f32_16x16x32_bf16 v[54:57], v[148:151], v[188:191], v[54:57]
	v_mfma_f32_16x16x32_bf16 v[50:53], v[156:159], v[188:191], v[50:53]
	v_mfma_f32_16x16x32_bf16 v[38:41], v[148:151], v[196:199], v[38:41]
	v_mfma_f32_16x16x32_bf16 v[34:37], v[156:159], v[196:199], v[34:37]
	v_mfma_f32_16x16x32_bf16 v[22:25], v[148:151], v[204:207], v[22:25]
	v_mfma_f32_16x16x32_bf16 v[18:21], v[156:159], v[204:207], v[18:21]
	v_mfma_f32_16x16x32_bf16 v[62:65], v[152:155], v[184:187], v[62:65]
	v_mfma_f32_16x16x32_bf16 v[58:61], v[160:163], v[184:187], v[58:61]
	v_mfma_f32_16x16x32_bf16 v[54:57], v[152:155], v[192:195], v[54:57]
	v_mfma_f32_16x16x32_bf16 v[50:53], v[160:163], v[192:195], v[50:53]
	v_mfma_f32_16x16x32_bf16 v[38:41], v[152:155], v[200:203], v[38:41]
	v_mfma_f32_16x16x32_bf16 v[34:37], v[160:163], v[200:203], v[34:37]
	v_mfma_f32_16x16x32_bf16 v[22:25], v[152:155], v[208:211], v[22:25]
	v_mfma_f32_16x16x32_bf16 v[18:21], v[160:163], v[208:211], v[18:21]
	v_mfma_f32_16x16x32_bf16 v[46:49], v[164:167], v[180:183], v[46:49]
	v_mfma_f32_16x16x32_bf16 v[42:45], v[172:175], v[180:183], v[42:45]
	v_mfma_f32_16x16x32_bf16 v[30:33], v[164:167], v[188:191], v[30:33]
	v_mfma_f32_16x16x32_bf16 v[26:29], v[172:175], v[188:191], v[26:29]
	v_mfma_f32_16x16x32_bf16 v[14:17], v[164:167], v[196:199], v[14:17]
	v_mfma_f32_16x16x32_bf16 v[10:13], v[172:175], v[196:199], v[10:13]
	v_mfma_f32_16x16x32_bf16 v[6:9], v[164:167], v[204:207], v[6:9]
	v_mfma_f32_16x16x32_bf16 v[2:5], v[172:175], v[204:207], v[2:5]
	v_mfma_f32_16x16x32_bf16 v[46:49], v[168:171], v[184:187], v[46:49]
	v_mfma_f32_16x16x32_bf16 v[42:45], v[176:179], v[184:187], v[42:45]
	v_mfma_f32_16x16x32_bf16 v[30:33], v[168:171], v[192:195], v[30:33]
	v_mfma_f32_16x16x32_bf16 v[26:29], v[176:179], v[192:195], v[26:29]
	v_mfma_f32_16x16x32_bf16 v[14:17], v[168:171], v[200:203], v[14:17]
	v_mfma_f32_16x16x32_bf16 v[10:13], v[176:179], v[200:203], v[10:13]
	v_mfma_f32_16x16x32_bf16 v[6:9], v[168:171], v[208:211], v[6:9]
	v_mfma_f32_16x16x32_bf16 v[2:5], v[176:179], v[208:211], v[2:5]
	s_barrier
	s_add_i32 s34, s34, 2
	s_add_u32 s20, s20, 0x100
	s_addc_u32 s21, s21, 0
	s_cmp_gt_u32 s34, 5
	s_cbranch_scc0 .LBB0_865
	s_cmpk_lt_u32 s0, 0x100
	s_cbranch_scc0 .LBB0_868
	s_barrier
; #define LAS __attribute__((address_space(3)))
; __device__ __forceinline__ unsigned cvt_pk_bf16(float lo, float hi) { const f32x2 v = {lo, hi}; return __builtin_bit_cast(unsigned, __builtin_convertvector(v, bf16x2_t)); }
; #define PG8_WAIT_V(n) asm volatile("s_waitcnt vmcnt(" #n ")" ::: "memory")
; #define PG8_BAR __builtin_amdgcn_s_barrier()
; template <class Epi, class Sched, bool GATHER, bool LIGHTSKIP = false>
; __device__ __forceinline__ void gemm_phase(LAS unsigned char* lds, LAS unsigned char* xl, const int lda, const int ldb, const int K, const Sched& S, const Epi& E) {
;     ...
;     PG8_WAIT_V(0);
;     PG8_BAR;
;     __device__ __forceinline__ void operator()(Acc& acc, const GUnit& u, int wr, int wc, int fr, int fq, LAS unsigned char*, int, int) const {
;         const int row0 = u.x0 + wr * 64 + fr, col0 = u.x1 + wc * 32 + 8 * fq;
; #pragma unroll
;         for (int ai = 0; ai < 2; ++ai)
; #pragma unroll
;             for (int m = 0; m < 4; ++m) { bf16_t* rowp = O + (size_t)(row0 + ai * HALF + m * 16) * ldc + col0;
; #pragma unroll
;                 for (int bj = 0; bj < 2; ++bj) { const f32x4 v0 = acc[ai][bj][m][0], v1 = acc[ai][bj][m][1];
;                     u32x4 w; w.x = cvt_pk_bf16(v0[0], v0[1]); w.y = cvt_pk_bf16(v0[2], v0[3]); w.z = cvt_pk_bf16(v1[0], v1[1]); w.w = cvt_pk_bf16(v1[2], v1[3]);
;                     if constexpr (NT) __builtin_nontemporal_store(w, (u32x4*)(rowp + bj * HALF)); else *(u32x4*)(rowp + bj * HALF) = w; } }
.LBB0_868:
	s_lshl_b32 s0, s3, 8
	s_lshl_b32 s2, s2, 11
	s_or_b32 s0, s2, s0
	v_add_u32_e32 v130, s0, v1
	s_add_u32 s2, s10, 0x2c810000
	v_lshl_or_b32 v1, s1, 8, v142
	v_ashrrev_i32_e32 v131, 31, v130
	s_addc_u32 s3, s11, 0
	v_or_b32_e32 v1, s26, v1
	v_lshlrev_b64 v[132:133], 11, v[130:131]
	v_lshl_add_u64 v[132:133], s[2:3], 0, v[132:133]
	v_lshlrev_b32_e32 v134, 1, v1
	v_mov_b32_e32 v135, 0
	v_lshl_add_u64 v[132:133], v[132:133], 0, v[134:135]
	s_mov_b64 s[0:1], 0x40000
	v_cvt_pk_bf16_f32 v70, v70, v71
	v_cvt_pk_bf16_f32 v71, v72, v73
	v_cvt_pk_bf16_f32 v72, v66, v67
	v_lshl_add_u64 v[66:67], v[132:133], 0, s[0:1]
	s_mov_b32 s0, 0x40000
	v_cvt_pk_bf16_f32 v62, v62, v63
	v_cvt_pk_bf16_f32 v63, v64, v65
	v_cvt_pk_bf16_f32 v64, v58, v59
	v_add_co_u32_e32 v58, vcc, s0, v132
	v_cvt_pk_bf16_f32 v46, v46, v47
	v_cvt_pk_bf16_f32 v47, v48, v49
	v_cvt_pk_bf16_f32 v48, v42, v43
	v_cvt_pk_bf16_f32 v49, v44, v45
	s_mov_b64 s[0:1], 0x48000
	v_cvt_pk_bf16_f32 v110, v110, v111
	v_cvt_pk_bf16_f32 v111, v112, v113
	v_cvt_pk_bf16_f32 v112, v106, v107
	v_or_b32_e32 v106, 16, v130
	v_addc_co_u32_e32 v59, vcc, 0, v133, vcc
	global_store_dwordx4 v[66:67], v[46:49], off offset:256
	v_ashrrev_i32_e32 v107, 31, v106
	v_cvt_pk_bf16_f32 v94, v94, v95
	v_lshl_add_u64 v[46:47], v[132:133], 0, s[0:1]
	s_mov_b32 s0, 0x48000
	v_cvt_pk_bf16_f32 v95, v96, v97
	v_cvt_pk_bf16_f32 v96, v90, v91
	v_or_b32_e32 v90, 32, v130
	v_add_co_u32_e32 v48, vcc, s0, v132
	v_cvt_pk_bf16_f32 v30, v30, v31
	v_cvt_pk_bf16_f32 v31, v32, v33
	v_cvt_pk_bf16_f32 v32, v26, v27
	v_cvt_pk_bf16_f32 v33, v28, v29
	s_mov_b64 s[0:1], 0x50000
	v_lshlrev_b64 v[106:107], 11, v[106:107]
	v_ashrrev_i32_e32 v91, 31, v90
	v_cvt_pk_bf16_f32 v78, v78, v79
	v_cvt_pk_bf16_f32 v79, v80, v81
	v_cvt_pk_bf16_f32 v80, v74, v75
	v_or_b32_e32 v74, 48, v130
	v_addc_co_u32_e32 v49, vcc, 0, v133, vcc
	global_store_dwordx4 v[46:47], v[30:33], off offset:256
	v_cvt_pk_bf16_f32 v113, v108, v109
	v_lshl_add_u64 v[106:107], s[2:3], 0, v[106:107]
	v_lshl_add_u64 v[30:31], v[132:133], 0, s[0:1]
	s_mov_b32 s0, 0x50000
	v_lshlrev_b64 v[90:91], 11, v[90:91]
	v_ashrrev_i32_e32 v75, 31, v74
	v_add_co_u32_e32 v32, vcc, s0, v132
	v_cvt_pk_bf16_f32 v14, v14, v15
	v_cvt_pk_bf16_f32 v15, v16, v17
	v_cvt_pk_bf16_f32 v16, v10, v11
	v_cvt_pk_bf16_f32 v17, v12, v13
	s_mov_b64 s[0:1], 0x58000
	global_store_dwordx4 v[132:133], v[110:113], off offset:256
	v_cvt_pk_bf16_f32 v97, v92, v93
	v_lshl_add_u64 v[90:91], s[2:3], 0, v[90:91]
	v_lshl_add_u64 v[110:111], v[106:107], 0, v[134:135]
	v_lshlrev_b64 v[74:75], 11, v[74:75]
	v_addc_co_u32_e32 v33, vcc, 0, v133, vcc
	global_store_dwordx4 v[30:31], v[14:17], off offset:256
	global_store_dwordx4 v[110:111], v[94:97], off offset:256
	v_cvt_pk_bf16_f32 v81, v76, v77
	v_lshl_add_u64 v[14:15], v[132:133], 0, s[0:1]
	s_mov_b32 s0, 0x58000
	v_lshl_add_u64 v[94:95], v[90:91], 0, v[134:135]
	v_lshl_add_u64 v[74:75], s[2:3], 0, v[74:75]
	v_add_co_u32_e32 v16, vcc, s0, v132
	v_cvt_pk_bf16_f32 v126, v126, v127
	v_cvt_pk_bf16_f32 v127, v128, v129
	v_cvt_pk_bf16_f32 v128, v122, v123
	v_cvt_pk_bf16_f32 v129, v124, v125
	v_cvt_pk_bf16_f32 v106, v118, v119
	v_cvt_pk_bf16_f32 v107, v120, v121
	v_cvt_pk_bf16_f32 v108, v114, v115
	v_cvt_pk_bf16_f32 v109, v116, v117
	v_cvt_pk_bf16_f32 v90, v102, v103
	v_cvt_pk_bf16_f32 v91, v104, v105
	v_cvt_pk_bf16_f32 v92, v98, v99
	v_cvt_pk_bf16_f32 v93, v100, v101
	global_store_dwordx4 v[94:95], v[78:81], off offset:256
	v_cvt_pk_bf16_f32 v76, v82, v83
	v_cvt_pk_bf16_f32 v77, v84, v85
	v_lshl_add_u64 v[78:79], v[74:75], 0, v[134:135]
	v_cvt_pk_bf16_f32 v74, v86, v87
	v_cvt_pk_bf16_f32 v75, v88, v89
	v_cvt_pk_bf16_f32 v73, v68, v69
	v_cvt_pk_bf16_f32 v65, v60, v61
	v_cvt_pk_bf16_f32 v42, v54, v55
	v_cvt_pk_bf16_f32 v43, v56, v57
	v_cvt_pk_bf16_f32 v44, v50, v51
	v_cvt_pk_bf16_f32 v45, v52, v53
	v_cvt_pk_bf16_f32 v26, v38, v39
	v_cvt_pk_bf16_f32 v27, v40, v41
	v_cvt_pk_bf16_f32 v28, v34, v35
	v_cvt_pk_bf16_f32 v29, v36, v37
	v_cvt_pk_bf16_f32 v10, v22, v23
	v_cvt_pk_bf16_f32 v11, v24, v25
	v_cvt_pk_bf16_f32 v12, v18, v19
	v_cvt_pk_bf16_f32 v13, v20, v21
	v_addc_co_u32_e32 v17, vcc, 0, v133, vcc
	v_cvt_pk_bf16_f32 v6, v6, v7
	v_cvt_pk_bf16_f32 v7, v8, v9
	v_cvt_pk_bf16_f32 v8, v2, v3
	v_cvt_pk_bf16_f32 v9, v4, v5
	global_store_dwordx4 v[132:133], v[126:129], off
	global_store_dwordx4 v[110:111], v[106:109], off
	global_store_dwordx4 v[94:95], v[90:93], off
	global_store_dwordx4 v[78:79], v[74:77], off
	global_store_dwordx4 v[78:79], v[70:73], off offset:256
	global_store_dwordx4 v[58:59], v[62:65], off
	global_store_dwordx4 v[48:49], v[42:45], off
	global_store_dwordx4 v[32:33], v[26:29], off
	global_store_dwordx4 v[16:17], v[10:13], off
	global_store_dwordx4 v[14:15], v[6:9], off offset:256
	s_waitcnt vmcnt(0)
	s_barrier
	s_setprio 0

; __device__ __forceinline__ int otid() { int t = threadIdx.x; asm volatile("" : "+v"(t)); return t; }
; #define PG8_STAGE_B(b, h, bp) PG8_STAGE2(PG8_SB(b, h), (bp) + (h) * hstepB, voffB[0], voffB[1])
; #define PG8_STAGE_A(b, h, ap, NX) do { if constexpr (GATHER) { const unsigned _o0 = (NX) ? vn[h][0] : vc[h][0], _o1 = (NX) ? vn[h][1] : vc[h][1]; PG8_STAGE2(PG8_SA(b, h), (ap), _o0, _o1); } \
;         else { PG8_STAGE2(PG8_SA(b, h), (ap) + (h) * hstepA, voffA[0], voffA[1]); } } while (0)
; #define PG8_BAR __builtin_amdgcn_s_barrier()
; template <class Epi, class Sched, bool GATHER, bool LIGHTSKIP = false>
; __device__ __forceinline__ void gemm_phase(LAS unsigned char* lds, LAS unsigned char* xl, const int lda, const int ldb, const int K, const Sched& S, const Epi& E) {
;     const int tid = otid(), wid = __builtin_amdgcn_readfirstlane(tid >> 6), lane = tid & 63, wr = wid >> 2, wc = wid & 3, fr = lane & 15, fq = lane >> 4;
;     const int nt = K / BK;
;     int Rr[2], Cc[2]; unsigned voffA[2], voffB[2];
; #pragma unroll
;     for (int i = 0; i < 2; ++i) { stage_rc(tid * 16 + i * 8192, Rr[i], Cc[i]); const int Rb = Epi::PERM ? ((Rr[i] & ~31) + perm32(Rr[i] & 31)) : Rr[i];
;         voffA[i] = (unsigned)(Rr[i] * lda + Cc[i]) * 2u; voffB[i] = (unsigned)(Rb * ldb + Cc[i]) * 2u; }
;     unsigned vc[2][2], vn[2][2];
;     const size_t kstep = (size_t)(BK * 2);
;     const size_t hstepA = (size_t)HALF * lda * 2, hstepB = (size_t)HALF * ldb * 2;
;     const unsigned ldsw = (unsigned)wid * 1024u;
;     const int aoff = lds_byte(wr * 64 + fr, fq * 8), boff = lds_byte(wc * 32 + fr, fq * 8);
;     ...
;     GUnit cur, nxt; int ui = 0;
;     if (!S.next(0, cur)) return;
;     Acc acc;
; #pragma unroll
;     for (int a = 0; a < 2; ++a)
; #pragma unroll
;         for (int b = 0; b < 2; ++b)
; #pragma unroll
;             for (int m = 0; m < 4; ++m)
; #pragma unroll
;                 for (int n = 0; n < 2; ++n) acc[a][b][m][n] = (f32x4){0.f, 0.f, 0.f, 0.f};
;     bf16x8 At[4][2], B0[2][2], B1[2][2];
;     const char* cA = cur.A; const char* cB = cur.B;
;     if constexpr (GATHER) { S.offsets(cur, lda, vc);
; #pragma unroll
;         for (int h = 0; h < 2; ++h) { vn[h][0] = vc[h][0]; vn[h][1] = vc[h][1]; } }
;     PG8_STAGE_B(0, 0, cB); PG8_STAGE_B(0, 1, cB); PG8_STAGE_A(0, 0, cA, false); PG8_STAGE_A(0, 1, cA, false);
;     if (wr == 1) PG8_BAR;
;     PG8_WAIT_V(2); PG8_BAR;
.LBB0_930:
	v_ashrrev_i32_e32 v2, 31, v10
	v_lshrrev_b32_e32 v2, 26, v2
	v_add_u32_e32 v2, v10, v2
	v_ashrrev_i32_e32 v11, 6, v2
	v_bfe_i32 v2, v10, 27, 1
	v_lshlrev_b32_e32 v1, 4, v10
	v_lshrrev_b32_e32 v2, 22, v2
	v_add_u32_e32 v2, v1, v2
	v_and_b32_e32 v2, 0xfffffc00, v2
	v_sub_u32_e32 v2, v1, v2
	v_lshrrev_b32_e32 v3, 4, v2
	v_bitop3_b32 v3, v3, v2, 32 bitop3:0x6c
	v_ashrrev_i32_e32 v2, 31, v2
	v_lshrrev_b32_e32 v2, 26, v2
	v_add_u32_e32 v2, v3, v2
	v_ashrrev_i32_e32 v12, 6, v2
	v_lshlrev_b32_e32 v4, 3, v11
	v_mul_i32_i24_e32 v5, 64, v12
	v_and_b32_e32 v4, -16, v4
	v_sub_u32_e32 v3, v3, v5
	v_mov_b32_e32 v5, 1
	v_add_u32_e32 v2, v12, v4
	v_lshlrev_b32_e32 v4, 5, v11
	v_ashrrev_i16_sdwa v3, v5, sext(v3) dst_sel:DWORD dst_unused:UNUSED_PAD src0_sel:DWORD src1_sel:BYTE_0
	v_and_b32_e32 v4, 32, v4
	v_bfe_i32 v13, v3, 0, 16
	v_and_b32_e32 v7, 3, v12
	s_mov_b32 s4, 0xfffe0
	v_add_lshl_u32 v4, v4, v13, 1
	v_add_u32_e32 v1, 0x2000, v1
	v_lshlrev_b32_e32 v3, 1, v2
	v_lshrrev_b32_e32 v6, 2, v2
	v_and_or_b32 v7, v2, s4, v7
	v_lshl_add_u32 v162, v2, 12, v4
	v_ashrrev_i32_e32 v2, 31, v1
	v_lshrrev_b32_e32 v2, 22, v2
	v_add_u32_e32 v2, v1, v2
	v_ashrrev_i32_e32 v14, 10, v2
	v_mul_i32_i24_e32 v2, 0x400, v14
	v_sub_u32_e32 v1, v1, v2
	v_and_b32_e32 v3, 24, v3
	v_and_b32_e32 v6, 4, v6
	v_lshrrev_b32_e32 v2, 4, v1
	v_or3_b32 v3, v7, v6, v3
	v_bitop3_b32 v1, v2, v1, 32 bitop3:0x6c
	v_lshl_add_u32 v164, v3, 12, v4
	v_ashrrev_i32_e32 v3, 31, v1
	v_lshrrev_b32_e32 v3, 26, v3
	v_add_u32_e32 v3, v1, v3
	v_lshlrev_b32_e32 v2, 3, v14
	v_ashrrev_i32_e32 v15, 6, v3
	v_and_b32_e32 v3, 0xc0, v3
	v_and_b32_e32 v2, -16, v2
	v_sub_u32_e32 v1, v1, v3
	s_ashr_i32 s12, s36, 6
	v_add_u32_e32 v2, v15, v2
	v_ashrrev_i16_sdwa v1, v5, sext(v1) dst_sel:DWORD dst_unused:UNUSED_PAD src0_sel:DWORD src1_sel:BYTE_0
	v_and_b32_e32 v5, 3, v15
	v_and_or_b32 v5, v2, s4, v5
	s_lshl_b32 s4, s12, 10
	v_lshlrev_b32_e32 v4, 5, v14
	v_bfe_i32 v16, v1, 0, 16
	v_lshlrev_b32_e32 v1, 1, v2
	v_lshrrev_b32_e32 v3, 2, v2
	s_add_i32 s5, s4, 0
	v_and_b32_e32 v4, 32, v4
	v_and_b32_e32 v1, 24, v1
	v_and_b32_e32 v3, 4, v3
	s_add_i32 m0, s5, 0x10000
	v_or3_b32 v1, v5, v3, v1
	v_add_lshl_u32 v3, v4, v16, 1
	s_ashr_i32 s13, s36, 8
	global_load_lds_dwordx4 v164, s[64:65]
	s_add_i32 m0, s5, 0x12000
	v_lshl_add_u32 v168, v1, 12, v3
	s_add_u32 s6, s64, 0x80000
	global_load_lds_dwordx4 v168, s[64:65]
	s_addc_u32 s7, s65, 0
	s_add_i32 m0, s5, 0x14000
	v_lshl_add_u32 v166, v2, 12, v3
	global_load_lds_dwordx4 v164, s[6:7]
	s_add_i32 m0, s5, 0x16000
	v_mov_b32_e32 v165, 0
	global_load_lds_dwordx4 v168, s[6:7]
	s_add_i32 s6, s5, 0x2000
	s_mov_b32 m0, s5
	s_add_u32 s14, s62, 0x80000
	global_load_lds_dwordx4 v162, s[62:63]
	s_mov_b32 m0, s6
	s_addc_u32 s15, s63, 0
	s_add_i32 s7, s5, 0x4000
	global_load_lds_dwordx4 v166, s[62:63]
	s_mov_b32 m0, s7
	s_add_i32 s26, s5, 0x6000
	global_load_lds_dwordx4 v162, s[14:15]
	s_mov_b32 m0, s26
	v_mov_b32_e32 v169, v165
	global_load_lds_dwordx4 v166, s[14:15]
	v_mov_b32_e32 v163, v165
	v_mov_b32_e32 v167, v165
	s_cmp_eq_u32 s13, 1
	v_lshl_add_u64 v[8:9], s[64:65], 0, v[164:165]
	s_mov_b32 s27, 0
	s_mov_b32 s33, 0x10000
	v_lshl_add_u64 v[6:7], s[64:65], 0, v[168:169]
	v_lshl_add_u64 v[2:3], s[62:63], 0, v[162:163]
	s_cselect_b64 s[14:15], -1, 0
	s_cmp_lg_u32 s13, 1
	v_lshl_add_u64 v[4:5], s[62:63], 0, v[166:167]
	s_cbranch_scc1 .LBB0_932
	s_barrier
	s_setprio 1

; #define PG8_STAGE_B(b, h, bp) PG8_STAGE2(PG8_SB(b, h), (bp) + (h) * hstepB, voffB[0], voffB[1])
; #define PG8_STAGE_A(b, h, ap, NX) do { if constexpr (GATHER) { const unsigned _o0 = (NX) ? vn[h][0] : vc[h][0], _o1 = (NX) ? vn[h][1] : vc[h][1]; PG8_STAGE2(PG8_SA(b, h), (ap), _o0, _o1); } \
;         else { PG8_STAGE2(PG8_SA(b, h), (ap) + (h) * hstepA, voffA[0], voffA[1]); } } while (0)
; #define PG8_LDA(dst, b, h) do { _Pragma("unroll") for (int m = 0; m < 4; ++m) _Pragma("unroll") for (int k = 0; k < 2; ++k) dst[m][k] = *(const LAS bf16x8*)(lds + PG8_SA(b, h) + aoff + m * 2048 + k * 1024); } while (0)
; #define PG8_LDB(dst, b, h) do { _Pragma("unroll") for (int n = 0; n < 2; ++n) _Pragma("unroll") for (int k = 0; k < 2; ++k) dst[n][k] = *(const LAS bf16x8*)(lds + PG8_SB(b, h) + boff + n * 2048 + k * 1024); } while (0)
; #define PG8_MMA(ai, bj, At, Bt) do { __builtin_amdgcn_s_setprio(1); _Pragma("unroll") for (int m = 0; m < 4; ++m) _Pragma("unroll") for (int n = 0; n < 2; ++n) _Pragma("unroll") for (int k = 0; k < 2; ++k) \
;         acc[ai][bj][m][n] = __builtin_amdgcn_mfma_f32_16x16x32_bf16(Bt[n][k], At[m][k], acc[ai][bj][m][n], 0, 0, 0); __builtin_amdgcn_s_setprio(0); } while (0)
; #define PG8_WAIT_V(n) asm volatile("s_waitcnt vmcnt(" #n ")" ::: "memory")
; #define PG8_WAIT_L(n) asm volatile("s_waitcnt lgkmcnt(" #n ")" ::: "memory")
; #define PG8_BAR __builtin_amdgcn_s_barrier()
; #define PG8_SCHED __builtin_amdgcn_sched_barrier(0)
; template <class Epi, class Sched, bool GATHER, bool LIGHTSKIP = false>
; __device__ __forceinline__ void gemm_phase(LAS unsigned char* lds, LAS unsigned char* xl, const int lda, const int ldb, const int K, const Sched& S, const Epi& E) {
;     ...
;             PG8_LDB(B0, 0, 0); PG8_LDB(B1, 0, 1); PG8_SCHED; PG8_LDA(At, 0, 0); PG8_STAGE_A(1, 1, a1, false);
;             PG8_WAIT_V(8); PG8_WAIT_L(0); PG8_BAR; PG8_MMA(0, 0, At, B0); PG8_MMA(0, 1, At, B1); PG8_BAR; PG8_SCHED;
;             PG8_LDA(At, 0, 1); PG8_STAGE_B(0, 0, b2); PG8_STAGE_B(0, 1, b2); PG8_STAGE_A(0, 0, a2, last);
;             PG8_WAIT_V(8); PG8_WAIT_L(0); PG8_BAR; if (!light) { PG8_MMA(1, 0, At, B0); PG8_MMA(1, 1, At, B1); } PG8_BAR; PG8_SCHED;
.LBB0_938:
	ds_read_b128 v[98:101], v210
	ds_read_b128 v[102:105], v210 offset:1024
	ds_read_b128 v[106:109], v210 offset:2048
	ds_read_b128 v[110:113], v210 offset:3072
	ds_read_b128 v[118:121], v211
	ds_read_b128 v[122:125], v211 offset:1024
	ds_read_b128 v[126:129], v211 offset:2048
	ds_read_b128 v[130:133], v211 offset:3072
	s_add_u32 s64, s62, 0xfff80080
	s_addc_u32 s65, s63, -1
	s_cmp_eq_u32 s86, 28
	s_cselect_b32 s67, s55, s65
	s_cselect_b32 s66, s54, s64
	s_cselect_b32 s65, s57, s85
	s_cselect_b32 s64, s56, s84
	v_lshl_add_u64 v[230:231], s[62:63], 0, v[170:171]
	s_add_i32 m0, s5, 0xc000
	ds_read_b128 v[174:177], v212
	ds_read_b128 v[178:181], v212 offset:1024
	ds_read_b128 v[182:185], v212 offset:2048
	ds_read_b128 v[186:189], v212 offset:3072
	ds_read_b128 v[214:217], v212 offset:4096
	ds_read_b128 v[218:221], v212 offset:5120
	ds_read_b128 v[222:225], v212 offset:6144
	ds_read_b128 v[226:229], v212 offset:7168
	global_load_lds_dwordx4 v[230:231], off
	v_lshl_add_u64 v[230:231], s[62:63], 0, v[172:173]
	s_add_i32 m0, s5, 0xe000
	s_nop 0
	global_load_lds_dwordx4 v[230:231], off
	s_waitcnt vmcnt(8)
	s_waitcnt lgkmcnt(0)
	s_barrier
	s_waitcnt lgkmcnt(0)
	v_mfma_f32_16x16x32_bf16 v[158:161], v[98:101], v[174:177], v[158:161]
	v_mfma_f32_16x16x32_bf16 v[154:157], v[106:109], v[174:177], v[154:157]
	v_mfma_f32_16x16x32_bf16 v[142:145], v[98:101], v[182:185], v[142:145]
	v_mfma_f32_16x16x32_bf16 v[138:141], v[106:109], v[182:185], v[138:141]
	v_mfma_f32_16x16x32_bf16 v[94:97], v[98:101], v[214:217], v[94:97]
	v_mfma_f32_16x16x32_bf16 v[90:93], v[106:109], v[214:217], v[90:93]
	v_mfma_f32_16x16x32_bf16 v[78:81], v[98:101], v[222:225], v[78:81]
	v_mfma_f32_16x16x32_bf16 v[74:77], v[106:109], v[222:225], v[74:77]
	v_mfma_f32_16x16x32_bf16 v[158:161], v[102:105], v[178:181], v[158:161]
	v_mfma_f32_16x16x32_bf16 v[154:157], v[110:113], v[178:181], v[154:157]
	v_mfma_f32_16x16x32_bf16 v[142:145], v[102:105], v[186:189], v[142:145]
	v_mfma_f32_16x16x32_bf16 v[138:141], v[110:113], v[186:189], v[138:141]
	v_mfma_f32_16x16x32_bf16 v[94:97], v[102:105], v[218:221], v[94:97]
	v_mfma_f32_16x16x32_bf16 v[90:93], v[110:113], v[218:221], v[90:93]
	v_mfma_f32_16x16x32_bf16 v[78:81], v[102:105], v[226:229], v[78:81]
	v_mfma_f32_16x16x32_bf16 v[74:77], v[110:113], v[226:229], v[74:77]
	v_mfma_f32_16x16x32_bf16 v[150:153], v[118:121], v[174:177], v[150:153]
	v_mfma_f32_16x16x32_bf16 v[146:149], v[126:129], v[174:177], v[146:149]
	v_mfma_f32_16x16x32_bf16 v[134:137], v[118:121], v[182:185], v[134:137]
	v_mfma_f32_16x16x32_bf16 v[114:117], v[126:129], v[182:185], v[114:117]
	v_mfma_f32_16x16x32_bf16 v[86:89], v[118:121], v[214:217], v[86:89]
	v_mfma_f32_16x16x32_bf16 v[82:85], v[126:129], v[214:217], v[82:85]
	v_mfma_f32_16x16x32_bf16 v[70:73], v[118:121], v[222:225], v[70:73]
	v_mfma_f32_16x16x32_bf16 v[66:69], v[126:129], v[222:225], v[66:69]
	v_mfma_f32_16x16x32_bf16 v[150:153], v[122:125], v[178:181], v[150:153]
	v_mfma_f32_16x16x32_bf16 v[146:149], v[130:133], v[178:181], v[146:149]
	v_mfma_f32_16x16x32_bf16 v[134:137], v[122:125], v[186:189], v[134:137]
	v_mfma_f32_16x16x32_bf16 v[114:117], v[130:133], v[186:189], v[114:117]
	v_mfma_f32_16x16x32_bf16 v[86:89], v[122:125], v[218:221], v[86:89]
	v_mfma_f32_16x16x32_bf16 v[82:85], v[130:133], v[218:221], v[82:85]
	v_mfma_f32_16x16x32_bf16 v[70:73], v[122:125], v[226:229], v[70:73]
	v_mfma_f32_16x16x32_bf16 v[66:69], v[130:133], v[226:229], v[66:69]
	s_barrier
	s_add_i32 s87, s72, s4
	v_lshl_add_u64 v[230:231], s[64:65], 0, v[164:165]
	s_mov_b32 m0, s87
	ds_read_b128 v[174:177], v212 offset:16384
	ds_read_b128 v[178:181], v212 offset:17408
	ds_read_b128 v[182:185], v212 offset:18432
	ds_read_b128 v[186:189], v212 offset:19456
	ds_read_b128 v[214:217], v212 offset:20480
	ds_read_b128 v[218:221], v212 offset:21504
	ds_read_b128 v[222:225], v212 offset:22528
	ds_read_b128 v[226:229], v212 offset:23552
	global_load_lds_dwordx4 v[230:231], off
	s_add_i32 m0, s87, 0x2000
	s_add_u32 s88, s64, 0x80000
	v_lshl_add_u64 v[232:233], s[64:65], 0, v[168:169]
	s_addc_u32 s89, s65, 0
	s_add_i32 s87, s73, s4
	global_load_lds_dwordx4 v[232:233], off
	v_lshl_add_u64 v[234:235], s[88:89], 0, v[164:165]
	s_mov_b32 m0, s87
	v_lshl_add_u64 v[236:237], s[66:67], 0, v[166:167]
	global_load_lds_dwordx4 v[234:235], off
	v_lshl_add_u64 v[234:235], s[88:89], 0, v[168:169]
	s_add_i32 m0, s87, 0x2000
	s_nop 0
	global_load_lds_dwordx4 v[234:235], off
	v_lshl_add_u64 v[234:235], s[66:67], 0, v[162:163]
	s_mov_b32 m0, s5
	s_nop 0
	global_load_lds_dwordx4 v[234:235], off
	s_mov_b32 m0, s6
	s_nop 0
	global_load_lds_dwordx4 v[236:237], off
	s_waitcnt vmcnt(8)
	s_waitcnt lgkmcnt(0)
	s_barrier
; #define PG8_STAGE_A(b, h, ap, NX) do { if constexpr (GATHER) { const unsigned _o0 = (NX) ? vn[h][0] : vc[h][0], _o1 = (NX) ? vn[h][1] : vc[h][1]; PG8_STAGE2(PG8_SA(b, h), (ap), _o0, _o1); } \
;         else { PG8_STAGE2(PG8_SA(b, h), (ap) + (h) * hstepA, voffA[0], voffA[1]); } } while (0)
; #define PG8_LDA(dst, b, h) do { _Pragma("unroll") for (int m = 0; m < 4; ++m) _Pragma("unroll") for (int k = 0; k < 2; ++k) dst[m][k] = *(const LAS bf16x8*)(lds + PG8_SA(b, h) + aoff + m * 2048 + k * 1024); } while (0)
; #define PG8_LDB(dst, b, h) do { _Pragma("unroll") for (int n = 0; n < 2; ++n) _Pragma("unroll") for (int k = 0; k < 2; ++k) dst[n][k] = *(const LAS bf16x8*)(lds + PG8_SB(b, h) + boff + n * 2048 + k * 1024); } while (0)
; #define PG8_MMA(ai, bj, At, Bt) do { __builtin_amdgcn_s_setprio(1); _Pragma("unroll") for (int m = 0; m < 4; ++m) _Pragma("unroll") for (int n = 0; n < 2; ++n) _Pragma("unroll") for (int k = 0; k < 2; ++k) \
;         acc[ai][bj][m][n] = __builtin_amdgcn_mfma_f32_16x16x32_bf16(Bt[n][k], At[m][k], acc[ai][bj][m][n], 0, 0, 0); __builtin_amdgcn_s_setprio(0); } while (0)
; #define PG8_WAIT_V(n) asm volatile("s_waitcnt vmcnt(" #n ")" ::: "memory")
; #define PG8_WAIT_L(n) asm volatile("s_waitcnt lgkmcnt(" #n ")" ::: "memory")
; #define PG8_BAR __builtin_amdgcn_s_barrier()
; #define PG8_SCHED __builtin_amdgcn_sched_barrier(0)
; template <class Epi, class Sched, bool GATHER, bool LIGHTSKIP = false>
; __device__ __forceinline__ void gemm_phase(LAS unsigned char* lds, LAS unsigned char* xl, const int lda, const int ldb, const int K, const Sched& S, const Epi& E) {
;     ...
;             PG8_WAIT_V(8); PG8_WAIT_L(0); PG8_BAR; if (!light) { PG8_MMA(1, 0, At, B0); PG8_MMA(1, 1, At, B1); } PG8_BAR; PG8_SCHED;
;             PG8_LDB(B0, 1, 0); PG8_LDB(B1, 1, 1); PG8_SCHED; PG8_LDA(At, 1, 0); PG8_STAGE_A(0, 1, a2, last);
;             PG8_WAIT_V(8); PG8_WAIT_L(0); PG8_BAR; PG8_MMA(0, 0, At, B0); PG8_MMA(0, 1, At, B1); PG8_BAR; PG8_SCHED;
	s_waitcnt lgkmcnt(0)
	v_mfma_f32_16x16x32_bf16 v[62:65], v[98:101], v[174:177], v[62:65]
	v_mfma_f32_16x16x32_bf16 v[58:61], v[106:109], v[174:177], v[58:61]
	v_mfma_f32_16x16x32_bf16 v[46:49], v[98:101], v[182:185], v[46:49]
	v_mfma_f32_16x16x32_bf16 v[42:45], v[106:109], v[182:185], v[42:45]
	v_mfma_f32_16x16x32_bf16 v[30:33], v[98:101], v[214:217], v[30:33]
	v_mfma_f32_16x16x32_bf16 v[26:29], v[106:109], v[214:217], v[26:29]
	v_mfma_f32_16x16x32_bf16 v[14:17], v[98:101], v[222:225], v[14:17]
	v_mfma_f32_16x16x32_bf16 v[10:13], v[106:109], v[222:225], v[10:13]
	v_mfma_f32_16x16x32_bf16 v[62:65], v[102:105], v[178:181], v[62:65]
	v_mfma_f32_16x16x32_bf16 v[58:61], v[110:113], v[178:181], v[58:61]
	v_mfma_f32_16x16x32_bf16 v[46:49], v[102:105], v[186:189], v[46:49]
	v_mfma_f32_16x16x32_bf16 v[42:45], v[110:113], v[186:189], v[42:45]
	v_mfma_f32_16x16x32_bf16 v[30:33], v[102:105], v[218:221], v[30:33]
	v_mfma_f32_16x16x32_bf16 v[26:29], v[110:113], v[218:221], v[26:29]
	v_mfma_f32_16x16x32_bf16 v[14:17], v[102:105], v[226:229], v[14:17]
	v_mfma_f32_16x16x32_bf16 v[10:13], v[110:113], v[226:229], v[10:13]
	v_mfma_f32_16x16x32_bf16 v[54:57], v[118:121], v[174:177], v[54:57]
	v_mfma_f32_16x16x32_bf16 v[50:53], v[126:129], v[174:177], v[50:53]
	v_mfma_f32_16x16x32_bf16 v[38:41], v[118:121], v[182:185], v[38:41]
	v_mfma_f32_16x16x32_bf16 v[34:37], v[126:129], v[182:185], v[34:37]
	v_mfma_f32_16x16x32_bf16 v[22:25], v[118:121], v[214:217], v[22:25]
	v_mfma_f32_16x16x32_bf16 v[18:21], v[126:129], v[214:217], v[18:21]
	v_mfma_f32_16x16x32_bf16 v[6:9], v[118:121], v[222:225], v[6:9]
	v_mfma_f32_16x16x32_bf16 v[2:5], v[126:129], v[222:225], v[2:5]
	v_mfma_f32_16x16x32_bf16 v[54:57], v[122:125], v[178:181], v[54:57]
	v_mfma_f32_16x16x32_bf16 v[50:53], v[130:133], v[178:181], v[50:53]
	v_mfma_f32_16x16x32_bf16 v[38:41], v[122:125], v[186:189], v[38:41]
	v_mfma_f32_16x16x32_bf16 v[34:37], v[130:133], v[186:189], v[34:37]
	v_mfma_f32_16x16x32_bf16 v[22:25], v[122:125], v[218:221], v[22:25]
	v_mfma_f32_16x16x32_bf16 v[18:21], v[130:133], v[218:221], v[18:21]
	v_mfma_f32_16x16x32_bf16 v[6:9], v[122:125], v[226:229], v[6:9]
	v_mfma_f32_16x16x32_bf16 v[2:5], v[130:133], v[226:229], v[2:5]
	s_barrier
	s_add_i32 s87, 0, 0x18000
	s_add_i32 s88, 0, 0x1c000
	v_add_u32_e32 v110, s87, v190
	v_add_u32_e32 v130, s88, v190
	ds_read_b128 v[98:101], v110
	ds_read_b128 v[102:105], v110 offset:1024
	ds_read_b128 v[106:109], v110 offset:2048
	ds_read_b128 v[110:113], v110 offset:3072
	ds_read_b128 v[118:121], v130
	ds_read_b128 v[122:125], v130 offset:1024
	ds_read_b128 v[126:129], v130 offset:2048
	ds_read_b128 v[130:133], v130 offset:3072
	s_add_u32 s66, s66, 0x80000
	s_addc_u32 s67, s67, 0
	s_mov_b32 m0, s7
	v_lshl_add_u64 v[238:239], s[66:67], 0, v[162:163]
	ds_read_b128 v[174:177], v212 offset:32768
	ds_read_b128 v[178:181], v212 offset:33792
	ds_read_b128 v[182:185], v212 offset:34816
	ds_read_b128 v[186:189], v212 offset:35840
	ds_read_b128 v[214:217], v212 offset:36864
	ds_read_b128 v[218:221], v212 offset:37888
	ds_read_b128 v[222:225], v212 offset:38912
	ds_read_b128 v[226:229], v212 offset:39936
	global_load_lds_dwordx4 v[238:239], off
	v_lshl_add_u64 v[238:239], s[66:67], 0, v[166:167]
	s_mov_b32 m0, s26
	s_nop 0
	global_load_lds_dwordx4 v[238:239], off
	s_waitcnt vmcnt(8)
	s_waitcnt lgkmcnt(0)
	s_barrier
	s_waitcnt lgkmcnt(0)
	v_mfma_f32_16x16x32_bf16 v[158:161], v[98:101], v[174:177], v[158:161]
	v_mfma_f32_16x16x32_bf16 v[154:157], v[106:109], v[174:177], v[154:157]
	v_mfma_f32_16x16x32_bf16 v[142:145], v[98:101], v[182:185], v[142:145]
	v_mfma_f32_16x16x32_bf16 v[138:141], v[106:109], v[182:185], v[138:141]
	v_mfma_f32_16x16x32_bf16 v[94:97], v[98:101], v[214:217], v[94:97]
	v_mfma_f32_16x16x32_bf16 v[90:93], v[106:109], v[214:217], v[90:93]
	v_mfma_f32_16x16x32_bf16 v[78:81], v[98:101], v[222:225], v[78:81]
	v_mfma_f32_16x16x32_bf16 v[74:77], v[106:109], v[222:225], v[74:77]
	v_mfma_f32_16x16x32_bf16 v[158:161], v[102:105], v[178:181], v[158:161]
	v_mfma_f32_16x16x32_bf16 v[154:157], v[110:113], v[178:181], v[154:157]
	v_mfma_f32_16x16x32_bf16 v[142:145], v[102:105], v[186:189], v[142:145]
	v_mfma_f32_16x16x32_bf16 v[138:141], v[110:113], v[186:189], v[138:141]
	v_mfma_f32_16x16x32_bf16 v[94:97], v[102:105], v[218:221], v[94:97]
	v_mfma_f32_16x16x32_bf16 v[90:93], v[110:113], v[218:221], v[90:93]
	v_mfma_f32_16x16x32_bf16 v[78:81], v[102:105], v[226:229], v[78:81]
	v_mfma_f32_16x16x32_bf16 v[74:77], v[110:113], v[226:229], v[74:77]
	v_mfma_f32_16x16x32_bf16 v[150:153], v[118:121], v[174:177], v[150:153]
	v_mfma_f32_16x16x32_bf16 v[146:149], v[126:129], v[174:177], v[146:149]
	v_mfma_f32_16x16x32_bf16 v[134:137], v[118:121], v[182:185], v[134:137]
	v_mfma_f32_16x16x32_bf16 v[114:117], v[126:129], v[182:185], v[114:117]
	v_mfma_f32_16x16x32_bf16 v[86:89], v[118:121], v[214:217], v[86:89]
	v_mfma_f32_16x16x32_bf16 v[82:85], v[126:129], v[214:217], v[82:85]
	v_mfma_f32_16x16x32_bf16 v[70:73], v[118:121], v[222:225], v[70:73]
	v_mfma_f32_16x16x32_bf16 v[66:69], v[126:129], v[222:225], v[66:69]
	v_mfma_f32_16x16x32_bf16 v[150:153], v[122:125], v[178:181], v[150:153]
	v_mfma_f32_16x16x32_bf16 v[146:149], v[130:133], v[178:181], v[146:149]
	v_mfma_f32_16x16x32_bf16 v[134:137], v[122:125], v[186:189], v[134:137]
	v_mfma_f32_16x16x32_bf16 v[114:117], v[130:133], v[186:189], v[114:117]
	v_mfma_f32_16x16x32_bf16 v[86:89], v[122:125], v[218:221], v[86:89]
	v_mfma_f32_16x16x32_bf16 v[82:85], v[130:133], v[218:221], v[82:85]
	v_mfma_f32_16x16x32_bf16 v[70:73], v[122:125], v[226:229], v[70:73]
	v_mfma_f32_16x16x32_bf16 v[66:69], v[130:133], v[226:229], v[66:69]
	s_barrier
; #define PG8_STAGE_B(b, h, bp) PG8_STAGE2(PG8_SB(b, h), (bp) + (h) * hstepB, voffB[0], voffB[1])
; #define PG8_STAGE_A(b, h, ap, NX) do { if constexpr (GATHER) { const unsigned _o0 = (NX) ? vn[h][0] : vc[h][0], _o1 = (NX) ? vn[h][1] : vc[h][1]; PG8_STAGE2(PG8_SA(b, h), (ap), _o0, _o1); } \
;         else { PG8_STAGE2(PG8_SA(b, h), (ap) + (h) * hstepA, voffA[0], voffA[1]); } } while (0)
; #define PG8_LDA(dst, b, h) do { _Pragma("unroll") for (int m = 0; m < 4; ++m) _Pragma("unroll") for (int k = 0; k < 2; ++k) dst[m][k] = *(const LAS bf16x8*)(lds + PG8_SA(b, h) + aoff + m * 2048 + k * 1024); } while (0)
; #define PG8_MMA(ai, bj, At, Bt) do { __builtin_amdgcn_s_setprio(1); _Pragma("unroll") for (int m = 0; m < 4; ++m) _Pragma("unroll") for (int n = 0; n < 2; ++n) _Pragma("unroll") for (int k = 0; k < 2; ++k) \
;         acc[ai][bj][m][n] = __builtin_amdgcn_mfma_f32_16x16x32_bf16(Bt[n][k], At[m][k], acc[ai][bj][m][n], 0, 0, 0); __builtin_amdgcn_s_setprio(0); } while (0)
; #define PG8_WAIT_V(n) asm volatile("s_waitcnt vmcnt(" #n ")" ::: "memory")
; #define PG8_WAIT_L(n) asm volatile("s_waitcnt lgkmcnt(" #n ")" ::: "memory")
; #define PG8_BAR __builtin_amdgcn_s_barrier()
; #define PG8_SCHED __builtin_amdgcn_sched_barrier(0)
; template <class Epi, class Sched, bool GATHER, bool LIGHTSKIP = false>
; __device__ __forceinline__ void gemm_phase(LAS unsigned char* lds, LAS unsigned char* xl, const int lda, const int ldb, const int K, const Sched& S, const Epi& E) {
;     ...
;             PG8_LDA(At, 1, 1); PG8_STAGE_B(1, 0, b3); PG8_STAGE_B(1, 1, b3); PG8_STAGE_A(1, 0, a3, last);
;             PG8_WAIT_V(8); PG8_WAIT_L(0); PG8_BAR; if (!light) { PG8_MMA(1, 0, At, B0); PG8_MMA(1, 1, At, B1); } PG8_BAR; PG8_SCHED;
;         }
;         if (wr == 0) PG8_BAR;
	s_add_i32 s66, s87, s4
	v_lshl_add_u64 v[230:231], v[230:231], 0, s[30:31]
	s_mov_b32 m0, s66
	ds_read_b128 v[174:177], v212 offset:49152
	ds_read_b128 v[178:181], v212 offset:50176
	ds_read_b128 v[182:185], v212 offset:51200
	ds_read_b128 v[186:189], v212 offset:52224
	ds_read_b128 v[214:217], v212 offset:53248
	ds_read_b128 v[218:221], v212 offset:54272
	ds_read_b128 v[222:225], v212 offset:55296
	ds_read_b128 v[226:229], v212 offset:56320
	global_load_lds_dwordx4 v[230:231], off
	s_add_i32 m0, s66, 0x2000
	s_add_u32 s64, s64, 0x80080
	v_lshl_add_u64 v[230:231], v[232:233], 0, s[30:31]
	s_addc_u32 s65, s65, 0
	s_add_i32 s66, s88, s4
	global_load_lds_dwordx4 v[230:231], off
	v_lshl_add_u64 v[230:231], s[64:65], 0, v[164:165]
	s_mov_b32 m0, s66
	s_nop 0
	global_load_lds_dwordx4 v[230:231], off
	v_lshl_add_u64 v[230:231], s[64:65], 0, v[168:169]
	s_add_i32 m0, s66, 0x2000
	s_nop 0
	global_load_lds_dwordx4 v[230:231], off
	v_lshl_add_u64 v[230:231], v[234:235], 0, s[30:31]
	s_mov_b32 m0, s69
	s_nop 0
	global_load_lds_dwordx4 v[230:231], off
	v_lshl_add_u64 v[230:231], v[236:237], 0, s[30:31]
	s_mov_b32 m0, s70
	s_nop 0
	global_load_lds_dwordx4 v[230:231], off
	s_waitcnt vmcnt(8)
	s_waitcnt lgkmcnt(0)
	s_barrier
	s_waitcnt lgkmcnt(0)
	v_mfma_f32_16x16x32_bf16 v[62:65], v[98:101], v[174:177], v[62:65]
	v_mfma_f32_16x16x32_bf16 v[58:61], v[106:109], v[174:177], v[58:61]
	v_mfma_f32_16x16x32_bf16 v[46:49], v[98:101], v[182:185], v[46:49]
	v_mfma_f32_16x16x32_bf16 v[42:45], v[106:109], v[182:185], v[42:45]
	v_mfma_f32_16x16x32_bf16 v[30:33], v[98:101], v[214:217], v[30:33]
	v_mfma_f32_16x16x32_bf16 v[26:29], v[106:109], v[214:217], v[26:29]
	v_mfma_f32_16x16x32_bf16 v[14:17], v[98:101], v[222:225], v[14:17]
	v_mfma_f32_16x16x32_bf16 v[10:13], v[106:109], v[222:225], v[10:13]
	v_mfma_f32_16x16x32_bf16 v[62:65], v[102:105], v[178:181], v[62:65]
	v_mfma_f32_16x16x32_bf16 v[58:61], v[110:113], v[178:181], v[58:61]
	v_mfma_f32_16x16x32_bf16 v[46:49], v[102:105], v[186:189], v[46:49]
	v_mfma_f32_16x16x32_bf16 v[42:45], v[110:113], v[186:189], v[42:45]
	v_mfma_f32_16x16x32_bf16 v[30:33], v[102:105], v[218:221], v[30:33]
	v_mfma_f32_16x16x32_bf16 v[26:29], v[110:113], v[218:221], v[26:29]
	v_mfma_f32_16x16x32_bf16 v[14:17], v[102:105], v[226:229], v[14:17]
	v_mfma_f32_16x16x32_bf16 v[10:13], v[110:113], v[226:229], v[10:13]
	v_mfma_f32_16x16x32_bf16 v[54:57], v[118:121], v[174:177], v[54:57]
	v_mfma_f32_16x16x32_bf16 v[50:53], v[126:129], v[174:177], v[50:53]
	v_mfma_f32_16x16x32_bf16 v[38:41], v[118:121], v[182:185], v[38:41]
	v_mfma_f32_16x16x32_bf16 v[34:37], v[126:129], v[182:185], v[34:37]
	v_mfma_f32_16x16x32_bf16 v[22:25], v[118:121], v[214:217], v[22:25]
	v_mfma_f32_16x16x32_bf16 v[18:21], v[126:129], v[214:217], v[18:21]
	v_mfma_f32_16x16x32_bf16 v[6:9], v[118:121], v[222:225], v[6:9]
	v_mfma_f32_16x16x32_bf16 v[2:5], v[126:129], v[222:225], v[2:5]
	v_mfma_f32_16x16x32_bf16 v[54:57], v[122:125], v[178:181], v[54:57]
	v_mfma_f32_16x16x32_bf16 v[50:53], v[130:133], v[178:181], v[50:53]
	v_mfma_f32_16x16x32_bf16 v[38:41], v[122:125], v[186:189], v[38:41]
	v_mfma_f32_16x16x32_bf16 v[34:37], v[130:133], v[186:189], v[34:37]
	v_mfma_f32_16x16x32_bf16 v[22:25], v[122:125], v[218:221], v[22:25]
	v_mfma_f32_16x16x32_bf16 v[18:21], v[130:133], v[218:221], v[18:21]
	v_mfma_f32_16x16x32_bf16 v[6:9], v[122:125], v[226:229], v[6:9]
	v_mfma_f32_16x16x32_bf16 v[2:5], v[130:133], v[226:229], v[2:5]
	s_barrier
	s_add_i32 s86, s86, 2
	s_add_u32 s62, s62, 0x100
	s_addc_u32 s63, s63, 0
	s_add_u32 s84, s84, 0x100
	s_addc_u32 s85, s85, 0
	s_cmp_gt_u32 s86, 29
	s_cbranch_scc0 .LBB0_938
	s_and_b64 vcc, exec, s[34:35]
	s_cbranch_vccz .LBB0_941
	s_barrier

; #define PG8_WAIT_V(n) asm volatile("s_waitcnt vmcnt(" #n ")" ::: "memory")
; #define PG8_BAR __builtin_amdgcn_s_barrier()
; __device__ __forceinline__ void xcd_barrier(const XcdBarrier& b) {
;     asm volatile("s_waitcnt vmcnt(0)" ::: "memory");
;     __syncthreads();
;     if (threadIdx.x == 0) {
;         unsigned* bar = b.bar;
;         __builtin_amdgcn_s_waitcnt(0);
;         unsigned nloc = b.st[0], nx = b.st[1];
;         if (nloc == 0u) { xcd_barrier_complete(bar, b.x, nloc, nx); b.st[0] = nloc; b.st[1] = nx; }
; template <class Epi, class Sched, bool GATHER, bool LIGHTSKIP = false>
; __device__ __forceinline__ void gemm_phase(LAS unsigned char* lds, LAS unsigned char* xl, const int lda, const int ldb, const int K, const Sched& S, const Epi& E) {
;     ...
;     PG8_WAIT_V(0);
;     PG8_BAR;
.LBB0_964:
	s_waitcnt vmcnt(0)
	s_barrier
	s_setprio 0
	s_mov_b64 s[10:11], exec
	v_readlane_b32 s0, v240, 0
	v_readlane_b32 s1, v240, 1
	s_and_b64 s[0:1], s[10:11], s[0:1]
	s_mov_b64 exec, s[0:1]
	s_cbranch_execz .LBB0_1016
	s_add_i32 s0, 0, 0x25ff0
	v_mov_b32_e32 v1, s0
	s_waitcnt vmcnt(0) expcnt(0) lgkmcnt(0)
	ds_read_b32 v3, v1
	s_add_i32 s0, 0, 0x25ff4
	v_mov_b32_e32 v1, s0
	ds_read_b32 v1, v1
	s_waitcnt lgkmcnt(1)
	v_cmp_ne_u32_e32 vcc, 0, v3
	s_cbranch_vccnz .LBB0_980
	s_add_u32 s12, s24, 0x1000
	s_load_dwordx2 s[0:1], s[96:97], 0x4
	s_addc_u32 s13, s25, 0
	s_add_u32 s14, s24, 0x1100
	s_addc_u32 s15, s25, 0
	s_add_u32 s16, s24, 0x1200
	s_addc_u32 s17, s25, 0
	s_waitcnt lgkmcnt(0)
	s_mul_i32 s0, s0, s94
	s_add_u32 s18, s24, 0x1300
	s_mul_i32 s0, s0, s1
	s_addc_u32 s19, s25, 0
	s_mov_b32 s1, 1
	v_mov_b32_e32 v17, 0
	s_branch .LBB0_968

; __device__ __forceinline__ int otid() { int t = threadIdx.x; asm volatile("" : "+v"(t)); return t; }
; #define PG8_STAGE_B(b, h, bp) PG8_STAGE2(PG8_SB(b, h), (bp) + (h) * hstepB, voffB[0], voffB[1])
; #define PG8_STAGE_A(b, h, ap, NX) do { if constexpr (GATHER) { const unsigned _o0 = (NX) ? vn[h][0] : vc[h][0], _o1 = (NX) ? vn[h][1] : vc[h][1]; PG8_STAGE2(PG8_SA(b, h), (ap), _o0, _o1); } \
;         else { PG8_STAGE2(PG8_SA(b, h), (ap) + (h) * hstepA, voffA[0], voffA[1]); } } while (0)
; #define PG8_BAR __builtin_amdgcn_s_barrier()
; template <class Epi, class Sched, bool GATHER, bool LIGHTSKIP = false>
; __device__ __forceinline__ void gemm_phase(LAS unsigned char* lds, LAS unsigned char* xl, const int lda, const int ldb, const int K, const Sched& S, const Epi& E) {
;     const int tid = otid(), wid = __builtin_amdgcn_readfirstlane(tid >> 6), lane = tid & 63, wr = wid >> 2, wc = wid & 3, fr = lane & 15, fq = lane >> 4;
;     const int nt = K / BK;
;     int Rr[2], Cc[2]; unsigned voffA[2], voffB[2];
; #pragma unroll
;     for (int i = 0; i < 2; ++i) { stage_rc(tid * 16 + i * 8192, Rr[i], Cc[i]); const int Rb = Epi::PERM ? ((Rr[i] & ~31) + perm32(Rr[i] & 31)) : Rr[i];
;         voffA[i] = (unsigned)(Rr[i] * lda + Cc[i]) * 2u; voffB[i] = (unsigned)(Rb * ldb + Cc[i]) * 2u; }
;     unsigned vc[2][2], vn[2][2];
;     const size_t kstep = (size_t)(BK * 2);
;     const size_t hstepA = (size_t)HALF * lda * 2, hstepB = (size_t)HALF * ldb * 2;
;     const unsigned ldsw = (unsigned)wid * 1024u;
;     const int aoff = lds_byte(wr * 64 + fr, fq * 8), boff = lds_byte(wc * 32 + fr, fq * 8);
;     ...
;     GUnit cur, nxt; int ui = 0;
;     if (!S.next(0, cur)) return;
;     Acc acc;
; #pragma unroll
;     for (int a = 0; a < 2; ++a)
; #pragma unroll
;         for (int b = 0; b < 2; ++b)
; #pragma unroll
;             for (int m = 0; m < 4; ++m)
; #pragma unroll
;                 for (int n = 0; n < 2; ++n) acc[a][b][m][n] = (f32x4){0.f, 0.f, 0.f, 0.f};
;     bf16x8 At[4][2], B0[2][2], B1[2][2];
;     const char* cA = cur.A; const char* cB = cur.B;
;     if constexpr (GATHER) { S.offsets(cur, lda, vc);
; #pragma unroll
;         for (int h = 0; h < 2; ++h) { vn[h][0] = vc[h][0]; vn[h][1] = vc[h][1]; } }
;     PG8_STAGE_B(0, 0, cB); PG8_STAGE_B(0, 1, cB); PG8_STAGE_A(0, 0, cA, false); PG8_STAGE_A(0, 1, cA, false);
;     if (wr == 1) PG8_BAR;
;     PG8_WAIT_V(2); PG8_BAR;
.LBB0_1019:
	v_ashrrev_i32_e32 v2, 31, v10
	v_lshrrev_b32_e32 v2, 26, v2
	v_add_u32_e32 v2, v10, v2
	v_ashrrev_i32_e32 v11, 6, v2
	v_bfe_i32 v2, v10, 27, 1
	v_lshlrev_b32_e32 v1, 4, v10
	v_lshrrev_b32_e32 v2, 22, v2
	v_add_u32_e32 v2, v1, v2
	v_and_b32_e32 v2, 0xfffffc00, v2
	v_sub_u32_e32 v2, v1, v2
	v_lshrrev_b32_e32 v3, 4, v2
	v_bitop3_b32 v3, v3, v2, 32 bitop3:0x6c
	v_ashrrev_i32_e32 v2, 31, v2
	v_lshrrev_b32_e32 v2, 26, v2
	v_add_u32_e32 v2, v3, v2
	v_ashrrev_i32_e32 v12, 6, v2
	v_lshlrev_b32_e32 v4, 3, v11
	v_mul_i32_i24_e32 v5, 64, v12
	v_and_b32_e32 v4, -16, v4
	v_sub_u32_e32 v3, v3, v5
	v_mov_b32_e32 v5, 1
	v_add_u32_e32 v2, v12, v4
	v_lshlrev_b32_e32 v4, 5, v11
	v_ashrrev_i16_sdwa v3, v5, sext(v3) dst_sel:DWORD dst_unused:UNUSED_PAD src0_sel:DWORD src1_sel:BYTE_0
	v_and_b32_e32 v4, 32, v4
	v_bfe_i32 v13, v3, 0, 16
	v_and_b32_e32 v7, 3, v12
	s_mov_b32 s5, 0x1fffe0
	v_add_lshl_u32 v4, v4, v13, 1
	v_add_u32_e32 v1, 0x2000, v1
	v_lshlrev_b32_e32 v3, 1, v2
	v_lshrrev_b32_e32 v6, 2, v2
	v_and_or_b32 v7, v2, s5, v7
	v_lshl_add_u32 v130, v2, 11, v4
	v_ashrrev_i32_e32 v2, 31, v1
	v_lshrrev_b32_e32 v2, 22, v2
	v_add_u32_e32 v2, v1, v2
	v_ashrrev_i32_e32 v14, 10, v2
	v_mul_i32_i24_e32 v2, 0x400, v14
	v_sub_u32_e32 v1, v1, v2
	v_and_b32_e32 v3, 24, v3
	v_and_b32_e32 v6, 4, v6
	v_lshrrev_b32_e32 v2, 4, v1
	v_or3_b32 v3, v7, v6, v3
	v_bitop3_b32 v1, v2, v1, 32 bitop3:0x6c
	v_lshl_add_u32 v132, v3, 11, v4
	v_ashrrev_i32_e32 v3, 31, v1
	v_lshrrev_b32_e32 v3, 26, v3
	v_add_u32_e32 v3, v1, v3
	v_lshlrev_b32_e32 v2, 3, v14
	v_ashrrev_i32_e32 v15, 6, v3
	v_and_b32_e32 v3, 0xc0, v3
	v_and_b32_e32 v2, -16, v2
	v_sub_u32_e32 v1, v1, v3
	s_ashr_i32 s8, s34, 6
	v_add_u32_e32 v2, v15, v2
	v_ashrrev_i16_sdwa v1, v5, sext(v1) dst_sel:DWORD dst_unused:UNUSED_PAD src0_sel:DWORD src1_sel:BYTE_0
	v_and_b32_e32 v5, 3, v15
	v_and_or_b32 v5, v2, s5, v5
	s_lshl_b32 s5, s8, 10
	v_lshlrev_b32_e32 v4, 5, v14
	v_bfe_i32 v16, v1, 0, 16
	v_lshlrev_b32_e32 v1, 1, v2
	v_lshrrev_b32_e32 v3, 2, v2
	s_add_i32 s6, s5, 0
	v_and_b32_e32 v4, 32, v4
	v_and_b32_e32 v1, 24, v1
	v_and_b32_e32 v3, 4, v3
	s_add_i32 m0, s6, 0x10000
	v_or3_b32 v1, v5, v3, v1
	v_add_lshl_u32 v3, v4, v16, 1
	s_ashr_i32 s9, s34, 8
	global_load_lds_dwordx4 v132, s[44:45]
	s_add_i32 m0, s6, 0x12000
	v_lshl_add_u32 v136, v1, 11, v3
	s_add_u32 s12, s44, 0x40000
	global_load_lds_dwordx4 v136, s[44:45]
	s_addc_u32 s13, s45, 0
	s_add_i32 m0, s6, 0x14000
	s_add_i32 s7, s6, 0x2000
	global_load_lds_dwordx4 v132, s[12:13]
	s_add_i32 m0, s6, 0x16000
	v_lshl_add_u32 v134, v2, 11, v3
	global_load_lds_dwordx4 v136, s[12:13]
	s_mov_b32 m0, s6
	s_add_u32 s12, s42, 0x40000
	global_load_lds_dwordx4 v130, s[42:43]
	s_mov_b32 m0, s7
	s_addc_u32 s13, s43, 0
	s_add_i32 s26, s6, 0x4000
	global_load_lds_dwordx4 v134, s[42:43]
	s_mov_b32 m0, s26
	s_add_i32 s27, s6, 0x6000
	global_load_lds_dwordx4 v130, s[12:13]
	s_mov_b32 m0, s27
	v_mov_b32_e32 v133, 0
	global_load_lds_dwordx4 v134, s[12:13]
	s_load_dwordx4 s[12:15], s[70:71], 0x58
	v_mov_b32_e32 v137, v133
	v_mov_b32_e32 v131, v133
	v_mov_b32_e32 v135, v133
	s_cmp_eq_u32 s9, 1
	v_lshl_add_u64 v[8:9], s[44:45], 0, v[132:133]
	s_mov_b32 s33, 0
	v_lshl_add_u64 v[6:7], s[44:45], 0, v[136:137]
	v_lshl_add_u64 v[2:3], s[42:43], 0, v[130:131]
	s_cselect_b64 s[16:17], -1, 0
	s_cmp_lg_u32 s9, 1
	v_lshl_add_u64 v[4:5], s[42:43], 0, v[134:135]
	s_cbranch_scc1 .LBB0_1021
	s_barrier
	s_setprio 1

; #define PG8_STAGE_B(b, h, bp) PG8_STAGE2(PG8_SB(b, h), (bp) + (h) * hstepB, voffB[0], voffB[1])
; #define PG8_STAGE_A(b, h, ap, NX) do { if constexpr (GATHER) { const unsigned _o0 = (NX) ? vn[h][0] : vc[h][0], _o1 = (NX) ? vn[h][1] : vc[h][1]; PG8_STAGE2(PG8_SA(b, h), (ap), _o0, _o1); } \
;         else { PG8_STAGE2(PG8_SA(b, h), (ap) + (h) * hstepA, voffA[0], voffA[1]); } } while (0)
; #define PG8_LDA(dst, b, h) do { _Pragma("unroll") for (int m = 0; m < 4; ++m) _Pragma("unroll") for (int k = 0; k < 2; ++k) dst[m][k] = *(const LAS bf16x8*)(lds + PG8_SA(b, h) + aoff + m * 2048 + k * 1024); } while (0)
; #define PG8_LDB(dst, b, h) do { _Pragma("unroll") for (int n = 0; n < 2; ++n) _Pragma("unroll") for (int k = 0; k < 2; ++k) dst[n][k] = *(const LAS bf16x8*)(lds + PG8_SB(b, h) + boff + n * 2048 + k * 1024); } while (0)
; #define PG8_MMA(ai, bj, At, Bt) do { __builtin_amdgcn_s_setprio(1); _Pragma("unroll") for (int m = 0; m < 4; ++m) _Pragma("unroll") for (int n = 0; n < 2; ++n) _Pragma("unroll") for (int k = 0; k < 2; ++k) \
;         acc[ai][bj][m][n] = __builtin_amdgcn_mfma_f32_16x16x32_bf16(Bt[n][k], At[m][k], acc[ai][bj][m][n], 0, 0, 0); __builtin_amdgcn_s_setprio(0); } while (0)
; #define PG8_WAIT_V(n) asm volatile("s_waitcnt vmcnt(" #n ")" ::: "memory")
; #define PG8_WAIT_L(n) asm volatile("s_waitcnt lgkmcnt(" #n ")" ::: "memory")
; #define PG8_BAR __builtin_amdgcn_s_barrier()
; #define PG8_SCHED __builtin_amdgcn_sched_barrier(0)
; template <class Epi, class Sched, bool GATHER, bool LIGHTSKIP = false>
; __device__ __forceinline__ void gemm_phase(LAS unsigned char* lds, LAS unsigned char* xl, const int lda, const int ldb, const int K, const Sched& S, const Epi& E) {
;     ...
;             PG8_LDB(B0, 0, 0); PG8_LDB(B1, 0, 1); PG8_SCHED; PG8_LDA(At, 0, 0); PG8_STAGE_A(1, 1, a1, false);
;             PG8_WAIT_V(8); PG8_WAIT_L(0); PG8_BAR; PG8_MMA(0, 0, At, B0); PG8_MMA(0, 1, At, B1); PG8_BAR; PG8_SCHED;
;             PG8_LDA(At, 0, 1); PG8_STAGE_B(0, 0, b2); PG8_STAGE_B(0, 1, b2); PG8_STAGE_A(0, 0, a2, last);
;             PG8_WAIT_V(8); PG8_WAIT_L(0); PG8_BAR; if (!light) { PG8_MMA(1, 0, At, B0); PG8_MMA(1, 1, At, B1); } PG8_BAR; PG8_SCHED;
.LBB0_1027:
	ds_read_b128 v[146:149], v184
	ds_read_b128 v[150:153], v184 offset:1024
	ds_read_b128 v[154:157], v184 offset:2048
	ds_read_b128 v[158:161], v184 offset:3072
	ds_read_b128 v[162:165], v185
	ds_read_b128 v[166:169], v185 offset:1024
	ds_read_b128 v[170:173], v185 offset:2048
	ds_read_b128 v[174:177], v185 offset:3072
	s_add_u32 s44, s42, 0xfffc0080
	s_addc_u32 s45, s43, -1
	s_cmp_eq_u32 s61, 12
	s_cselect_b32 s47, s39, s45
	s_cselect_b32 s46, s38, s44
	s_cselect_b32 s45, s41, s60
	s_cselect_b32 s44, s40, s59
	v_lshl_add_u64 v[216:217], s[42:43], 0, v[138:139]
	s_add_i32 m0, s6, 0xc000
	ds_read_b128 v[178:181], v186
	ds_read_b128 v[188:191], v186 offset:1024
	ds_read_b128 v[192:195], v186 offset:2048
	ds_read_b128 v[196:199], v186 offset:3072
	ds_read_b128 v[200:203], v186 offset:4096
	ds_read_b128 v[204:207], v186 offset:5120
	ds_read_b128 v[208:211], v186 offset:6144
	ds_read_b128 v[212:215], v186 offset:7168
	global_load_lds_dwordx4 v[216:217], off
	v_lshl_add_u64 v[216:217], s[42:43], 0, v[140:141]
	s_add_i32 m0, s6, 0xe000
	s_nop 0
	global_load_lds_dwordx4 v[216:217], off
	s_waitcnt vmcnt(8)
	s_waitcnt lgkmcnt(0)
	s_barrier
	s_waitcnt lgkmcnt(0)
	v_mfma_f32_16x16x32_bf16 v[126:129], v[146:149], v[178:181], v[126:129]
	v_mfma_f32_16x16x32_bf16 v[122:125], v[154:157], v[178:181], v[122:125]
	v_mfma_f32_16x16x32_bf16 v[110:113], v[146:149], v[192:195], v[110:113]
	v_mfma_f32_16x16x32_bf16 v[106:109], v[154:157], v[192:195], v[106:109]
	v_mfma_f32_16x16x32_bf16 v[94:97], v[146:149], v[200:203], v[94:97]
	v_mfma_f32_16x16x32_bf16 v[90:93], v[154:157], v[200:203], v[90:93]
	v_mfma_f32_16x16x32_bf16 v[78:81], v[146:149], v[208:211], v[78:81]
	v_mfma_f32_16x16x32_bf16 v[74:77], v[154:157], v[208:211], v[74:77]
	v_mfma_f32_16x16x32_bf16 v[126:129], v[150:153], v[188:191], v[126:129]
	v_mfma_f32_16x16x32_bf16 v[122:125], v[158:161], v[188:191], v[122:125]
	v_mfma_f32_16x16x32_bf16 v[110:113], v[150:153], v[196:199], v[110:113]
	v_mfma_f32_16x16x32_bf16 v[106:109], v[158:161], v[196:199], v[106:109]
	v_mfma_f32_16x16x32_bf16 v[94:97], v[150:153], v[204:207], v[94:97]
	v_mfma_f32_16x16x32_bf16 v[90:93], v[158:161], v[204:207], v[90:93]
	v_mfma_f32_16x16x32_bf16 v[78:81], v[150:153], v[212:215], v[78:81]
	v_mfma_f32_16x16x32_bf16 v[74:77], v[158:161], v[212:215], v[74:77]
	v_mfma_f32_16x16x32_bf16 v[118:121], v[162:165], v[178:181], v[118:121]
	v_mfma_f32_16x16x32_bf16 v[114:117], v[170:173], v[178:181], v[114:117]
	v_mfma_f32_16x16x32_bf16 v[102:105], v[162:165], v[192:195], v[102:105]
	v_mfma_f32_16x16x32_bf16 v[98:101], v[170:173], v[192:195], v[98:101]
	v_mfma_f32_16x16x32_bf16 v[86:89], v[162:165], v[200:203], v[86:89]
	v_mfma_f32_16x16x32_bf16 v[82:85], v[170:173], v[200:203], v[82:85]
	v_mfma_f32_16x16x32_bf16 v[70:73], v[162:165], v[208:211], v[70:73]
	v_mfma_f32_16x16x32_bf16 v[66:69], v[170:173], v[208:211], v[66:69]
	v_mfma_f32_16x16x32_bf16 v[118:121], v[166:169], v[188:191], v[118:121]
	v_mfma_f32_16x16x32_bf16 v[114:117], v[174:177], v[188:191], v[114:117]
	v_mfma_f32_16x16x32_bf16 v[102:105], v[166:169], v[196:199], v[102:105]
	v_mfma_f32_16x16x32_bf16 v[98:101], v[174:177], v[196:199], v[98:101]
	v_mfma_f32_16x16x32_bf16 v[86:89], v[166:169], v[204:207], v[86:89]
	v_mfma_f32_16x16x32_bf16 v[82:85], v[174:177], v[204:207], v[82:85]
	v_mfma_f32_16x16x32_bf16 v[70:73], v[166:169], v[212:215], v[70:73]
	v_mfma_f32_16x16x32_bf16 v[66:69], v[174:177], v[212:215], v[66:69]
	s_barrier
	s_add_i32 s62, s52, s5
	v_lshl_add_u64 v[216:217], s[44:45], 0, v[132:133]
	s_mov_b32 m0, s62
	ds_read_b128 v[178:181], v186 offset:16384
	ds_read_b128 v[188:191], v186 offset:17408
	ds_read_b128 v[192:195], v186 offset:18432
	ds_read_b128 v[196:199], v186 offset:19456
	ds_read_b128 v[200:203], v186 offset:20480
	ds_read_b128 v[204:207], v186 offset:21504
	ds_read_b128 v[208:211], v186 offset:22528
	ds_read_b128 v[212:215], v186 offset:23552
	global_load_lds_dwordx4 v[216:217], off
	s_add_i32 m0, s62, 0x2000
	s_add_u32 s62, s44, 0x40000
	v_lshl_add_u64 v[218:219], s[44:45], 0, v[136:137]
	s_addc_u32 s63, s45, 0
	s_add_i32 s64, s53, s5
	global_load_lds_dwordx4 v[218:219], off
	v_lshl_add_u64 v[220:221], s[62:63], 0, v[132:133]
	s_mov_b32 m0, s64
	v_lshl_add_u64 v[222:223], s[46:47], 0, v[134:135]
	global_load_lds_dwordx4 v[220:221], off
	v_lshl_add_u64 v[220:221], s[62:63], 0, v[136:137]
	s_add_i32 m0, s64, 0x2000
	s_nop 0
	global_load_lds_dwordx4 v[220:221], off
	v_lshl_add_u64 v[220:221], s[46:47], 0, v[130:131]
	s_mov_b32 m0, s6
	s_nop 0
	global_load_lds_dwordx4 v[220:221], off
	s_mov_b32 m0, s7
	s_nop 0
	global_load_lds_dwordx4 v[222:223], off
	s_waitcnt vmcnt(8)
	s_waitcnt lgkmcnt(0)
	s_barrier
; #define PG8_STAGE_A(b, h, ap, NX) do { if constexpr (GATHER) { const unsigned _o0 = (NX) ? vn[h][0] : vc[h][0], _o1 = (NX) ? vn[h][1] : vc[h][1]; PG8_STAGE2(PG8_SA(b, h), (ap), _o0, _o1); } \
;         else { PG8_STAGE2(PG8_SA(b, h), (ap) + (h) * hstepA, voffA[0], voffA[1]); } } while (0)
; #define PG8_LDA(dst, b, h) do { _Pragma("unroll") for (int m = 0; m < 4; ++m) _Pragma("unroll") for (int k = 0; k < 2; ++k) dst[m][k] = *(const LAS bf16x8*)(lds + PG8_SA(b, h) + aoff + m * 2048 + k * 1024); } while (0)
; #define PG8_LDB(dst, b, h) do { _Pragma("unroll") for (int n = 0; n < 2; ++n) _Pragma("unroll") for (int k = 0; k < 2; ++k) dst[n][k] = *(const LAS bf16x8*)(lds + PG8_SB(b, h) + boff + n * 2048 + k * 1024); } while (0)
; #define PG8_MMA(ai, bj, At, Bt) do { __builtin_amdgcn_s_setprio(1); _Pragma("unroll") for (int m = 0; m < 4; ++m) _Pragma("unroll") for (int n = 0; n < 2; ++n) _Pragma("unroll") for (int k = 0; k < 2; ++k) \
;         acc[ai][bj][m][n] = __builtin_amdgcn_mfma_f32_16x16x32_bf16(Bt[n][k], At[m][k], acc[ai][bj][m][n], 0, 0, 0); __builtin_amdgcn_s_setprio(0); } while (0)
; #define PG8_WAIT_V(n) asm volatile("s_waitcnt vmcnt(" #n ")" ::: "memory")
; #define PG8_WAIT_L(n) asm volatile("s_waitcnt lgkmcnt(" #n ")" ::: "memory")
; #define PG8_BAR __builtin_amdgcn_s_barrier()
; #define PG8_SCHED __builtin_amdgcn_sched_barrier(0)
; template <class Epi, class Sched, bool GATHER, bool LIGHTSKIP = false>
; __device__ __forceinline__ void gemm_phase(LAS unsigned char* lds, LAS unsigned char* xl, const int lda, const int ldb, const int K, const Sched& S, const Epi& E) {
;     ...
;             PG8_WAIT_V(8); PG8_WAIT_L(0); PG8_BAR; if (!light) { PG8_MMA(1, 0, At, B0); PG8_MMA(1, 1, At, B1); } PG8_BAR; PG8_SCHED;
;             PG8_LDB(B0, 1, 0); PG8_LDB(B1, 1, 1); PG8_SCHED; PG8_LDA(At, 1, 0); PG8_STAGE_A(0, 1, a2, last);
;             PG8_WAIT_V(8); PG8_WAIT_L(0); PG8_BAR; PG8_MMA(0, 0, At, B0); PG8_MMA(0, 1, At, B1); PG8_BAR; PG8_SCHED;
	s_waitcnt lgkmcnt(0)
	v_mfma_f32_16x16x32_bf16 v[62:65], v[146:149], v[178:181], v[62:65]
	v_mfma_f32_16x16x32_bf16 v[58:61], v[154:157], v[178:181], v[58:61]
	v_mfma_f32_16x16x32_bf16 v[46:49], v[146:149], v[192:195], v[46:49]
	v_mfma_f32_16x16x32_bf16 v[42:45], v[154:157], v[192:195], v[42:45]
	v_mfma_f32_16x16x32_bf16 v[30:33], v[146:149], v[200:203], v[30:33]
	v_mfma_f32_16x16x32_bf16 v[26:29], v[154:157], v[200:203], v[26:29]
	v_mfma_f32_16x16x32_bf16 v[14:17], v[146:149], v[208:211], v[14:17]
	v_mfma_f32_16x16x32_bf16 v[10:13], v[154:157], v[208:211], v[10:13]
	v_mfma_f32_16x16x32_bf16 v[62:65], v[150:153], v[188:191], v[62:65]
	v_mfma_f32_16x16x32_bf16 v[58:61], v[158:161], v[188:191], v[58:61]
	v_mfma_f32_16x16x32_bf16 v[46:49], v[150:153], v[196:199], v[46:49]
	v_mfma_f32_16x16x32_bf16 v[42:45], v[158:161], v[196:199], v[42:45]
	v_mfma_f32_16x16x32_bf16 v[30:33], v[150:153], v[204:207], v[30:33]
	v_mfma_f32_16x16x32_bf16 v[26:29], v[158:161], v[204:207], v[26:29]
	v_mfma_f32_16x16x32_bf16 v[14:17], v[150:153], v[212:215], v[14:17]
	v_mfma_f32_16x16x32_bf16 v[10:13], v[158:161], v[212:215], v[10:13]
	v_mfma_f32_16x16x32_bf16 v[54:57], v[162:165], v[178:181], v[54:57]
	v_mfma_f32_16x16x32_bf16 v[50:53], v[170:173], v[178:181], v[50:53]
	v_mfma_f32_16x16x32_bf16 v[38:41], v[162:165], v[192:195], v[38:41]
	v_mfma_f32_16x16x32_bf16 v[34:37], v[170:173], v[192:195], v[34:37]
	v_mfma_f32_16x16x32_bf16 v[22:25], v[162:165], v[200:203], v[22:25]
	v_mfma_f32_16x16x32_bf16 v[18:21], v[170:173], v[200:203], v[18:21]
	v_mfma_f32_16x16x32_bf16 v[6:9], v[162:165], v[208:211], v[6:9]
	v_mfma_f32_16x16x32_bf16 v[2:5], v[170:173], v[208:211], v[2:5]
	v_mfma_f32_16x16x32_bf16 v[54:57], v[166:169], v[188:191], v[54:57]
	v_mfma_f32_16x16x32_bf16 v[50:53], v[174:177], v[188:191], v[50:53]
	v_mfma_f32_16x16x32_bf16 v[38:41], v[166:169], v[196:199], v[38:41]
	v_mfma_f32_16x16x32_bf16 v[34:37], v[174:177], v[196:199], v[34:37]
	v_mfma_f32_16x16x32_bf16 v[22:25], v[166:169], v[204:207], v[22:25]
	v_mfma_f32_16x16x32_bf16 v[18:21], v[174:177], v[204:207], v[18:21]
	v_mfma_f32_16x16x32_bf16 v[6:9], v[166:169], v[212:215], v[6:9]
	v_mfma_f32_16x16x32_bf16 v[2:5], v[174:177], v[212:215], v[2:5]
	s_barrier
	s_add_i32 s62, 0, 0x18000
	s_add_i32 s63, 0, 0x1c000
	v_add_u32_e32 v158, s62, v182
	v_add_u32_e32 v174, s63, v182
	ds_read_b128 v[146:149], v158
	ds_read_b128 v[150:153], v158 offset:1024
	ds_read_b128 v[154:157], v158 offset:2048
	ds_read_b128 v[158:161], v158 offset:3072
	ds_read_b128 v[162:165], v174
	ds_read_b128 v[166:169], v174 offset:1024
	ds_read_b128 v[170:173], v174 offset:2048
	ds_read_b128 v[174:177], v174 offset:3072
	s_add_u32 s46, s46, 0x40000
	s_addc_u32 s47, s47, 0
	s_mov_b32 m0, s26
	v_lshl_add_u64 v[224:225], s[46:47], 0, v[130:131]
	ds_read_b128 v[178:181], v186 offset:32768
	ds_read_b128 v[188:191], v186 offset:33792
	ds_read_b128 v[192:195], v186 offset:34816
	ds_read_b128 v[196:199], v186 offset:35840
	ds_read_b128 v[200:203], v186 offset:36864
	ds_read_b128 v[204:207], v186 offset:37888
	ds_read_b128 v[208:211], v186 offset:38912
	ds_read_b128 v[212:215], v186 offset:39936
	global_load_lds_dwordx4 v[224:225], off
	v_lshl_add_u64 v[224:225], s[46:47], 0, v[134:135]
	s_mov_b32 m0, s27
	s_nop 0
	global_load_lds_dwordx4 v[224:225], off
	s_waitcnt vmcnt(8)
	s_waitcnt lgkmcnt(0)
	s_barrier
	s_waitcnt lgkmcnt(0)
	v_mfma_f32_16x16x32_bf16 v[126:129], v[146:149], v[178:181], v[126:129]
	v_mfma_f32_16x16x32_bf16 v[122:125], v[154:157], v[178:181], v[122:125]
	v_mfma_f32_16x16x32_bf16 v[110:113], v[146:149], v[192:195], v[110:113]
	v_mfma_f32_16x16x32_bf16 v[106:109], v[154:157], v[192:195], v[106:109]
	v_mfma_f32_16x16x32_bf16 v[94:97], v[146:149], v[200:203], v[94:97]
	v_mfma_f32_16x16x32_bf16 v[90:93], v[154:157], v[200:203], v[90:93]
	v_mfma_f32_16x16x32_bf16 v[78:81], v[146:149], v[208:211], v[78:81]
	v_mfma_f32_16x16x32_bf16 v[74:77], v[154:157], v[208:211], v[74:77]
	v_mfma_f32_16x16x32_bf16 v[126:129], v[150:153], v[188:191], v[126:129]
	v_mfma_f32_16x16x32_bf16 v[122:125], v[158:161], v[188:191], v[122:125]
	v_mfma_f32_16x16x32_bf16 v[110:113], v[150:153], v[196:199], v[110:113]
	v_mfma_f32_16x16x32_bf16 v[106:109], v[158:161], v[196:199], v[106:109]
	v_mfma_f32_16x16x32_bf16 v[94:97], v[150:153], v[204:207], v[94:97]
	v_mfma_f32_16x16x32_bf16 v[90:93], v[158:161], v[204:207], v[90:93]
	v_mfma_f32_16x16x32_bf16 v[78:81], v[150:153], v[212:215], v[78:81]
	v_mfma_f32_16x16x32_bf16 v[74:77], v[158:161], v[212:215], v[74:77]
	v_mfma_f32_16x16x32_bf16 v[118:121], v[162:165], v[178:181], v[118:121]
	v_mfma_f32_16x16x32_bf16 v[114:117], v[170:173], v[178:181], v[114:117]
	v_mfma_f32_16x16x32_bf16 v[102:105], v[162:165], v[192:195], v[102:105]
	v_mfma_f32_16x16x32_bf16 v[98:101], v[170:173], v[192:195], v[98:101]
	v_mfma_f32_16x16x32_bf16 v[86:89], v[162:165], v[200:203], v[86:89]
	v_mfma_f32_16x16x32_bf16 v[82:85], v[170:173], v[200:203], v[82:85]
	v_mfma_f32_16x16x32_bf16 v[70:73], v[162:165], v[208:211], v[70:73]
	v_mfma_f32_16x16x32_bf16 v[66:69], v[170:173], v[208:211], v[66:69]
	v_mfma_f32_16x16x32_bf16 v[118:121], v[166:169], v[188:191], v[118:121]
	v_mfma_f32_16x16x32_bf16 v[114:117], v[174:177], v[188:191], v[114:117]
	v_mfma_f32_16x16x32_bf16 v[102:105], v[166:169], v[196:199], v[102:105]
	v_mfma_f32_16x16x32_bf16 v[98:101], v[174:177], v[196:199], v[98:101]
	v_mfma_f32_16x16x32_bf16 v[86:89], v[166:169], v[204:207], v[86:89]
	v_mfma_f32_16x16x32_bf16 v[82:85], v[174:177], v[204:207], v[82:85]
	v_mfma_f32_16x16x32_bf16 v[70:73], v[166:169], v[212:215], v[70:73]
	v_mfma_f32_16x16x32_bf16 v[66:69], v[174:177], v[212:215], v[66:69]
	s_barrier
; #define PG8_STAGE_B(b, h, bp) PG8_STAGE2(PG8_SB(b, h), (bp) + (h) * hstepB, voffB[0], voffB[1])
; #define PG8_STAGE_A(b, h, ap, NX) do { if constexpr (GATHER) { const unsigned _o0 = (NX) ? vn[h][0] : vc[h][0], _o1 = (NX) ? vn[h][1] : vc[h][1]; PG8_STAGE2(PG8_SA(b, h), (ap), _o0, _o1); } \
;         else { PG8_STAGE2(PG8_SA(b, h), (ap) + (h) * hstepA, voffA[0], voffA[1]); } } while (0)
; #define PG8_LDA(dst, b, h) do { _Pragma("unroll") for (int m = 0; m < 4; ++m) _Pragma("unroll") for (int k = 0; k < 2; ++k) dst[m][k] = *(const LAS bf16x8*)(lds + PG8_SA(b, h) + aoff + m * 2048 + k * 1024); } while (0)
; #define PG8_MMA(ai, bj, At, Bt) do { __builtin_amdgcn_s_setprio(1); _Pragma("unroll") for (int m = 0; m < 4; ++m) _Pragma("unroll") for (int n = 0; n < 2; ++n) _Pragma("unroll") for (int k = 0; k < 2; ++k) \
;         acc[ai][bj][m][n] = __builtin_amdgcn_mfma_f32_16x16x32_bf16(Bt[n][k], At[m][k], acc[ai][bj][m][n], 0, 0, 0); __builtin_amdgcn_s_setprio(0); } while (0)
; #define PG8_WAIT_V(n) asm volatile("s_waitcnt vmcnt(" #n ")" ::: "memory")
; #define PG8_WAIT_L(n) asm volatile("s_waitcnt lgkmcnt(" #n ")" ::: "memory")
; #define PG8_BAR __builtin_amdgcn_s_barrier()
; #define PG8_SCHED __builtin_amdgcn_sched_barrier(0)
; template <class Epi, class Sched, bool GATHER, bool LIGHTSKIP = false>
; __device__ __forceinline__ void gemm_phase(LAS unsigned char* lds, LAS unsigned char* xl, const int lda, const int ldb, const int K, const Sched& S, const Epi& E) {
;     ...
;             PG8_LDA(At, 1, 1); PG8_STAGE_B(1, 0, b3); PG8_STAGE_B(1, 1, b3); PG8_STAGE_A(1, 0, a3, last);
;             PG8_WAIT_V(8); PG8_WAIT_L(0); PG8_BAR; if (!light) { PG8_MMA(1, 0, At, B0); PG8_MMA(1, 1, At, B1); } PG8_BAR; PG8_SCHED;
;         }
;         if (wr == 0) PG8_BAR;
	s_add_i32 s46, s62, s5
	v_lshl_add_u64 v[216:217], v[216:217], 0, s[30:31]
	s_mov_b32 m0, s46
	ds_read_b128 v[178:181], v186 offset:49152
	ds_read_b128 v[188:191], v186 offset:50176
	ds_read_b128 v[192:195], v186 offset:51200
	ds_read_b128 v[196:199], v186 offset:52224
	ds_read_b128 v[200:203], v186 offset:53248
	ds_read_b128 v[204:207], v186 offset:54272
	ds_read_b128 v[208:211], v186 offset:55296
	ds_read_b128 v[212:215], v186 offset:56320
	global_load_lds_dwordx4 v[216:217], off
	s_add_i32 m0, s46, 0x2000
	s_add_u32 s44, s44, 0x40080
	v_lshl_add_u64 v[216:217], v[218:219], 0, s[30:31]
	s_addc_u32 s45, s45, 0
	s_add_i32 s46, s63, s5
	global_load_lds_dwordx4 v[216:217], off
	v_lshl_add_u64 v[216:217], s[44:45], 0, v[132:133]
	s_mov_b32 m0, s46
	s_nop 0
	global_load_lds_dwordx4 v[216:217], off
	v_lshl_add_u64 v[216:217], s[44:45], 0, v[136:137]
	s_add_i32 m0, s46, 0x2000
	s_nop 0
	global_load_lds_dwordx4 v[216:217], off
	v_lshl_add_u64 v[216:217], v[220:221], 0, s[30:31]
	s_mov_b32 m0, s48
	s_nop 0
	global_load_lds_dwordx4 v[216:217], off
	v_lshl_add_u64 v[216:217], v[222:223], 0, s[30:31]
	s_mov_b32 m0, s49
	s_nop 0
	global_load_lds_dwordx4 v[216:217], off
	s_waitcnt vmcnt(8)
	s_waitcnt lgkmcnt(0)
	s_barrier
	s_waitcnt lgkmcnt(0)
	v_mfma_f32_16x16x32_bf16 v[62:65], v[146:149], v[178:181], v[62:65]
	v_mfma_f32_16x16x32_bf16 v[58:61], v[154:157], v[178:181], v[58:61]
	v_mfma_f32_16x16x32_bf16 v[46:49], v[146:149], v[192:195], v[46:49]
	v_mfma_f32_16x16x32_bf16 v[42:45], v[154:157], v[192:195], v[42:45]
	v_mfma_f32_16x16x32_bf16 v[30:33], v[146:149], v[200:203], v[30:33]
	v_mfma_f32_16x16x32_bf16 v[26:29], v[154:157], v[200:203], v[26:29]
	v_mfma_f32_16x16x32_bf16 v[14:17], v[146:149], v[208:211], v[14:17]
	v_mfma_f32_16x16x32_bf16 v[10:13], v[154:157], v[208:211], v[10:13]
	v_mfma_f32_16x16x32_bf16 v[62:65], v[150:153], v[188:191], v[62:65]
	v_mfma_f32_16x16x32_bf16 v[58:61], v[158:161], v[188:191], v[58:61]
	v_mfma_f32_16x16x32_bf16 v[46:49], v[150:153], v[196:199], v[46:49]
	v_mfma_f32_16x16x32_bf16 v[42:45], v[158:161], v[196:199], v[42:45]
	v_mfma_f32_16x16x32_bf16 v[30:33], v[150:153], v[204:207], v[30:33]
	v_mfma_f32_16x16x32_bf16 v[26:29], v[158:161], v[204:207], v[26:29]
	v_mfma_f32_16x16x32_bf16 v[14:17], v[150:153], v[212:215], v[14:17]
	v_mfma_f32_16x16x32_bf16 v[10:13], v[158:161], v[212:215], v[10:13]
	v_mfma_f32_16x16x32_bf16 v[54:57], v[162:165], v[178:181], v[54:57]
	v_mfma_f32_16x16x32_bf16 v[50:53], v[170:173], v[178:181], v[50:53]
	v_mfma_f32_16x16x32_bf16 v[38:41], v[162:165], v[192:195], v[38:41]
	v_mfma_f32_16x16x32_bf16 v[34:37], v[170:173], v[192:195], v[34:37]
	v_mfma_f32_16x16x32_bf16 v[22:25], v[162:165], v[200:203], v[22:25]
	v_mfma_f32_16x16x32_bf16 v[18:21], v[170:173], v[200:203], v[18:21]
	v_mfma_f32_16x16x32_bf16 v[6:9], v[162:165], v[208:211], v[6:9]
	v_mfma_f32_16x16x32_bf16 v[2:5], v[170:173], v[208:211], v[2:5]
	v_mfma_f32_16x16x32_bf16 v[54:57], v[166:169], v[188:191], v[54:57]
	v_mfma_f32_16x16x32_bf16 v[50:53], v[174:177], v[188:191], v[50:53]
	v_mfma_f32_16x16x32_bf16 v[38:41], v[166:169], v[196:199], v[38:41]
	v_mfma_f32_16x16x32_bf16 v[34:37], v[174:177], v[196:199], v[34:37]
	v_mfma_f32_16x16x32_bf16 v[22:25], v[166:169], v[204:207], v[22:25]
	v_mfma_f32_16x16x32_bf16 v[18:21], v[174:177], v[204:207], v[18:21]
	v_mfma_f32_16x16x32_bf16 v[6:9], v[166:169], v[212:215], v[6:9]
	v_mfma_f32_16x16x32_bf16 v[2:5], v[174:177], v[212:215], v[2:5]
	s_barrier
	s_add_i32 s61, s61, 2
	s_add_u32 s42, s42, 0x100
	s_addc_u32 s43, s43, 0
	s_add_u32 s59, s59, 0x100
	s_addc_u32 s60, s60, 0
	s_cmp_gt_u32 s61, 13
	s_cbranch_scc0 .LBB0_1027
	s_and_b64 vcc, exec, s[34:35]
	s_cbranch_vccz .LBB0_1030
	s_barrier

; __device__ __forceinline__ int otid() { int t = threadIdx.x; asm volatile("" : "+v"(t)); return t; }
; #define PG8_STAGE_B(b, h, bp) PG8_STAGE2(PG8_SB(b, h), (bp) + (h) * hstepB, voffB[0], voffB[1])
; template <class Epi, class Sched, bool GATHER, bool LIGHTSKIP = false>
; __device__ __forceinline__ void gemm_phase(LAS unsigned char* lds, LAS unsigned char* xl, const int lda, const int ldb, const int K, const Sched& S, const Epi& E) {
;     const int tid = otid(), wid = __builtin_amdgcn_readfirstlane(tid >> 6), lane = tid & 63, wr = wid >> 2, wc = wid & 3, fr = lane & 15, fq = lane >> 4;
;     const int nt = K / BK;
;     int Rr[2], Cc[2]; unsigned voffA[2], voffB[2];
; #pragma unroll
;     for (int i = 0; i < 2; ++i) { stage_rc(tid * 16 + i * 8192, Rr[i], Cc[i]); const int Rb = Epi::PERM ? ((Rr[i] & ~31) + perm32(Rr[i] & 31)) : Rr[i];
;         voffA[i] = (unsigned)(Rr[i] * lda + Cc[i]) * 2u; voffB[i] = (unsigned)(Rb * ldb + Cc[i]) * 2u; }
;     unsigned vc[2][2], vn[2][2];
;     const size_t kstep = (size_t)(BK * 2);
;     const size_t hstepA = (size_t)HALF * lda * 2, hstepB = (size_t)HALF * ldb * 2;
;     const unsigned ldsw = (unsigned)wid * 1024u;
;     const int aoff = lds_byte(wr * 64 + fr, fq * 8), boff = lds_byte(wc * 32 + fr, fq * 8);
;     ...
;     GUnit cur, nxt; int ui = 0;
;     if (!S.next(0, cur)) return;
;     Acc acc;
; #pragma unroll
;     for (int a = 0; a < 2; ++a)
; #pragma unroll
;         for (int b = 0; b < 2; ++b)
; #pragma unroll
;             for (int m = 0; m < 4; ++m)
; #pragma unroll
;                 for (int n = 0; n < 2; ++n) acc[a][b][m][n] = (f32x4){0.f, 0.f, 0.f, 0.f};
;     bf16x8 At[4][2], B0[2][2], B1[2][2];
;     const char* cA = cur.A; const char* cB = cur.B;
;     if constexpr (GATHER) { S.offsets(cur, lda, vc);
; #pragma unroll
;         for (int h = 0; h < 2; ++h) { vn[h][0] = vc[h][0]; vn[h][1] = vc[h][1]; } }
;     PG8_STAGE_B(0, 0, cB); PG8_STAGE_B(0, 1, cB); PG8_STAGE_A(0, 0, cA, false); PG8_STAGE_A(0, 1, cA, false);
;     if (wr == 1) PG8_BAR;
;     PG8_WAIT_V(2); PG8_BAR;
;     __device__ __forceinline__ void offsets(const GUnit& u, int lda, unsigned (&vo)[2][2]) const {
;     ...
;             for (int i = 0; i < 2; ++i) { const int idx = j * 256 + h * 128 + R[i]; int tok = 0; if (idx < n) tok = slot[(size_t)e * CAP + idx] >> 1;
;                 vo[h][i] = (unsigned)(tok * lda + C[i]) * 2u; }
.LBB0_1330:
	s_or_b64 exec, exec, s[10:11]
	v_lshlrev_b32_e32 v1, 5, v1
	v_and_b32_e32 v2, 32, v1
	v_mul_i32_i24_e32 v1, 64, v7
	v_sub_u32_e32 v3, v6, v1
	v_mov_b32_e32 v1, 1
	v_ashrrev_i16_sdwa v3, v1, sext(v3) dst_sel:DWORD dst_unused:UNUSED_PAD src0_sel:DWORD src1_sel:BYTE_0
	v_add_u32_sdwa v2, v2, sext(v3) dst_sel:DWORD dst_unused:UNUSED_PAD src0_sel:DWORD src1_sel:WORD_0
	v_bfe_i32 v5, v12, 27, 1
	v_add_lshl_u32 v206, v17, v2, 1
	v_add_lshl_u32 v210, v10, v2, 1
	v_lshlrev_b32_e32 v2, 4, v12
	v_lshrrev_b32_e32 v5, 22, v5
	v_lshlrev_b32_e32 v4, 6, v15
	v_add_u32_e32 v5, v2, v5
	v_lshlrev_b32_e32 v3, 5, v13
	v_sub_u32_e32 v4, v14, v4
	v_and_b32_e32 v5, 0xfffffc00, v5
	v_and_b32_e32 v3, 32, v3
	v_ashrrev_i16_sdwa v4, v1, sext(v4) dst_sel:DWORD dst_unused:UNUSED_PAD src0_sel:DWORD src1_sel:BYTE_0
	v_sub_u32_e32 v5, v2, v5
	v_add_u32_sdwa v3, v3, sext(v4) dst_sel:DWORD dst_unused:UNUSED_PAD src0_sel:DWORD src1_sel:WORD_0
	v_ashrrev_i32_e32 v4, 31, v12
	v_lshrrev_b32_e32 v6, 4, v5
	v_lshrrev_b32_e32 v4, 26, v4
	v_bitop3_b32 v6, v6, v5, 32 bitop3:0x6c
	v_ashrrev_i32_e32 v5, 31, v5
	v_add_u32_e32 v4, v12, v4
	v_lshrrev_b32_e32 v5, 26, v5
	v_ashrrev_i32_e32 v4, 6, v4
	v_add_u32_e32 v5, v6, v5
	v_lshlrev_b32_e32 v7, 3, v4
	v_ashrrev_i32_e32 v5, 6, v5
	v_add_lshl_u32 v208, v9, v3, 1
	v_and_b32_e32 v7, -16, v7
	v_mul_i32_i24_e32 v9, 64, v5
	v_add_u32_e32 v7, v5, v7
	v_sub_u32_e32 v6, v6, v9
	v_lshlrev_b32_e32 v4, 5, v4
	v_ashrrev_i16_sdwa v6, v1, sext(v6) dst_sel:DWORD dst_unused:UNUSED_PAD src0_sel:DWORD src1_sel:BYTE_0
	v_lshlrev_b32_e32 v9, 1, v7
	v_lshrrev_b32_e32 v10, 2, v7
	v_and_b32_e32 v5, 3, v5
	s_mov_b32 s0, 0xfffe0
	v_and_b32_e32 v4, 32, v4
	v_bfe_i32 v6, v6, 0, 16
	v_and_b32_e32 v9, 24, v9
	v_and_b32_e32 v10, 4, v10
	v_and_or_b32 v5, v7, s0, v5
	v_or3_b32 v5, v5, v10, v9
	v_add_lshl_u32 v4, v4, v6, 1
	v_add_u32_e32 v2, 0x2000, v2
	v_lshl_add_u32 v200, v5, 12, v4
	v_ashrrev_i32_e32 v4, 31, v2
	v_lshrrev_b32_e32 v4, 22, v4
	v_add_u32_e32 v4, v2, v4
	v_ashrrev_i32_e32 v4, 10, v4
	v_mul_i32_i24_e32 v5, 0x400, v4
	v_sub_u32_e32 v2, v2, v5
	v_lshrrev_b32_e32 v5, 4, v2
	v_bitop3_b32 v2, v5, v2, 32 bitop3:0x6c
	v_ashrrev_i32_e32 v6, 31, v2
	v_lshrrev_b32_e32 v6, 26, v6
	v_lshlrev_b32_e32 v5, 3, v4
	v_add_u32_e32 v6, v2, v6
	v_and_b32_e32 v5, -16, v5
	v_ashrrev_i32_e32 v7, 6, v6
	v_add_u32_e32 v5, v7, v5
	v_and_b32_e32 v6, 0xc0, v6
	v_and_b32_e32 v7, 3, v7
	s_ashr_i32 s9, s14, 6
	v_sub_u32_e32 v2, v2, v6
	v_lshlrev_b32_e32 v6, 1, v5
	v_lshrrev_b32_e32 v9, 2, v5
	v_and_or_b32 v5, v5, s0, v7
	s_lshl_b32 s0, s9, 10
	v_lshlrev_b32_e32 v4, 5, v4
	v_ashrrev_i16_sdwa v2, v1, sext(v2) dst_sel:DWORD dst_unused:UNUSED_PAD src0_sel:DWORD src1_sel:BYTE_0
	s_add_i32 s1, s0, 0
	v_and_b32_e32 v4, 32, v4
	v_bfe_i32 v2, v2, 0, 16
	v_and_b32_e32 v6, 24, v6
	v_and_b32_e32 v9, 4, v9
	s_add_i32 m0, s1, 0x10000
	s_ashr_i32 s8, s14, 8
	v_or3_b32 v5, v5, v9, v6
	v_add_lshl_u32 v2, v4, v2, 1
	global_load_lds_dwordx4 v200, s[6:7]
	s_add_i32 m0, s1, 0x12000
	v_lshl_add_u32 v202, v5, 12, v2
	s_add_u32 s4, s6, 0x80000
	global_load_lds_dwordx4 v202, s[6:7]
	s_addc_u32 s5, s7, 0
	s_add_i32 m0, s1, 0x14000
	s_add_i32 s2, s1, 0x2000
	global_load_lds_dwordx4 v200, s[4:5]
	s_add_i32 m0, s1, 0x16000
	v_add_lshl_u32 v212, v8, v3, 1
	global_load_lds_dwordx4 v202, s[4:5]
	s_mov_b32 m0, s1
	s_add_i32 s4, s1, 0x4000
	global_load_lds_dwordx4 v210, s[30:31]
	s_mov_b32 m0, s2
	s_add_i32 s5, s1, 0x6000
	global_load_lds_dwordx4 v208, s[30:31]
	s_mov_b32 m0, s4
	v_mov_b32_e32 v3, 0
	global_load_lds_dwordx4 v206, s[30:31]
	s_mov_b32 m0, s5
	v_mov_b32_e32 v201, v3
	global_load_lds_dwordx4 v212, s[30:31]
	v_mov_b32_e32 v203, v3
	v_mov_b32_e32 v211, v3
	v_mov_b32_e32 v209, v3
	s_cmp_eq_u32 s8, 1
	v_lshl_add_u64 v[10:11], s[6:7], 0, v[200:201]
	s_mov_b32 s26, 0
	v_lshl_add_u64 v[8:9], s[6:7], 0, v[202:203]
	v_lshl_add_u64 v[4:5], s[30:31], 0, v[210:211]
	s_cselect_b64 s[10:11], -1, 0
	s_cmp_lg_u32 s8, 1
	v_lshl_add_u64 v[6:7], s[30:31], 0, v[208:209]
	s_cbranch_scc1 .LBB0_1332
	s_barrier
	s_setprio 1

; #define PG8_STAGE_B(b, h, bp) PG8_STAGE2(PG8_SB(b, h), (bp) + (h) * hstepB, voffB[0], voffB[1])
; #define PG8_STAGE_A(b, h, ap, NX) do { if constexpr (GATHER) { const unsigned _o0 = (NX) ? vn[h][0] : vc[h][0], _o1 = (NX) ? vn[h][1] : vc[h][1]; PG8_STAGE2(PG8_SA(b, h), (ap), _o0, _o1); } \
;         else { PG8_STAGE2(PG8_SA(b, h), (ap) + (h) * hstepA, voffA[0], voffA[1]); } } while (0)
; #define PG8_LDA(dst, b, h) do { _Pragma("unroll") for (int m = 0; m < 4; ++m) _Pragma("unroll") for (int k = 0; k < 2; ++k) dst[m][k] = *(const LAS bf16x8*)(lds + PG8_SA(b, h) + aoff + m * 2048 + k * 1024); } while (0)
; #define PG8_LDB(dst, b, h) do { _Pragma("unroll") for (int n = 0; n < 2; ++n) _Pragma("unroll") for (int k = 0; k < 2; ++k) dst[n][k] = *(const LAS bf16x8*)(lds + PG8_SB(b, h) + boff + n * 2048 + k * 1024); } while (0)
; #define PG8_MMA(ai, bj, At, Bt) do { __builtin_amdgcn_s_setprio(1); _Pragma("unroll") for (int m = 0; m < 4; ++m) _Pragma("unroll") for (int n = 0; n < 2; ++n) _Pragma("unroll") for (int k = 0; k < 2; ++k) \
;         acc[ai][bj][m][n] = __builtin_amdgcn_mfma_f32_16x16x32_bf16(Bt[n][k], At[m][k], acc[ai][bj][m][n], 0, 0, 0); __builtin_amdgcn_s_setprio(0); } while (0)
; #define PG8_WAIT_V(n) asm volatile("s_waitcnt vmcnt(" #n ")" ::: "memory")
; #define PG8_WAIT_L(n) asm volatile("s_waitcnt lgkmcnt(" #n ")" ::: "memory")
; #define PG8_BAR __builtin_amdgcn_s_barrier()
; #define PG8_SCHED __builtin_amdgcn_sched_barrier(0)
; template <class Epi, class Sched, bool GATHER, bool LIGHTSKIP = false>
; __device__ __forceinline__ void gemm_phase(LAS unsigned char* lds, LAS unsigned char* xl, const int lda, const int ldb, const int K, const Sched& S, const Epi& E) {
;     ...
;             PG8_LDB(B0, 0, 0); PG8_LDB(B1, 0, 1); PG8_SCHED; PG8_LDA(At, 0, 0); PG8_STAGE_A(1, 1, a1, false);
;             PG8_WAIT_V(8); PG8_WAIT_L(0); PG8_BAR; PG8_MMA(0, 0, At, B0); PG8_MMA(0, 1, At, B1); PG8_BAR; PG8_SCHED;
;             PG8_LDA(At, 0, 1); PG8_STAGE_B(0, 0, b2); PG8_STAGE_B(0, 1, b2); PG8_STAGE_A(0, 0, a2, last);
;             PG8_WAIT_V(8); PG8_WAIT_L(0); PG8_BAR; if (!light) { PG8_MMA(1, 0, At, B0); PG8_MMA(1, 1, At, B1); } PG8_BAR; PG8_SCHED;
.LBB0_1349:
	s_add_u32 s8, s30, s38
	s_addc_u32 s9, s31, s39
	s_add_u32 s40, s8, 0x100
	s_addc_u32 s41, s9, 0
	s_and_b64 s[8:9], s[6:7], exec
	s_cselect_b32 s43, s19, s41
	s_cselect_b32 s42, s18, s40
	s_add_u32 s40, s57, s38
	s_addc_u32 s41, s58, s39
	s_and_b64 s[8:9], s[6:7], exec
	s_cselect_b32 s41, s21, s41
	s_cselect_b32 s40, s20, s40
	s_add_i32 s8, 0, 0x10000
	v_add_u32_e32 v2, s8, v211
	ds_read_b128 v[150:153], v2
	ds_read_b128 v[154:157], v2 offset:1024
	ds_read_b128 v[158:161], v2 offset:2048
	ds_read_b128 v[162:165], v2 offset:3072
	v_add_u32_e32 v2, s47, v211
	ds_read_b128 v[134:137], v2
	ds_read_b128 v[138:141], v2 offset:1024
	ds_read_b128 v[142:145], v2 offset:2048
	ds_read_b128 v[146:149], v2 offset:3072
	v_lshl_add_u64 v[4:5], v[216:217], 0, s[38:39]
	s_add_i32 m0, s1, 0xc000
	s_waitcnt lgkmcnt(0)
	ds_read_b128 v[166:169], v229
	ds_read_b128 v[170:173], v229 offset:1024
	ds_read_b128 v[174:177], v229 offset:2048
	ds_read_b128 v[178:181], v229 offset:3072
	ds_read_b128 v[182:185], v229 offset:4096
	ds_read_b128 v[186:189], v229 offset:5120
	ds_read_b128 v[190:193], v229 offset:6144
	ds_read_b128 v[194:197], v229 offset:7168
	global_load_lds_dwordx4 v[4:5], off
	v_lshl_add_u64 v[4:5], v[214:215], 0, s[38:39]
	s_add_i32 m0, s1, 0xe000
	s_nop 0
	global_load_lds_dwordx4 v[4:5], off
	s_waitcnt vmcnt(8)
	s_waitcnt lgkmcnt(0)
	s_barrier
	s_waitcnt lgkmcnt(0)
	v_mfma_f32_16x16x32_bf16 v[130:133], v[150:153], v[166:169], v[130:133]
	v_mfma_f32_16x16x32_bf16 v[122:125], v[158:161], v[166:169], v[122:125]
	v_mfma_f32_16x16x32_bf16 v[114:117], v[150:153], v[174:177], v[114:117]
	v_mfma_f32_16x16x32_bf16 v[106:109], v[158:161], v[174:177], v[106:109]
	v_mfma_f32_16x16x32_bf16 v[98:101], v[150:153], v[182:185], v[98:101]
	v_mfma_f32_16x16x32_bf16 v[90:93], v[158:161], v[182:185], v[90:93]
	v_mfma_f32_16x16x32_bf16 v[82:85], v[150:153], v[190:193], v[82:85]
	v_mfma_f32_16x16x32_bf16 v[74:77], v[158:161], v[190:193], v[74:77]
	v_mfma_f32_16x16x32_bf16 v[130:133], v[154:157], v[170:173], v[130:133]
	v_mfma_f32_16x16x32_bf16 v[122:125], v[162:165], v[170:173], v[122:125]
	v_mfma_f32_16x16x32_bf16 v[114:117], v[154:157], v[178:181], v[114:117]
	v_mfma_f32_16x16x32_bf16 v[106:109], v[162:165], v[178:181], v[106:109]
	v_mfma_f32_16x16x32_bf16 v[98:101], v[154:157], v[186:189], v[98:101]
	v_mfma_f32_16x16x32_bf16 v[90:93], v[162:165], v[186:189], v[90:93]
	v_mfma_f32_16x16x32_bf16 v[82:85], v[154:157], v[194:197], v[82:85]
	v_mfma_f32_16x16x32_bf16 v[74:77], v[162:165], v[194:197], v[74:77]
	v_mfma_f32_16x16x32_bf16 v[126:129], v[134:137], v[166:169], v[126:129]
	v_mfma_f32_16x16x32_bf16 v[118:121], v[142:145], v[166:169], v[118:121]
	v_mfma_f32_16x16x32_bf16 v[110:113], v[134:137], v[174:177], v[110:113]
	v_mfma_f32_16x16x32_bf16 v[102:105], v[142:145], v[174:177], v[102:105]
	v_mfma_f32_16x16x32_bf16 v[94:97], v[134:137], v[182:185], v[94:97]
	v_mfma_f32_16x16x32_bf16 v[86:89], v[142:145], v[182:185], v[86:89]
	v_mfma_f32_16x16x32_bf16 v[78:81], v[134:137], v[190:193], v[78:81]
	v_mfma_f32_16x16x32_bf16 v[70:73], v[142:145], v[190:193], v[70:73]
	v_mfma_f32_16x16x32_bf16 v[126:129], v[138:141], v[170:173], v[126:129]
	v_mfma_f32_16x16x32_bf16 v[118:121], v[146:149], v[170:173], v[118:121]
	v_mfma_f32_16x16x32_bf16 v[110:113], v[138:141], v[178:181], v[110:113]
	v_mfma_f32_16x16x32_bf16 v[102:105], v[146:149], v[178:181], v[102:105]
	v_mfma_f32_16x16x32_bf16 v[94:97], v[138:141], v[186:189], v[94:97]
	v_mfma_f32_16x16x32_bf16 v[86:89], v[146:149], v[186:189], v[86:89]
	v_mfma_f32_16x16x32_bf16 v[78:81], v[138:141], v[194:197], v[78:81]
	v_mfma_f32_16x16x32_bf16 v[70:73], v[146:149], v[194:197], v[70:73]
	s_barrier
	s_add_i32 s8, s8, s0
	v_lshl_add_u64 v[4:5], s[40:41], 0, v[200:201]
	s_mov_b32 m0, s8
	ds_read_b128 v[190:193], v229 offset:16384
	ds_read_b128 v[194:197], v229 offset:17408
	ds_read_b128 v[182:185], v229 offset:18432
	ds_read_b128 v[186:189], v229 offset:19456
	ds_read_b128 v[174:177], v229 offset:20480
	ds_read_b128 v[178:181], v229 offset:21504
	ds_read_b128 v[166:169], v229 offset:22528
	ds_read_b128 v[170:173], v229 offset:23552
	global_load_lds_dwordx4 v[4:5], off
	s_add_i32 m0, s8, 0x2000
	s_add_u32 s8, s40, 0x80000
	v_lshl_add_u64 v[218:219], s[40:41], 0, v[202:203]
	s_addc_u32 s9, s41, 0
	s_add_i32 s60, s47, s0
	global_load_lds_dwordx4 v[218:219], off
	v_lshl_add_u64 v[220:221], s[8:9], 0, v[200:201]
	s_mov_b32 m0, s60
	v_cndmask_b32_e64 v2, v210, v230, s[6:7]
	global_load_lds_dwordx4 v[220:221], off
	v_lshl_add_u64 v[220:221], s[8:9], 0, v[202:203]
	s_add_i32 m0, s60, 0x2000
	s_andn2_b64 vcc, exec, s[34:35]
	global_load_lds_dwordx4 v[220:221], off
	s_mov_b32 m0, s1
	v_cndmask_b32_e64 v220, v208, v213, s[6:7]
	global_load_lds_dwordx4 v2, s[42:43]
	s_mov_b32 m0, s2
	v_cndmask_b32_e64 v221, 0, 1, s[34:35]
	global_load_lds_dwordx4 v220, s[42:43]
	s_waitcnt vmcnt(8)
	s_waitcnt lgkmcnt(0)
	v_cmp_ne_u32_e64 s[8:9], 1, v221
	s_barrier
	s_cbranch_vccnz .LBB0_1351
; #define PG8_STAGE_A(b, h, ap, NX) do { if constexpr (GATHER) { const unsigned _o0 = (NX) ? vn[h][0] : vc[h][0], _o1 = (NX) ? vn[h][1] : vc[h][1]; PG8_STAGE2(PG8_SA(b, h), (ap), _o0, _o1); } \
;         else { PG8_STAGE2(PG8_SA(b, h), (ap) + (h) * hstepA, voffA[0], voffA[1]); } } while (0)
; #define PG8_LDA(dst, b, h) do { _Pragma("unroll") for (int m = 0; m < 4; ++m) _Pragma("unroll") for (int k = 0; k < 2; ++k) dst[m][k] = *(const LAS bf16x8*)(lds + PG8_SA(b, h) + aoff + m * 2048 + k * 1024); } while (0)
; #define PG8_LDB(dst, b, h) do { _Pragma("unroll") for (int n = 0; n < 2; ++n) _Pragma("unroll") for (int k = 0; k < 2; ++k) dst[n][k] = *(const LAS bf16x8*)(lds + PG8_SB(b, h) + boff + n * 2048 + k * 1024); } while (0)
; #define PG8_MMA(ai, bj, At, Bt) do { __builtin_amdgcn_s_setprio(1); _Pragma("unroll") for (int m = 0; m < 4; ++m) _Pragma("unroll") for (int n = 0; n < 2; ++n) _Pragma("unroll") for (int k = 0; k < 2; ++k) \
;         acc[ai][bj][m][n] = __builtin_amdgcn_mfma_f32_16x16x32_bf16(Bt[n][k], At[m][k], acc[ai][bj][m][n], 0, 0, 0); __builtin_amdgcn_s_setprio(0); } while (0)
; #define PG8_WAIT_V(n) asm volatile("s_waitcnt vmcnt(" #n ")" ::: "memory")
; #define PG8_WAIT_L(n) asm volatile("s_waitcnt lgkmcnt(" #n ")" ::: "memory")
; #define PG8_BAR __builtin_amdgcn_s_barrier()
; #define PG8_SCHED __builtin_amdgcn_sched_barrier(0)
; template <class Epi, class Sched, bool GATHER, bool LIGHTSKIP = false>
; __device__ __forceinline__ void gemm_phase(LAS unsigned char* lds, LAS unsigned char* xl, const int lda, const int ldb, const int K, const Sched& S, const Epi& E) {
;     ...
;             PG8_WAIT_V(8); PG8_WAIT_L(0); PG8_BAR; if (!light) { PG8_MMA(1, 0, At, B0); PG8_MMA(1, 1, At, B1); } PG8_BAR; PG8_SCHED;
;             PG8_LDB(B0, 1, 0); PG8_LDB(B1, 1, 1); PG8_SCHED; PG8_LDA(At, 1, 0); PG8_STAGE_A(0, 1, a2, last);
	s_waitcnt lgkmcnt(0)
	v_mfma_f32_16x16x32_bf16 v[66:69], v[150:153], v[190:193], v[66:69]
	v_mfma_f32_16x16x32_bf16 v[58:61], v[158:161], v[190:193], v[58:61]
	v_mfma_f32_16x16x32_bf16 v[50:53], v[150:153], v[182:185], v[50:53]
	v_mfma_f32_16x16x32_bf16 v[42:45], v[158:161], v[182:185], v[42:45]
	v_mfma_f32_16x16x32_bf16 v[34:37], v[150:153], v[174:177], v[34:37]
	v_mfma_f32_16x16x32_bf16 v[26:29], v[158:161], v[174:177], v[26:29]
	v_mfma_f32_16x16x32_bf16 v[18:21], v[150:153], v[166:169], v[18:21]
	v_mfma_f32_16x16x32_bf16 v[10:13], v[158:161], v[166:169], v[10:13]
	v_mfma_f32_16x16x32_bf16 v[66:69], v[154:157], v[194:197], v[66:69]
	v_mfma_f32_16x16x32_bf16 v[58:61], v[162:165], v[194:197], v[58:61]
	v_mfma_f32_16x16x32_bf16 v[50:53], v[154:157], v[186:189], v[50:53]
	v_mfma_f32_16x16x32_bf16 v[42:45], v[162:165], v[186:189], v[42:45]
	v_mfma_f32_16x16x32_bf16 v[34:37], v[154:157], v[178:181], v[34:37]
	v_mfma_f32_16x16x32_bf16 v[26:29], v[162:165], v[178:181], v[26:29]
	v_mfma_f32_16x16x32_bf16 v[18:21], v[154:157], v[170:173], v[18:21]
	v_mfma_f32_16x16x32_bf16 v[10:13], v[162:165], v[170:173], v[10:13]
	v_mfma_f32_16x16x32_bf16 v[62:65], v[134:137], v[190:193], v[62:65]
	v_mfma_f32_16x16x32_bf16 v[54:57], v[142:145], v[190:193], v[54:57]
	v_mfma_f32_16x16x32_bf16 v[46:49], v[134:137], v[182:185], v[46:49]
	v_mfma_f32_16x16x32_bf16 v[38:41], v[142:145], v[182:185], v[38:41]
	v_mfma_f32_16x16x32_bf16 v[30:33], v[134:137], v[174:177], v[30:33]
	v_mfma_f32_16x16x32_bf16 v[22:25], v[142:145], v[174:177], v[22:25]
	v_mfma_f32_16x16x32_bf16 v[14:17], v[134:137], v[166:169], v[14:17]
	v_mfma_f32_16x16x32_bf16 v[6:9], v[142:145], v[166:169], v[6:9]
	v_mfma_f32_16x16x32_bf16 v[62:65], v[138:141], v[194:197], v[62:65]
	v_mfma_f32_16x16x32_bf16 v[54:57], v[146:149], v[194:197], v[54:57]
	v_mfma_f32_16x16x32_bf16 v[46:49], v[138:141], v[186:189], v[46:49]
	v_mfma_f32_16x16x32_bf16 v[38:41], v[146:149], v[186:189], v[38:41]
	v_mfma_f32_16x16x32_bf16 v[30:33], v[138:141], v[178:181], v[30:33]
	v_mfma_f32_16x16x32_bf16 v[22:25], v[146:149], v[178:181], v[22:25]
	v_mfma_f32_16x16x32_bf16 v[14:17], v[138:141], v[170:173], v[14:17]
	v_mfma_f32_16x16x32_bf16 v[6:9], v[146:149], v[170:173], v[6:9]
; #define PG8_STAGE_B(b, h, bp) PG8_STAGE2(PG8_SB(b, h), (bp) + (h) * hstepB, voffB[0], voffB[1])
; #define PG8_STAGE_A(b, h, ap, NX) do { if constexpr (GATHER) { const unsigned _o0 = (NX) ? vn[h][0] : vc[h][0], _o1 = (NX) ? vn[h][1] : vc[h][1]; PG8_STAGE2(PG8_SA(b, h), (ap), _o0, _o1); } \
;         else { PG8_STAGE2(PG8_SA(b, h), (ap) + (h) * hstepA, voffA[0], voffA[1]); } } while (0)
; #define PG8_LDA(dst, b, h) do { _Pragma("unroll") for (int m = 0; m < 4; ++m) _Pragma("unroll") for (int k = 0; k < 2; ++k) dst[m][k] = *(const LAS bf16x8*)(lds + PG8_SA(b, h) + aoff + m * 2048 + k * 1024); } while (0)
; #define PG8_LDB(dst, b, h) do { _Pragma("unroll") for (int n = 0; n < 2; ++n) _Pragma("unroll") for (int k = 0; k < 2; ++k) dst[n][k] = *(const LAS bf16x8*)(lds + PG8_SB(b, h) + boff + n * 2048 + k * 1024); } while (0)
; #define PG8_MMA(ai, bj, At, Bt) do { __builtin_amdgcn_s_setprio(1); _Pragma("unroll") for (int m = 0; m < 4; ++m) _Pragma("unroll") for (int n = 0; n < 2; ++n) _Pragma("unroll") for (int k = 0; k < 2; ++k) \
;         acc[ai][bj][m][n] = __builtin_amdgcn_mfma_f32_16x16x32_bf16(Bt[n][k], At[m][k], acc[ai][bj][m][n], 0, 0, 0); __builtin_amdgcn_s_setprio(0); } while (0)
; #define PG8_WAIT_V(n) asm volatile("s_waitcnt vmcnt(" #n ")" ::: "memory")
; #define PG8_WAIT_L(n) asm volatile("s_waitcnt lgkmcnt(" #n ")" ::: "memory")
; #define PG8_BAR __builtin_amdgcn_s_barrier()
; #define PG8_SCHED __builtin_amdgcn_sched_barrier(0)
; template <class Epi, class Sched, bool GATHER, bool LIGHTSKIP = false>
; __device__ __forceinline__ void gemm_phase(LAS unsigned char* lds, LAS unsigned char* xl, const int lda, const int ldb, const int K, const Sched& S, const Epi& E) {
;     ...
;             PG8_LDB(B0, 1, 0); PG8_LDB(B1, 1, 1); PG8_SCHED; PG8_LDA(At, 1, 0); PG8_STAGE_A(0, 1, a2, last);
;             PG8_WAIT_V(8); PG8_WAIT_L(0); PG8_BAR; PG8_MMA(0, 0, At, B0); PG8_MMA(0, 1, At, B1); PG8_BAR; PG8_SCHED;
;             PG8_LDA(At, 1, 1); PG8_STAGE_B(1, 0, b3); PG8_STAGE_B(1, 1, b3); PG8_STAGE_A(1, 0, a3, last);
;             PG8_WAIT_V(8); PG8_WAIT_L(0); PG8_BAR; if (!light) { PG8_MMA(1, 0, At, B0); PG8_MMA(1, 1, At, B1); } PG8_BAR; PG8_SCHED;
.LBB0_1351:
	v_mov_b32_e32 v221, v3
	v_lshl_add_u64 v[232:233], s[42:43], 0, v[2:3]
	v_lshl_add_u64 v[220:221], s[42:43], 0, v[220:221]
	s_barrier
	s_add_i32 s60, 0, 0x18000
	v_add_u32_e32 v2, s60, v211
	s_add_i32 s61, 0, 0x1c000
	ds_read_b128 v[150:153], v2
	ds_read_b128 v[154:157], v2 offset:1024
	ds_read_b128 v[158:161], v2 offset:2048
	ds_read_b128 v[162:165], v2 offset:3072
	v_add_u32_e32 v2, s61, v211
	ds_read_b128 v[134:137], v2
	ds_read_b128 v[138:141], v2 offset:1024
	ds_read_b128 v[142:145], v2 offset:2048
	ds_read_b128 v[146:149], v2 offset:3072
	s_mov_b32 m0, s4
	v_cndmask_b32_e64 v2, v206, v207, s[6:7]
	s_waitcnt lgkmcnt(0)
	ds_read_b128 v[166:169], v229 offset:32768
	ds_read_b128 v[170:173], v229 offset:33792
	ds_read_b128 v[174:177], v229 offset:34816
	ds_read_b128 v[178:181], v229 offset:35840
	ds_read_b128 v[182:185], v229 offset:36864
	ds_read_b128 v[186:189], v229 offset:37888
	ds_read_b128 v[190:193], v229 offset:38912
	ds_read_b128 v[194:197], v229 offset:39936
	v_cndmask_b32_e64 v234, v212, v231, s[6:7]
	global_load_lds_dwordx4 v2, s[42:43]
	s_mov_b32 m0, s5
	s_nop 0
	global_load_lds_dwordx4 v234, s[42:43]
	s_waitcnt vmcnt(8)
	s_waitcnt lgkmcnt(0)
	s_barrier
	s_waitcnt lgkmcnt(0)
	v_mfma_f32_16x16x32_bf16 v[130:133], v[150:153], v[166:169], v[130:133]
	v_mfma_f32_16x16x32_bf16 v[122:125], v[158:161], v[166:169], v[122:125]
	v_mfma_f32_16x16x32_bf16 v[114:117], v[150:153], v[174:177], v[114:117]
	v_mfma_f32_16x16x32_bf16 v[106:109], v[158:161], v[174:177], v[106:109]
	v_mfma_f32_16x16x32_bf16 v[98:101], v[150:153], v[182:185], v[98:101]
	v_mfma_f32_16x16x32_bf16 v[90:93], v[158:161], v[182:185], v[90:93]
	v_mfma_f32_16x16x32_bf16 v[82:85], v[150:153], v[190:193], v[82:85]
	v_mfma_f32_16x16x32_bf16 v[74:77], v[158:161], v[190:193], v[74:77]
	v_mfma_f32_16x16x32_bf16 v[130:133], v[154:157], v[170:173], v[130:133]
	v_mfma_f32_16x16x32_bf16 v[122:125], v[162:165], v[170:173], v[122:125]
	v_mfma_f32_16x16x32_bf16 v[114:117], v[154:157], v[178:181], v[114:117]
	v_mfma_f32_16x16x32_bf16 v[106:109], v[162:165], v[178:181], v[106:109]
	v_mfma_f32_16x16x32_bf16 v[98:101], v[154:157], v[186:189], v[98:101]
	v_mfma_f32_16x16x32_bf16 v[90:93], v[162:165], v[186:189], v[90:93]
	v_mfma_f32_16x16x32_bf16 v[82:85], v[154:157], v[194:197], v[82:85]
	v_mfma_f32_16x16x32_bf16 v[74:77], v[162:165], v[194:197], v[74:77]
	v_mfma_f32_16x16x32_bf16 v[126:129], v[134:137], v[166:169], v[126:129]
	v_mfma_f32_16x16x32_bf16 v[118:121], v[142:145], v[166:169], v[118:121]
	v_mfma_f32_16x16x32_bf16 v[110:113], v[134:137], v[174:177], v[110:113]
	v_mfma_f32_16x16x32_bf16 v[102:105], v[142:145], v[174:177], v[102:105]
	v_mfma_f32_16x16x32_bf16 v[94:97], v[134:137], v[182:185], v[94:97]
	v_mfma_f32_16x16x32_bf16 v[86:89], v[142:145], v[182:185], v[86:89]
	v_mfma_f32_16x16x32_bf16 v[78:81], v[134:137], v[190:193], v[78:81]
	v_mfma_f32_16x16x32_bf16 v[70:73], v[142:145], v[190:193], v[70:73]
	v_mfma_f32_16x16x32_bf16 v[126:129], v[138:141], v[170:173], v[126:129]
	v_mfma_f32_16x16x32_bf16 v[118:121], v[146:149], v[170:173], v[118:121]
	v_mfma_f32_16x16x32_bf16 v[110:113], v[138:141], v[178:181], v[110:113]
	v_mfma_f32_16x16x32_bf16 v[102:105], v[146:149], v[178:181], v[102:105]
	v_mfma_f32_16x16x32_bf16 v[94:97], v[138:141], v[186:189], v[94:97]
	v_mfma_f32_16x16x32_bf16 v[86:89], v[146:149], v[186:189], v[86:89]
	v_mfma_f32_16x16x32_bf16 v[78:81], v[138:141], v[194:197], v[78:81]
	v_mfma_f32_16x16x32_bf16 v[70:73], v[146:149], v[194:197], v[70:73]
	s_barrier
	s_add_i32 s6, s60, s0
	v_lshl_add_u64 v[4:5], v[4:5], 0, s[12:13]
	s_mov_b32 m0, s6
	ds_read_b128 v[190:193], v229 offset:49152
	ds_read_b128 v[194:197], v229 offset:50176
	ds_read_b128 v[182:185], v229 offset:51200
	ds_read_b128 v[186:189], v229 offset:52224
	ds_read_b128 v[174:177], v229 offset:53248
	ds_read_b128 v[178:181], v229 offset:54272
	ds_read_b128 v[166:169], v229 offset:55296
	ds_read_b128 v[170:173], v229 offset:56320
	global_load_lds_dwordx4 v[4:5], off
	s_add_i32 m0, s6, 0x2000
	s_add_u32 s6, s40, 0x80080
	v_lshl_add_u64 v[4:5], v[218:219], 0, s[12:13]
	s_addc_u32 s7, s41, 0
	s_add_i32 s40, s61, s0
	global_load_lds_dwordx4 v[4:5], off
	v_lshl_add_u64 v[4:5], s[6:7], 0, v[200:201]
	s_mov_b32 m0, s40
	s_and_b64 vcc, exec, s[8:9]
	global_load_lds_dwordx4 v[4:5], off
	v_lshl_add_u64 v[4:5], s[6:7], 0, v[202:203]
	s_add_i32 m0, s40, 0x2000
	s_nop 0
	global_load_lds_dwordx4 v[4:5], off
	v_lshl_add_u64 v[4:5], v[232:233], 0, s[12:13]
	s_mov_b32 m0, s27
	s_nop 0
	global_load_lds_dwordx4 v[4:5], off
	v_lshl_add_u64 v[4:5], v[220:221], 0, s[12:13]
	s_mov_b32 m0, s33
	s_nop 0
	global_load_lds_dwordx4 v[4:5], off
	s_waitcnt vmcnt(8)
	s_waitcnt lgkmcnt(0)
	s_barrier
	s_cbranch_vccnz .LBB0_1338
	s_waitcnt lgkmcnt(0)
	v_mfma_f32_16x16x32_bf16 v[66:69], v[150:153], v[190:193], v[66:69]
	v_mfma_f32_16x16x32_bf16 v[58:61], v[158:161], v[190:193], v[58:61]
	v_mfma_f32_16x16x32_bf16 v[50:53], v[150:153], v[182:185], v[50:53]
	v_mfma_f32_16x16x32_bf16 v[42:45], v[158:161], v[182:185], v[42:45]
	v_mfma_f32_16x16x32_bf16 v[34:37], v[150:153], v[174:177], v[34:37]
	v_mfma_f32_16x16x32_bf16 v[26:29], v[158:161], v[174:177], v[26:29]
	v_mfma_f32_16x16x32_bf16 v[18:21], v[150:153], v[166:169], v[18:21]
	v_mfma_f32_16x16x32_bf16 v[10:13], v[158:161], v[166:169], v[10:13]
	v_mfma_f32_16x16x32_bf16 v[66:69], v[154:157], v[194:197], v[66:69]
	v_mfma_f32_16x16x32_bf16 v[58:61], v[162:165], v[194:197], v[58:61]
	v_mfma_f32_16x16x32_bf16 v[50:53], v[154:157], v[186:189], v[50:53]
	v_mfma_f32_16x16x32_bf16 v[42:45], v[162:165], v[186:189], v[42:45]
	v_mfma_f32_16x16x32_bf16 v[34:37], v[154:157], v[178:181], v[34:37]
	v_mfma_f32_16x16x32_bf16 v[26:29], v[162:165], v[178:181], v[26:29]
	v_mfma_f32_16x16x32_bf16 v[18:21], v[154:157], v[170:173], v[18:21]
	v_mfma_f32_16x16x32_bf16 v[10:13], v[162:165], v[170:173], v[10:13]
	v_mfma_f32_16x16x32_bf16 v[62:65], v[134:137], v[190:193], v[62:65]
	v_mfma_f32_16x16x32_bf16 v[54:57], v[142:145], v[190:193], v[54:57]
	v_mfma_f32_16x16x32_bf16 v[46:49], v[134:137], v[182:185], v[46:49]
	v_mfma_f32_16x16x32_bf16 v[38:41], v[142:145], v[182:185], v[38:41]
	v_mfma_f32_16x16x32_bf16 v[30:33], v[134:137], v[174:177], v[30:33]
	v_mfma_f32_16x16x32_bf16 v[22:25], v[142:145], v[174:177], v[22:25]
	v_mfma_f32_16x16x32_bf16 v[14:17], v[134:137], v[166:169], v[14:17]
	v_mfma_f32_16x16x32_bf16 v[4:7], v[142:145], v[166:169], v[6:9]
	v_mfma_f32_16x16x32_bf16 v[62:65], v[138:141], v[194:197], v[62:65]
	v_mfma_f32_16x16x32_bf16 v[54:57], v[146:149], v[194:197], v[54:57]
	v_mfma_f32_16x16x32_bf16 v[46:49], v[138:141], v[186:189], v[46:49]
	v_mfma_f32_16x16x32_bf16 v[38:41], v[146:149], v[186:189], v[38:41]
	v_mfma_f32_16x16x32_bf16 v[30:33], v[138:141], v[178:181], v[30:33]
	v_mfma_f32_16x16x32_bf16 v[22:25], v[146:149], v[178:181], v[22:25]
	v_mfma_f32_16x16x32_bf16 v[14:17], v[138:141], v[170:173], v[14:17]
	v_mfma_f32_16x16x32_bf16 v[6:9], v[146:149], v[170:173], v[4:7]
	s_branch .LBB0_1338

; __device__ __forceinline__ int otid() { int t = threadIdx.x; asm volatile("" : "+v"(t)); return t; }
; #define PG8_STAGE_B(b, h, bp) PG8_STAGE2(PG8_SB(b, h), (bp) + (h) * hstepB, voffB[0], voffB[1])
; #define PG8_STAGE_A(b, h, ap, NX) do { if constexpr (GATHER) { const unsigned _o0 = (NX) ? vn[h][0] : vc[h][0], _o1 = (NX) ? vn[h][1] : vc[h][1]; PG8_STAGE2(PG8_SA(b, h), (ap), _o0, _o1); } \
;         else { PG8_STAGE2(PG8_SA(b, h), (ap) + (h) * hstepA, voffA[0], voffA[1]); } } while (0)
; #define PG8_BAR __builtin_amdgcn_s_barrier()
; template <class Epi, class Sched, bool GATHER, bool LIGHTSKIP = false>
; __device__ __forceinline__ void gemm_phase(LAS unsigned char* lds, LAS unsigned char* xl, const int lda, const int ldb, const int K, const Sched& S, const Epi& E) {
;     const int tid = otid(), wid = __builtin_amdgcn_readfirstlane(tid >> 6), lane = tid & 63, wr = wid >> 2, wc = wid & 3, fr = lane & 15, fq = lane >> 4;
;     const int nt = K / BK;
;     int Rr[2], Cc[2]; unsigned voffA[2], voffB[2];
; #pragma unroll
;     for (int i = 0; i < 2; ++i) { stage_rc(tid * 16 + i * 8192, Rr[i], Cc[i]); const int Rb = Epi::PERM ? ((Rr[i] & ~31) + perm32(Rr[i] & 31)) : Rr[i];
;         voffA[i] = (unsigned)(Rr[i] * lda + Cc[i]) * 2u; voffB[i] = (unsigned)(Rb * ldb + Cc[i]) * 2u; }
;     unsigned vc[2][2], vn[2][2];
;     const size_t kstep = (size_t)(BK * 2);
;     const size_t hstepA = (size_t)HALF * lda * 2, hstepB = (size_t)HALF * ldb * 2;
;     const unsigned ldsw = (unsigned)wid * 1024u;
;     const int aoff = lds_byte(wr * 64 + fr, fq * 8), boff = lds_byte(wc * 32 + fr, fq * 8);
;     ...
;     GUnit cur, nxt; int ui = 0;
;     if (!S.next(0, cur)) return;
;     Acc acc;
; #pragma unroll
;     for (int a = 0; a < 2; ++a)
; #pragma unroll
;         for (int b = 0; b < 2; ++b)
; #pragma unroll
;             for (int m = 0; m < 4; ++m)
; #pragma unroll
;                 for (int n = 0; n < 2; ++n) acc[a][b][m][n] = (f32x4){0.f, 0.f, 0.f, 0.f};
;     bf16x8 At[4][2], B0[2][2], B1[2][2];
;     const char* cA = cur.A; const char* cB = cur.B;
;     if constexpr (GATHER) { S.offsets(cur, lda, vc);
; #pragma unroll
;         for (int h = 0; h < 2; ++h) { vn[h][0] = vc[h][0]; vn[h][1] = vc[h][1]; } }
;     PG8_STAGE_B(0, 0, cB); PG8_STAGE_B(0, 1, cB); PG8_STAGE_A(0, 0, cA, false); PG8_STAGE_A(0, 1, cA, false);
;     if (wr == 1) PG8_BAR;
;     PG8_WAIT_V(2); PG8_BAR;
.LBB0_1420:
	v_ashrrev_i32_e32 v2, 31, v3
	v_lshrrev_b32_e32 v2, 26, v2
	v_add_u32_e32 v2, v3, v2
	v_ashrrev_i32_e32 v12, 6, v2
	v_bfe_i32 v2, v3, 27, 1
	v_lshlrev_b32_e32 v1, 4, v3
	v_lshrrev_b32_e32 v2, 22, v2
	v_add_u32_e32 v2, v1, v2
	v_and_b32_e32 v2, 0xfffffc00, v2
	v_sub_u32_e32 v2, v1, v2
	v_lshrrev_b32_e32 v4, 4, v2
	v_bitop3_b32 v4, v4, v2, 32 bitop3:0x6c
	v_ashrrev_i32_e32 v2, 31, v2
	v_lshrrev_b32_e32 v2, 26, v2
	v_add_u32_e32 v2, v4, v2
	v_ashrrev_i32_e32 v13, 6, v2
	v_lshlrev_b32_e32 v5, 3, v12
	v_mul_i32_i24_e32 v6, 64, v13
	v_and_b32_e32 v5, -16, v5
	v_sub_u32_e32 v4, v4, v6
	v_mov_b32_e32 v6, 1
	v_add_u32_e32 v2, v13, v5
	v_lshlrev_b32_e32 v5, 5, v12
	v_ashrrev_i16_sdwa v4, v6, sext(v4) dst_sel:DWORD dst_unused:UNUSED_PAD src0_sel:DWORD src1_sel:BYTE_0
	v_and_b32_e32 v5, 32, v5
	v_bfe_i32 v14, v4, 0, 16
	v_and_b32_e32 v8, 3, v13
	s_mov_b32 s0, 0x3fffe0
	v_add_lshl_u32 v5, v5, v14, 1
	v_add_u32_e32 v1, 0x2000, v1
	v_lshlrev_b32_e32 v4, 1, v2
	v_lshrrev_b32_e32 v7, 2, v2
	v_and_or_b32 v8, v2, s0, v8
	v_lshl_add_u32 v198, v2, 10, v5
	v_ashrrev_i32_e32 v2, 31, v1
	v_lshrrev_b32_e32 v2, 22, v2
	v_add_u32_e32 v2, v1, v2
	v_ashrrev_i32_e32 v15, 10, v2
	v_mul_i32_i24_e32 v2, 0x400, v15
	v_sub_u32_e32 v1, v1, v2
	v_and_b32_e32 v4, 24, v4
	v_and_b32_e32 v7, 4, v7
	v_lshrrev_b32_e32 v2, 4, v1
	v_or3_b32 v4, v8, v7, v4
	v_bitop3_b32 v1, v2, v1, 32 bitop3:0x6c
	v_lshl_add_u32 v200, v4, 10, v5
	v_ashrrev_i32_e32 v4, 31, v1
	v_lshrrev_b32_e32 v4, 26, v4
	v_add_u32_e32 v4, v1, v4
	v_lshlrev_b32_e32 v2, 3, v15
	v_ashrrev_i32_e32 v16, 6, v4
	v_and_b32_e32 v4, 0xc0, v4
	v_and_b32_e32 v2, -16, v2
	v_sub_u32_e32 v1, v1, v4
	v_add_u32_e32 v2, v16, v2
	v_ashrrev_i16_sdwa v1, v6, sext(v1) dst_sel:DWORD dst_unused:UNUSED_PAD src0_sel:DWORD src1_sel:BYTE_0
	v_and_b32_e32 v6, 3, v16
	s_ashr_i32 s14, s16, 6
	v_and_or_b32 v6, v2, s0, v6
	s_lshl_b32 s0, s14, 10
	v_lshlrev_b32_e32 v5, 5, v15
	v_bfe_i32 v17, v1, 0, 16
	v_lshlrev_b32_e32 v1, 1, v2
	v_lshrrev_b32_e32 v4, 2, v2
	s_add_i32 s1, s0, 0
	v_and_b32_e32 v5, 32, v5
	v_and_b32_e32 v1, 24, v1
	v_and_b32_e32 v4, 4, v4
	s_add_i32 m0, s1, 0x10000
	s_ashr_i32 s17, s16, 8
	v_or3_b32 v1, v6, v4, v1
	v_add_lshl_u32 v4, v5, v17, 1
	global_load_lds_dwordx4 v200, s[34:35]
	s_add_i32 m0, s1, 0x12000
	v_lshl_add_u32 v204, v1, 10, v4
	s_add_u32 s4, s34, 0x20000
	global_load_lds_dwordx4 v204, s[34:35]
	s_addc_u32 s5, s35, 0
	s_add_i32 m0, s1, 0x14000
	s_add_i32 s2, s1, 0x2000
	global_load_lds_dwordx4 v200, s[4:5]
	s_add_i32 m0, s1, 0x16000
	s_add_u32 s12, s6, 0x20000
	global_load_lds_dwordx4 v204, s[4:5]
	s_mov_b32 m0, s1
	v_lshl_add_u32 v202, v2, 10, v4
	global_load_lds_dwordx4 v198, s[6:7]
	s_mov_b32 m0, s2
	s_addc_u32 s13, s7, 0
	s_add_i32 s4, s1, 0x4000
	global_load_lds_dwordx4 v202, s[6:7]
	s_mov_b32 m0, s4
	s_add_i32 s5, s1, 0x6000
	global_load_lds_dwordx4 v198, s[12:13]
	s_mov_b32 m0, s5
	v_mov_b32_e32 v2, 0
	global_load_lds_dwordx4 v202, s[12:13]
	v_mov_b32_e32 v201, v2
	v_mov_b32_e32 v205, v2
	v_mov_b32_e32 v199, v2
	v_mov_b32_e32 v203, v2
	s_cmp_eq_u32 s17, 1
	v_lshl_add_u64 v[10:11], s[34:35], 0, v[200:201]
	s_mov_b32 s26, 0
	v_lshl_add_u64 v[8:9], s[34:35], 0, v[204:205]
	v_lshl_add_u64 v[4:5], s[6:7], 0, v[198:199]
	s_cselect_b64 s[12:13], -1, 0
	s_cmp_lg_u32 s17, 1
	v_lshl_add_u64 v[6:7], s[6:7], 0, v[202:203]
	s_cbranch_scc1 .LBB0_1422
	s_barrier
	s_setprio 1

; #define PG8_STAGE_B(b, h, bp) PG8_STAGE2(PG8_SB(b, h), (bp) + (h) * hstepB, voffB[0], voffB[1])
; #define PG8_STAGE_A(b, h, ap, NX) do { if constexpr (GATHER) { const unsigned _o0 = (NX) ? vn[h][0] : vc[h][0], _o1 = (NX) ? vn[h][1] : vc[h][1]; PG8_STAGE2(PG8_SA(b, h), (ap), _o0, _o1); } \
;         else { PG8_STAGE2(PG8_SA(b, h), (ap) + (h) * hstepA, voffA[0], voffA[1]); } } while (0)
; #define PG8_LDA(dst, b, h) do { _Pragma("unroll") for (int m = 0; m < 4; ++m) _Pragma("unroll") for (int k = 0; k < 2; ++k) dst[m][k] = *(const LAS bf16x8*)(lds + PG8_SA(b, h) + aoff + m * 2048 + k * 1024); } while (0)
; #define PG8_LDB(dst, b, h) do { _Pragma("unroll") for (int n = 0; n < 2; ++n) _Pragma("unroll") for (int k = 0; k < 2; ++k) dst[n][k] = *(const LAS bf16x8*)(lds + PG8_SB(b, h) + boff + n * 2048 + k * 1024); } while (0)
; #define PG8_MMA(ai, bj, At, Bt) do { __builtin_amdgcn_s_setprio(1); _Pragma("unroll") for (int m = 0; m < 4; ++m) _Pragma("unroll") for (int n = 0; n < 2; ++n) _Pragma("unroll") for (int k = 0; k < 2; ++k) \
;         acc[ai][bj][m][n] = __builtin_amdgcn_mfma_f32_16x16x32_bf16(Bt[n][k], At[m][k], acc[ai][bj][m][n], 0, 0, 0); __builtin_amdgcn_s_setprio(0); } while (0)
; #define PG8_WAIT_V(n) asm volatile("s_waitcnt vmcnt(" #n ")" ::: "memory")
; #define PG8_WAIT_L(n) asm volatile("s_waitcnt lgkmcnt(" #n ")" ::: "memory")
; #define PG8_BAR __builtin_amdgcn_s_barrier()
; #define PG8_SCHED __builtin_amdgcn_sched_barrier(0)
; template <class Epi, class Sched, bool GATHER, bool LIGHTSKIP = false>
; __device__ __forceinline__ void gemm_phase(LAS unsigned char* lds, LAS unsigned char* xl, const int lda, const int ldb, const int K, const Sched& S, const Epi& E) {
;     ...
;             PG8_LDB(B0, 0, 0); PG8_LDB(B1, 0, 1); PG8_SCHED; PG8_LDA(At, 0, 0); PG8_STAGE_A(1, 1, a1, false);
;             PG8_WAIT_V(8); PG8_WAIT_L(0); PG8_BAR; PG8_MMA(0, 0, At, B0); PG8_MMA(0, 1, At, B1); PG8_BAR; PG8_SCHED;
;             PG8_LDA(At, 0, 1); PG8_STAGE_B(0, 0, b2); PG8_STAGE_B(0, 1, b2); PG8_STAGE_A(0, 0, a2, last);
;             PG8_WAIT_V(8); PG8_WAIT_L(0); PG8_BAR; if (!light) { PG8_MMA(1, 0, At, B0); PG8_MMA(1, 1, At, B1); } PG8_BAR; PG8_SCHED;
.LBB0_1429:
	s_add_u32 s6, s34, 0xfffe0080
	s_addc_u32 s7, s35, -1
	s_add_i32 s51, 0, 0x10000
	v_add_u32_e32 v3, s51, v216
	ds_read_b128 v[150:153], v3
	ds_read_b128 v[154:157], v3 offset:1024
	ds_read_b128 v[158:161], v3 offset:2048
	ds_read_b128 v[162:165], v3 offset:3072
	ds_read_b128 v[134:137], v219
	ds_read_b128 v[138:141], v219 offset:1024
	ds_read_b128 v[142:145], v219 offset:2048
	ds_read_b128 v[146:149], v219 offset:3072
	s_cmp_eq_u32 s50, 4
	s_cselect_b32 s39, s19, s7
	s_cselect_b32 s38, s18, s6
	s_cselect_b32 s37, s21, s49
	s_cselect_b32 s36, s20, s29
	v_lshl_add_u64 v[4:5], s[34:35], 0, v[208:209]
	s_add_i32 m0, s1, 0xc000
	s_waitcnt lgkmcnt(0)
	ds_read_b128 v[166:169], v220
	ds_read_b128 v[170:173], v220 offset:1024
	ds_read_b128 v[174:177], v220 offset:2048
	ds_read_b128 v[178:181], v220 offset:3072
	ds_read_b128 v[182:185], v220 offset:4096
	ds_read_b128 v[186:189], v220 offset:5120
	ds_read_b128 v[190:193], v220 offset:6144
	ds_read_b128 v[194:197], v220 offset:7168
	global_load_lds_dwordx4 v[4:5], off
	v_lshl_add_u64 v[4:5], s[34:35], 0, v[206:207]
	s_add_i32 m0, s1, 0xe000
	s_nop 0
	global_load_lds_dwordx4 v[4:5], off
	s_waitcnt vmcnt(8)
	s_waitcnt lgkmcnt(0)
	s_barrier
	s_waitcnt lgkmcnt(0)
	v_mfma_f32_16x16x32_bf16 v[130:133], v[150:153], v[166:169], v[130:133]
	v_mfma_f32_16x16x32_bf16 v[126:129], v[158:161], v[166:169], v[126:129]
	v_mfma_f32_16x16x32_bf16 v[114:117], v[150:153], v[174:177], v[114:117]
	v_mfma_f32_16x16x32_bf16 v[110:113], v[158:161], v[174:177], v[110:113]
	v_mfma_f32_16x16x32_bf16 v[98:101], v[150:153], v[182:185], v[98:101]
	v_mfma_f32_16x16x32_bf16 v[94:97], v[158:161], v[182:185], v[94:97]
	v_mfma_f32_16x16x32_bf16 v[82:85], v[150:153], v[190:193], v[82:85]
	v_mfma_f32_16x16x32_bf16 v[78:81], v[158:161], v[190:193], v[78:81]
	v_mfma_f32_16x16x32_bf16 v[130:133], v[154:157], v[170:173], v[130:133]
	v_mfma_f32_16x16x32_bf16 v[126:129], v[162:165], v[170:173], v[126:129]
	v_mfma_f32_16x16x32_bf16 v[114:117], v[154:157], v[178:181], v[114:117]
	v_mfma_f32_16x16x32_bf16 v[110:113], v[162:165], v[178:181], v[110:113]
	v_mfma_f32_16x16x32_bf16 v[98:101], v[154:157], v[186:189], v[98:101]
	v_mfma_f32_16x16x32_bf16 v[94:97], v[162:165], v[186:189], v[94:97]
	v_mfma_f32_16x16x32_bf16 v[82:85], v[154:157], v[194:197], v[82:85]
	v_mfma_f32_16x16x32_bf16 v[78:81], v[162:165], v[194:197], v[78:81]
	v_mfma_f32_16x16x32_bf16 v[122:125], v[134:137], v[166:169], v[122:125]
	v_mfma_f32_16x16x32_bf16 v[118:121], v[142:145], v[166:169], v[118:121]
	v_mfma_f32_16x16x32_bf16 v[106:109], v[134:137], v[174:177], v[106:109]
	v_mfma_f32_16x16x32_bf16 v[102:105], v[142:145], v[174:177], v[102:105]
	v_mfma_f32_16x16x32_bf16 v[90:93], v[134:137], v[182:185], v[90:93]
	v_mfma_f32_16x16x32_bf16 v[86:89], v[142:145], v[182:185], v[86:89]
	v_mfma_f32_16x16x32_bf16 v[74:77], v[134:137], v[190:193], v[74:77]
	v_mfma_f32_16x16x32_bf16 v[70:73], v[142:145], v[190:193], v[70:73]
	v_mfma_f32_16x16x32_bf16 v[122:125], v[138:141], v[170:173], v[122:125]
	v_mfma_f32_16x16x32_bf16 v[118:121], v[146:149], v[170:173], v[118:121]
	v_mfma_f32_16x16x32_bf16 v[106:109], v[138:141], v[178:181], v[106:109]
	v_mfma_f32_16x16x32_bf16 v[102:105], v[146:149], v[178:181], v[102:105]
	v_mfma_f32_16x16x32_bf16 v[90:93], v[138:141], v[186:189], v[90:93]
	v_mfma_f32_16x16x32_bf16 v[86:89], v[146:149], v[186:189], v[86:89]
	v_mfma_f32_16x16x32_bf16 v[74:77], v[138:141], v[194:197], v[74:77]
	v_mfma_f32_16x16x32_bf16 v[70:73], v[146:149], v[194:197], v[70:73]
	s_barrier
	s_add_i32 s6, s51, s0
	v_lshl_add_u64 v[4:5], s[36:37], 0, v[200:201]
	s_mov_b32 m0, s6
	ds_read_b128 v[190:193], v220 offset:16384
	ds_read_b128 v[194:197], v220 offset:17408
	ds_read_b128 v[182:185], v220 offset:18432
	ds_read_b128 v[186:189], v220 offset:19456
	ds_read_b128 v[174:177], v220 offset:20480
	ds_read_b128 v[178:181], v220 offset:21504
	ds_read_b128 v[166:169], v220 offset:22528
	ds_read_b128 v[170:173], v220 offset:23552
	global_load_lds_dwordx4 v[4:5], off
	s_add_i32 m0, s6, 0x2000
	s_add_u32 s6, s36, 0x20000
	v_lshl_add_u64 v[210:211], s[36:37], 0, v[204:205]
	s_addc_u32 s7, s37, 0
	s_add_i32 s51, s43, s0
	global_load_lds_dwordx4 v[210:211], off
	v_lshl_add_u64 v[212:213], s[6:7], 0, v[200:201]
	s_mov_b32 m0, s51
	v_lshl_add_u64 v[214:215], s[38:39], 0, v[202:203]
	global_load_lds_dwordx4 v[212:213], off
	v_lshl_add_u64 v[212:213], s[6:7], 0, v[204:205]
	s_add_i32 m0, s51, 0x2000
	v_cmp_ne_u32_e64 s[6:7], 1, v221
	global_load_lds_dwordx4 v[212:213], off
	v_lshl_add_u64 v[212:213], s[38:39], 0, v[198:199]
	s_mov_b32 m0, s1
	s_andn2_b64 vcc, exec, s[30:31]
	global_load_lds_dwordx4 v[212:213], off
	s_mov_b32 m0, s2
	s_nop 0
	global_load_lds_dwordx4 v[214:215], off
	s_waitcnt vmcnt(8)
	s_waitcnt lgkmcnt(0)
	s_barrier
	s_cbranch_vccnz .LBB0_1431
	s_waitcnt lgkmcnt(0)
	v_mfma_f32_16x16x32_bf16 v[66:69], v[150:153], v[190:193], v[66:69]
	v_mfma_f32_16x16x32_bf16 v[62:65], v[158:161], v[190:193], v[62:65]
	v_mfma_f32_16x16x32_bf16 v[50:53], v[150:153], v[182:185], v[50:53]
	v_mfma_f32_16x16x32_bf16 v[46:49], v[158:161], v[182:185], v[46:49]
	v_mfma_f32_16x16x32_bf16 v[34:37], v[150:153], v[174:177], v[34:37]
	v_mfma_f32_16x16x32_bf16 v[30:33], v[158:161], v[174:177], v[30:33]
	v_mfma_f32_16x16x32_bf16 v[18:21], v[150:153], v[166:169], v[18:21]
	v_mfma_f32_16x16x32_bf16 v[14:17], v[158:161], v[166:169], v[14:17]
	v_mfma_f32_16x16x32_bf16 v[66:69], v[154:157], v[194:197], v[66:69]
	v_mfma_f32_16x16x32_bf16 v[62:65], v[162:165], v[194:197], v[62:65]
	v_mfma_f32_16x16x32_bf16 v[50:53], v[154:157], v[186:189], v[50:53]
	v_mfma_f32_16x16x32_bf16 v[46:49], v[162:165], v[186:189], v[46:49]
	v_mfma_f32_16x16x32_bf16 v[34:37], v[154:157], v[178:181], v[34:37]
	v_mfma_f32_16x16x32_bf16 v[30:33], v[162:165], v[178:181], v[30:33]
	v_mfma_f32_16x16x32_bf16 v[18:21], v[154:157], v[170:173], v[18:21]
	v_mfma_f32_16x16x32_bf16 v[14:17], v[162:165], v[170:173], v[14:17]
	v_mfma_f32_16x16x32_bf16 v[58:61], v[134:137], v[190:193], v[58:61]
	v_mfma_f32_16x16x32_bf16 v[54:57], v[142:145], v[190:193], v[54:57]
	v_mfma_f32_16x16x32_bf16 v[42:45], v[134:137], v[182:185], v[42:45]
	v_mfma_f32_16x16x32_bf16 v[38:41], v[142:145], v[182:185], v[38:41]
	v_mfma_f32_16x16x32_bf16 v[26:29], v[134:137], v[174:177], v[26:29]
	v_mfma_f32_16x16x32_bf16 v[22:25], v[142:145], v[174:177], v[22:25]
	v_mfma_f32_16x16x32_bf16 v[10:13], v[134:137], v[166:169], v[10:13]
	v_mfma_f32_16x16x32_bf16 v[6:9], v[142:145], v[166:169], v[6:9]
	v_mfma_f32_16x16x32_bf16 v[58:61], v[138:141], v[194:197], v[58:61]
	v_mfma_f32_16x16x32_bf16 v[54:57], v[146:149], v[194:197], v[54:57]
	v_mfma_f32_16x16x32_bf16 v[42:45], v[138:141], v[186:189], v[42:45]
	v_mfma_f32_16x16x32_bf16 v[38:41], v[146:149], v[186:189], v[38:41]
	v_mfma_f32_16x16x32_bf16 v[26:29], v[138:141], v[178:181], v[26:29]
	v_mfma_f32_16x16x32_bf16 v[22:25], v[146:149], v[178:181], v[22:25]
	v_mfma_f32_16x16x32_bf16 v[10:13], v[138:141], v[170:173], v[10:13]
	v_mfma_f32_16x16x32_bf16 v[6:9], v[146:149], v[170:173], v[6:9]
; #define PG8_STAGE_B(b, h, bp) PG8_STAGE2(PG8_SB(b, h), (bp) + (h) * hstepB, voffB[0], voffB[1])
; #define PG8_STAGE_A(b, h, ap, NX) do { if constexpr (GATHER) { const unsigned _o0 = (NX) ? vn[h][0] : vc[h][0], _o1 = (NX) ? vn[h][1] : vc[h][1]; PG8_STAGE2(PG8_SA(b, h), (ap), _o0, _o1); } \
;         else { PG8_STAGE2(PG8_SA(b, h), (ap) + (h) * hstepA, voffA[0], voffA[1]); } } while (0)
; #define PG8_LDA(dst, b, h) do { _Pragma("unroll") for (int m = 0; m < 4; ++m) _Pragma("unroll") for (int k = 0; k < 2; ++k) dst[m][k] = *(const LAS bf16x8*)(lds + PG8_SA(b, h) + aoff + m * 2048 + k * 1024); } while (0)
; #define PG8_LDB(dst, b, h) do { _Pragma("unroll") for (int n = 0; n < 2; ++n) _Pragma("unroll") for (int k = 0; k < 2; ++k) dst[n][k] = *(const LAS bf16x8*)(lds + PG8_SB(b, h) + boff + n * 2048 + k * 1024); } while (0)
; #define PG8_MMA(ai, bj, At, Bt) do { __builtin_amdgcn_s_setprio(1); _Pragma("unroll") for (int m = 0; m < 4; ++m) _Pragma("unroll") for (int n = 0; n < 2; ++n) _Pragma("unroll") for (int k = 0; k < 2; ++k) \
;         acc[ai][bj][m][n] = __builtin_amdgcn_mfma_f32_16x16x32_bf16(Bt[n][k], At[m][k], acc[ai][bj][m][n], 0, 0, 0); __builtin_amdgcn_s_setprio(0); } while (0)
; #define PG8_WAIT_V(n) asm volatile("s_waitcnt vmcnt(" #n ")" ::: "memory")
; #define PG8_WAIT_L(n) asm volatile("s_waitcnt lgkmcnt(" #n ")" ::: "memory")
; #define PG8_BAR __builtin_amdgcn_s_barrier()
; #define PG8_SCHED __builtin_amdgcn_sched_barrier(0)
; template <class Epi, class Sched, bool GATHER, bool LIGHTSKIP = false>
; __device__ __forceinline__ void gemm_phase(LAS unsigned char* lds, LAS unsigned char* xl, const int lda, const int ldb, const int K, const Sched& S, const Epi& E) {
;     ...
;             PG8_LDB(B0, 1, 0); PG8_LDB(B1, 1, 1); PG8_SCHED; PG8_LDA(At, 1, 0); PG8_STAGE_A(0, 1, a2, last);
;             PG8_WAIT_V(8); PG8_WAIT_L(0); PG8_BAR; PG8_MMA(0, 0, At, B0); PG8_MMA(0, 1, At, B1); PG8_BAR; PG8_SCHED;
;             PG8_LDA(At, 1, 1); PG8_STAGE_B(1, 0, b3); PG8_STAGE_B(1, 1, b3); PG8_STAGE_A(1, 0, a3, last);
;             PG8_WAIT_V(8); PG8_WAIT_L(0); PG8_BAR; if (!light) { PG8_MMA(1, 0, At, B0); PG8_MMA(1, 1, At, B1); } PG8_BAR; PG8_SCHED;
.LBB0_1431:
	s_barrier
	s_add_i32 s51, 0, 0x18000
	v_add_u32_e32 v3, s51, v216
	s_add_i32 s52, 0, 0x1c000
	ds_read_b128 v[150:153], v3
	ds_read_b128 v[154:157], v3 offset:1024
	ds_read_b128 v[158:161], v3 offset:2048
	ds_read_b128 v[162:165], v3 offset:3072
	v_add_u32_e32 v3, s52, v216
	ds_read_b128 v[134:137], v3
	ds_read_b128 v[138:141], v3 offset:1024
	ds_read_b128 v[142:145], v3 offset:2048
	ds_read_b128 v[146:149], v3 offset:3072
	s_add_u32 s38, s38, 0x20000
	s_addc_u32 s39, s39, 0
	s_mov_b32 m0, s4
	v_lshl_add_u64 v[222:223], s[38:39], 0, v[198:199]
	s_waitcnt lgkmcnt(0)
	ds_read_b128 v[166:169], v220 offset:32768
	ds_read_b128 v[170:173], v220 offset:33792
	ds_read_b128 v[174:177], v220 offset:34816
	ds_read_b128 v[178:181], v220 offset:35840
	ds_read_b128 v[182:185], v220 offset:36864
	ds_read_b128 v[186:189], v220 offset:37888
	ds_read_b128 v[190:193], v220 offset:38912
	ds_read_b128 v[194:197], v220 offset:39936
	global_load_lds_dwordx4 v[222:223], off
	v_lshl_add_u64 v[222:223], s[38:39], 0, v[202:203]
	s_mov_b32 m0, s5
	s_nop 0
	global_load_lds_dwordx4 v[222:223], off
	s_waitcnt vmcnt(8)
	s_waitcnt lgkmcnt(0)
	s_barrier
	s_waitcnt lgkmcnt(0)
	v_mfma_f32_16x16x32_bf16 v[130:133], v[150:153], v[166:169], v[130:133]
	v_mfma_f32_16x16x32_bf16 v[126:129], v[158:161], v[166:169], v[126:129]
	v_mfma_f32_16x16x32_bf16 v[114:117], v[150:153], v[174:177], v[114:117]
	v_mfma_f32_16x16x32_bf16 v[110:113], v[158:161], v[174:177], v[110:113]
	v_mfma_f32_16x16x32_bf16 v[98:101], v[150:153], v[182:185], v[98:101]
	v_mfma_f32_16x16x32_bf16 v[94:97], v[158:161], v[182:185], v[94:97]
	v_mfma_f32_16x16x32_bf16 v[82:85], v[150:153], v[190:193], v[82:85]
	v_mfma_f32_16x16x32_bf16 v[78:81], v[158:161], v[190:193], v[78:81]
	v_mfma_f32_16x16x32_bf16 v[130:133], v[154:157], v[170:173], v[130:133]
	v_mfma_f32_16x16x32_bf16 v[126:129], v[162:165], v[170:173], v[126:129]
	v_mfma_f32_16x16x32_bf16 v[114:117], v[154:157], v[178:181], v[114:117]
	v_mfma_f32_16x16x32_bf16 v[110:113], v[162:165], v[178:181], v[110:113]
	v_mfma_f32_16x16x32_bf16 v[98:101], v[154:157], v[186:189], v[98:101]
	v_mfma_f32_16x16x32_bf16 v[94:97], v[162:165], v[186:189], v[94:97]
	v_mfma_f32_16x16x32_bf16 v[82:85], v[154:157], v[194:197], v[82:85]
	v_mfma_f32_16x16x32_bf16 v[78:81], v[162:165], v[194:197], v[78:81]
	v_mfma_f32_16x16x32_bf16 v[122:125], v[134:137], v[166:169], v[122:125]
	v_mfma_f32_16x16x32_bf16 v[118:121], v[142:145], v[166:169], v[118:121]
	v_mfma_f32_16x16x32_bf16 v[106:109], v[134:137], v[174:177], v[106:109]
	v_mfma_f32_16x16x32_bf16 v[102:105], v[142:145], v[174:177], v[102:105]
	v_mfma_f32_16x16x32_bf16 v[90:93], v[134:137], v[182:185], v[90:93]
	v_mfma_f32_16x16x32_bf16 v[86:89], v[142:145], v[182:185], v[86:89]
	v_mfma_f32_16x16x32_bf16 v[74:77], v[134:137], v[190:193], v[74:77]
	v_mfma_f32_16x16x32_bf16 v[70:73], v[142:145], v[190:193], v[70:73]
	v_mfma_f32_16x16x32_bf16 v[122:125], v[138:141], v[170:173], v[122:125]
	v_mfma_f32_16x16x32_bf16 v[118:121], v[146:149], v[170:173], v[118:121]
	v_mfma_f32_16x16x32_bf16 v[106:109], v[138:141], v[178:181], v[106:109]
	v_mfma_f32_16x16x32_bf16 v[102:105], v[146:149], v[178:181], v[102:105]
	v_mfma_f32_16x16x32_bf16 v[90:93], v[138:141], v[186:189], v[90:93]
	v_mfma_f32_16x16x32_bf16 v[86:89], v[146:149], v[186:189], v[86:89]
	v_mfma_f32_16x16x32_bf16 v[74:77], v[138:141], v[194:197], v[74:77]
	v_mfma_f32_16x16x32_bf16 v[70:73], v[146:149], v[194:197], v[70:73]
	s_barrier
	s_add_i32 s38, s51, s0
	v_lshl_add_u64 v[4:5], v[4:5], 0, s[14:15]
	s_mov_b32 m0, s38
	ds_read_b128 v[190:193], v220 offset:49152
	ds_read_b128 v[194:197], v220 offset:50176
	ds_read_b128 v[182:185], v220 offset:51200
	ds_read_b128 v[186:189], v220 offset:52224
	ds_read_b128 v[174:177], v220 offset:53248
	ds_read_b128 v[178:181], v220 offset:54272
	ds_read_b128 v[166:169], v220 offset:55296
	ds_read_b128 v[170:173], v220 offset:56320
	global_load_lds_dwordx4 v[4:5], off
	s_add_i32 m0, s38, 0x2000
	s_add_u32 s36, s36, 0x20080
	v_lshl_add_u64 v[4:5], v[210:211], 0, s[14:15]
	s_addc_u32 s37, s37, 0
	s_add_i32 s38, s52, s0
	global_load_lds_dwordx4 v[4:5], off
	v_lshl_add_u64 v[4:5], s[36:37], 0, v[200:201]
	s_mov_b32 m0, s38
	s_and_b64 vcc, exec, s[6:7]
	global_load_lds_dwordx4 v[4:5], off
	v_lshl_add_u64 v[4:5], s[36:37], 0, v[204:205]
	s_add_i32 m0, s38, 0x2000
	s_nop 0
	global_load_lds_dwordx4 v[4:5], off
	v_lshl_add_u64 v[4:5], v[212:213], 0, s[14:15]
	s_mov_b32 m0, s40
	s_nop 0
	global_load_lds_dwordx4 v[4:5], off
	v_lshl_add_u64 v[4:5], v[214:215], 0, s[14:15]
	s_mov_b32 m0, s41
	s_nop 0
	global_load_lds_dwordx4 v[4:5], off
	s_waitcnt vmcnt(8)
	s_waitcnt lgkmcnt(0)
	s_barrier
	s_cbranch_vccnz .LBB0_1428
	s_waitcnt lgkmcnt(0)
	v_mfma_f32_16x16x32_bf16 v[66:69], v[150:153], v[190:193], v[66:69]
	v_mfma_f32_16x16x32_bf16 v[62:65], v[158:161], v[190:193], v[62:65]
	v_mfma_f32_16x16x32_bf16 v[50:53], v[150:153], v[182:185], v[50:53]
	v_mfma_f32_16x16x32_bf16 v[46:49], v[158:161], v[182:185], v[46:49]
	v_mfma_f32_16x16x32_bf16 v[34:37], v[150:153], v[174:177], v[34:37]
	v_mfma_f32_16x16x32_bf16 v[30:33], v[158:161], v[174:177], v[30:33]
	v_mfma_f32_16x16x32_bf16 v[18:21], v[150:153], v[166:169], v[18:21]
	v_mfma_f32_16x16x32_bf16 v[14:17], v[158:161], v[166:169], v[14:17]
	v_mfma_f32_16x16x32_bf16 v[66:69], v[154:157], v[194:197], v[66:69]
	v_mfma_f32_16x16x32_bf16 v[62:65], v[162:165], v[194:197], v[62:65]
	v_mfma_f32_16x16x32_bf16 v[50:53], v[154:157], v[186:189], v[50:53]
	v_mfma_f32_16x16x32_bf16 v[46:49], v[162:165], v[186:189], v[46:49]
	v_mfma_f32_16x16x32_bf16 v[34:37], v[154:157], v[178:181], v[34:37]
	v_mfma_f32_16x16x32_bf16 v[30:33], v[162:165], v[178:181], v[30:33]
	v_mfma_f32_16x16x32_bf16 v[18:21], v[154:157], v[170:173], v[18:21]
	v_mfma_f32_16x16x32_bf16 v[14:17], v[162:165], v[170:173], v[14:17]
	v_mfma_f32_16x16x32_bf16 v[58:61], v[134:137], v[190:193], v[58:61]
	v_mfma_f32_16x16x32_bf16 v[54:57], v[142:145], v[190:193], v[54:57]
	v_mfma_f32_16x16x32_bf16 v[42:45], v[134:137], v[182:185], v[42:45]
	v_mfma_f32_16x16x32_bf16 v[38:41], v[142:145], v[182:185], v[38:41]
	v_mfma_f32_16x16x32_bf16 v[26:29], v[134:137], v[174:177], v[26:29]
	v_mfma_f32_16x16x32_bf16 v[22:25], v[142:145], v[174:177], v[22:25]
	v_mfma_f32_16x16x32_bf16 v[10:13], v[134:137], v[166:169], v[10:13]
	v_mfma_f32_16x16x32_bf16 v[4:7], v[142:145], v[166:169], v[6:9]
	v_mfma_f32_16x16x32_bf16 v[58:61], v[138:141], v[194:197], v[58:61]
	v_mfma_f32_16x16x32_bf16 v[54:57], v[146:149], v[194:197], v[54:57]
	v_mfma_f32_16x16x32_bf16 v[42:45], v[138:141], v[186:189], v[42:45]
	v_mfma_f32_16x16x32_bf16 v[38:41], v[146:149], v[186:189], v[38:41]
	v_mfma_f32_16x16x32_bf16 v[26:29], v[138:141], v[178:181], v[26:29]
	v_mfma_f32_16x16x32_bf16 v[22:25], v[146:149], v[178:181], v[22:25]
	v_mfma_f32_16x16x32_bf16 v[10:13], v[138:141], v[170:173], v[10:13]
	v_mfma_f32_16x16x32_bf16 v[6:9], v[146:149], v[170:173], v[4:7]
	s_branch .LBB0_1428
